# attention: waves 4-7 take the per-tile barrier before the softmax (half-step stagger vs waves 0-3), all three attention bodies
# speedup vs baseline: 1.0039x; 1.0039x over previous
_Z10hybrid_fwd4Args:
	s_load_dword s64, s[0:1], 0xc8
	s_mov_b32 s65, s2
	s_add_u32 s2, s0, 0xc8
	s_addc_u32 s3, s1, 0
	v_readfirstlane_b32 s10, v0
	v_writelane_b32 v255, s2, 0
	s_mov_b32 s66, s65
	s_mov_b32 s100, s10
	s_nop 0
	v_writelane_b32 v255, s3, 1
	s_waitcnt lgkmcnt(0)
	s_and_b32 s2, s64, 7
	s_cmp_lg_u32 s2, 0
	s_cbranch_scc1 .LBB0_1
	s_getpc_b64 s[98:99]

.LBB0_514:
	v_readlane_b32 s2, v255, 46
	v_readlane_b32 s3, v255, 47
	v_readlane_b32 s3, v255, 56
	s_or_b32 s6, s3, s2
	v_readlane_b32 s2, v255, 54
	v_readlane_b32 s3, v255, 55
	s_lshl_b64 s[2:3], s[2:3], 2
	v_readlane_b32 s4, v255, 19
	s_add_u32 s4, s4, s2
	v_readlane_b32 s2, v255, 20
	v_readlane_b32 s80, v255, 43
	s_addc_u32 s5, s2, s3
	s_mul_hi_i32 s2, s6, 0x6800
	s_mulk_i32 s6, 0x6800
	v_readlane_b32 s85, v255, 44
	s_add_u32 s3, s80, s6
	s_addc_u32 s6, s85, s2
	v_readlane_b32 s2, v255, 48
	s_lshl_b32 s2, s2, 1
	s_add_u32 s2, s3, s2
	v_readlane_b32 s89, v255, 45
	s_addc_u32 s3, s6, 0
	s_lshl_b32 s6, s33, 2
	s_add_i32 s6, s89, s6
	v_mov_b32_e32 v166, s6
	ds_read_b32 v166, v166
	s_movk_i32 s84, 0x6800
	v_readlane_b32 s79, v255, 41
	v_readlane_b32 s15, v255, 40
	v_readlane_b32 s10, v255, 53
	s_waitcnt lgkmcnt(0)
	v_sub_f32_e32 v166, v166, v178
	v_mul_f32_e32 v166, 0x3fb8aa3b, v166
	v_exp_f32_e32 v166, v166
	s_nop 0
	v_fma_f32 v204, v144, v166, 0
	v_fmac_f32_e32 v204, v145, v166
	v_fmac_f32_e32 v204, v146, v166
	v_fmac_f32_e32 v204, v147, v166
	v_fmac_f32_e32 v204, v148, v166
	v_fmac_f32_e32 v204, v149, v166
	v_fmac_f32_e32 v204, v150, v166
	v_fmac_f32_e32 v204, v151, v166
	v_fmac_f32_e32 v204, v152, v166
	v_fmac_f32_e32 v204, v153, v166
	v_fmac_f32_e32 v204, v154, v166
	v_fmac_f32_e32 v204, v155, v166
	v_fmac_f32_e32 v204, v156, v166
	v_fmac_f32_e32 v204, v157, v166
	v_fmac_f32_e32 v204, v158, v166
	v_fmac_f32_e32 v204, v159, v166
	v_fmac_f32_e32 v204, v128, v166
	v_fmac_f32_e32 v204, v129, v166
	v_fmac_f32_e32 v204, v130, v166
	v_fmac_f32_e32 v204, v131, v166
	v_fmac_f32_e32 v204, v132, v166
	v_fmac_f32_e32 v204, v133, v166
	v_fmac_f32_e32 v204, v134, v166
	v_fmac_f32_e32 v204, v135, v166
	v_fmac_f32_e32 v204, v136, v166
	v_fmac_f32_e32 v204, v137, v166
	v_fmac_f32_e32 v204, v138, v166
	v_fmac_f32_e32 v204, v139, v166
	v_fmac_f32_e32 v204, v140, v166
	v_fmac_f32_e32 v204, v141, v166
	v_fmac_f32_e32 v204, v142, v166
	v_mul_f32_e32 v167, v144, v166
	v_mul_f32_e32 v168, v128, v166
	v_mul_f32_e32 v169, v145, v166
	v_mul_f32_e32 v170, v129, v166
	v_mul_f32_e32 v171, v146, v166
	v_mul_f32_e32 v172, v130, v166
	v_mul_f32_e32 v173, v147, v166
	v_mul_f32_e32 v178, v131, v166
	v_mul_f32_e32 v180, v148, v166
	v_mul_f32_e32 v181, v132, v166
	v_mul_f32_e32 v182, v149, v166
	v_mul_f32_e32 v183, v133, v166
	v_mul_f32_e32 v184, v150, v166
	v_mul_f32_e32 v185, v134, v166
	v_mul_f32_e32 v186, v151, v166
	v_mul_f32_e32 v187, v135, v166
	v_mul_f32_e32 v188, v152, v166
	v_mul_f32_e32 v189, v136, v166
	v_mul_f32_e32 v190, v153, v166
	v_mul_f32_e32 v191, v137, v166
	v_mul_f32_e32 v192, v154, v166
	v_mul_f32_e32 v193, v138, v166
	v_mul_f32_e32 v194, v155, v166
	v_mul_f32_e32 v195, v139, v166
	v_mul_f32_e32 v196, v156, v166
	v_mul_f32_e32 v197, v140, v166
	v_mul_f32_e32 v198, v157, v166
	v_mul_f32_e32 v199, v141, v166
	v_mul_f32_e32 v200, v158, v166
	v_mul_f32_e32 v201, v142, v166
	v_mul_f32_e32 v202, v159, v166
	v_mul_f32_e32 v203, v143, v166
	v_fmac_f32_e32 v204, v143, v166
	v_cvt_pk_bf16_f32 v128, v167, v169
	v_cvt_pk_bf16_f32 v129, v171, v173
	v_cvt_pk_bf16_f32 v130, v180, v182
	v_cvt_pk_bf16_f32 v131, v184, v186
	v_cvt_pk_bf16_f32 v132, v188, v190
	v_cvt_pk_bf16_f32 v133, v192, v194
	v_cvt_pk_bf16_f32 v134, v196, v198
	v_cvt_pk_bf16_f32 v135, v200, v202
	v_cvt_pk_bf16_f32 v136, v168, v170
	v_cvt_pk_bf16_f32 v137, v172, v178
	v_cvt_pk_bf16_f32 v138, v181, v183
	v_cvt_pk_bf16_f32 v139, v185, v187
	v_cvt_pk_bf16_f32 v140, v189, v191
	v_cvt_pk_bf16_f32 v141, v193, v195
	v_cvt_pk_bf16_f32 v142, v197, v199
	v_cvt_pk_bf16_f32 v143, v201, v203
	s_nop 0
	v_permlane32_swap_b32_e32 v128, v130
	v_permlane32_swap_b32_e32 v129, v131
	v_permlane32_swap_b32_e32 v132, v134
	v_permlane32_swap_b32_e32 v133, v135
	v_permlane32_swap_b32_e32 v136, v138
	v_permlane32_swap_b32_e32 v137, v139
	v_permlane32_swap_b32_e32 v140, v142
	v_permlane32_swap_b32_e32 v141, v143
	s_bitcmp1_b32 s100, 8
	s_cbranch_scc1 .Lstg_b8
	s_waitcnt vmcnt(0)
	s_waitcnt lgkmcnt(0)
	s_barrier
.Lstg_b8:
	v_mov_b64_e32 v[144:145], s[70:71]
	flat_load_dword v146, v[144:145] sc0 sc1
	s_waitcnt vmcnt(0)
	v_mov_b64_e32 v[144:145], s[76:77]
	flat_load_dword v144, v[144:145] sc0 sc1
	s_waitcnt vmcnt(0) lgkmcnt(0)
	v_readfirstlane_b32 s6, v146
	v_readfirstlane_b32 s7, v144
	s_nop 1
	v_lshl_add_u64 v[144:145], s[6:7], 0, v[162:163]
	s_mov_b32 s6, m0
	s_mov_b32 m0, s81
	s_nop 0
	global_load_lds_dwordx4 v[144:145], off
	s_mov_b32 m0, s6
	v_lshl_add_u64 v[146:147], v[144:145], 0, s[86:87]
	s_mov_b32 s6, m0
	s_mov_b32 m0, s78
	s_nop 0
	global_load_lds_dwordx4 v[146:147], off
	s_mov_b32 m0, s6
	v_lshl_add_u64 v[146:147], v[144:145], 0, s[62:63]
	s_mov_b32 s6, m0
	s_mov_b32 m0, s69
	s_nop 0
	global_load_lds_dwordx4 v[146:147], off
	s_mov_b32 m0, s6
	s_mov_b64 s[6:7], 0x180
	v_lshl_add_u64 v[144:145], v[144:145], 0, s[6:7]
	s_mov_b32 s6, m0
	s_mov_b32 m0, s68
	s_nop 0
	global_load_lds_dwordx4 v[144:145], off
	s_mov_b32 m0, s6
	ds_read_b64_tr_b16 v[144:145], v177 offset:0x8000
	ds_read_b64_tr_b16 v[146:147], v177 offset:0x9000
	ds_read_b64_tr_b16 v[148:149], v177 offset:0xa000
	ds_read_b64_tr_b16 v[150:151], v177 offset:0xb000
	ds_read_b64_tr_b16 v[152:153], v177 offset:0xc000
	ds_read_b64_tr_b16 v[154:155], v177 offset:0xd000
	ds_read_b64_tr_b16 v[156:157], v177 offset:0xe000
	ds_read_b64_tr_b16 v[158:159], v177 offset:0xf000
	ds_read_b64_tr_b16 v[166:167], v177 offset:0x8200
	ds_read_b64_tr_b16 v[168:169], v177 offset:0x9200
	ds_read_b64_tr_b16 v[170:171], v177 offset:0xa200
	ds_read_b64_tr_b16 v[172:173], v177 offset:0xb200
	ds_read_b64_tr_b16 v[180:181], v177 offset:0xc200
	ds_read_b64_tr_b16 v[182:183], v177 offset:0xd200
	ds_read_b64_tr_b16 v[184:185], v177 offset:0xe200
	ds_read_b64_tr_b16 v[186:187], v177 offset:0xf200
	s_waitcnt lgkmcnt(8)
	s_nop 1
	v_mfma_f32_32x32x16_bf16 v[112:127], v[144:147], v[128:131], v[112:127]
	v_mfma_f32_32x32x16_bf16 v[112:127], v[148:151], v[132:135], v[112:127]
	v_mfma_f32_32x32x16_bf16 v[112:127], v[152:155], v[136:139], v[112:127]
	v_mfma_f32_32x32x16_bf16 v[112:127], v[156:159], v[140:143], v[112:127]
	ds_read_b64_tr_b16 v[144:145], v177 offset:0x8400
	ds_read_b64_tr_b16 v[146:147], v177 offset:0x9400
	ds_read_b64_tr_b16 v[148:149], v177 offset:0xa400
	ds_read_b64_tr_b16 v[150:151], v177 offset:0xb400
	ds_read_b64_tr_b16 v[152:153], v177 offset:0xc400
	ds_read_b64_tr_b16 v[154:155], v177 offset:0xd400
	ds_read_b64_tr_b16 v[156:157], v177 offset:0xe400
	ds_read_b64_tr_b16 v[158:159], v177 offset:0xf400
	s_waitcnt lgkmcnt(8)
	v_mfma_f32_32x32x16_bf16 v[0:15], v[166:169], v[128:131], v[0:15]
	v_mfma_f32_32x32x16_bf16 v[0:15], v[170:173], v[132:135], v[0:15]
	v_mfma_f32_32x32x16_bf16 v[0:15], v[180:183], v[136:139], v[0:15]
	v_mfma_f32_32x32x16_bf16 v[0:15], v[184:187], v[140:143], v[0:15]
	ds_read_b64_tr_b16 v[166:167], v177 offset:0x8600
	ds_read_b64_tr_b16 v[168:169], v177 offset:0x9600
	ds_read_b64_tr_b16 v[170:171], v177 offset:0xa600
	ds_read_b64_tr_b16 v[172:173], v177 offset:0xb600
	ds_read_b64_tr_b16 v[180:181], v177 offset:0xc600
	ds_read_b64_tr_b16 v[182:183], v177 offset:0xd600
	ds_read_b64_tr_b16 v[184:185], v177 offset:0xe600
	ds_read_b64_tr_b16 v[186:187], v177 offset:0xf600
	s_waitcnt lgkmcnt(8)
	v_mfma_f32_32x32x16_bf16 v[16:31], v[144:147], v[128:131], v[16:31]
	v_mfma_f32_32x32x16_bf16 v[16:31], v[148:151], v[132:135], v[16:31]
	v_mfma_f32_32x32x16_bf16 v[16:31], v[152:155], v[136:139], v[16:31]
	v_mfma_f32_32x32x16_bf16 v[16:31], v[156:159], v[140:143], v[16:31]
	ds_read_b64_tr_b16 v[144:145], v177 offset:0x8800
	ds_read_b64_tr_b16 v[146:147], v177 offset:0x9800
	ds_read_b64_tr_b16 v[148:149], v177 offset:0xa800
	ds_read_b64_tr_b16 v[150:151], v177 offset:0xb800
	ds_read_b64_tr_b16 v[152:153], v177 offset:0xc800
	ds_read_b64_tr_b16 v[154:155], v177 offset:0xd800
	ds_read_b64_tr_b16 v[156:157], v177 offset:0xe800
	ds_read_b64_tr_b16 v[158:159], v177 offset:0xf800
	s_waitcnt lgkmcnt(8)
	v_mfma_f32_32x32x16_bf16 v[32:47], v[166:169], v[128:131], v[32:47]
	v_mfma_f32_32x32x16_bf16 v[32:47], v[170:173], v[132:135], v[32:47]
	v_mfma_f32_32x32x16_bf16 v[32:47], v[180:183], v[136:139], v[32:47]
	v_mfma_f32_32x32x16_bf16 v[32:47], v[184:187], v[140:143], v[32:47]
	ds_read_b64_tr_b16 v[166:167], v177 offset:0x8a00
	ds_read_b64_tr_b16 v[168:169], v177 offset:0x9a00
	ds_read_b64_tr_b16 v[170:171], v177 offset:0xaa00
	ds_read_b64_tr_b16 v[172:173], v177 offset:0xba00
	ds_read_b64_tr_b16 v[180:181], v177 offset:0xca00
	ds_read_b64_tr_b16 v[182:183], v177 offset:0xda00
	ds_read_b64_tr_b16 v[184:185], v177 offset:0xea00
	ds_read_b64_tr_b16 v[186:187], v177 offset:0xfa00
	s_waitcnt lgkmcnt(8)
	v_mfma_f32_32x32x16_bf16 v[48:63], v[144:147], v[128:131], v[48:63]
	v_mfma_f32_32x32x16_bf16 v[48:63], v[148:151], v[132:135], v[48:63]
	v_mfma_f32_32x32x16_bf16 v[48:63], v[152:155], v[136:139], v[48:63]
	v_mfma_f32_32x32x16_bf16 v[48:63], v[156:159], v[140:143], v[48:63]
	ds_read_b64_tr_b16 v[144:145], v177 offset:0x8c00
	ds_read_b64_tr_b16 v[146:147], v177 offset:0x9c00
	ds_read_b64_tr_b16 v[148:149], v177 offset:0xac00
	ds_read_b64_tr_b16 v[150:151], v177 offset:0xbc00
	ds_read_b64_tr_b16 v[152:153], v177 offset:0xcc00
	ds_read_b64_tr_b16 v[154:155], v177 offset:0xdc00
	ds_read_b64_tr_b16 v[156:157], v177 offset:0xec00
	ds_read_b64_tr_b16 v[158:159], v177 offset:0xfc00
	s_waitcnt lgkmcnt(8)
	v_mfma_f32_32x32x16_bf16 v[64:79], v[166:169], v[128:131], v[64:79]
	v_mfma_f32_32x32x16_bf16 v[64:79], v[170:173], v[132:135], v[64:79]
	v_mfma_f32_32x32x16_bf16 v[64:79], v[180:183], v[136:139], v[64:79]
	v_mfma_f32_32x32x16_bf16 v[64:79], v[184:187], v[140:143], v[64:79]
	ds_read_b64_tr_b16 v[166:167], v177 offset:0x8e00
	ds_read_b64_tr_b16 v[168:169], v177 offset:0x9e00
	ds_read_b64_tr_b16 v[170:171], v177 offset:0xae00
	ds_read_b64_tr_b16 v[172:173], v177 offset:0xbe00
	ds_read_b64_tr_b16 v[180:181], v177 offset:0xce00
	ds_read_b64_tr_b16 v[182:183], v177 offset:0xde00
	ds_read_b64_tr_b16 v[184:185], v177 offset:0xee00
	ds_read_b64_tr_b16 v[186:187], v177 offset:0xfe00
	s_waitcnt lgkmcnt(8)
	v_mfma_f32_32x32x16_bf16 v[80:95], v[144:147], v[128:131], v[80:95]
	v_mfma_f32_32x32x16_bf16 v[80:95], v[148:151], v[132:135], v[80:95]
	v_mfma_f32_32x32x16_bf16 v[80:95], v[152:155], v[136:139], v[80:95]
	v_mfma_f32_32x32x16_bf16 v[80:95], v[156:159], v[140:143], v[80:95]
	s_waitcnt lgkmcnt(0)
	v_mfma_f32_32x32x16_bf16 v[96:111], v[166:169], v[128:131], v[96:111]
	v_mfma_f32_32x32x16_bf16 v[96:111], v[170:173], v[132:135], v[96:111]
	v_mfma_f32_32x32x16_bf16 v[96:111], v[180:183], v[136:139], v[96:111]
	v_mfma_f32_32x32x16_bf16 v[96:111], v[184:187], v[140:143], v[96:111]
	v_readlane_b32 s6, v255, 31
	v_readlane_b32 s7, v255, 32
	v_readlane_b32 s12, v255, 49
	v_readlane_b32 s13, v255, 50
	v_mov_b64_e32 v[128:129], s[6:7]
	v_readlane_b32 s6, v255, 35
	v_readlane_b32 s7, v255, 36
	flat_load_dword v130, v[128:129] sc0 sc1
	s_waitcnt vmcnt(0)
	s_ashr_i32 s13, s12, 31
	v_mov_b64_e32 v[128:129], s[6:7]
	flat_load_dword v131, v[128:129] sc0 sc1
	s_waitcnt vmcnt(0)
	s_lshl_b64 s[6:7], s[12:13], 11
	v_lshl_or_b32 v128, v175, 11, v174
	v_mov_b32_e32 v129, v161
	s_waitcnt lgkmcnt(0)
	s_barrier
	v_add_f32_e32 v158, v179, v204
	s_waitcnt lgkmcnt(0)
	v_readfirstlane_b32 s9, v130
	s_add_u32 s6, s9, s6
	v_readfirstlane_b32 s8, v131
	s_addc_u32 s7, s8, s7
	v_lshl_add_u64 v[156:157], s[6:7], 0, v[128:129]
	flat_load_dwordx4 v[128:131], v[156:157]
	flat_load_dwordx4 v[132:135], v[156:157] offset:32
	flat_load_dwordx4 v[136:139], v[156:157] offset:64
	flat_load_dwordx4 v[140:143], v[156:157] offset:96
	flat_load_dwordx4 v[144:147], v[156:157] offset:128
	flat_load_dwordx4 v[148:151], v[156:157] offset:160
	flat_load_dwordx4 v[152:155], v[156:157] offset:192
	flat_load_dwordx4 v[166:169], v[156:157] offset:224
	v_readlane_b32 s6, v255, 51
	v_readlane_b32 s7, v255, 52
	s_add_u32 s4, s4, s6
	s_addc_u32 s5, s5, s7
	v_lshl_add_u64 v[156:157], s[4:5], 0, v[160:161]
	flat_load_dword v156, v[156:157]
	v_mov_b32_e32 v157, v158
	s_nop 1
	v_permlane32_swap_b32_e32 v158, v157
	v_add_f32_e32 v157, v158, v157
	s_mul_i32 s5, s12, 0x6800
	s_mul_hi_i32 s4, s12, 0x6800
	s_add_u32 s2, s2, s5
	s_addc_u32 s3, s3, s4
	s_add_u32 s4, s2, 0x1000
	s_addc_u32 s5, s3, 0
	v_readlane_b32 s2, v255, 27
	s_waitcnt vmcnt(0) lgkmcnt(0)
	v_max_f32_e32 v156, v156, v156
	v_max_f32_e64 v156, |v157|, v156
	v_rcp_f32_e32 v194, v156
	s_nop 0
	v_mul_f32_e32 v196, v113, v194
	v_mul_f32_e32 v213, v115, v194
	v_mul_f32_e32 v195, v112, v194
	v_mul_f32_e32 v197, v114, v194
	v_mul_f32_e32 v217, v119, v194
	v_mul_f32_e32 v119, v52, v194
	v_mul_f32_e32 v115, v54, v194
	v_mul_f32_e32 v54, v56, v194
	v_mul_f32_e32 v52, v57, v194
	v_mul_f32_e32 v56, v196, v196
	v_mul_f32_e32 v57, v213, v213
	v_mul_f32_e32 v215, v117, v194
	v_fmac_f32_e32 v56, v195, v195
	v_fmac_f32_e32 v57, v197, v197
	v_mul_f32_e32 v214, v116, v194
	v_mul_f32_e32 v216, v118, v194
	v_mul_f32_e32 v114, v50, v194
	v_mul_f32_e32 v50, v58, v194
	v_add_f32_e32 v56, v56, v57
	v_mul_f32_e32 v57, v215, v215
	v_mul_f32_e32 v58, v217, v217
	v_mul_f32_e32 v219, v121, v194
	v_mul_f32_e32 v210, v123, v194
	v_fmac_f32_e32 v57, v214, v214
	v_fmac_f32_e32 v58, v216, v216
	v_mul_f32_e32 v218, v120, v194
	v_mul_f32_e32 v212, v122, v194
	v_mul_f32_e32 v118, v48, v194
	v_mul_f32_e32 v48, v59, v194
	v_add_f32_e32 v57, v57, v58
	v_mul_f32_e32 v58, v219, v219
	v_mul_f32_e32 v59, v210, v210
	v_mul_f32_e32 v221, v125, v194
	v_mul_f32_e32 v211, v127, v194
	v_fmac_f32_e32 v58, v218, v218
	v_fmac_f32_e32 v59, v212, v212
	v_mul_f32_e32 v220, v124, v194
	v_mul_f32_e32 v222, v126, v194
	v_mul_f32_e32 v113, v55, v194
	v_mul_f32_e32 v55, v60, v194
	v_add_f32_e32 v58, v58, v59
	v_mul_f32_e32 v59, v221, v221
	v_mul_f32_e32 v60, v211, v211
	v_fmac_f32_e32 v59, v220, v220
	v_fmac_f32_e32 v60, v222, v222
	v_add_f32_e32 v59, v59, v60
	v_mul_f32_e32 v206, v1, v194
	v_mul_f32_e32 v202, v3, v194
	v_add_f32_e32 v56, v56, v57
	v_add_f32_e32 v57, v58, v59
	v_mul_f32_e32 v208, v0, v194
	v_mul_f32_e32 v204, v2, v194
	v_add_f32_e32 v56, v56, v57
	v_mul_f32_e32 v57, v206, v206
	v_mul_f32_e32 v58, v202, v202
	v_mul_f32_e32 v207, v5, v194
	v_mul_f32_e32 v203, v7, v194
	v_fmac_f32_e32 v57, v208, v208
	v_fmac_f32_e32 v58, v204, v204
	v_mul_f32_e32 v209, v4, v194
	v_mul_f32_e32 v205, v6, v194
	v_add_f32_e32 v57, v57, v58
	v_mul_f32_e32 v58, v207, v207
	v_mul_f32_e32 v59, v203, v203
	v_mul_f32_e32 v198, v9, v194
	v_mul_f32_e32 v190, v11, v194
	v_fmac_f32_e32 v58, v209, v209
	v_fmac_f32_e32 v59, v205, v205
	v_mul_f32_e32 v200, v8, v194
	v_mul_f32_e32 v192, v10, v194
	v_add_f32_e32 v58, v58, v59
	v_mul_f32_e32 v59, v198, v198
	v_mul_f32_e32 v60, v190, v190
	v_mul_f32_e32 v199, v13, v194
	v_mul_f32_e32 v191, v15, v194
	v_fmac_f32_e32 v59, v200, v200
	v_fmac_f32_e32 v60, v192, v192
	v_mul_f32_e32 v201, v12, v194
	v_mul_f32_e32 v193, v14, v194
	v_mul_f32_e32 v117, v53, v194
	v_mul_f32_e32 v53, v61, v194
	v_add_f32_e32 v59, v59, v60
	v_mul_f32_e32 v60, v199, v199
	v_mul_f32_e32 v61, v191, v191
	v_fmac_f32_e32 v60, v201, v201
	v_fmac_f32_e32 v61, v193, v193
	v_add_f32_e32 v60, v60, v61
	v_add_f32_e32 v57, v57, v58
	v_add_f32_e32 v58, v59, v60
	v_mul_f32_e32 v186, v17, v194
	v_mul_f32_e32 v182, v19, v194
	v_add_f32_e32 v57, v57, v58
	v_mul_f32_e32 v188, v16, v194
	v_mul_f32_e32 v184, v18, v194
	v_add_f32_e32 v56, v56, v57
	v_mul_f32_e32 v57, v186, v186
	v_mul_f32_e32 v58, v182, v182
	v_mul_f32_e32 v187, v21, v194
	v_mul_f32_e32 v183, v23, v194
	v_fmac_f32_e32 v57, v188, v188
	v_fmac_f32_e32 v58, v184, v184
	v_mul_f32_e32 v189, v20, v194
	v_mul_f32_e32 v185, v22, v194
	v_add_f32_e32 v57, v57, v58
	v_mul_f32_e32 v58, v187, v187
	v_mul_f32_e32 v59, v183, v183
	v_mul_f32_e32 v178, v25, v194
	v_mul_f32_e32 v171, v27, v194
	v_fmac_f32_e32 v58, v189, v189
	v_fmac_f32_e32 v59, v185, v185
	v_mul_f32_e32 v180, v24, v194
	v_mul_f32_e32 v173, v26, v194
	v_add_f32_e32 v58, v58, v59
	v_mul_f32_e32 v59, v178, v178
	v_mul_f32_e32 v60, v171, v171
	v_mul_f32_e32 v179, v29, v194
	v_mul_f32_e32 v172, v31, v194
	v_fmac_f32_e32 v59, v180, v180
	v_fmac_f32_e32 v60, v173, v173
	v_mul_f32_e32 v181, v28, v194
	v_mul_f32_e32 v177, v30, v194
	v_add_f32_e32 v59, v59, v60
	v_mul_f32_e32 v60, v179, v179
	v_mul_f32_e32 v61, v172, v172
	v_fmac_f32_e32 v60, v181, v181
	v_fmac_f32_e32 v61, v177, v177
	v_add_f32_e32 v60, v60, v61
	v_add_f32_e32 v57, v57, v58
	v_add_f32_e32 v58, v59, v60
	v_mul_f32_e32 v160, v33, v194
	v_mul_f32_e32 v156, v35, v194
	v_add_f32_e32 v57, v57, v58
	v_mul_f32_e32 v163, v32, v194
	v_mul_f32_e32 v158, v34, v194
	v_add_f32_e32 v56, v57, v56
	v_mul_f32_e32 v57, v160, v160
	v_mul_f32_e32 v58, v156, v156
	v_mul_f32_e32 v162, v37, v194
	v_mul_f32_e32 v157, v39, v194
	v_fmac_f32_e32 v57, v163, v163
	v_fmac_f32_e32 v58, v158, v158
	v_mul_f32_e32 v170, v36, v194
	v_mul_f32_e32 v159, v38, v194
	v_add_f32_e32 v57, v57, v58
	v_mul_f32_e32 v58, v162, v162
	v_mul_f32_e32 v59, v157, v157
	v_mul_f32_e32 v124, v41, v194
	v_mul_f32_e32 v120, v43, v194
	v_fmac_f32_e32 v58, v170, v170
	v_fmac_f32_e32 v59, v159, v159
	v_mul_f32_e32 v126, v40, v194
	v_mul_f32_e32 v122, v42, v194
	v_add_f32_e32 v58, v58, v59
	v_mul_f32_e32 v59, v124, v124
	v_mul_f32_e32 v60, v120, v120
	v_mul_f32_e32 v125, v45, v194
	v_mul_f32_e32 v121, v47, v194
	v_fmac_f32_e32 v59, v126, v126
	v_fmac_f32_e32 v60, v122, v122
	v_mul_f32_e32 v127, v44, v194
	v_mul_f32_e32 v123, v46, v194
	v_add_f32_e32 v59, v59, v60
	v_mul_f32_e32 v60, v125, v125
	v_mul_f32_e32 v61, v121, v121
	v_fmac_f32_e32 v60, v127, v127
	v_fmac_f32_e32 v61, v123, v123
	v_add_f32_e32 v60, v60, v61
	v_add_f32_e32 v57, v57, v58
	v_add_f32_e32 v58, v59, v60
	v_mul_f32_e32 v116, v49, v194
	v_mul_f32_e32 v112, v51, v194
	v_add_f32_e32 v57, v57, v58
	v_add_f32_e32 v56, v57, v56
	v_mul_f32_e32 v57, v116, v116
	v_mul_f32_e32 v58, v112, v112
	v_fmac_f32_e32 v57, v118, v118
	v_fmac_f32_e32 v58, v114, v114
	v_add_f32_e32 v57, v57, v58
	v_mul_f32_e32 v58, v117, v117
	v_mul_f32_e32 v59, v113, v113
	v_fmac_f32_e32 v58, v119, v119
	v_fmac_f32_e32 v59, v115, v115
	v_add_f32_e32 v58, v58, v59
	v_mul_f32_e32 v59, v52, v52
	v_mul_f32_e32 v60, v48, v48
	v_mul_f32_e32 v49, v63, v194
	v_fmac_f32_e32 v59, v54, v54
	v_fmac_f32_e32 v60, v50, v50
	v_mul_f32_e32 v51, v62, v194
	v_add_f32_e32 v59, v59, v60
	v_mul_f32_e32 v60, v53, v53
	v_mul_f32_e32 v61, v49, v49
	v_fmac_f32_e32 v60, v55, v55
	v_fmac_f32_e32 v61, v51, v51
	v_add_f32_e32 v60, v60, v61
	v_add_f32_e32 v57, v57, v58
	v_add_f32_e32 v58, v59, v60
	v_mul_f32_e32 v44, v65, v194
	v_mul_f32_e32 v40, v67, v194
	v_add_f32_e32 v57, v57, v58
	v_mul_f32_e32 v46, v64, v194
	v_mul_f32_e32 v42, v66, v194
	v_add_f32_e32 v56, v57, v56
	v_mul_f32_e32 v57, v44, v44
	v_mul_f32_e32 v58, v40, v40
	v_mul_f32_e32 v45, v69, v194
	v_mul_f32_e32 v41, v71, v194
	v_fmac_f32_e32 v57, v46, v46
	v_fmac_f32_e32 v58, v42, v42
	v_mul_f32_e32 v47, v68, v194
	v_mul_f32_e32 v43, v70, v194
	v_add_f32_e32 v57, v57, v58
	v_mul_f32_e32 v58, v45, v45
	v_mul_f32_e32 v59, v41, v41
	v_mul_f32_e32 v36, v73, v194
	v_mul_f32_e32 v32, v75, v194
	v_fmac_f32_e32 v58, v47, v47
	v_fmac_f32_e32 v59, v43, v43
	v_mul_f32_e32 v38, v72, v194
	v_mul_f32_e32 v34, v74, v194
	v_add_f32_e32 v58, v58, v59
	v_mul_f32_e32 v59, v36, v36
	v_mul_f32_e32 v60, v32, v32
	v_mul_f32_e32 v37, v77, v194
	v_mul_f32_e32 v33, v79, v194
	v_fmac_f32_e32 v59, v38, v38
	v_fmac_f32_e32 v60, v34, v34
	v_mul_f32_e32 v39, v76, v194
	v_mul_f32_e32 v35, v78, v194
	v_add_f32_e32 v59, v59, v60
	v_mul_f32_e32 v60, v37, v37
	v_mul_f32_e32 v61, v33, v33
	v_fmac_f32_e32 v60, v39, v39
	v_fmac_f32_e32 v61, v35, v35
	v_mul_f32_e32 v31, v84, v194
	v_add_f32_e32 v60, v60, v61
	v_mul_u32_u24_e32 v84, 0x6800, v175
	v_add_f32_e32 v57, v57, v58
	v_add_f32_e32 v58, v59, v60
	v_lshl_or_b32 v59, v176, 3, v84
	global_load_dwordx2 v[68:69], v59, s[4:5]
	global_load_dwordx2 v[70:71], v59, s[4:5] offset:16
	global_load_dwordx2 v[72:73], v59, s[4:5] offset:32
	global_load_dwordx2 v[74:75], v59, s[4:5] offset:48
	v_mul_f32_e32 v30, v80, v194
	v_mul_f32_e32 v28, v81, v194
	v_mul_f32_e32 v26, v82, v194
	v_mul_f32_e32 v24, v83, v194
	v_add_f32_e32 v57, v57, v58
	global_load_dwordx2 v[76:77], v59, s[4:5] offset:64
	global_load_dwordx2 v[78:79], v59, s[4:5] offset:80
	global_load_dwordx2 v[80:81], v59, s[4:5] offset:96
	global_load_dwordx2 v[82:83], v59, s[4:5] offset:112
	v_add_f32_e32 v56, v57, v56
	v_mul_f32_e32 v57, v28, v28
	v_mul_f32_e32 v58, v24, v24
	v_mul_f32_e32 v29, v85, v194
	v_mul_f32_e32 v25, v87, v194
	v_fmac_f32_e32 v57, v30, v30
	v_fmac_f32_e32 v58, v26, v26
	v_mul_f32_e32 v27, v86, v194
	v_add_f32_e32 v57, v57, v58
	v_mul_f32_e32 v58, v29, v29
	v_mul_f32_e32 v60, v25, v25
	v_mul_f32_e32 v20, v89, v194
	v_mul_f32_e32 v16, v91, v194
	v_fmac_f32_e32 v58, v31, v31
	v_fmac_f32_e32 v60, v27, v27
	v_mul_f32_e32 v22, v88, v194
	v_mul_f32_e32 v18, v90, v194
	v_add_f32_e32 v58, v58, v60
	v_mul_f32_e32 v60, v20, v20
	v_mul_f32_e32 v61, v16, v16
	v_mul_f32_e32 v21, v93, v194
	v_mul_f32_e32 v17, v95, v194
	v_fmac_f32_e32 v60, v22, v22
	v_fmac_f32_e32 v61, v18, v18
	v_mul_f32_e32 v23, v92, v194
	v_mul_f32_e32 v19, v94, v194
	v_add_f32_e32 v60, v60, v61
	v_mul_f32_e32 v61, v21, v21
	v_mul_f32_e32 v62, v17, v17
	v_fmac_f32_e32 v61, v23, v23
	v_fmac_f32_e32 v62, v19, v19
	v_add_f32_e32 v61, v61, v62
	v_add_f32_e32 v57, v57, v58
	v_add_f32_e32 v58, v60, v61
	v_mul_f32_e32 v12, v97, v194
	v_mul_f32_e32 v8, v99, v194
	v_add_f32_e32 v57, v57, v58
	v_mul_f32_e32 v14, v96, v194
	v_mul_f32_e32 v10, v98, v194
	v_add_f32_e32 v56, v57, v56
	v_mul_f32_e32 v57, v12, v12
	v_mul_f32_e32 v58, v8, v8
	v_mul_f32_e32 v13, v101, v194
	v_mul_f32_e32 v9, v103, v194
	v_fmac_f32_e32 v57, v14, v14
	v_fmac_f32_e32 v58, v10, v10
	v_mul_f32_e32 v15, v100, v194
	v_mul_f32_e32 v11, v102, v194
	v_add_f32_e32 v57, v57, v58
	v_mul_f32_e32 v58, v13, v13
	v_mul_f32_e32 v60, v9, v9
	v_mul_f32_e32 v4, v105, v194
	v_mul_f32_e32 v0, v107, v194
	v_fmac_f32_e32 v58, v15, v15
	v_fmac_f32_e32 v60, v11, v11
	v_mul_f32_e32 v6, v104, v194
	v_mul_f32_e32 v2, v106, v194
	v_add_f32_e32 v58, v58, v60
	v_mul_f32_e32 v60, v4, v4
	v_mul_f32_e32 v61, v0, v0
	v_mul_f32_e32 v5, v109, v194
	v_mul_f32_e32 v1, v111, v194
	v_fmac_f32_e32 v60, v6, v6
	v_fmac_f32_e32 v61, v2, v2
	v_mul_f32_e32 v7, v108, v194
	v_mul_f32_e32 v3, v110, v194
	v_add_f32_e32 v60, v60, v61
	v_mul_f32_e32 v61, v5, v5
	v_mul_f32_e32 v62, v1, v1
	v_fmac_f32_e32 v61, v7, v7
	v_fmac_f32_e32 v62, v3, v3
	v_add_f32_e32 v61, v61, v62
	v_add_f32_e32 v57, v57, v58
	v_add_f32_e32 v58, v60, v61
	v_add_f32_e32 v57, v57, v58
	v_add_f32_e32 v56, v57, v56
	v_mov_b32_e32 v57, v56
	s_nop 1
	v_permlane32_swap_b32_e32 v56, v57
	v_add_f32_e32 v56, v56, v57
	v_fmamk_f32 v56, v56, 0x3b800000, v254
	v_rsq_f32_e32 v56, v56
	v_add_u32_e32 v57, s2, v174
	ds_read_b128 v[60:63], v57
	ds_read_b128 v[64:67], v57 offset:32
	v_mul_f32_e32 v58, v195, v56
	v_mul_f32_e32 v54, v54, v56
	v_mul_f32_e32 v52, v52, v56
	s_waitcnt lgkmcnt(1)
	v_mul_f32_e32 v58, v58, v60
	v_mul_f32_e32 v60, v214, v56
	s_waitcnt lgkmcnt(0)
	v_mul_f32_e32 v60, v60, v64
	v_mul_f32_e32 v64, v196, v56
	v_mul_f32_e32 v61, v64, v61
	v_mul_f32_e32 v64, v215, v56
	v_mul_f32_e32 v64, v64, v65
	v_mul_f32_e32 v65, v197, v56
	v_mul_f32_e32 v62, v65, v62
	v_mul_f32_e32 v65, v216, v56
	v_mul_f32_e32 v65, v65, v66
	v_mul_f32_e32 v66, v213, v56
	v_mul_f32_e32 v63, v66, v63
	v_mul_f32_e32 v66, v217, v56
	v_mul_f32_e32 v66, v66, v67
	s_waitcnt vmcnt(7)
	v_lshlrev_b32_e32 v67, 16, v68
	v_mul_f32_e32 v58, v58, v67
	v_and_b32_e32 v67, 0xffff0000, v68
	v_mul_f32_e32 v61, v61, v67
	v_lshlrev_b32_e32 v67, 16, v69
	v_mul_f32_e32 v62, v62, v67
	v_and_b32_e32 v67, 0xffff0000, v69
	v_mul_f32_e32 v63, v63, v67
	s_waitcnt vmcnt(6)
	v_lshlrev_b32_e32 v67, 16, v70
	v_mul_f32_e32 v67, v60, v67
	v_and_b32_e32 v60, 0xffff0000, v70
	v_mul_f32_e32 v64, v64, v60
	v_lshlrev_b32_e32 v60, 16, v71
	v_mul_f32_e32 v65, v65, v60
	v_and_b32_e32 v60, 0xffff0000, v71
	v_mul_f32_e32 v66, v66, v60
	v_cvt_pk_bf16_f32 v60, v58, v61
	v_cvt_pk_bf16_f32 v61, v62, v63
	v_cvt_pk_bf16_f32 v62, v67, v64
	v_cvt_pk_bf16_f32 v63, v65, v66
	ds_read_b128 v[64:67], v57 offset:64
	ds_read_b128 v[68:71], v57 offset:96
	v_permlane32_swap_b32_e32 v60, v62
	v_permlane32_swap_b32_e32 v61, v63
	v_or_b32_e32 v58, v174, v84
	global_store_dwordx4 v58, v[60:63], s[4:5]
	v_mul_f32_e32 v50, v50, v56
	v_mul_f32_e32 v48, v48, v56
	v_mul_f32_e32 v60, v218, v56
	v_mul_f32_e32 v61, v220, v56
	s_waitcnt lgkmcnt(1)
	v_mul_f32_e32 v60, v60, v64
	s_waitcnt lgkmcnt(0)
	v_mul_f32_e32 v61, v61, v68
	v_mul_f32_e32 v62, v219, v56
	s_waitcnt vmcnt(6)
	v_lshlrev_b32_e32 v68, 16, v72
	v_mul_f32_e32 v62, v62, v65
	v_mul_f32_e32 v64, v212, v56
	v_mul_f32_e32 v60, v60, v68
	v_and_b32_e32 v68, 0xffff0000, v72
	v_mul_f32_e32 v64, v64, v66
	v_mul_f32_e32 v66, v210, v56
	v_mul_f32_e32 v62, v62, v68
	v_lshlrev_b32_e32 v68, 16, v73
	v_mul_f32_e32 v66, v66, v67
	v_mul_f32_e32 v64, v64, v68
	v_and_b32_e32 v68, 0xffff0000, v73
	v_mul_f32_e32 v63, v221, v56
	v_mul_f32_e32 v66, v66, v68
	s_waitcnt vmcnt(5)
	v_lshlrev_b32_e32 v68, 16, v74
	v_mul_f32_e32 v63, v63, v69
	v_mul_f32_e32 v65, v222, v56
	v_mul_f32_e32 v68, v61, v68
	v_and_b32_e32 v61, 0xffff0000, v74
	v_mul_f32_e32 v65, v65, v70
	v_mul_f32_e32 v67, v211, v56
	v_mul_f32_e32 v63, v63, v61
	v_lshlrev_b32_e32 v61, 16, v75
	v_mul_f32_e32 v67, v67, v71
	v_mul_f32_e32 v65, v65, v61
	v_and_b32_e32 v61, 0xffff0000, v75
	v_mul_f32_e32 v67, v67, v61
	v_cvt_pk_bf16_f32 v60, v60, v62
	v_cvt_pk_bf16_f32 v61, v64, v66
	v_cvt_pk_bf16_f32 v62, v68, v63
	v_cvt_pk_bf16_f32 v63, v65, v67
	v_mul_f32_e32 v68, v208, v56
	v_permlane32_swap_b32_e32 v60, v62
	v_permlane32_swap_b32_e32 v61, v63
	global_store_dwordx4 v58, v[60:63], s[4:5] offset:32
	global_load_dwordx2 v[72:73], v59, s[4:5] offset:128
	global_load_dwordx2 v[74:75], v59, s[4:5] offset:144
	global_load_dwordx2 v[84:85], v59, s[4:5] offset:160
	global_load_dwordx2 v[86:87], v59, s[4:5] offset:176
	ds_read_b128 v[60:63], v57 offset:128
	ds_read_b128 v[64:67], v57 offset:160
	v_mul_f32_e32 v55, v55, v56
	v_mul_f32_e32 v53, v53, v56
	v_mul_f32_e32 v51, v51, v56
	s_waitcnt lgkmcnt(1)
	v_mul_f32_e32 v60, v68, v60
	v_mul_f32_e32 v68, v209, v56
	s_waitcnt lgkmcnt(0)
	v_mul_f32_e32 v64, v68, v64
	v_mul_f32_e32 v68, v206, v56
	v_mul_f32_e32 v61, v68, v61
	v_mul_f32_e32 v68, v207, v56
	v_mul_f32_e32 v65, v68, v65
	v_mul_f32_e32 v68, v204, v56
	v_mul_f32_e32 v62, v68, v62
	v_mul_f32_e32 v68, v205, v56
	v_mul_f32_e32 v66, v68, v66
	v_mul_f32_e32 v68, v202, v56
	v_mul_f32_e32 v63, v68, v63
	v_mul_f32_e32 v68, v203, v56
	v_mul_f32_e32 v67, v68, v67
	s_waitcnt vmcnt(9)
	v_lshlrev_b32_e32 v68, 16, v76
	v_mul_f32_e32 v60, v60, v68
	v_and_b32_e32 v68, 0xffff0000, v76
	v_mul_f32_e32 v61, v61, v68
	v_lshlrev_b32_e32 v68, 16, v77
	v_mul_f32_e32 v62, v62, v68
	v_and_b32_e32 v68, 0xffff0000, v77
	v_mul_f32_e32 v63, v63, v68
	s_waitcnt vmcnt(8)
	v_lshlrev_b32_e32 v68, 16, v78
	v_mul_f32_e32 v64, v64, v68
	v_and_b32_e32 v68, 0xffff0000, v78
	v_mul_f32_e32 v65, v65, v68
	v_lshlrev_b32_e32 v68, 16, v79
	v_mul_f32_e32 v66, v66, v68
	v_and_b32_e32 v68, 0xffff0000, v79
	v_mul_f32_e32 v67, v67, v68
	v_cvt_pk_bf16_f32 v60, v60, v61
	v_cvt_pk_bf16_f32 v61, v62, v63
	v_cvt_pk_bf16_f32 v62, v64, v65
	v_cvt_pk_bf16_f32 v63, v66, v67
	ds_read_b128 v[64:67], v57 offset:192
	ds_read_b128 v[68:71], v57 offset:224
	v_permlane32_swap_b32_e32 v60, v62
	v_permlane32_swap_b32_e32 v61, v63
	global_store_dwordx4 v58, v[60:63], s[4:5] offset:64
	v_mul_f32_e32 v49, v49, v56
	v_mul_f32_e32 v46, v46, v56
	v_mul_f32_e32 v60, v200, v56
	v_mul_f32_e32 v61, v201, v56
	s_waitcnt lgkmcnt(1)
	v_mul_f32_e32 v60, v60, v64
	s_waitcnt lgkmcnt(0)
	v_mul_f32_e32 v61, v61, v68
	v_mul_f32_e32 v62, v198, v56
	s_waitcnt vmcnt(8)
	v_lshlrev_b32_e32 v68, 16, v80
	v_mul_f32_e32 v62, v62, v65
	v_mul_f32_e32 v64, v192, v56
	v_mul_f32_e32 v60, v60, v68
	v_and_b32_e32 v68, 0xffff0000, v80
	v_mul_f32_e32 v64, v64, v66
	v_mul_f32_e32 v66, v190, v56
	v_mul_f32_e32 v62, v62, v68
	v_lshlrev_b32_e32 v68, 16, v81
	v_mul_f32_e32 v66, v66, v67
	v_mul_f32_e32 v64, v64, v68
	v_and_b32_e32 v68, 0xffff0000, v81
	v_mul_f32_e32 v63, v199, v56
	v_mul_f32_e32 v66, v66, v68
	s_waitcnt vmcnt(7)
	v_lshlrev_b32_e32 v68, 16, v82
	v_mul_f32_e32 v63, v63, v69
	v_mul_f32_e32 v65, v193, v56
	v_mul_f32_e32 v68, v61, v68
	v_and_b32_e32 v61, 0xffff0000, v82
	v_mul_f32_e32 v65, v65, v70
	v_mul_f32_e32 v67, v191, v56
	v_mul_f32_e32 v63, v63, v61
	v_lshlrev_b32_e32 v61, 16, v83
	v_mul_f32_e32 v67, v67, v71
	v_mul_f32_e32 v65, v65, v61
	v_and_b32_e32 v61, 0xffff0000, v83
	v_mul_f32_e32 v67, v67, v61
	v_cvt_pk_bf16_f32 v60, v60, v62
	v_cvt_pk_bf16_f32 v61, v64, v66
	v_cvt_pk_bf16_f32 v62, v68, v63
	v_cvt_pk_bf16_f32 v63, v65, v67
	v_or_b32_e32 v64, 64, v58
	v_permlane32_swap_b32_e32 v60, v62
	v_permlane32_swap_b32_e32 v61, v63
	global_store_dwordx4 v64, v[60:63], s[4:5] offset:32
	global_load_dwordx2 v[76:77], v59, s[4:5] offset:192
	global_load_dwordx2 v[78:79], v59, s[4:5] offset:208
	global_load_dwordx2 v[80:81], v59, s[4:5] offset:224
	global_load_dwordx2 v[82:83], v59, s[4:5] offset:240
	ds_read_b128 v[60:63], v57 offset:256
	ds_read_b128 v[64:67], v57 offset:288
	v_mul_f32_e32 v68, v188, v56
	v_mul_f32_e32 v44, v44, v56
	v_mul_f32_e32 v42, v42, v56
	s_waitcnt lgkmcnt(1)
	v_mul_f32_e32 v60, v68, v60
	v_mul_f32_e32 v68, v189, v56
	s_waitcnt lgkmcnt(0)
	v_mul_f32_e32 v64, v68, v64
	v_mul_f32_e32 v68, v186, v56
	v_mul_f32_e32 v61, v68, v61
	v_mul_f32_e32 v68, v187, v56
	v_mul_f32_e32 v65, v68, v65
	v_mul_f32_e32 v68, v184, v56
	v_mul_f32_e32 v62, v68, v62
	v_mul_f32_e32 v68, v185, v56
	v_mul_f32_e32 v66, v68, v66
	v_mul_f32_e32 v68, v182, v56
	v_mul_f32_e32 v63, v68, v63
	v_mul_f32_e32 v68, v183, v56
	v_mul_f32_e32 v67, v68, v67
	s_waitcnt vmcnt(9)
	v_lshlrev_b32_e32 v68, 16, v72
	v_mul_f32_e32 v60, v60, v68
	v_and_b32_e32 v68, 0xffff0000, v72
	v_mul_f32_e32 v61, v61, v68
	v_lshlrev_b32_e32 v68, 16, v73
	v_mul_f32_e32 v62, v62, v68
	v_and_b32_e32 v68, 0xffff0000, v73
	v_mul_f32_e32 v63, v63, v68
	s_waitcnt vmcnt(8)
	v_lshlrev_b32_e32 v68, 16, v74
	v_mul_f32_e32 v64, v64, v68
	v_and_b32_e32 v68, 0xffff0000, v74
	v_mul_f32_e32 v65, v65, v68
	v_lshlrev_b32_e32 v68, 16, v75
	v_mul_f32_e32 v66, v66, v68
	v_and_b32_e32 v68, 0xffff0000, v75
	v_mul_f32_e32 v67, v67, v68
	v_cvt_pk_bf16_f32 v60, v60, v61
	v_cvt_pk_bf16_f32 v61, v62, v63
	v_cvt_pk_bf16_f32 v62, v64, v65
	v_cvt_pk_bf16_f32 v63, v66, v67
	ds_read_b128 v[64:67], v57 offset:320
	ds_read_b128 v[68:71], v57 offset:352
	v_permlane32_swap_b32_e32 v60, v62
	v_permlane32_swap_b32_e32 v61, v63
	global_store_dwordx4 v58, v[60:63], s[4:5] offset:128
	v_mul_f32_e32 v40, v40, v56
	v_mul_f32_e32 v47, v47, v56
	v_mul_f32_e32 v60, v180, v56
	v_mul_f32_e32 v61, v181, v56
	s_waitcnt lgkmcnt(1)
	v_mul_f32_e32 v60, v60, v64
	s_waitcnt lgkmcnt(0)
	v_mul_f32_e32 v61, v61, v68
	v_mul_f32_e32 v62, v178, v56
	s_waitcnt vmcnt(8)
	v_lshlrev_b32_e32 v68, 16, v84
	v_mul_f32_e32 v62, v62, v65
	v_mul_f32_e32 v64, v173, v56
	v_mul_f32_e32 v60, v60, v68
	v_and_b32_e32 v68, 0xffff0000, v84
	v_mul_f32_e32 v64, v64, v66
	v_mul_f32_e32 v66, v171, v56
	v_mul_f32_e32 v62, v62, v68
	v_lshlrev_b32_e32 v68, 16, v85
	v_mul_f32_e32 v66, v66, v67
	v_mul_f32_e32 v64, v64, v68
	v_and_b32_e32 v68, 0xffff0000, v85
	v_mul_f32_e32 v63, v179, v56
	v_mul_f32_e32 v66, v66, v68
	s_waitcnt vmcnt(7)
	v_lshlrev_b32_e32 v68, 16, v86
	v_mul_f32_e32 v63, v63, v69
	v_mul_f32_e32 v65, v177, v56
	v_mul_f32_e32 v68, v61, v68
	v_and_b32_e32 v61, 0xffff0000, v86
	v_mul_f32_e32 v65, v65, v70
	v_mul_f32_e32 v67, v172, v56
	v_mul_f32_e32 v63, v63, v61
	v_lshlrev_b32_e32 v61, 16, v87
	v_mul_f32_e32 v67, v67, v71
	v_mul_f32_e32 v65, v65, v61
	v_and_b32_e32 v61, 0xffff0000, v87
	v_mul_f32_e32 v67, v67, v61
	v_cvt_pk_bf16_f32 v60, v60, v62
	v_cvt_pk_bf16_f32 v61, v64, v66
	v_cvt_pk_bf16_f32 v62, v68, v63
	v_cvt_pk_bf16_f32 v63, v65, v67
	v_or_b32_e32 v64, 0x80, v58
	v_permlane32_swap_b32_e32 v60, v62
	v_permlane32_swap_b32_e32 v61, v63
	global_store_dwordx4 v64, v[60:63], s[4:5] offset:32
	global_load_dwordx2 v[72:73], v59, s[4:5] offset:256
	global_load_dwordx2 v[74:75], v59, s[4:5] offset:272
	global_load_dwordx2 v[84:85], v59, s[4:5] offset:288
	global_load_dwordx2 v[86:87], v59, s[4:5] offset:304
	ds_read_b128 v[60:63], v57 offset:384
	ds_read_b128 v[64:67], v57 offset:416
	v_mul_f32_e32 v68, v163, v56
	v_mul_f32_e32 v45, v45, v56
	v_mul_f32_e32 v43, v43, v56
	s_waitcnt lgkmcnt(1)
	v_mul_f32_e32 v60, v68, v60
	v_mul_f32_e32 v68, v170, v56
	s_waitcnt lgkmcnt(0)
	v_mul_f32_e32 v64, v68, v64
	v_mul_f32_e32 v68, v160, v56
	v_mul_f32_e32 v61, v68, v61
	v_mul_f32_e32 v68, v162, v56
	v_mul_f32_e32 v65, v68, v65
	v_mul_f32_e32 v68, v158, v56
	v_mul_f32_e32 v62, v68, v62
	v_mul_f32_e32 v68, v159, v56
	v_mul_f32_e32 v66, v68, v66
	v_mul_f32_e32 v68, v156, v56
	v_mul_f32_e32 v63, v68, v63
	v_mul_f32_e32 v68, v157, v56
	v_mul_f32_e32 v67, v68, v67
	s_waitcnt vmcnt(9)
	v_lshlrev_b32_e32 v68, 16, v76
	v_mul_f32_e32 v60, v60, v68
	v_and_b32_e32 v68, 0xffff0000, v76
	v_mul_f32_e32 v61, v61, v68
	v_lshlrev_b32_e32 v68, 16, v77
	v_mul_f32_e32 v62, v62, v68
	v_and_b32_e32 v68, 0xffff0000, v77
	v_mul_f32_e32 v63, v63, v68
	s_waitcnt vmcnt(8)
	v_lshlrev_b32_e32 v68, 16, v78
	v_mul_f32_e32 v64, v64, v68
	v_and_b32_e32 v68, 0xffff0000, v78
	v_mul_f32_e32 v65, v65, v68
	v_lshlrev_b32_e32 v68, 16, v79
	v_mul_f32_e32 v66, v66, v68
	v_and_b32_e32 v68, 0xffff0000, v79
	v_mul_f32_e32 v67, v67, v68
	v_cvt_pk_bf16_f32 v60, v60, v61
	v_cvt_pk_bf16_f32 v61, v62, v63
	v_cvt_pk_bf16_f32 v62, v64, v65
	v_cvt_pk_bf16_f32 v63, v66, v67
	ds_read_b128 v[64:67], v57 offset:448
	ds_read_b128 v[68:71], v57 offset:480
	v_permlane32_swap_b32_e32 v60, v62
	v_permlane32_swap_b32_e32 v61, v63
	global_store_dwordx4 v58, v[60:63], s[4:5] offset:192
	v_mul_f32_e32 v41, v41, v56
	v_mul_f32_e32 v38, v38, v56
	v_mul_f32_e32 v60, v126, v56
	v_mul_f32_e32 v61, v127, v56
	s_waitcnt lgkmcnt(1)
	v_mul_f32_e32 v60, v60, v64
	s_waitcnt lgkmcnt(0)
	v_mul_f32_e32 v61, v61, v68
	v_mul_f32_e32 v62, v124, v56
	s_waitcnt vmcnt(8)
	v_lshlrev_b32_e32 v68, 16, v80
	v_mul_f32_e32 v62, v62, v65
	v_mul_f32_e32 v64, v122, v56
	v_mul_f32_e32 v60, v60, v68
	v_and_b32_e32 v68, 0xffff0000, v80
	v_mul_f32_e32 v64, v64, v66
	v_mul_f32_e32 v66, v120, v56
	v_mul_f32_e32 v62, v62, v68
	v_lshlrev_b32_e32 v68, 16, v81
	v_mul_f32_e32 v66, v66, v67
	v_mul_f32_e32 v64, v64, v68
	v_and_b32_e32 v68, 0xffff0000, v81
	v_mul_f32_e32 v63, v125, v56
	v_mul_f32_e32 v66, v66, v68
	s_waitcnt vmcnt(7)
	v_lshlrev_b32_e32 v68, 16, v82
	v_mul_f32_e32 v63, v63, v69
	v_mul_f32_e32 v65, v123, v56
	v_mul_f32_e32 v68, v61, v68
	v_and_b32_e32 v61, 0xffff0000, v82
	v_mul_f32_e32 v65, v65, v70
	v_mul_f32_e32 v67, v121, v56
	v_mul_f32_e32 v63, v63, v61
	v_lshlrev_b32_e32 v61, 16, v83
	v_mul_f32_e32 v67, v67, v71
	v_mul_f32_e32 v65, v65, v61
	v_and_b32_e32 v61, 0xffff0000, v83
	v_mul_f32_e32 v67, v67, v61
	v_cvt_pk_bf16_f32 v60, v60, v62
	v_cvt_pk_bf16_f32 v61, v64, v66
	v_cvt_pk_bf16_f32 v62, v68, v63
	v_cvt_pk_bf16_f32 v63, v65, v67
	v_or_b32_e32 v64, 0xc0, v58
	v_permlane32_swap_b32_e32 v60, v62
	v_permlane32_swap_b32_e32 v61, v63
	global_store_dwordx4 v64, v[60:63], s[4:5] offset:32
	global_load_dwordx2 v[76:77], v59, s[4:5] offset:320
	global_load_dwordx2 v[78:79], v59, s[4:5] offset:336
	global_load_dwordx2 v[80:81], v59, s[4:5] offset:352
	global_load_dwordx2 v[82:83], v59, s[4:5] offset:368
	ds_read_b128 v[60:63], v57 offset:512
	ds_read_b128 v[64:67], v57 offset:544
	v_mul_f32_e32 v68, v118, v56
	v_mul_f32_e32 v36, v36, v56
	v_mul_f32_e32 v34, v34, v56
	s_waitcnt lgkmcnt(1)
	v_mul_f32_e32 v60, v68, v60
	v_mul_f32_e32 v68, v119, v56
	s_waitcnt lgkmcnt(0)
	v_mul_f32_e32 v64, v68, v64
	v_mul_f32_e32 v68, v116, v56
	v_mul_f32_e32 v61, v68, v61
	v_mul_f32_e32 v68, v117, v56
	v_mul_f32_e32 v65, v68, v65
	v_mul_f32_e32 v68, v114, v56
	v_mul_f32_e32 v62, v68, v62
	v_mul_f32_e32 v68, v115, v56
	v_mul_f32_e32 v66, v68, v66
	v_mul_f32_e32 v68, v112, v56
	v_mul_f32_e32 v63, v68, v63
	v_mul_f32_e32 v68, v113, v56
	v_mul_f32_e32 v67, v68, v67
	s_waitcnt vmcnt(9)
	v_lshlrev_b32_e32 v68, 16, v72
	v_mul_f32_e32 v60, v60, v68
	v_and_b32_e32 v68, 0xffff0000, v72
	v_mul_f32_e32 v61, v61, v68
	v_lshlrev_b32_e32 v68, 16, v73
	v_mul_f32_e32 v62, v62, v68
	v_and_b32_e32 v68, 0xffff0000, v73
	v_mul_f32_e32 v63, v63, v68
	s_waitcnt vmcnt(8)
	v_lshlrev_b32_e32 v68, 16, v74
	v_mul_f32_e32 v64, v64, v68
	v_and_b32_e32 v68, 0xffff0000, v74
	v_mul_f32_e32 v65, v65, v68
	v_lshlrev_b32_e32 v68, 16, v75
	v_mul_f32_e32 v66, v66, v68
	v_and_b32_e32 v68, 0xffff0000, v75
	v_mul_f32_e32 v67, v67, v68
	v_cvt_pk_bf16_f32 v60, v60, v61
	v_cvt_pk_bf16_f32 v61, v62, v63
	v_cvt_pk_bf16_f32 v62, v64, v65
	v_cvt_pk_bf16_f32 v63, v66, v67
	ds_read_b128 v[64:67], v57 offset:576
	ds_read_b128 v[68:71], v57 offset:608
	v_permlane32_swap_b32_e32 v60, v62
	v_permlane32_swap_b32_e32 v61, v63
	global_store_dwordx4 v58, v[60:63], s[4:5] offset:256
	s_waitcnt lgkmcnt(1)
	v_mul_f32_e32 v54, v54, v64
	v_mul_f32_e32 v52, v52, v65
	s_waitcnt vmcnt(8)
	v_lshlrev_b32_e32 v60, 16, v84
	v_mul_f32_e32 v54, v54, v60
	v_and_b32_e32 v60, 0xffff0000, v84
	v_mul_f32_e32 v50, v50, v66
	v_mul_f32_e32 v52, v52, v60
	v_lshlrev_b32_e32 v60, 16, v85
	v_mul_f32_e32 v48, v48, v67
	v_mul_f32_e32 v50, v50, v60
	v_and_b32_e32 v60, 0xffff0000, v85
	s_waitcnt lgkmcnt(0)
	v_mul_f32_e32 v55, v55, v68
	v_mul_f32_e32 v60, v48, v60
	s_waitcnt vmcnt(7)
	v_lshlrev_b32_e32 v48, 16, v86
	v_mul_f32_e32 v53, v53, v69
	v_mul_f32_e32 v55, v55, v48
	v_and_b32_e32 v48, 0xffff0000, v86
	v_mul_f32_e32 v51, v51, v70
	v_mul_f32_e32 v53, v53, v48
	v_lshlrev_b32_e32 v48, 16, v87
	v_mul_f32_e32 v49, v49, v71
	v_mul_f32_e32 v51, v51, v48
	v_and_b32_e32 v48, 0xffff0000, v87
	v_mul_f32_e32 v61, v49, v48
	v_cvt_pk_bf16_f32 v48, v54, v52
	v_cvt_pk_bf16_f32 v49, v50, v60
	v_cvt_pk_bf16_f32 v50, v55, v53
	v_cvt_pk_bf16_f32 v51, v51, v61
	v_or_b32_e32 v52, 0x100, v58
	v_permlane32_swap_b32_e32 v48, v50
	v_permlane32_swap_b32_e32 v49, v51
	global_store_dwordx4 v52, v[48:51], s[4:5] offset:32
	global_load_dwordx2 v[60:61], v59, s[4:5] offset:384
	global_load_dwordx2 v[62:63], v59, s[4:5] offset:400
	global_load_dwordx2 v[64:65], v59, s[4:5] offset:416
	global_load_dwordx2 v[66:67], v59, s[4:5] offset:432
	ds_read_b128 v[48:51], v57 offset:640
	ds_read_b128 v[52:55], v57 offset:672
	v_mul_f32_e32 v32, v32, v56
	v_mul_f32_e32 v39, v39, v56
	v_mul_f32_e32 v37, v37, v56
	s_waitcnt lgkmcnt(1)
	v_mul_f32_e32 v46, v46, v48
	s_waitcnt vmcnt(9)
	v_lshlrev_b32_e32 v48, 16, v76
	v_mul_f32_e32 v44, v44, v49
	v_mul_f32_e32 v46, v46, v48
	v_and_b32_e32 v48, 0xffff0000, v76
	v_mul_f32_e32 v42, v42, v50
	v_mul_f32_e32 v44, v44, v48
	v_lshlrev_b32_e32 v48, 16, v77
	v_mul_f32_e32 v40, v40, v51
	v_mul_f32_e32 v42, v42, v48
	v_and_b32_e32 v48, 0xffff0000, v77
	s_waitcnt lgkmcnt(0)
	v_mul_f32_e32 v47, v47, v52
	v_mul_f32_e32 v48, v40, v48
	s_waitcnt vmcnt(8)
	v_lshlrev_b32_e32 v40, 16, v78
	v_mul_f32_e32 v45, v45, v53
	v_mul_f32_e32 v47, v47, v40
	v_and_b32_e32 v40, 0xffff0000, v78
	v_mul_f32_e32 v43, v43, v54
	v_mul_f32_e32 v45, v45, v40
	v_lshlrev_b32_e32 v40, 16, v79
	v_mul_f32_e32 v41, v41, v55
	v_mul_f32_e32 v43, v43, v40
	v_and_b32_e32 v40, 0xffff0000, v79
	v_mul_f32_e32 v49, v41, v40
	v_cvt_pk_bf16_f32 v40, v46, v44
	v_cvt_pk_bf16_f32 v41, v42, v48
	v_cvt_pk_bf16_f32 v42, v47, v45
	v_cvt_pk_bf16_f32 v43, v43, v49
	ds_read_b128 v[44:47], v57 offset:704
	ds_read_b128 v[48:51], v57 offset:736
	v_permlane32_swap_b32_e32 v40, v42
	v_permlane32_swap_b32_e32 v41, v43
	global_store_dwordx4 v58, v[40:43], s[4:5] offset:320
	s_waitcnt lgkmcnt(1)
	v_mul_f32_e32 v38, v38, v44
	v_mul_f32_e32 v36, v36, v45
	s_waitcnt vmcnt(8)
	v_lshlrev_b32_e32 v40, 16, v80
	v_mul_f32_e32 v38, v38, v40
	v_and_b32_e32 v40, 0xffff0000, v80
	v_mul_f32_e32 v34, v34, v46
	v_mul_f32_e32 v36, v36, v40
	v_lshlrev_b32_e32 v40, 16, v81
	v_mul_f32_e32 v32, v32, v47
	v_mul_f32_e32 v34, v34, v40
	v_and_b32_e32 v40, 0xffff0000, v81
	s_waitcnt lgkmcnt(0)
	v_mul_f32_e32 v39, v39, v48
	v_mul_f32_e32 v40, v32, v40
	s_waitcnt vmcnt(7)
	v_lshlrev_b32_e32 v32, 16, v82
	v_mul_f32_e32 v37, v37, v49
	v_mul_f32_e32 v35, v35, v56
	v_mul_f32_e32 v39, v39, v32
	v_and_b32_e32 v32, 0xffff0000, v82
	v_mul_f32_e32 v35, v35, v50
	v_mul_f32_e32 v33, v33, v56
	v_mul_f32_e32 v37, v37, v32
	v_lshlrev_b32_e32 v32, 16, v83
	v_mul_f32_e32 v33, v33, v51
	v_mul_f32_e32 v35, v35, v32
	v_and_b32_e32 v32, 0xffff0000, v83
	v_mul_f32_e32 v41, v33, v32
	v_cvt_pk_bf16_f32 v32, v38, v36
	v_cvt_pk_bf16_f32 v33, v34, v40
	v_cvt_pk_bf16_f32 v34, v39, v37
	v_cvt_pk_bf16_f32 v35, v35, v41
	v_or_b32_e32 v36, 0x140, v58
	v_permlane32_swap_b32_e32 v32, v34
	v_permlane32_swap_b32_e32 v33, v35
	global_store_dwordx4 v36, v[32:35], s[4:5] offset:32
	global_load_dwordx2 v[40:41], v59, s[4:5] offset:448
	global_load_dwordx2 v[42:43], v59, s[4:5] offset:464
	global_load_dwordx2 v[44:45], v59, s[4:5] offset:480
	global_load_dwordx2 v[46:47], v59, s[4:5] offset:496
	ds_read_b128 v[32:35], v57 offset:768
	ds_read_b128 v[36:39], v57 offset:800
	v_mul_f32_e32 v30, v30, v56
	v_mul_f32_e32 v28, v28, v56
	v_mul_f32_e32 v26, v26, v56
	s_waitcnt lgkmcnt(1)
	v_mul_f32_e32 v30, v30, v32
	s_waitcnt vmcnt(9)
	v_lshlrev_b32_e32 v32, 16, v60
	v_mul_f32_e32 v28, v28, v33
	v_mul_f32_e32 v30, v30, v32
	v_and_b32_e32 v32, 0xffff0000, v60
	v_mul_f32_e32 v26, v26, v34
	v_mul_f32_e32 v24, v24, v56
	v_mul_f32_e32 v28, v28, v32
	v_lshlrev_b32_e32 v32, 16, v61
	v_mul_f32_e32 v31, v31, v56
	v_mul_f32_e32 v24, v24, v35
	v_mul_f32_e32 v26, v26, v32
	v_and_b32_e32 v32, 0xffff0000, v61
	s_waitcnt lgkmcnt(0)
	v_mul_f32_e32 v31, v31, v36
	v_mul_f32_e32 v29, v29, v56
	v_mul_f32_e32 v32, v24, v32
	s_waitcnt vmcnt(8)
	v_lshlrev_b32_e32 v24, 16, v62
	v_mul_f32_e32 v29, v29, v37
	v_mul_f32_e32 v27, v27, v56
	v_mul_f32_e32 v31, v31, v24
	v_and_b32_e32 v24, 0xffff0000, v62
	v_mul_f32_e32 v27, v27, v38
	v_mul_f32_e32 v25, v25, v56
	v_mul_f32_e32 v29, v29, v24
	v_lshlrev_b32_e32 v24, 16, v63
	v_mul_f32_e32 v25, v25, v39
	v_mul_f32_e32 v27, v27, v24
	v_and_b32_e32 v24, 0xffff0000, v63
	v_mul_f32_e32 v33, v25, v24
	v_cvt_pk_bf16_f32 v24, v30, v28
	v_cvt_pk_bf16_f32 v25, v26, v32
	v_cvt_pk_bf16_f32 v26, v31, v29
	v_cvt_pk_bf16_f32 v27, v27, v33
	ds_read_b128 v[28:31], v57 offset:832
	ds_read_b128 v[32:35], v57 offset:864
	v_permlane32_swap_b32_e32 v24, v26
	v_permlane32_swap_b32_e32 v25, v27
	v_mul_f32_e32 v22, v22, v56
	global_store_dwordx4 v58, v[24:27], s[4:5] offset:384
	s_waitcnt lgkmcnt(1)
	v_mul_f32_e32 v22, v22, v28
	v_mul_f32_e32 v20, v20, v56
	s_waitcnt vmcnt(8)
	v_lshlrev_b32_e32 v24, 16, v64
	v_mul_f32_e32 v20, v20, v29
	v_mul_f32_e32 v18, v18, v56
	v_mul_f32_e32 v22, v22, v24
	v_and_b32_e32 v24, 0xffff0000, v64
	v_mul_f32_e32 v18, v18, v30
	v_mul_f32_e32 v16, v16, v56
	v_mul_f32_e32 v20, v20, v24
	v_lshlrev_b32_e32 v24, 16, v65
	v_mul_f32_e32 v23, v23, v56
	v_mul_f32_e32 v16, v16, v31
	v_mul_f32_e32 v18, v18, v24
	v_and_b32_e32 v24, 0xffff0000, v65
	s_waitcnt lgkmcnt(0)
	v_mul_f32_e32 v23, v23, v32
	v_mul_f32_e32 v21, v21, v56
	v_mul_f32_e32 v24, v16, v24
	s_waitcnt vmcnt(7)
	v_lshlrev_b32_e32 v16, 16, v66
	v_mul_f32_e32 v21, v21, v33
	v_mul_f32_e32 v19, v19, v56
	v_mul_f32_e32 v23, v23, v16
	v_and_b32_e32 v16, 0xffff0000, v66
	v_mul_f32_e32 v19, v19, v34
	v_mul_f32_e32 v17, v17, v56
	v_mul_f32_e32 v21, v21, v16
	v_lshlrev_b32_e32 v16, 16, v67
	v_mul_f32_e32 v17, v17, v35
	v_mul_f32_e32 v19, v19, v16
	v_and_b32_e32 v16, 0xffff0000, v67
	v_mul_f32_e32 v25, v17, v16
	v_cvt_pk_bf16_f32 v16, v22, v20
	v_cvt_pk_bf16_f32 v17, v18, v24
	v_cvt_pk_bf16_f32 v18, v23, v21
	v_cvt_pk_bf16_f32 v19, v19, v25
	v_or_b32_e32 v20, 0x180, v58
	v_permlane32_swap_b32_e32 v16, v18
	v_permlane32_swap_b32_e32 v17, v19
	global_store_dwordx4 v20, v[16:19], s[4:5] offset:32
	ds_read_b128 v[16:19], v57 offset:896
	ds_read_b128 v[20:23], v57 offset:928
	v_mul_f32_e32 v14, v14, v56
	v_mul_f32_e32 v12, v12, v56
	v_mul_f32_e32 v10, v10, v56
	s_waitcnt lgkmcnt(1)
	v_mul_f32_e32 v14, v14, v16
	s_waitcnt vmcnt(5)
	v_lshlrev_b32_e32 v16, 16, v40
	v_mul_f32_e32 v12, v12, v17
	v_mul_f32_e32 v14, v14, v16
	v_and_b32_e32 v16, 0xffff0000, v40
	v_mul_f32_e32 v10, v10, v18
	v_mul_f32_e32 v8, v8, v56
	v_mul_f32_e32 v12, v12, v16
	v_lshlrev_b32_e32 v16, 16, v41
	v_mul_f32_e32 v15, v15, v56
	v_mul_f32_e32 v8, v8, v19
	v_mul_f32_e32 v10, v10, v16
	v_and_b32_e32 v16, 0xffff0000, v41
	s_waitcnt lgkmcnt(0)
	v_mul_f32_e32 v15, v15, v20
	v_mul_f32_e32 v13, v13, v56
	v_mul_f32_e32 v16, v8, v16
	s_waitcnt vmcnt(4)
	v_lshlrev_b32_e32 v8, 16, v42
	v_mul_f32_e32 v13, v13, v21
	v_mul_f32_e32 v11, v11, v56
	v_mul_f32_e32 v15, v15, v8
	v_and_b32_e32 v8, 0xffff0000, v42
	v_mul_f32_e32 v11, v11, v22
	v_mul_f32_e32 v9, v9, v56
	v_mul_f32_e32 v13, v13, v8
	v_lshlrev_b32_e32 v8, 16, v43
	v_mul_f32_e32 v9, v9, v23
	v_mul_f32_e32 v11, v11, v8
	v_and_b32_e32 v8, 0xffff0000, v43
	v_mul_f32_e32 v17, v9, v8
	v_cvt_pk_bf16_f32 v8, v14, v12
	v_cvt_pk_bf16_f32 v9, v10, v16
	v_cvt_pk_bf16_f32 v10, v15, v13
	v_cvt_pk_bf16_f32 v11, v11, v17
	ds_read_b128 v[12:15], v57 offset:960
	ds_read_b128 v[16:19], v57 offset:992
	v_permlane32_swap_b32_e32 v8, v10
	v_permlane32_swap_b32_e32 v9, v11
	v_mul_f32_e32 v6, v6, v56
	global_store_dwordx4 v58, v[8:11], s[4:5] offset:448
	s_waitcnt lgkmcnt(1)
	v_mul_f32_e32 v6, v6, v12
	v_mul_f32_e32 v4, v4, v56
	s_waitcnt vmcnt(4)
	v_lshlrev_b32_e32 v8, 16, v44
	v_mul_f32_e32 v4, v4, v13
	v_mul_f32_e32 v2, v2, v56
	v_mul_f32_e32 v6, v6, v8
	v_and_b32_e32 v8, 0xffff0000, v44
	v_mul_f32_e32 v2, v2, v14
	v_mul_f32_e32 v0, v0, v56
	v_mul_f32_e32 v4, v4, v8
	v_lshlrev_b32_e32 v8, 16, v45
	v_mul_f32_e32 v7, v7, v56
	v_mul_f32_e32 v0, v0, v15
	v_mul_f32_e32 v2, v2, v8
	v_and_b32_e32 v8, 0xffff0000, v45
	s_waitcnt lgkmcnt(0)
	v_mul_f32_e32 v7, v7, v16
	v_mul_f32_e32 v5, v5, v56
	v_mul_f32_e32 v8, v0, v8
	s_waitcnt vmcnt(3)
	v_lshlrev_b32_e32 v0, 16, v46
	v_mul_f32_e32 v5, v5, v17
	v_mul_f32_e32 v3, v3, v56
	v_mul_f32_e32 v7, v7, v0
	v_and_b32_e32 v0, 0xffff0000, v46
	v_mul_f32_e32 v3, v3, v18
	v_mul_f32_e32 v1, v1, v56
	v_mul_f32_e32 v5, v5, v0
	v_lshlrev_b32_e32 v0, 16, v47
	v_mul_f32_e32 v1, v1, v19
	v_mul_f32_e32 v3, v3, v0
	v_and_b32_e32 v0, 0xffff0000, v47
	v_mul_f32_e32 v9, v1, v0
	v_cvt_pk_bf16_f32 v0, v6, v4
	v_cvt_pk_bf16_f32 v1, v2, v8
	v_cvt_pk_bf16_f32 v2, v7, v5
	v_cvt_pk_bf16_f32 v3, v3, v9
	v_readlane_b32 s2, v255, 38
	v_permlane32_swap_b32_e32 v0, v2
	v_permlane32_swap_b32_e32 v1, v3
	v_or_b32_e32 v4, 0x1c0, v58
	s_cmp_lg_u32 s10, s2
	s_mov_b32 s2, s10
	global_store_dwordx4 v4, v[0:3], s[4:5] offset:32
	s_cbranch_scc0 .LBB0_541

.LBB0_517:
	s_or_b64 exec, exec, s[4:5]
	s_lshr_b32 s3, s2, 1
	s_mul_i32 s3, s15, s3
	v_readlane_b32 s4, v255, 16
	s_add_i32 s33, s4, s3
	s_lshl_b32 s3, s33, 7
	s_and_b32 s6, s3, 0xfffff000
	s_lshl_b32 s3, s33, 8
	s_ashr_i32 s82, s33, 3
	s_and_b32 s3, s3, 0x700
	s_and_b32 s2, s2, 1
	s_and_b32 s69, s82, 3
	s_xor_b32 s4, s3, 0xf00
	s_cmp_eq_u32 s2, 0
	s_mov_b32 s2, s6
	s_cselect_b32 s84, s4, s3
	v_writelane_b32 v255, s2, 46
	s_ashr_i32 s7, s6, 31
	s_lshl_b64 s[66:67], s[6:7], 11
	v_writelane_b32 v255, s3, 47
	v_mov_b32_e32 v0, v165
	v_readlane_b32 s2, v255, 25
	s_add_u32 s2, s2, s66
	v_readlane_b32 s3, v255, 26
	s_addc_u32 s3, s3, s67
	s_lshl_b32 s4, s69, 8
	s_add_u32 s6, s2, s4
	s_addc_u32 s7, s3, 0
	s_add_u32 s3, s6, 0x400
	v_writelane_b32 v255, s4, 48
	s_addc_u32 s68, s7, 0
	s_ashr_i32 s83, s82, 31
	s_lshl_b64 s[4:5], s[82:83], 14
	v_readlane_b32 s2, v255, 17
	s_add_u32 s8, s2, s4
	v_readlane_b32 s2, v255, 18
	s_addc_u32 s9, s2, s5
	s_lshl_b32 s4, s82, 6
	s_ashr_i32 s5, s4, 31
	s_lshl_b64 s[4:5], s[4:5], 2
	v_readlane_b32 s2, v255, 21
	s_add_u32 s4, s2, s4
	v_readlane_b32 s2, v255, 22
	s_addc_u32 s5, s2, s5
	v_mov_b32_e32 v3, v161
	v_readfirstlane_b32 s2, v0
	s_ashr_i32 s10, s2, 6
	s_lshl_b32 s12, s10, 5
	s_mov_b32 s2, s12
	v_and_b32_e32 v39, 63, v0
	v_writelane_b32 v255, s2, 49
	s_add_i32 s94, s12, s84
	v_lshlrev_b32_e32 v2, 2, v39
	v_writelane_b32 v255, s3, 50
	s_lshl_b32 s2, s10, 11
	v_lshl_add_u64 v[4:5], s[4:5], 0, v[2:3]
	v_readlane_b32 s11, v255, 28
	s_lshl_b32 s4, s10, 12
	s_ashr_i32 s95, s94, 31
	s_lshl_b32 s78, s10, 3
	flat_load_dword v3, v[4:5]
	s_add_i32 s2, s2, s11
	s_add_i32 s81, s4, s79
	s_lshl_b64 s[12:13], s[94:95], 2
	v_and_b32_e32 v175, 31, v0
	s_add_u32 s4, s8, s12
	v_writelane_b32 v255, s12, 51
	s_addc_u32 s5, s9, s13
	v_lshlrev_b32_e32 v160, 2, v175
	v_lshl_add_u64 v[4:5], s[4:5], 0, v[160:161]
	flat_load_dword v178, v[4:5]
	v_bfe_u32 v4, v0, 4, 2
	v_bitop3_b32 v6, v4, v0, 15 bitop3:0x78
	v_add_u32_e32 v2, s89, v2
	v_writelane_b32 v255, s13, 52
	v_bfe_u32 v176, v0, 5, 1
	v_lshlrev_b32_e32 v6, 4, v6
	v_or_b32_e32 v4, s78, v4
	v_and_b32_e32 v5, 15, v0
	v_lshlrev_b32_e32 v1, 2, v176
	s_mulk_i32 s10, 0x1c00
	v_lshl_or_b32 v170, v4, 11, v6
	v_or_b32_e32 v4, 4, v4
	v_readlane_b32 s4, v255, 33
	v_lshlrev_b32_e32 v40, 4, v39
	v_sub_u32_e32 v7, v175, v1
	v_bitop3_b32 v5, v4, v5, 7 bitop3:0x6c
	v_lshlrev_b32_e32 v4, 11, v4
	s_add_i32 s4, s4, s10
	v_add_u32_e32 v180, s94, v7
	v_lshl_or_b32 v172, v5, 4, v4
	v_add_u32_e32 v181, s4, v40
	v_lshlrev_b32_e32 v174, 4, v176
	s_waitcnt vmcnt(0) lgkmcnt(0)
	ds_write_b32 v2, v3
	s_waitcnt vmcnt(0)
	ds_write_b128 v181, v[128:131]
	ds_write_b128 v181, v[132:135] offset:1024
	ds_write_b128 v181, v[136:139] offset:2048
	ds_write_b128 v181, v[140:143] offset:3072
	ds_write_b128 v181, v[144:147] offset:4096
	ds_write_b128 v181, v[148:151] offset:5120
	ds_write_b128 v181, v[152:155] offset:6144
	s_add_u32 s4, s6, 0x20400
	s_addc_u32 s5, s7, 0
	v_mov_b32_e32 v171, v161
	v_lshl_add_u64 v[2:3], s[4:5], 0, v[170:171]
	s_add_i32 s96, s2, 0x4000
	s_mov_b32 s6, m0
	s_mov_b32 m0, s96
	s_nop 0
	global_load_lds_dwordx4 v[2:3], off
	s_mov_b32 m0, s6
	v_mov_b32_e32 v173, v161
	v_lshl_add_u64 v[2:3], s[4:5], 0, v[172:173]
	s_add_i32 s97, s2, 0x4400
	s_mov_b32 s4, m0
	s_mov_b32 m0, s97
	s_nop 0
	global_load_lds_dwordx4 v[2:3], off
	s_mov_b32 m0, s4
	s_waitcnt lgkmcnt(0)
	s_barrier
	v_lshlrev_b32_e32 v2, 4, v0
	s_movk_i32 s4, 0x70
	v_lshlrev_b32_e32 v34, 8, v175
	v_and_b32_e32 v3, 0x70, v2
	v_bitop3_b32 v35, v174, v2, s4 bitop3:0x78
	s_movk_i32 s4, 0x60
	v_add_u32_e32 v4, s11, v34
	v_bitop3_b32 v36, v174, v3, 32 bitop3:0x36
	v_bitop3_b32 v37, v174, v3, 64 bitop3:0x36
	v_bitop3_b32 v38, v174, v3, s4 bitop3:0x36
	v_add_u32_e32 v182, v35, v4
	v_add_u32_e32 v183, v36, v4
	v_add_u32_e32 v184, v37, v4
	v_add_u32_e32 v185, v38, v4
	ds_read_b128 v[2:5], v182 offset:0
	ds_read_b128 v[6:9], v182 offset:0x2000
	ds_read_b128 v[10:13], v181 offset:0
	ds_read_b128 v[42:45], v183 offset:0
	ds_read_b128 v[46:49], v183 offset:0x2000
	ds_read_b128 v[50:53], v181 offset:0x400
	s_waitcnt lgkmcnt(3)
	s_nop 0
	v_mfma_f32_32x32x16_bf16 v[18:33], v[2:5], v[10:13], 0
	v_mfma_f32_32x32x16_bf16 v[2:17], v[6:9], v[10:13], 0
	ds_read_b128 v[54:57], v184 offset:0
	ds_read_b128 v[58:61], v184 offset:0x2000
	ds_read_b128 v[62:65], v181 offset:0x800
	s_waitcnt lgkmcnt(3)
	v_mfma_f32_32x32x16_bf16 v[18:33], v[42:45], v[50:53], v[18:33]
	v_mfma_f32_32x32x16_bf16 v[2:17], v[46:49], v[50:53], v[2:17]
	ds_read_b128 v[42:45], v185 offset:0
	ds_read_b128 v[46:49], v185 offset:0x2000
	ds_read_b128 v[50:53], v181 offset:0xc00
	s_waitcnt lgkmcnt(3)
	v_mfma_f32_32x32x16_bf16 v[18:33], v[54:57], v[62:65], v[18:33]
	v_mfma_f32_32x32x16_bf16 v[2:17], v[58:61], v[62:65], v[2:17]
	ds_read_b128 v[54:57], v182 offset:0x80
	ds_read_b128 v[58:61], v182 offset:0x2080
	ds_read_b128 v[62:65], v181 offset:0x1000
	s_waitcnt lgkmcnt(3)
	v_mfma_f32_32x32x16_bf16 v[18:33], v[42:45], v[50:53], v[18:33]
	v_mfma_f32_32x32x16_bf16 v[2:17], v[46:49], v[50:53], v[2:17]
	ds_read_b128 v[42:45], v183 offset:0x80
	ds_read_b128 v[46:49], v183 offset:0x2080
	ds_read_b128 v[50:53], v181 offset:0x1400
	s_waitcnt lgkmcnt(3)
	v_mfma_f32_32x32x16_bf16 v[18:33], v[54:57], v[62:65], v[18:33]
	v_mfma_f32_32x32x16_bf16 v[2:17], v[58:61], v[62:65], v[2:17]
	ds_read_b128 v[54:57], v184 offset:0x80
	ds_read_b128 v[58:61], v184 offset:0x2080
	ds_read_b128 v[62:65], v181 offset:0x1800
	s_waitcnt lgkmcnt(3)
	v_mfma_f32_32x32x16_bf16 v[18:33], v[42:45], v[50:53], v[18:33]
	v_mfma_f32_32x32x16_bf16 v[2:17], v[46:49], v[50:53], v[2:17]
	ds_read_b128 v[42:45], v185 offset:0x80
	ds_read_b128 v[46:49], v185 offset:0x2080
	s_waitcnt lgkmcnt(2)
	v_mfma_f32_32x32x16_bf16 v[18:33], v[54:57], v[62:65], v[18:33]
	v_mfma_f32_32x32x16_bf16 v[2:17], v[58:61], v[62:65], v[2:17]
	s_waitcnt lgkmcnt(0)
	v_mfma_f32_32x32x16_bf16 v[18:33], v[42:45], v[166:169], v[18:33]
	v_mfma_f32_32x32x16_bf16 v[2:17], v[46:49], v[166:169], v[2:17]
	s_bitcmp0_b32 s100, 8
	s_cbranch_scc1 .Lstg_a1
	s_waitcnt vmcnt(0)
	s_waitcnt lgkmcnt(0)
	s_barrier
.Lstg_a1:
	s_cmp_gt_i32 s94, 62
	v_writelane_b32 v255, s17, 53
	s_cbranch_scc1 .LBB0_519
	v_cmp_gt_i32_e64 s[62:63], 26, v180
	v_cmp_gt_i32_e64 s[64:65], 27, v180
	v_cmp_gt_i32_e64 s[60:61], 25, v180
	s_and_b64 s[62:63], s[64:65], s[62:63]
	v_cmp_gt_i32_e64 s[58:59], 24, v180
	s_and_b64 s[60:61], s[62:63], s[60:61]
	v_cmp_gt_i32_e64 s[56:57], 19, v180
	s_and_b64 s[58:59], s[60:61], s[58:59]
	v_cmp_gt_i32_e64 s[54:55], 18, v180
	s_and_b64 s[56:57], s[58:59], s[56:57]
	v_cmp_gt_i32_e64 s[52:53], 17, v180
	s_and_b64 s[54:55], s[56:57], s[54:55]
	v_cmp_gt_i32_e64 s[50:51], 16, v180
	s_and_b64 s[52:53], s[54:55], s[52:53]
	v_cmp_gt_i32_e64 s[48:49], 11, v180
	s_and_b64 s[50:51], s[52:53], s[50:51]
	v_cmp_gt_i32_e64 s[46:47], 10, v180
	s_and_b64 s[48:49], s[50:51], s[48:49]
	v_cmp_gt_i32_e64 s[44:45], 9, v180
	s_and_b64 s[46:47], s[48:49], s[46:47]
	v_cmp_gt_i32_e64 s[42:43], 8, v180
	s_and_b64 s[44:45], s[46:47], s[44:45]
	v_cmp_gt_i32_e64 s[40:41], 3, v180
	s_and_b64 s[42:43], s[44:45], s[42:43]
	v_cmp_gt_i32_e64 s[38:39], 2, v180
	s_and_b64 s[40:41], s[42:43], s[40:41]
	v_cmp_gt_i32_e64 s[36:37], 1, v180
	s_and_b64 s[38:39], s[40:41], s[38:39]
	v_cmp_gt_i32_e64 s[34:35], 0, v180
	s_and_b64 s[36:37], s[38:39], s[36:37]
	s_and_b64 s[34:35], s[36:37], s[34:35]
	v_cmp_gt_i32_e64 s[30:31], 58, v180
	v_cndmask_b32_e64 v18, v18, 0, s[34:35]
	v_cmp_gt_i32_e64 s[34:35], 59, v180
	v_cmp_gt_i32_e64 s[28:29], 57, v180
	s_and_b64 s[30:31], s[34:35], s[30:31]
	v_cmp_gt_i32_e64 s[26:27], 56, v180
	s_and_b64 s[28:29], s[30:31], s[28:29]
	v_cmp_gt_i32_e64 s[24:25], 51, v180
	s_and_b64 s[26:27], s[28:29], s[26:27]
	v_cmp_gt_i32_e64 s[22:23], 50, v180
	s_and_b64 s[24:25], s[26:27], s[24:25]
	v_cmp_gt_i32_e64 s[20:21], 49, v180
	s_and_b64 s[22:23], s[24:25], s[22:23]
	v_cmp_gt_i32_e64 s[18:19], 48, v180
	s_and_b64 s[20:21], s[22:23], s[20:21]
	v_cmp_gt_i32_e64 s[16:17], 43, v180
	s_and_b64 s[18:19], s[20:21], s[18:19]
	v_cmp_gt_i32_e64 s[14:15], 42, v180
	s_and_b64 s[16:17], s[18:19], s[16:17]
	v_cmp_gt_i32_e64 s[12:13], 41, v180
	s_and_b64 s[14:15], s[16:17], s[14:15]
	v_cmp_gt_i32_e64 s[10:11], 40, v180
	s_and_b64 s[12:13], s[14:15], s[12:13]
	v_cmp_gt_i32_e64 s[8:9], 35, v180
	s_and_b64 s[10:11], s[12:13], s[10:11]
	v_cmp_gt_i32_e64 s[6:7], 34, v180
	s_and_b64 s[8:9], s[10:11], s[8:9]
	v_cmp_gt_i32_e64 s[4:5], 33, v180
	s_and_b64 s[6:7], s[8:9], s[6:7]
	v_cmp_gt_i32_e32 vcc, 32, v180
	s_and_b64 s[4:5], s[6:7], s[4:5]
	v_cndmask_b32_e64 v3, v3, 0, s[4:5]
	s_and_b64 s[4:5], s[4:5], vcc
	v_cndmask_b32_e64 v33, v33, 0, s[64:65]
	v_cndmask_b32_e64 v32, v32, 0, s[62:63]
	s_mov_b64 s[62:63], 0x100
	v_cndmask_b32_e64 v31, v31, 0, s[60:61]
	v_cndmask_b32_e64 v30, v30, 0, s[58:59]
	v_cndmask_b32_e64 v29, v29, 0, s[56:57]
	v_cndmask_b32_e64 v28, v28, 0, s[54:55]
	v_cndmask_b32_e64 v27, v27, 0, s[52:53]
	v_cndmask_b32_e64 v26, v26, 0, s[50:51]
	v_cndmask_b32_e64 v25, v25, 0, s[48:49]
	v_cndmask_b32_e64 v24, v24, 0, s[46:47]
	v_cndmask_b32_e64 v23, v23, 0, s[44:45]
	v_cndmask_b32_e64 v22, v22, 0, s[42:43]
	v_cndmask_b32_e64 v21, v21, 0, s[40:41]
	v_cndmask_b32_e64 v20, v20, 0, s[38:39]
	v_cndmask_b32_e64 v19, v19, 0, s[36:37]
	v_cndmask_b32_e64 v17, v17, 0, s[34:35]
	v_cndmask_b32_e64 v16, v16, 0, s[30:31]
	v_cndmask_b32_e64 v15, v15, 0, s[28:29]
	v_cndmask_b32_e64 v14, v14, 0, s[26:27]
	v_cndmask_b32_e64 v13, v13, 0, s[24:25]
	v_cndmask_b32_e64 v12, v12, 0, s[22:23]
	v_cndmask_b32_e64 v11, v11, 0, s[20:21]
	v_cndmask_b32_e64 v10, v10, 0, s[18:19]
	v_cndmask_b32_e64 v9, v9, 0, s[16:17]
	v_cndmask_b32_e64 v8, v8, 0, s[14:15]
	v_cndmask_b32_e64 v7, v7, 0, s[12:13]
	v_cndmask_b32_e64 v6, v6, 0, s[10:11]
	v_cndmask_b32_e64 v5, v5, 0, s[8:9]
	v_cndmask_b32_e64 v4, v4, 0, s[6:7]
	v_cndmask_b32_e64 v2, v2, 0, s[4:5]
.LBB0_519:
	s_lshl_b64 s[4:5], s[82:83], 12
	v_writelane_b32 v255, s4, 54
	v_lshlrev_b32_e32 v41, 3, v39
	v_and_b32_e32 v40, 0xc0, v40
	v_writelane_b32 v255, s5, 55
	v_lshlrev_b32_e32 v39, 1, v39
	v_readlane_b32 s8, v255, 46
	s_mul_i32 s5, s8, 0x6800
	s_mul_hi_i32 s4, s8, 0x6800
	s_add_u32 s5, s80, s5
	s_addc_u32 s6, s85, s4
	s_lshl_b32 s4, s69, 9
	v_and_or_b32 v40, v41, 24, v40
	v_and_b32_e32 v39, 32, v39
	v_and_b32_e32 v41, 0x100, v41
	s_add_u32 s4, s5, s4
	v_or3_b32 v39, v40, v39, v41
	v_mov_b32_e32 v41, s89
	s_addc_u32 s5, s6, 0
	v_add_u32_e32 v177, s79, v39
	v_lshrrev_b32_e32 v39, 2, v175
	v_lshrrev_b32_e32 v40, 1, v175
	s_lshr_b32 s6, s78, 1
	ds_read_b32 v41, v41
	v_bitop3_b32 v39, s78, v228, v39 bitop3:0xc8
	v_and_b32_e32 v40, 8, v40
	s_and_b32 s6, s6, 4
	v_or3_b32 v39, v40, v39, s6
	v_and_b32_e32 v40, 32, v0
	v_lshlrev_b32_e32 v0, 3, v0
	v_and_b32_e32 v0, 24, v0
	v_mul_u32_u24_e32 v39, 0x3400, v39
	v_or3_b32 v0, v40, v0, v39
	v_lshlrev_b32_e32 v162, 1, v0
	s_waitcnt lgkmcnt(0)
	v_sub_f32_e32 v0, v41, v178
	v_mul_f32_e32 v0, 0x3fb8aa3b, v0
	v_exp_f32_e32 v40, v0
	v_readlane_b32 s9, v255, 47
	v_writelane_b32 v255, s84, 56
	s_lshr_b32 s7, s84, 6
	v_mul_f32_e32 v39, v18, v40
	v_fma_f32 v18, v18, v40, 0
	v_fmac_f32_e32 v18, v19, v40
	v_fmac_f32_e32 v18, v20, v40
	v_fmac_f32_e32 v18, v21, v40
	v_fmac_f32_e32 v18, v22, v40
	v_fmac_f32_e32 v18, v23, v40
	v_fmac_f32_e32 v18, v24, v40
	v_fmac_f32_e32 v18, v25, v40
	v_fmac_f32_e32 v18, v26, v40
	v_fmac_f32_e32 v18, v27, v40
	v_fmac_f32_e32 v18, v28, v40
	v_fmac_f32_e32 v18, v29, v40
	v_fmac_f32_e32 v18, v30, v40
	v_fmac_f32_e32 v18, v31, v40
	v_fmac_f32_e32 v18, v32, v40
	v_fmac_f32_e32 v18, v33, v40
	v_fmac_f32_e32 v18, v2, v40
	v_fmac_f32_e32 v18, v3, v40
	v_mul_f32_e32 v41, v2, v40
	v_fmac_f32_e32 v18, v4, v40
	v_pk_mul_f32 v[6:7], v[6:7], v[40:41] op_sel_hi:[1,0]
	v_fmac_f32_e32 v18, v5, v40
	v_add_f32_e32 v2, v6, v18
	v_pk_mul_f32 v[8:9], v[8:9], v[40:41] op_sel_hi:[1,0]
	v_add_f32_e32 v2, v7, v2
	v_add_f32_e32 v2, v8, v2
	v_pk_mul_f32 v[10:11], v[10:11], v[40:41] op_sel_hi:[1,0]
	v_add_f32_e32 v2, v9, v2
	v_add_f32_e32 v2, v10, v2
	v_pk_mul_f32 v[12:13], v[12:13], v[40:41] op_sel_hi:[1,0]
	v_add_f32_e32 v2, v11, v2
	v_add_f32_e32 v2, v12, v2
	v_pk_mul_f32 v[14:15], v[14:15], v[40:41] op_sel_hi:[1,0]
	v_add_f32_e32 v2, v13, v2
	v_add_f32_e32 v2, v14, v2
	v_pk_mul_f32 v[16:17], v[16:17], v[40:41] op_sel_hi:[1,0]
	v_add_f32_e32 v2, v15, v2
	v_add_f32_e32 v2, v16, v2
	v_mul_f32_e32 v42, v19, v40
	v_mul_f32_e32 v43, v3, v40
	v_mul_f32_e32 v44, v20, v40
	v_mul_f32_e32 v45, v4, v40
	v_mul_f32_e32 v46, v21, v40
	v_mul_f32_e32 v47, v5, v40
	v_mul_f32_e32 v48, v22, v40
	v_mul_f32_e32 v49, v23, v40
	v_mul_f32_e32 v50, v24, v40
	v_mul_f32_e32 v51, v25, v40
	v_mul_f32_e32 v52, v26, v40
	v_mul_f32_e32 v53, v27, v40
	v_mul_f32_e32 v54, v28, v40
	v_mul_f32_e32 v55, v29, v40
	v_mul_f32_e32 v56, v30, v40
	v_mul_f32_e32 v57, v31, v40
	v_mul_f32_e32 v58, v32, v40
	v_mul_f32_e32 v59, v33, v40
	v_add_f32_e32 v2, v17, v2
	v_cvt_pk_bf16_f32 v128, v39, v42
	v_cvt_pk_bf16_f32 v129, v44, v46
	v_cvt_pk_bf16_f32 v130, v48, v49
	v_cvt_pk_bf16_f32 v131, v50, v51
	v_cvt_pk_bf16_f32 v132, v52, v53
	v_cvt_pk_bf16_f32 v133, v54, v55
	v_cvt_pk_bf16_f32 v134, v56, v57
	v_cvt_pk_bf16_f32 v135, v58, v59
	v_cvt_pk_bf16_f32 v136, v41, v43
	v_cvt_pk_bf16_f32 v137, v45, v47
	v_cvt_pk_bf16_f32 v138, v6, v7
	v_cvt_pk_bf16_f32 v139, v8, v9
	v_cvt_pk_bf16_f32 v140, v10, v11
	v_cvt_pk_bf16_f32 v141, v12, v13
	v_cvt_pk_bf16_f32 v142, v14, v15
	v_cvt_pk_bf16_f32 v143, v16, v17
	s_mov_b32 s88, 4
	v_writelane_b32 v255, s7, 57
	s_add_i32 s89, s7, 4
	s_mul_hi_i32 s90, s8, 0x6800
	v_mov_b32_e32 v0, 0
	v_add_f32_e32 v179, 0, v2
	v_permlane32_swap_b32_e32 v128, v130
	v_permlane32_swap_b32_e32 v129, v131
	v_permlane32_swap_b32_e32 v132, v134
	v_permlane32_swap_b32_e32 v133, v135
	v_permlane32_swap_b32_e32 v136, v138
	v_permlane32_swap_b32_e32 v137, v139
	v_permlane32_swap_b32_e32 v140, v142
	v_permlane32_swap_b32_e32 v141, v143
	s_bitcmp1_b32 s100, 8
	s_cbranch_scc1 .Lstg_b5
	s_waitcnt vmcnt(0)
	s_waitcnt lgkmcnt(0)
	s_barrier
.Lstg_b5:
	s_add_u32 s6, s3, 0x40000
	s_addc_u32 s7, s68, 0
	s_add_i32 s91, s2, 0x400
	v_lshl_add_u64 v[2:3], s[6:7], 0, v[170:171]
	s_mov_b32 s3, m0
	s_mov_b32 m0, s2
	s_nop 0
	global_load_lds_dwordx4 v[2:3], off
	s_mov_b32 m0, s3
	s_add_u32 s4, s4, 0x1a0800
	v_lshl_add_u64 v[2:3], s[6:7], 0, v[172:173]
	s_mov_b32 s3, m0
	s_mov_b32 m0, s91
	s_nop 0
	global_load_lds_dwordx4 v[2:3], off
	s_mov_b32 m0, s3
	s_addc_u32 s5, s5, 0
	v_mov_b32_e32 v163, v161
	v_lshl_add_u64 v[2:3], s[4:5], 0, v[162:163]
	s_add_i32 s3, s81, 0x8000
	s_mov_b32 s4, m0
	s_mov_b32 m0, s3
	s_nop 0
	global_load_lds_dwordx4 v[2:3], off
	s_mov_b32 m0, s4
	v_lshl_add_u64 v[4:5], v[2:3], 0, s[86:87]
	s_add_i32 s95, s81, 0x8400
	s_mov_b32 s4, m0
	s_mov_b32 m0, s95
	s_nop 0
	global_load_lds_dwordx4 v[4:5], off
	s_mov_b32 m0, s4
	v_lshl_add_u64 v[4:5], v[2:3], 0, s[62:63]
	s_add_i32 s93, s81, 0x8800
	s_mov_b32 s4, m0
	s_mov_b32 m0, s93
	s_nop 0
	global_load_lds_dwordx4 v[4:5], off
	s_mov_b32 m0, s4
	s_mov_b64 s[4:5], 0x180
	v_lshl_add_u64 v[2:3], v[2:3], 0, s[4:5]
	s_add_i32 s79, s81, 0x8c00
	s_mov_b32 s4, m0
	s_mov_b32 m0, s79
	s_nop 0
	global_load_lds_dwordx4 v[2:3], off
	s_mov_b32 m0, s4
	s_nop 0
	v_readlane_b32 s4, v255, 34
	s_mul_i32 s5, s8, 0x6800
	s_add_i32 s78, s81, 0x400
	v_add_u32_e32 v2, s4, v34
	s_add_i32 s4, s94, 0xffffff80
	v_add_u32_e32 v189, v35, v2
	v_add_u32_e32 v188, v36, v2
	v_add_u32_e32 v187, v37, v2
	v_add_u32_e32 v186, v38, v2
	v_add_u32_e32 v2, s4, v175
	s_lshl_b32 s4, s33, 6
	s_and_b32 s4, s4, 0x600
	s_or_b32 s84, s5, s4
	v_readlane_b32 s4, v255, 48
	s_add_i32 s69, s81, 0x800
	s_add_i32 s68, s81, 0xc00
	v_sub_u32_e32 v190, v2, v1
	s_or_b32 s66, s66, s4
	s_movk_i32 s85, 0xbf
	v_readlane_b32 s80, v255, 39
	v_mov_b32_e32 v1, v0
	v_mov_b32_e32 v2, v0
	v_mov_b32_e32 v3, v0
	v_mov_b32_e32 v4, v0
	v_mov_b32_e32 v5, v0
	v_mov_b32_e32 v6, v0
	v_mov_b32_e32 v7, v0
	v_mov_b32_e32 v8, v0
	v_mov_b32_e32 v9, v0
	v_mov_b32_e32 v10, v0
	v_mov_b32_e32 v11, v0
	v_mov_b32_e32 v12, v0
	v_mov_b32_e32 v13, v0
	v_mov_b32_e32 v14, v0
	v_mov_b32_e32 v15, v0
	v_mov_b32_e32 v112, v0
	v_mov_b32_e32 v113, v0
	v_mov_b32_e32 v114, v0
	v_mov_b32_e32 v115, v0
	v_mov_b32_e32 v116, v0
	v_mov_b32_e32 v117, v0
	v_mov_b32_e32 v118, v0
	v_mov_b32_e32 v119, v0
	v_mov_b32_e32 v120, v0
	v_mov_b32_e32 v121, v0
	v_mov_b32_e32 v122, v0
	v_mov_b32_e32 v123, v0
	v_mov_b32_e32 v124, v0
	v_mov_b32_e32 v125, v0
	v_mov_b32_e32 v126, v0
	v_mov_b32_e32 v127, v0
	v_mov_b32_e32 v16, v0
	v_mov_b32_e32 v17, v0
	v_mov_b32_e32 v18, v0
	v_mov_b32_e32 v19, v0
	v_mov_b32_e32 v20, v0
	v_mov_b32_e32 v21, v0
	v_mov_b32_e32 v22, v0
	v_mov_b32_e32 v23, v0
	v_mov_b32_e32 v24, v0
	v_mov_b32_e32 v25, v0
	v_mov_b32_e32 v26, v0
	v_mov_b32_e32 v27, v0
	v_mov_b32_e32 v28, v0
	v_mov_b32_e32 v29, v0
	v_mov_b32_e32 v30, v0
	v_mov_b32_e32 v31, v0
	v_mov_b32_e32 v32, v0
	v_mov_b32_e32 v33, v0
	v_mov_b32_e32 v34, v0
	v_mov_b32_e32 v35, v0
	v_mov_b32_e32 v36, v0
	v_mov_b32_e32 v37, v0
	v_mov_b32_e32 v38, v0
	v_mov_b32_e32 v39, v0
	v_mov_b32_e32 v40, v0
	v_mov_b32_e32 v41, v0
	v_mov_b32_e32 v42, v0
	v_mov_b32_e32 v43, v0
	v_mov_b32_e32 v44, v0
	v_mov_b32_e32 v45, v0
	v_mov_b32_e32 v46, v0
	v_mov_b32_e32 v47, v0
	v_mov_b32_e32 v48, v0
	v_mov_b32_e32 v49, v0
	v_mov_b32_e32 v50, v0
	v_mov_b32_e32 v51, v0
	v_mov_b32_e32 v52, v0
	v_mov_b32_e32 v53, v0
	v_mov_b32_e32 v54, v0
	v_mov_b32_e32 v55, v0
	v_mov_b32_e32 v56, v0
	v_mov_b32_e32 v57, v0
	v_mov_b32_e32 v58, v0
	v_mov_b32_e32 v59, v0
	v_mov_b32_e32 v60, v0
	v_mov_b32_e32 v61, v0
	v_mov_b32_e32 v62, v0
	v_mov_b32_e32 v63, v0
	v_mov_b32_e32 v64, v0
	v_mov_b32_e32 v65, v0
	v_mov_b32_e32 v66, v0
	v_mov_b32_e32 v67, v0
	v_mov_b32_e32 v68, v0
	v_mov_b32_e32 v69, v0
	v_mov_b32_e32 v70, v0
	v_mov_b32_e32 v71, v0
	v_mov_b32_e32 v72, v0
	v_mov_b32_e32 v73, v0
	v_mov_b32_e32 v74, v0
	v_mov_b32_e32 v75, v0
	v_mov_b32_e32 v76, v0
	v_mov_b32_e32 v77, v0
	v_mov_b32_e32 v78, v0
	v_mov_b32_e32 v79, v0
	v_mov_b32_e32 v80, v0
	v_mov_b32_e32 v81, v0
	v_mov_b32_e32 v82, v0
	v_mov_b32_e32 v83, v0
	v_mov_b32_e32 v84, v0
	v_mov_b32_e32 v85, v0
	v_mov_b32_e32 v86, v0
	v_mov_b32_e32 v87, v0
	v_mov_b32_e32 v88, v0
	v_mov_b32_e32 v89, v0
	v_mov_b32_e32 v90, v0
	v_mov_b32_e32 v91, v0
	v_mov_b32_e32 v92, v0
	v_mov_b32_e32 v93, v0
	v_mov_b32_e32 v94, v0
	v_mov_b32_e32 v95, v0
	v_mov_b32_e32 v96, v0
	v_mov_b32_e32 v97, v0
	v_mov_b32_e32 v98, v0
	v_mov_b32_e32 v99, v0
	v_mov_b32_e32 v100, v0
	v_mov_b32_e32 v101, v0
	v_mov_b32_e32 v102, v0
	v_mov_b32_e32 v103, v0
	v_mov_b32_e32 v104, v0
	v_mov_b32_e32 v105, v0
	v_mov_b32_e32 v106, v0
	v_mov_b32_e32 v107, v0
	v_mov_b32_e32 v108, v0
	v_mov_b32_e32 v109, v0
	v_mov_b32_e32 v110, v0
	v_mov_b32_e32 v111, v0
.LBB0_520:
	ds_read_b64_tr_b16 v[144:145], v177 offset:0
	ds_read_b64_tr_b16 v[146:147], v177 offset:0x1000
	ds_read_b64_tr_b16 v[148:149], v177 offset:0x2000
	ds_read_b64_tr_b16 v[150:151], v177 offset:0x3000
	ds_read_b64_tr_b16 v[152:153], v177 offset:0x4000
	ds_read_b64_tr_b16 v[154:155], v177 offset:0x5000
	ds_read_b64_tr_b16 v[156:157], v177 offset:0x6000
	ds_read_b64_tr_b16 v[158:159], v177 offset:0x7000
	ds_read_b64_tr_b16 v[198:199], v177 offset:0x200
	ds_read_b64_tr_b16 v[200:201], v177 offset:0x1200
	ds_read_b64_tr_b16 v[202:203], v177 offset:0x2200
	ds_read_b64_tr_b16 v[204:205], v177 offset:0x3200
	ds_read_b64_tr_b16 v[206:207], v177 offset:0x4200
	ds_read_b64_tr_b16 v[208:209], v177 offset:0x5200
	ds_read_b64_tr_b16 v[210:211], v177 offset:0x6200
	ds_read_b64_tr_b16 v[212:213], v177 offset:0x7200
	s_waitcnt lgkmcnt(8)
	s_nop 0
	v_mfma_f32_32x32x16_bf16 v[112:127], v[144:147], v[128:131], v[112:127]
	v_mfma_f32_32x32x16_bf16 v[112:127], v[148:151], v[132:135], v[112:127]
	v_mfma_f32_32x32x16_bf16 v[112:127], v[152:155], v[136:139], v[112:127]
	v_mfma_f32_32x32x16_bf16 v[112:127], v[156:159], v[140:143], v[112:127]
	ds_read_b64_tr_b16 v[144:145], v177 offset:0x400
	ds_read_b64_tr_b16 v[146:147], v177 offset:0x1400
	ds_read_b64_tr_b16 v[148:149], v177 offset:0x2400
	ds_read_b64_tr_b16 v[150:151], v177 offset:0x3400
	ds_read_b64_tr_b16 v[152:153], v177 offset:0x4400
	ds_read_b64_tr_b16 v[154:155], v177 offset:0x5400
	ds_read_b64_tr_b16 v[156:157], v177 offset:0x6400
	ds_read_b64_tr_b16 v[158:159], v177 offset:0x7400
	s_waitcnt lgkmcnt(8)
	v_mfma_f32_32x32x16_bf16 v[0:15], v[198:201], v[128:131], v[0:15]
	v_mfma_f32_32x32x16_bf16 v[0:15], v[202:205], v[132:135], v[0:15]
	v_mfma_f32_32x32x16_bf16 v[0:15], v[206:209], v[136:139], v[0:15]
	v_mfma_f32_32x32x16_bf16 v[0:15], v[210:213], v[140:143], v[0:15]
	ds_read_b64_tr_b16 v[198:199], v177 offset:0x600
	ds_read_b64_tr_b16 v[200:201], v177 offset:0x1600
	ds_read_b64_tr_b16 v[202:203], v177 offset:0x2600
	ds_read_b64_tr_b16 v[204:205], v177 offset:0x3600
	ds_read_b64_tr_b16 v[206:207], v177 offset:0x4600
	ds_read_b64_tr_b16 v[208:209], v177 offset:0x5600
	ds_read_b64_tr_b16 v[210:211], v177 offset:0x6600
	ds_read_b64_tr_b16 v[212:213], v177 offset:0x7600
	s_waitcnt lgkmcnt(8)
	v_mfma_f32_32x32x16_bf16 v[16:31], v[144:147], v[128:131], v[16:31]
	v_mfma_f32_32x32x16_bf16 v[16:31], v[148:151], v[132:135], v[16:31]
	v_mfma_f32_32x32x16_bf16 v[16:31], v[152:155], v[136:139], v[16:31]
	v_mfma_f32_32x32x16_bf16 v[16:31], v[156:159], v[140:143], v[16:31]
	ds_read_b64_tr_b16 v[144:145], v177 offset:0x800
	ds_read_b64_tr_b16 v[146:147], v177 offset:0x1800
	ds_read_b64_tr_b16 v[148:149], v177 offset:0x2800
	ds_read_b64_tr_b16 v[150:151], v177 offset:0x3800
	ds_read_b64_tr_b16 v[152:153], v177 offset:0x4800
	ds_read_b64_tr_b16 v[154:155], v177 offset:0x5800
	ds_read_b64_tr_b16 v[156:157], v177 offset:0x6800
	ds_read_b64_tr_b16 v[158:159], v177 offset:0x7800
	s_waitcnt lgkmcnt(8)
	v_mfma_f32_32x32x16_bf16 v[32:47], v[198:201], v[128:131], v[32:47]
	v_mfma_f32_32x32x16_bf16 v[32:47], v[202:205], v[132:135], v[32:47]
	v_mfma_f32_32x32x16_bf16 v[32:47], v[206:209], v[136:139], v[32:47]
	v_mfma_f32_32x32x16_bf16 v[32:47], v[210:213], v[140:143], v[32:47]
	ds_read_b64_tr_b16 v[198:199], v177 offset:0xa00
	ds_read_b64_tr_b16 v[200:201], v177 offset:0x1a00
	ds_read_b64_tr_b16 v[202:203], v177 offset:0x2a00
	ds_read_b64_tr_b16 v[204:205], v177 offset:0x3a00
	ds_read_b64_tr_b16 v[206:207], v177 offset:0x4a00
	ds_read_b64_tr_b16 v[208:209], v177 offset:0x5a00
	ds_read_b64_tr_b16 v[210:211], v177 offset:0x6a00
	ds_read_b64_tr_b16 v[212:213], v177 offset:0x7a00
	s_waitcnt lgkmcnt(8)
	v_mfma_f32_32x32x16_bf16 v[48:63], v[144:147], v[128:131], v[48:63]
	v_mfma_f32_32x32x16_bf16 v[48:63], v[148:151], v[132:135], v[48:63]
	v_mfma_f32_32x32x16_bf16 v[48:63], v[152:155], v[136:139], v[48:63]
	v_mfma_f32_32x32x16_bf16 v[48:63], v[156:159], v[140:143], v[48:63]
	ds_read_b64_tr_b16 v[144:145], v177 offset:0xc00
	ds_read_b64_tr_b16 v[146:147], v177 offset:0x1c00
	ds_read_b64_tr_b16 v[148:149], v177 offset:0x2c00
	ds_read_b64_tr_b16 v[150:151], v177 offset:0x3c00
	ds_read_b64_tr_b16 v[152:153], v177 offset:0x4c00
	ds_read_b64_tr_b16 v[154:155], v177 offset:0x5c00
	ds_read_b64_tr_b16 v[156:157], v177 offset:0x6c00
	ds_read_b64_tr_b16 v[158:159], v177 offset:0x7c00
	s_waitcnt lgkmcnt(8)
	v_mfma_f32_32x32x16_bf16 v[64:79], v[198:201], v[128:131], v[64:79]
	v_mfma_f32_32x32x16_bf16 v[64:79], v[202:205], v[132:135], v[64:79]
	v_mfma_f32_32x32x16_bf16 v[64:79], v[206:209], v[136:139], v[64:79]
	v_mfma_f32_32x32x16_bf16 v[64:79], v[210:213], v[140:143], v[64:79]
	ds_read_b64_tr_b16 v[198:199], v177 offset:0xe00
	ds_read_b64_tr_b16 v[200:201], v177 offset:0x1e00
	ds_read_b64_tr_b16 v[202:203], v177 offset:0x2e00
	ds_read_b64_tr_b16 v[204:205], v177 offset:0x3e00
	ds_read_b64_tr_b16 v[206:207], v177 offset:0x4e00
	ds_read_b64_tr_b16 v[208:209], v177 offset:0x5e00
	ds_read_b64_tr_b16 v[210:211], v177 offset:0x6e00
	ds_read_b64_tr_b16 v[212:213], v177 offset:0x7e00
	s_waitcnt lgkmcnt(8)
	v_mfma_f32_32x32x16_bf16 v[80:95], v[144:147], v[128:131], v[80:95]
	v_mfma_f32_32x32x16_bf16 v[80:95], v[148:151], v[132:135], v[80:95]
	v_mfma_f32_32x32x16_bf16 v[80:95], v[152:155], v[136:139], v[80:95]
	v_mfma_f32_32x32x16_bf16 v[80:95], v[156:159], v[140:143], v[80:95]
	s_waitcnt lgkmcnt(0)
	v_mfma_f32_32x32x16_bf16 v[96:111], v[198:201], v[128:131], v[96:111]
	v_mfma_f32_32x32x16_bf16 v[96:111], v[202:205], v[132:135], v[96:111]
	v_mfma_f32_32x32x16_bf16 v[96:111], v[206:209], v[136:139], v[96:111]
	v_mfma_f32_32x32x16_bf16 v[96:111], v[210:213], v[140:143], v[96:111]
	ds_read_b128 v[128:131], v189 offset:0
	ds_read_b128 v[132:135], v189 offset:0x2000
	ds_read_b128 v[136:139], v181 offset:0
	ds_read_b128 v[198:201], v188 offset:0
	ds_read_b128 v[202:205], v188 offset:0x2000
	ds_read_b128 v[206:209], v181 offset:0x400
	s_waitcnt lgkmcnt(3)
	s_nop 0
	v_mfma_f32_32x32x16_bf16 v[144:159], v[128:131], v[136:139], 0
	v_mfma_f32_32x32x16_bf16 v[128:143], v[132:135], v[136:139], 0
	ds_read_b128 v[210:213], v187 offset:0
	ds_read_b128 v[214:217], v187 offset:0x2000
	ds_read_b128 v[218:221], v181 offset:0x800
	s_waitcnt lgkmcnt(3)
	v_mfma_f32_32x32x16_bf16 v[144:159], v[198:201], v[206:209], v[144:159]
	v_mfma_f32_32x32x16_bf16 v[128:143], v[202:205], v[206:209], v[128:143]
	ds_read_b128 v[198:201], v186 offset:0
	ds_read_b128 v[202:205], v186 offset:0x2000
	ds_read_b128 v[206:209], v181 offset:0xc00
	s_waitcnt lgkmcnt(3)
	v_mfma_f32_32x32x16_bf16 v[144:159], v[210:213], v[218:221], v[144:159]
	v_mfma_f32_32x32x16_bf16 v[128:143], v[214:217], v[218:221], v[128:143]
	ds_read_b128 v[210:213], v189 offset:0x80
	ds_read_b128 v[214:217], v189 offset:0x2080
	ds_read_b128 v[218:221], v181 offset:0x1000
	s_waitcnt lgkmcnt(3)
	v_mfma_f32_32x32x16_bf16 v[144:159], v[198:201], v[206:209], v[144:159]
	v_mfma_f32_32x32x16_bf16 v[128:143], v[202:205], v[206:209], v[128:143]
	ds_read_b128 v[198:201], v188 offset:0x80
	ds_read_b128 v[202:205], v188 offset:0x2080
	ds_read_b128 v[206:209], v181 offset:0x1400
	s_waitcnt lgkmcnt(3)
	v_mfma_f32_32x32x16_bf16 v[144:159], v[210:213], v[218:221], v[144:159]
	v_mfma_f32_32x32x16_bf16 v[128:143], v[214:217], v[218:221], v[128:143]
	ds_read_b128 v[210:213], v187 offset:0x80
	ds_read_b128 v[214:217], v187 offset:0x2080
	ds_read_b128 v[218:221], v181 offset:0x1800
	s_waitcnt lgkmcnt(3)
	v_mfma_f32_32x32x16_bf16 v[144:159], v[198:201], v[206:209], v[144:159]
	v_mfma_f32_32x32x16_bf16 v[128:143], v[202:205], v[206:209], v[128:143]
	ds_read_b128 v[198:201], v186 offset:0x80
	ds_read_b128 v[202:205], v186 offset:0x2080
	s_waitcnt lgkmcnt(2)
	v_mfma_f32_32x32x16_bf16 v[144:159], v[210:213], v[218:221], v[144:159]
	v_mfma_f32_32x32x16_bf16 v[128:143], v[214:217], v[218:221], v[128:143]
	s_waitcnt lgkmcnt(0)
	v_mfma_f32_32x32x16_bf16 v[144:159], v[198:201], v[166:169], v[144:159]
	v_mfma_f32_32x32x16_bf16 v[128:143], v[202:205], v[166:169], v[128:143]
	s_bitcmp0_b32 s100, 8
	s_cbranch_scc1 .Lstg_a2
	s_waitcnt vmcnt(0)
	s_waitcnt lgkmcnt(0)
	s_barrier
.Lstg_a2:
	s_sub_i32 s4, s85, 64
	s_cmp_le_i32 s4, s94
	s_cbranch_scc1 .LBB0_522
	v_add_u32_e32 v191, 64, v190
	v_cmp_gt_i32_e64 s[62:63], 26, v191
	v_cmp_gt_i32_e64 s[64:65], 27, v191
	v_cmp_gt_i32_e64 s[60:61], 25, v191
	s_and_b64 s[62:63], s[64:65], s[62:63]
	v_cmp_gt_i32_e64 s[58:59], 24, v191
	s_and_b64 s[60:61], s[62:63], s[60:61]
	v_cmp_gt_i32_e64 s[56:57], 19, v191
	s_and_b64 s[58:59], s[60:61], s[58:59]
	v_cmp_gt_i32_e64 s[54:55], 18, v191
	s_and_b64 s[56:57], s[58:59], s[56:57]
	v_cmp_gt_i32_e64 s[52:53], 17, v191
	s_and_b64 s[54:55], s[56:57], s[54:55]
	v_cmp_gt_i32_e64 s[50:51], 16, v191
	s_and_b64 s[52:53], s[54:55], s[52:53]
	v_cmp_gt_i32_e64 s[48:49], 11, v191
	s_and_b64 s[50:51], s[52:53], s[50:51]
	v_cmp_gt_i32_e64 s[46:47], 10, v191
	s_and_b64 s[48:49], s[50:51], s[48:49]
	v_cmp_gt_i32_e64 s[44:45], 9, v191
	s_and_b64 s[46:47], s[48:49], s[46:47]
	v_cmp_gt_i32_e64 s[42:43], 8, v191
	s_and_b64 s[44:45], s[46:47], s[44:45]
	v_cmp_gt_i32_e64 s[40:41], 3, v191
	s_and_b64 s[42:43], s[44:45], s[42:43]
	v_cmp_gt_i32_e64 s[38:39], 2, v191
	s_and_b64 s[40:41], s[42:43], s[40:41]
	v_cmp_gt_i32_e64 s[36:37], 1, v191
	s_and_b64 s[38:39], s[40:41], s[38:39]
	v_cmp_gt_i32_e64 s[34:35], 0, v191
	s_and_b64 s[36:37], s[38:39], s[36:37]
	s_and_b64 s[34:35], s[36:37], s[34:35]
	v_cmp_gt_i32_e64 s[30:31], 58, v191
	v_cndmask_b32_e64 v144, v144, 0, s[34:35]
	v_cmp_gt_i32_e64 s[34:35], 59, v191
	v_cmp_gt_i32_e64 s[28:29], 57, v191
	s_and_b64 s[30:31], s[34:35], s[30:31]
	v_cmp_gt_i32_e64 s[26:27], 56, v191
	s_and_b64 s[28:29], s[30:31], s[28:29]
	v_cmp_gt_i32_e64 s[24:25], 51, v191
	s_and_b64 s[26:27], s[28:29], s[26:27]
	v_cmp_gt_i32_e64 s[22:23], 50, v191
	s_and_b64 s[24:25], s[26:27], s[24:25]
	v_cmp_gt_i32_e64 s[20:21], 49, v191
	s_and_b64 s[22:23], s[24:25], s[22:23]
	v_cmp_gt_i32_e64 s[18:19], 48, v191
	s_and_b64 s[20:21], s[22:23], s[20:21]
	v_cmp_gt_i32_e64 s[16:17], 43, v191
	s_and_b64 s[18:19], s[20:21], s[18:19]
	v_cmp_gt_i32_e64 s[14:15], 42, v191
	s_and_b64 s[16:17], s[18:19], s[16:17]
	v_cmp_gt_i32_e64 s[12:13], 41, v191
	s_and_b64 s[14:15], s[16:17], s[14:15]
	v_cmp_gt_i32_e64 s[10:11], 40, v191
	s_and_b64 s[12:13], s[14:15], s[12:13]
	v_cmp_gt_i32_e64 s[8:9], 35, v191
	s_and_b64 s[10:11], s[12:13], s[10:11]
	v_cmp_gt_i32_e64 s[6:7], 34, v191
	s_and_b64 s[8:9], s[10:11], s[8:9]
	v_cmp_gt_i32_e64 s[4:5], 33, v191
	s_and_b64 s[6:7], s[8:9], s[6:7]
	v_cmp_gt_i32_e32 vcc, 32, v191
	s_and_b64 s[4:5], s[6:7], s[4:5]
	v_cndmask_b32_e64 v129, v129, 0, s[4:5]
	s_and_b64 s[4:5], s[4:5], vcc
	v_cndmask_b32_e64 v159, v159, 0, s[64:65]
	v_cndmask_b32_e64 v158, v158, 0, s[62:63]
	s_mov_b64 s[62:63], 0x100
	v_cndmask_b32_e64 v157, v157, 0, s[60:61]
	v_cndmask_b32_e64 v156, v156, 0, s[58:59]
	v_cndmask_b32_e64 v155, v155, 0, s[56:57]
	v_cndmask_b32_e64 v154, v154, 0, s[54:55]
	v_cndmask_b32_e64 v153, v153, 0, s[52:53]
	v_cndmask_b32_e64 v152, v152, 0, s[50:51]
	v_cndmask_b32_e64 v151, v151, 0, s[48:49]
	v_cndmask_b32_e64 v150, v150, 0, s[46:47]
	v_cndmask_b32_e64 v149, v149, 0, s[44:45]
	v_cndmask_b32_e64 v148, v148, 0, s[42:43]
	v_cndmask_b32_e64 v147, v147, 0, s[40:41]
	v_cndmask_b32_e64 v146, v146, 0, s[38:39]
	v_cndmask_b32_e64 v145, v145, 0, s[36:37]
	v_cndmask_b32_e64 v143, v143, 0, s[34:35]
	v_cndmask_b32_e64 v142, v142, 0, s[30:31]
	v_cndmask_b32_e64 v141, v141, 0, s[28:29]
	v_cndmask_b32_e64 v140, v140, 0, s[26:27]
	v_cndmask_b32_e64 v139, v139, 0, s[24:25]
	v_cndmask_b32_e64 v138, v138, 0, s[22:23]
	v_cndmask_b32_e64 v137, v137, 0, s[20:21]
	v_cndmask_b32_e64 v136, v136, 0, s[18:19]
	v_cndmask_b32_e64 v135, v135, 0, s[16:17]
	v_cndmask_b32_e64 v134, v134, 0, s[14:15]
	v_cndmask_b32_e64 v133, v133, 0, s[12:13]
	v_cndmask_b32_e64 v132, v132, 0, s[10:11]
	v_cndmask_b32_e64 v131, v131, 0, s[8:9]
	v_cndmask_b32_e64 v130, v130, 0, s[6:7]
	v_cndmask_b32_e64 v128, v128, 0, s[4:5]
.LBB0_522:
	v_mov_b32_e32 v191, s80
	ds_read_b32 v191, v191
	s_waitcnt lgkmcnt(0)
	v_sub_f32_e32 v191, v191, v178
	v_mul_f32_e32 v191, 0x3fb8aa3b, v191
	v_exp_f32_e32 v194, v191
	s_nop 1
	v_mul_f32_e32 v210, v144, v194
	v_mul_f32_e32 v191, v128, v194
	v_mul_f32_e32 v212, v145, v194
	v_mul_f32_e32 v192, v129, v194
	v_mul_f32_e32 v213, v146, v194
	v_mul_f32_e32 v193, v130, v194
	v_mul_f32_e32 v214, v147, v194
	v_mul_f32_e32 v198, v131, v194
	v_mul_f32_e32 v215, v148, v194
	v_mul_f32_e32 v199, v132, v194
	v_mul_f32_e32 v216, v149, v194
	v_mul_f32_e32 v200, v133, v194
	v_mul_f32_e32 v217, v150, v194
	v_mul_f32_e32 v201, v134, v194
	v_mul_f32_e32 v218, v151, v194
	v_mul_f32_e32 v202, v135, v194
	v_mul_f32_e32 v219, v152, v194
	v_mul_f32_e32 v203, v136, v194
	v_mul_f32_e32 v220, v153, v194
	v_mul_f32_e32 v204, v137, v194
	v_mul_f32_e32 v221, v154, v194
	v_mul_f32_e32 v205, v138, v194
	v_mul_f32_e32 v230, v155, v194
	v_mul_f32_e32 v206, v139, v194
	v_mul_f32_e32 v231, v156, v194
	v_mul_f32_e32 v207, v140, v194
	v_mul_f32_e32 v232, v157, v194
	v_mul_f32_e32 v208, v141, v194
	v_mul_f32_e32 v233, v158, v194
	v_mul_f32_e32 v209, v142, v194
	v_mul_f32_e32 v234, v159, v194
	v_mul_f32_e32 v211, v143, v194
	v_cvt_pk_bf16_f32 v128, v210, v212
	v_cvt_pk_bf16_f32 v129, v213, v214
	v_cvt_pk_bf16_f32 v130, v215, v216
	v_cvt_pk_bf16_f32 v131, v217, v218
	v_cvt_pk_bf16_f32 v132, v219, v220
	v_cvt_pk_bf16_f32 v133, v221, v230
	v_cvt_pk_bf16_f32 v134, v231, v232
	v_cvt_pk_bf16_f32 v135, v233, v234
	v_cvt_pk_bf16_f32 v136, v191, v192
	v_cvt_pk_bf16_f32 v137, v193, v198
	v_cvt_pk_bf16_f32 v138, v199, v200
	v_cvt_pk_bf16_f32 v139, v201, v202
	v_cvt_pk_bf16_f32 v140, v203, v204
	v_cvt_pk_bf16_f32 v141, v205, v206
	v_cvt_pk_bf16_f32 v142, v207, v208
	v_cvt_pk_bf16_f32 v143, v209, v211
	s_nop 0
	v_permlane32_swap_b32_e32 v128, v130
	v_permlane32_swap_b32_e32 v129, v131
	v_permlane32_swap_b32_e32 v132, v134
	v_permlane32_swap_b32_e32 v133, v135
	v_permlane32_swap_b32_e32 v136, v138
	v_permlane32_swap_b32_e32 v137, v139
	v_permlane32_swap_b32_e32 v140, v142
	v_permlane32_swap_b32_e32 v141, v143
	s_bitcmp1_b32 s100, 8
	s_cbranch_scc1 .Lstg_b6
	s_waitcnt vmcnt(0)
	s_waitcnt lgkmcnt(0)
	s_barrier
.Lstg_b6:
	s_add_i32 s6, s88, -1
	s_cmp_ge_u32 s6, s89
	s_cselect_b64 s[82:83], -1, 0
	s_mov_b64 s[4:5], -1
	s_and_b64 vcc, exec, s[82:83]
	s_cbranch_vccz .LBB0_524
	v_mov_b64_e32 v[144:145], s[0:1]
	flat_load_dword v146, v[144:145] sc0 sc1
	s_waitcnt vmcnt(0)
	v_mov_b64_e32 v[144:145], s[74:75]
	flat_load_dword v144, v[144:145] sc0 sc1
	s_waitcnt vmcnt(0) lgkmcnt(0)
	v_readfirstlane_b32 s4, v146
	v_readfirstlane_b32 s5, v144
	s_nop 1
	v_lshl_add_u64 v[144:145], s[4:5], 0, v[170:171]
	s_mov_b32 s6, m0
	s_mov_b32 m0, s2
	s_nop 0
	global_load_lds_dwordx4 v[144:145], off
	s_mov_b32 m0, s6
	v_lshl_add_u64 v[144:145], s[4:5], 0, v[172:173]
	s_mov_b32 s4, m0
	s_mov_b32 m0, s91
	s_nop 0
	global_load_lds_dwordx4 v[144:145], off
	s_mov_b32 m0, s4
	s_mov_b64 s[4:5], 0

.LBB0_526:
	s_add_u32 s33, s72, s84
	s_addc_u32 s92, s73, s90
	s_add_u32 s4, s33, 0x2dd40800
	s_addc_u32 s5, s92, 0
	v_lshl_add_u64 v[144:145], s[4:5], 0, v[162:163]
	s_mov_b32 s4, m0
	s_mov_b32 m0, s81
	s_nop 0
	global_load_lds_dwordx4 v[144:145], off
	s_mov_b32 m0, s4
	v_lshl_add_u64 v[146:147], v[144:145], 0, s[86:87]
	s_mov_b32 s4, m0
	s_mov_b32 m0, s78
	s_nop 0
	global_load_lds_dwordx4 v[146:147], off
	s_mov_b32 m0, s4
	v_lshl_add_u64 v[146:147], v[144:145], 0, s[62:63]
	s_mov_b32 s4, m0
	s_mov_b32 m0, s69
	s_nop 0
	global_load_lds_dwordx4 v[146:147], off
	s_mov_b32 m0, s4
	s_mov_b64 s[4:5], 0x180
	v_lshl_add_u64 v[144:145], v[144:145], 0, s[4:5]
	s_mov_b32 s4, m0
	s_mov_b32 m0, s68
	s_nop 0
	global_load_lds_dwordx4 v[144:145], off
	s_mov_b32 m0, s4
	ds_read_b64_tr_b16 v[144:145], v177 offset:0x8000
	ds_read_b64_tr_b16 v[146:147], v177 offset:0x9000
	ds_read_b64_tr_b16 v[148:149], v177 offset:0xa000
	ds_read_b64_tr_b16 v[150:151], v177 offset:0xb000
	ds_read_b64_tr_b16 v[152:153], v177 offset:0xc000
	ds_read_b64_tr_b16 v[154:155], v177 offset:0xd000
	ds_read_b64_tr_b16 v[156:157], v177 offset:0xe000
	ds_read_b64_tr_b16 v[158:159], v177 offset:0xf000
	ds_read_b64_tr_b16 v[236:237], v177 offset:0x8200
	ds_read_b64_tr_b16 v[238:239], v177 offset:0x9200
	ds_read_b64_tr_b16 v[240:241], v177 offset:0xa200
	ds_read_b64_tr_b16 v[242:243], v177 offset:0xb200
	ds_read_b64_tr_b16 v[244:245], v177 offset:0xc200
	ds_read_b64_tr_b16 v[246:247], v177 offset:0xd200
	ds_read_b64_tr_b16 v[248:249], v177 offset:0xe200
	ds_read_b64_tr_b16 v[250:251], v177 offset:0xf200
	s_waitcnt lgkmcnt(8)
	s_nop 1
	v_mfma_f32_32x32x16_bf16 v[112:127], v[144:147], v[128:131], v[112:127]
	v_mfma_f32_32x32x16_bf16 v[112:127], v[148:151], v[132:135], v[112:127]
	v_mfma_f32_32x32x16_bf16 v[112:127], v[152:155], v[136:139], v[112:127]
	v_mfma_f32_32x32x16_bf16 v[112:127], v[156:159], v[140:143], v[112:127]
	ds_read_b64_tr_b16 v[144:145], v177 offset:0x8400
	ds_read_b64_tr_b16 v[146:147], v177 offset:0x9400
	ds_read_b64_tr_b16 v[148:149], v177 offset:0xa400
	ds_read_b64_tr_b16 v[150:151], v177 offset:0xb400
	ds_read_b64_tr_b16 v[152:153], v177 offset:0xc400
	ds_read_b64_tr_b16 v[154:155], v177 offset:0xd400
	ds_read_b64_tr_b16 v[156:157], v177 offset:0xe400
	ds_read_b64_tr_b16 v[158:159], v177 offset:0xf400
	s_waitcnt lgkmcnt(8)
	v_mfma_f32_32x32x16_bf16 v[0:15], v[236:239], v[128:131], v[0:15]
	v_mfma_f32_32x32x16_bf16 v[0:15], v[240:243], v[132:135], v[0:15]
	v_mfma_f32_32x32x16_bf16 v[0:15], v[244:247], v[136:139], v[0:15]
	v_mfma_f32_32x32x16_bf16 v[0:15], v[248:251], v[140:143], v[0:15]
	ds_read_b64_tr_b16 v[236:237], v177 offset:0x8600
	ds_read_b64_tr_b16 v[238:239], v177 offset:0x9600
	ds_read_b64_tr_b16 v[240:241], v177 offset:0xa600
	ds_read_b64_tr_b16 v[242:243], v177 offset:0xb600
	ds_read_b64_tr_b16 v[244:245], v177 offset:0xc600
	ds_read_b64_tr_b16 v[246:247], v177 offset:0xd600
	ds_read_b64_tr_b16 v[248:249], v177 offset:0xe600
	ds_read_b64_tr_b16 v[250:251], v177 offset:0xf600
	s_waitcnt lgkmcnt(8)
	v_mfma_f32_32x32x16_bf16 v[16:31], v[144:147], v[128:131], v[16:31]
	v_mfma_f32_32x32x16_bf16 v[16:31], v[148:151], v[132:135], v[16:31]
	v_mfma_f32_32x32x16_bf16 v[16:31], v[152:155], v[136:139], v[16:31]
	v_mfma_f32_32x32x16_bf16 v[16:31], v[156:159], v[140:143], v[16:31]
	ds_read_b64_tr_b16 v[144:145], v177 offset:0x8800
	ds_read_b64_tr_b16 v[146:147], v177 offset:0x9800
	ds_read_b64_tr_b16 v[148:149], v177 offset:0xa800
	ds_read_b64_tr_b16 v[150:151], v177 offset:0xb800
	ds_read_b64_tr_b16 v[152:153], v177 offset:0xc800
	ds_read_b64_tr_b16 v[154:155], v177 offset:0xd800
	ds_read_b64_tr_b16 v[156:157], v177 offset:0xe800
	ds_read_b64_tr_b16 v[158:159], v177 offset:0xf800
	s_waitcnt lgkmcnt(8)
	v_mfma_f32_32x32x16_bf16 v[32:47], v[236:239], v[128:131], v[32:47]
	v_mfma_f32_32x32x16_bf16 v[32:47], v[240:243], v[132:135], v[32:47]
	v_mfma_f32_32x32x16_bf16 v[32:47], v[244:247], v[136:139], v[32:47]
	v_mfma_f32_32x32x16_bf16 v[32:47], v[248:251], v[140:143], v[32:47]
	ds_read_b64_tr_b16 v[236:237], v177 offset:0x8a00
	ds_read_b64_tr_b16 v[238:239], v177 offset:0x9a00
	ds_read_b64_tr_b16 v[240:241], v177 offset:0xaa00
	ds_read_b64_tr_b16 v[242:243], v177 offset:0xba00
	ds_read_b64_tr_b16 v[244:245], v177 offset:0xca00
	ds_read_b64_tr_b16 v[246:247], v177 offset:0xda00
	ds_read_b64_tr_b16 v[248:249], v177 offset:0xea00
	ds_read_b64_tr_b16 v[250:251], v177 offset:0xfa00
	s_waitcnt lgkmcnt(8)
	v_mfma_f32_32x32x16_bf16 v[48:63], v[144:147], v[128:131], v[48:63]
	v_mfma_f32_32x32x16_bf16 v[48:63], v[148:151], v[132:135], v[48:63]
	v_mfma_f32_32x32x16_bf16 v[48:63], v[152:155], v[136:139], v[48:63]
	v_mfma_f32_32x32x16_bf16 v[48:63], v[156:159], v[140:143], v[48:63]
	ds_read_b64_tr_b16 v[144:145], v177 offset:0x8c00
	ds_read_b64_tr_b16 v[146:147], v177 offset:0x9c00
	ds_read_b64_tr_b16 v[148:149], v177 offset:0xac00
	ds_read_b64_tr_b16 v[150:151], v177 offset:0xbc00
	ds_read_b64_tr_b16 v[152:153], v177 offset:0xcc00
	ds_read_b64_tr_b16 v[154:155], v177 offset:0xdc00
	ds_read_b64_tr_b16 v[156:157], v177 offset:0xec00
	ds_read_b64_tr_b16 v[158:159], v177 offset:0xfc00
	s_waitcnt lgkmcnt(8)
	v_mfma_f32_32x32x16_bf16 v[64:79], v[236:239], v[128:131], v[64:79]
	v_mfma_f32_32x32x16_bf16 v[64:79], v[240:243], v[132:135], v[64:79]
	v_mfma_f32_32x32x16_bf16 v[64:79], v[244:247], v[136:139], v[64:79]
	v_mfma_f32_32x32x16_bf16 v[64:79], v[248:251], v[140:143], v[64:79]
	ds_read_b64_tr_b16 v[236:237], v177 offset:0x8e00
	ds_read_b64_tr_b16 v[238:239], v177 offset:0x9e00
	ds_read_b64_tr_b16 v[240:241], v177 offset:0xae00
	ds_read_b64_tr_b16 v[242:243], v177 offset:0xbe00
	ds_read_b64_tr_b16 v[244:245], v177 offset:0xce00
	ds_read_b64_tr_b16 v[246:247], v177 offset:0xde00
	ds_read_b64_tr_b16 v[248:249], v177 offset:0xee00
	ds_read_b64_tr_b16 v[250:251], v177 offset:0xfe00
	s_waitcnt lgkmcnt(8)
	v_mfma_f32_32x32x16_bf16 v[80:95], v[144:147], v[128:131], v[80:95]
	v_mfma_f32_32x32x16_bf16 v[80:95], v[148:151], v[132:135], v[80:95]
	v_mfma_f32_32x32x16_bf16 v[80:95], v[152:155], v[136:139], v[80:95]
	v_mfma_f32_32x32x16_bf16 v[80:95], v[156:159], v[140:143], v[80:95]
	s_waitcnt lgkmcnt(0)
	v_mfma_f32_32x32x16_bf16 v[96:111], v[236:239], v[128:131], v[96:111]
	v_mfma_f32_32x32x16_bf16 v[96:111], v[240:243], v[132:135], v[96:111]
	v_mfma_f32_32x32x16_bf16 v[96:111], v[244:247], v[136:139], v[96:111]
	v_mfma_f32_32x32x16_bf16 v[96:111], v[248:251], v[140:143], v[96:111]
	ds_read_b128 v[128:131], v182 offset:0
	ds_read_b128 v[132:135], v182 offset:0x2000
	ds_read_b128 v[136:139], v181 offset:0
	ds_read_b128 v[236:239], v183 offset:0
	ds_read_b128 v[240:243], v183 offset:0x2000
	ds_read_b128 v[244:247], v181 offset:0x400
	s_waitcnt lgkmcnt(3)
	s_nop 0
	v_mfma_f32_32x32x16_bf16 v[144:159], v[128:131], v[136:139], 0
	v_mfma_f32_32x32x16_bf16 v[128:143], v[132:135], v[136:139], 0
	ds_read_b128 v[248:251], v184 offset:0
	ds_read_b128 v[194:197], v184 offset:0x2000
	ds_read_b128 v[222:225], v181 offset:0x800
	s_waitcnt lgkmcnt(3)
	v_mfma_f32_32x32x16_bf16 v[144:159], v[236:239], v[244:247], v[144:159]
	v_mfma_f32_32x32x16_bf16 v[128:143], v[240:243], v[244:247], v[128:143]
	ds_read_b128 v[236:239], v185 offset:0
	ds_read_b128 v[240:243], v185 offset:0x2000
	ds_read_b128 v[244:247], v181 offset:0xc00
	s_waitcnt lgkmcnt(3)
	v_mfma_f32_32x32x16_bf16 v[144:159], v[248:251], v[222:225], v[144:159]
	v_mfma_f32_32x32x16_bf16 v[128:143], v[194:197], v[222:225], v[128:143]
	ds_read_b128 v[194:197], v182 offset:0x80
	ds_read_b128 v[222:225], v182 offset:0x2080
	ds_read_b128 v[248:251], v181 offset:0x1000
	s_waitcnt lgkmcnt(3)
	v_mfma_f32_32x32x16_bf16 v[144:159], v[236:239], v[244:247], v[144:159]
	v_mfma_f32_32x32x16_bf16 v[128:143], v[240:243], v[244:247], v[128:143]
	ds_read_b128 v[236:239], v183 offset:0x80
	ds_read_b128 v[240:243], v183 offset:0x2080
	ds_read_b128 v[244:247], v181 offset:0x1400
	s_waitcnt lgkmcnt(3)
	v_mfma_f32_32x32x16_bf16 v[144:159], v[194:197], v[248:251], v[144:159]
	v_mfma_f32_32x32x16_bf16 v[128:143], v[222:225], v[248:251], v[128:143]
	ds_read_b128 v[194:197], v184 offset:0x80
	ds_read_b128 v[222:225], v184 offset:0x2080
	ds_read_b128 v[248:251], v181 offset:0x1800
	s_waitcnt lgkmcnt(3)
	v_mfma_f32_32x32x16_bf16 v[144:159], v[236:239], v[244:247], v[144:159]
	v_mfma_f32_32x32x16_bf16 v[128:143], v[240:243], v[244:247], v[128:143]
	ds_read_b128 v[236:239], v185 offset:0x80
	ds_read_b128 v[240:243], v185 offset:0x2080
	s_waitcnt lgkmcnt(2)
	v_mfma_f32_32x32x16_bf16 v[144:159], v[194:197], v[248:251], v[144:159]
	v_mfma_f32_32x32x16_bf16 v[128:143], v[222:225], v[248:251], v[128:143]
	s_waitcnt lgkmcnt(0)
	v_mfma_f32_32x32x16_bf16 v[144:159], v[236:239], v[166:169], v[144:159]
	v_mfma_f32_32x32x16_bf16 v[128:143], v[240:243], v[166:169], v[128:143]
	s_bitcmp0_b32 s100, 8
	s_cbranch_scc1 .Lstg_a3
	s_waitcnt vmcnt(0)
	s_waitcnt lgkmcnt(0)
	s_barrier
.Lstg_a3:
	s_cmp_le_i32 s85, s94
	s_cbranch_scc1 .LBB0_528
	v_cmp_gt_i32_e64 s[62:63], 26, v190
	v_cmp_gt_i32_e64 s[64:65], 27, v190
	v_cmp_gt_i32_e64 s[60:61], 25, v190
	s_and_b64 s[62:63], s[64:65], s[62:63]
	v_cmp_gt_i32_e64 s[58:59], 24, v190
	s_and_b64 s[60:61], s[62:63], s[60:61]
	v_cmp_gt_i32_e64 s[56:57], 19, v190
	s_and_b64 s[58:59], s[60:61], s[58:59]
	v_cmp_gt_i32_e64 s[54:55], 18, v190
	s_and_b64 s[56:57], s[58:59], s[56:57]
	v_cmp_gt_i32_e64 s[52:53], 17, v190
	s_and_b64 s[54:55], s[56:57], s[54:55]
	v_cmp_gt_i32_e64 s[50:51], 16, v190
	s_and_b64 s[52:53], s[54:55], s[52:53]
	v_cmp_gt_i32_e64 s[48:49], 11, v190
	s_and_b64 s[50:51], s[52:53], s[50:51]
	v_cmp_gt_i32_e64 s[46:47], 10, v190
	s_and_b64 s[48:49], s[50:51], s[48:49]
	v_cmp_gt_i32_e64 s[44:45], 9, v190
	s_and_b64 s[46:47], s[48:49], s[46:47]
	v_cmp_gt_i32_e64 s[42:43], 8, v190
	s_and_b64 s[44:45], s[46:47], s[44:45]
	v_cmp_gt_i32_e64 s[40:41], 3, v190
	s_and_b64 s[42:43], s[44:45], s[42:43]
	v_cmp_gt_i32_e64 s[38:39], 2, v190
	s_and_b64 s[40:41], s[42:43], s[40:41]
	v_cmp_gt_i32_e64 s[36:37], 1, v190
	s_and_b64 s[38:39], s[40:41], s[38:39]
	v_cmp_gt_i32_e64 s[34:35], 0, v190
	s_and_b64 s[36:37], s[38:39], s[36:37]
	s_and_b64 s[34:35], s[36:37], s[34:35]
	v_cmp_gt_i32_e64 s[30:31], 58, v190
	v_cndmask_b32_e64 v144, v144, 0, s[34:35]
	v_cmp_gt_i32_e64 s[34:35], 59, v190
	v_cmp_gt_i32_e64 s[28:29], 57, v190
	s_and_b64 s[30:31], s[34:35], s[30:31]
	v_cmp_gt_i32_e64 s[26:27], 56, v190
	s_and_b64 s[28:29], s[30:31], s[28:29]
	v_cmp_gt_i32_e64 s[24:25], 51, v190
	s_and_b64 s[26:27], s[28:29], s[26:27]
	v_cmp_gt_i32_e64 s[22:23], 50, v190
	s_and_b64 s[24:25], s[26:27], s[24:25]
	v_cmp_gt_i32_e64 s[20:21], 49, v190
	s_and_b64 s[22:23], s[24:25], s[22:23]
	v_cmp_gt_i32_e64 s[18:19], 48, v190
	s_and_b64 s[20:21], s[22:23], s[20:21]
	v_cmp_gt_i32_e64 s[16:17], 43, v190
	s_and_b64 s[18:19], s[20:21], s[18:19]
	v_cmp_gt_i32_e64 s[14:15], 42, v190
	s_and_b64 s[16:17], s[18:19], s[16:17]
	v_cmp_gt_i32_e64 s[12:13], 41, v190
	s_and_b64 s[14:15], s[16:17], s[14:15]
	v_cmp_gt_i32_e64 s[10:11], 40, v190
	s_and_b64 s[12:13], s[14:15], s[12:13]
	v_cmp_gt_i32_e64 s[8:9], 35, v190
	s_and_b64 s[10:11], s[12:13], s[10:11]
	v_cmp_gt_i32_e64 s[6:7], 34, v190
	s_and_b64 s[8:9], s[10:11], s[8:9]
	v_cmp_gt_i32_e64 s[4:5], 33, v190
	s_and_b64 s[6:7], s[8:9], s[6:7]
	v_cmp_gt_i32_e32 vcc, 32, v190
	s_and_b64 s[4:5], s[6:7], s[4:5]
	v_cndmask_b32_e64 v129, v129, 0, s[4:5]
	s_and_b64 s[4:5], s[4:5], vcc
	v_cndmask_b32_e64 v159, v159, 0, s[64:65]
	v_cndmask_b32_e64 v158, v158, 0, s[62:63]
	s_mov_b64 s[62:63], 0x100
	v_cndmask_b32_e64 v157, v157, 0, s[60:61]
	v_cndmask_b32_e64 v156, v156, 0, s[58:59]
	v_cndmask_b32_e64 v155, v155, 0, s[56:57]
	v_cndmask_b32_e64 v154, v154, 0, s[54:55]
	v_cndmask_b32_e64 v153, v153, 0, s[52:53]
	v_cndmask_b32_e64 v152, v152, 0, s[50:51]
	v_cndmask_b32_e64 v151, v151, 0, s[48:49]
	v_cndmask_b32_e64 v150, v150, 0, s[46:47]
	v_cndmask_b32_e64 v149, v149, 0, s[44:45]
	v_cndmask_b32_e64 v148, v148, 0, s[42:43]
	v_cndmask_b32_e64 v147, v147, 0, s[40:41]
	v_cndmask_b32_e64 v146, v146, 0, s[38:39]
	v_cndmask_b32_e64 v145, v145, 0, s[36:37]
	v_cndmask_b32_e64 v143, v143, 0, s[34:35]
	v_cndmask_b32_e64 v142, v142, 0, s[30:31]
	v_cndmask_b32_e64 v141, v141, 0, s[28:29]
	v_cndmask_b32_e64 v140, v140, 0, s[26:27]
	v_cndmask_b32_e64 v139, v139, 0, s[24:25]
	v_cndmask_b32_e64 v138, v138, 0, s[22:23]
	v_cndmask_b32_e64 v137, v137, 0, s[20:21]
	v_cndmask_b32_e64 v136, v136, 0, s[18:19]
	v_cndmask_b32_e64 v135, v135, 0, s[16:17]
	v_cndmask_b32_e64 v134, v134, 0, s[14:15]
	v_cndmask_b32_e64 v133, v133, 0, s[12:13]
	v_cndmask_b32_e64 v132, v132, 0, s[10:11]
	v_cndmask_b32_e64 v131, v131, 0, s[8:9]
	v_cndmask_b32_e64 v130, v130, 0, s[6:7]
	v_cndmask_b32_e64 v128, v128, 0, s[4:5]
.LBB0_528:
	v_mov_b32_e32 v194, s80
	ds_read_b32 v194, v194 offset:4
	s_waitcnt lgkmcnt(0)
	v_sub_f32_e32 v194, v194, v178
	v_mul_f32_e32 v194, 0x3fb8aa3b, v194
	v_exp_f32_e32 v194, v194
	s_nop 2
	v_mul_f32_e32 v235, v144, v194
	v_mul_f32_e32 v144, v128, v194
	v_mul_f32_e32 v236, v145, v194
	v_mul_f32_e32 v145, v129, v194
	v_mul_f32_e32 v237, v146, v194
	v_mul_f32_e32 v146, v130, v194
	v_mul_f32_e32 v238, v147, v194
	v_mul_f32_e32 v147, v131, v194
	v_mul_f32_e32 v239, v148, v194
	v_mul_f32_e32 v148, v132, v194
	v_mul_f32_e32 v240, v149, v194
	v_mul_f32_e32 v149, v133, v194
	v_mul_f32_e32 v241, v150, v194
	v_mul_f32_e32 v150, v134, v194
	v_mul_f32_e32 v242, v151, v194
	v_mul_f32_e32 v151, v135, v194
	v_mul_f32_e32 v243, v152, v194
	v_mul_f32_e32 v152, v136, v194
	v_mul_f32_e32 v244, v153, v194
	v_mul_f32_e32 v153, v137, v194
	v_mul_f32_e32 v245, v154, v194
	v_mul_f32_e32 v154, v138, v194
	v_mul_f32_e32 v246, v155, v194
	v_mul_f32_e32 v155, v139, v194
	v_mul_f32_e32 v247, v156, v194
	v_mul_f32_e32 v156, v140, v194
	v_mul_f32_e32 v248, v157, v194
	v_mul_f32_e32 v157, v141, v194
	v_mul_f32_e32 v249, v158, v194
	v_mul_f32_e32 v158, v142, v194
	v_mul_f32_e32 v250, v159, v194
	v_mul_f32_e32 v159, v143, v194
	v_cvt_pk_bf16_f32 v128, v235, v236
	v_cvt_pk_bf16_f32 v129, v237, v238
	v_cvt_pk_bf16_f32 v130, v239, v240
	v_cvt_pk_bf16_f32 v131, v241, v242
	v_cvt_pk_bf16_f32 v132, v243, v244
	v_cvt_pk_bf16_f32 v133, v245, v246
	v_cvt_pk_bf16_f32 v134, v247, v248
	v_cvt_pk_bf16_f32 v135, v249, v250
	v_cvt_pk_bf16_f32 v136, v144, v145
	v_cvt_pk_bf16_f32 v137, v146, v147
	v_cvt_pk_bf16_f32 v138, v148, v149
	v_cvt_pk_bf16_f32 v139, v150, v151
	v_cvt_pk_bf16_f32 v140, v152, v153
	v_cvt_pk_bf16_f32 v141, v154, v155
	v_cvt_pk_bf16_f32 v142, v156, v157
	v_cvt_pk_bf16_f32 v143, v158, v159
	s_nop 0
	v_permlane32_swap_b32_e32 v128, v130
	v_permlane32_swap_b32_e32 v129, v131
	v_permlane32_swap_b32_e32 v132, v134
	v_permlane32_swap_b32_e32 v133, v135
	v_permlane32_swap_b32_e32 v136, v138
	v_permlane32_swap_b32_e32 v137, v139
	v_permlane32_swap_b32_e32 v140, v142
	v_permlane32_swap_b32_e32 v141, v143
	s_bitcmp1_b32 s100, 8
	s_cbranch_scc1 .Lstg_b7
	s_waitcnt vmcnt(0)
	s_waitcnt lgkmcnt(0)
	s_barrier
.Lstg_b7:
	s_cmp_gt_u32 s88, s89
	s_cbranch_scc1 .LBB0_533
	s_cmp_ge_u32 s88, s89
	s_mov_b64 s[4:5], -1
	s_cbranch_scc0 .LBB0_531
	v_mov_b64_e32 v[194:195], s[0:1]
	flat_load_dword v196, v[194:195] sc0 sc1
	s_waitcnt vmcnt(0)
	v_mov_b64_e32 v[194:195], s[74:75]
	flat_load_dword v194, v[194:195] sc0 sc1
	s_waitcnt vmcnt(0) lgkmcnt(0)
	v_readfirstlane_b32 s4, v196
	v_readfirstlane_b32 s5, v194
	s_nop 1
	v_lshl_add_u64 v[194:195], s[4:5], 0, v[170:171]
	s_mov_b32 s6, m0
	s_mov_b32 m0, s2
	s_nop 0
	global_load_lds_dwordx4 v[194:195], off
	s_mov_b32 m0, s6
	v_lshl_add_u64 v[194:195], s[4:5], 0, v[172:173]
	s_mov_b32 s4, m0
	s_mov_b32 m0, s91
	s_nop 0
	global_load_lds_dwordx4 v[194:195], off
	s_mov_b32 m0, s4
	s_mov_b64 s[4:5], 0

.LBB0_539:
	ds_read_b64_tr_b16 v[144:145], v177 offset:0
	ds_read_b64_tr_b16 v[146:147], v177 offset:0x1000
	ds_read_b64_tr_b16 v[148:149], v177 offset:0x2000
	ds_read_b64_tr_b16 v[150:151], v177 offset:0x3000
	ds_read_b64_tr_b16 v[152:153], v177 offset:0x4000
	ds_read_b64_tr_b16 v[154:155], v177 offset:0x5000
	ds_read_b64_tr_b16 v[156:157], v177 offset:0x6000
	ds_read_b64_tr_b16 v[158:159], v177 offset:0x7000
	ds_read_b64_tr_b16 v[170:171], v177 offset:0x200
	ds_read_b64_tr_b16 v[172:173], v177 offset:0x1200
	ds_read_b64_tr_b16 v[182:183], v177 offset:0x2200
	ds_read_b64_tr_b16 v[184:185], v177 offset:0x3200
	ds_read_b64_tr_b16 v[190:191], v177 offset:0x4200
	ds_read_b64_tr_b16 v[192:193], v177 offset:0x5200
	ds_read_b64_tr_b16 v[198:199], v177 offset:0x6200
	ds_read_b64_tr_b16 v[200:201], v177 offset:0x7200
	s_waitcnt lgkmcnt(8)
	s_nop 0
	v_mfma_f32_32x32x16_bf16 v[112:127], v[144:147], v[128:131], v[112:127]
	v_mfma_f32_32x32x16_bf16 v[112:127], v[148:151], v[132:135], v[112:127]
	v_mfma_f32_32x32x16_bf16 v[112:127], v[152:155], v[136:139], v[112:127]
	v_mfma_f32_32x32x16_bf16 v[112:127], v[156:159], v[140:143], v[112:127]
	ds_read_b64_tr_b16 v[144:145], v177 offset:0x400
	ds_read_b64_tr_b16 v[146:147], v177 offset:0x1400
	ds_read_b64_tr_b16 v[148:149], v177 offset:0x2400
	ds_read_b64_tr_b16 v[150:151], v177 offset:0x3400
	ds_read_b64_tr_b16 v[152:153], v177 offset:0x4400
	ds_read_b64_tr_b16 v[154:155], v177 offset:0x5400
	ds_read_b64_tr_b16 v[156:157], v177 offset:0x6400
	ds_read_b64_tr_b16 v[158:159], v177 offset:0x7400
	s_waitcnt lgkmcnt(8)
	v_mfma_f32_32x32x16_bf16 v[0:15], v[170:173], v[128:131], v[0:15]
	v_mfma_f32_32x32x16_bf16 v[0:15], v[182:185], v[132:135], v[0:15]
	v_mfma_f32_32x32x16_bf16 v[0:15], v[190:193], v[136:139], v[0:15]
	v_mfma_f32_32x32x16_bf16 v[0:15], v[198:201], v[140:143], v[0:15]
	ds_read_b64_tr_b16 v[170:171], v177 offset:0x600
	ds_read_b64_tr_b16 v[172:173], v177 offset:0x1600
	ds_read_b64_tr_b16 v[182:183], v177 offset:0x2600
	ds_read_b64_tr_b16 v[184:185], v177 offset:0x3600
	ds_read_b64_tr_b16 v[190:191], v177 offset:0x4600
	ds_read_b64_tr_b16 v[192:193], v177 offset:0x5600
	ds_read_b64_tr_b16 v[198:199], v177 offset:0x6600
	ds_read_b64_tr_b16 v[200:201], v177 offset:0x7600
	s_waitcnt lgkmcnt(8)
	v_mfma_f32_32x32x16_bf16 v[16:31], v[144:147], v[128:131], v[16:31]
	v_mfma_f32_32x32x16_bf16 v[16:31], v[148:151], v[132:135], v[16:31]
	v_mfma_f32_32x32x16_bf16 v[16:31], v[152:155], v[136:139], v[16:31]
	v_mfma_f32_32x32x16_bf16 v[16:31], v[156:159], v[140:143], v[16:31]
	ds_read_b64_tr_b16 v[144:145], v177 offset:0x800
	ds_read_b64_tr_b16 v[146:147], v177 offset:0x1800
	ds_read_b64_tr_b16 v[148:149], v177 offset:0x2800
	ds_read_b64_tr_b16 v[150:151], v177 offset:0x3800
	ds_read_b64_tr_b16 v[152:153], v177 offset:0x4800
	ds_read_b64_tr_b16 v[154:155], v177 offset:0x5800
	ds_read_b64_tr_b16 v[156:157], v177 offset:0x6800
	ds_read_b64_tr_b16 v[158:159], v177 offset:0x7800
	s_waitcnt lgkmcnt(8)
	v_mfma_f32_32x32x16_bf16 v[32:47], v[170:173], v[128:131], v[32:47]
	v_mfma_f32_32x32x16_bf16 v[32:47], v[182:185], v[132:135], v[32:47]
	v_mfma_f32_32x32x16_bf16 v[32:47], v[190:193], v[136:139], v[32:47]
	v_mfma_f32_32x32x16_bf16 v[32:47], v[198:201], v[140:143], v[32:47]
	ds_read_b64_tr_b16 v[170:171], v177 offset:0xa00
	ds_read_b64_tr_b16 v[172:173], v177 offset:0x1a00
	ds_read_b64_tr_b16 v[182:183], v177 offset:0x2a00
	ds_read_b64_tr_b16 v[184:185], v177 offset:0x3a00
	ds_read_b64_tr_b16 v[190:191], v177 offset:0x4a00
	ds_read_b64_tr_b16 v[192:193], v177 offset:0x5a00
	ds_read_b64_tr_b16 v[198:199], v177 offset:0x6a00
	ds_read_b64_tr_b16 v[200:201], v177 offset:0x7a00
	s_waitcnt lgkmcnt(8)
	v_mfma_f32_32x32x16_bf16 v[48:63], v[144:147], v[128:131], v[48:63]
	v_mfma_f32_32x32x16_bf16 v[48:63], v[148:151], v[132:135], v[48:63]
	v_mfma_f32_32x32x16_bf16 v[48:63], v[152:155], v[136:139], v[48:63]
	v_mfma_f32_32x32x16_bf16 v[48:63], v[156:159], v[140:143], v[48:63]
	ds_read_b64_tr_b16 v[144:145], v177 offset:0xc00
	ds_read_b64_tr_b16 v[146:147], v177 offset:0x1c00
	ds_read_b64_tr_b16 v[148:149], v177 offset:0x2c00
	ds_read_b64_tr_b16 v[150:151], v177 offset:0x3c00
	ds_read_b64_tr_b16 v[152:153], v177 offset:0x4c00
	ds_read_b64_tr_b16 v[154:155], v177 offset:0x5c00
	ds_read_b64_tr_b16 v[156:157], v177 offset:0x6c00
	ds_read_b64_tr_b16 v[158:159], v177 offset:0x7c00
	s_waitcnt lgkmcnt(8)
	v_mfma_f32_32x32x16_bf16 v[64:79], v[170:173], v[128:131], v[64:79]
	v_mfma_f32_32x32x16_bf16 v[64:79], v[182:185], v[132:135], v[64:79]
	v_mfma_f32_32x32x16_bf16 v[64:79], v[190:193], v[136:139], v[64:79]
	v_mfma_f32_32x32x16_bf16 v[64:79], v[198:201], v[140:143], v[64:79]
	ds_read_b64_tr_b16 v[170:171], v177 offset:0xe00
	ds_read_b64_tr_b16 v[172:173], v177 offset:0x1e00
	ds_read_b64_tr_b16 v[182:183], v177 offset:0x2e00
	ds_read_b64_tr_b16 v[184:185], v177 offset:0x3e00
	ds_read_b64_tr_b16 v[190:191], v177 offset:0x4e00
	ds_read_b64_tr_b16 v[192:193], v177 offset:0x5e00
	ds_read_b64_tr_b16 v[198:199], v177 offset:0x6e00
	ds_read_b64_tr_b16 v[200:201], v177 offset:0x7e00
	s_waitcnt lgkmcnt(8)
	v_mfma_f32_32x32x16_bf16 v[80:95], v[144:147], v[128:131], v[80:95]
	v_mfma_f32_32x32x16_bf16 v[80:95], v[148:151], v[132:135], v[80:95]
	v_mfma_f32_32x32x16_bf16 v[80:95], v[152:155], v[136:139], v[80:95]
	v_mfma_f32_32x32x16_bf16 v[80:95], v[156:159], v[140:143], v[80:95]
	s_waitcnt lgkmcnt(0)
	v_mfma_f32_32x32x16_bf16 v[96:111], v[170:173], v[128:131], v[96:111]
	v_mfma_f32_32x32x16_bf16 v[96:111], v[182:185], v[132:135], v[96:111]
	v_mfma_f32_32x32x16_bf16 v[96:111], v[190:193], v[136:139], v[96:111]
	v_mfma_f32_32x32x16_bf16 v[96:111], v[198:201], v[140:143], v[96:111]
	ds_read_b128 v[128:131], v189 offset:0
	ds_read_b128 v[132:135], v189 offset:0x2000
	ds_read_b128 v[136:139], v181 offset:0
	ds_read_b128 v[170:173], v188 offset:0
	ds_read_b128 v[182:185], v188 offset:0x2000
	ds_read_b128 v[190:193], v181 offset:0x400
	s_waitcnt lgkmcnt(3)
	s_nop 0
	v_mfma_f32_32x32x16_bf16 v[144:159], v[128:131], v[136:139], 0
	v_mfma_f32_32x32x16_bf16 v[128:143], v[132:135], v[136:139], 0
	ds_read_b128 v[198:201], v187 offset:0
	ds_read_b128 v[202:205], v187 offset:0x2000
	ds_read_b128 v[206:209], v181 offset:0x800
	s_waitcnt lgkmcnt(3)
	v_mfma_f32_32x32x16_bf16 v[144:159], v[170:173], v[190:193], v[144:159]
	v_mfma_f32_32x32x16_bf16 v[128:143], v[182:185], v[190:193], v[128:143]
	ds_read_b128 v[170:173], v186 offset:0
	ds_read_b128 v[182:185], v186 offset:0x2000
	ds_read_b128 v[190:193], v181 offset:0xc00
	s_waitcnt lgkmcnt(3)
	v_mfma_f32_32x32x16_bf16 v[144:159], v[198:201], v[206:209], v[144:159]
	v_mfma_f32_32x32x16_bf16 v[128:143], v[202:205], v[206:209], v[128:143]
	ds_read_b128 v[198:201], v189 offset:0x80
	ds_read_b128 v[202:205], v189 offset:0x2080
	ds_read_b128 v[206:209], v181 offset:0x1000
	s_waitcnt lgkmcnt(3)
	v_mfma_f32_32x32x16_bf16 v[144:159], v[170:173], v[190:193], v[144:159]
	v_mfma_f32_32x32x16_bf16 v[128:143], v[182:185], v[190:193], v[128:143]
	ds_read_b128 v[170:173], v188 offset:0x80
	ds_read_b128 v[182:185], v188 offset:0x2080
	ds_read_b128 v[188:191], v181 offset:0x1400
	s_waitcnt lgkmcnt(3)
	v_mfma_f32_32x32x16_bf16 v[144:159], v[198:201], v[206:209], v[144:159]
	v_mfma_f32_32x32x16_bf16 v[128:143], v[202:205], v[206:209], v[128:143]
	ds_read_b128 v[198:201], v187 offset:0x80
	ds_read_b128 v[202:205], v187 offset:0x2080
	ds_read_b128 v[206:209], v181 offset:0x1800
	s_waitcnt lgkmcnt(3)
	v_mfma_f32_32x32x16_bf16 v[144:159], v[170:173], v[188:191], v[144:159]
	v_mfma_f32_32x32x16_bf16 v[128:143], v[182:185], v[188:191], v[128:143]
	ds_read_b128 v[170:173], v186 offset:0x80
	ds_read_b128 v[182:185], v186 offset:0x2080
	s_waitcnt lgkmcnt(2)
	v_mfma_f32_32x32x16_bf16 v[144:159], v[198:201], v[206:209], v[144:159]
	v_mfma_f32_32x32x16_bf16 v[128:143], v[202:205], v[206:209], v[128:143]
	s_waitcnt lgkmcnt(0)
	v_mfma_f32_32x32x16_bf16 v[144:159], v[170:173], v[166:169], v[144:159]
	v_mfma_f32_32x32x16_bf16 v[128:143], v[182:185], v[166:169], v[128:143]
	s_bitcmp0_b32 s100, 8
	s_cbranch_scc1 .Lstg_a4
	s_waitcnt vmcnt(0)
	s_waitcnt lgkmcnt(0)
	s_barrier
.Lstg_a4:
	v_readlane_b32 s2, v255, 57
	s_or_b32 s33, s2, 3
	s_lshl_b32 s2, s33, 6
	s_or_b32 s3, s2, 63
	s_cmp_gt_i32 s3, s94
	s_cbranch_scc0 .LBB0_514
	v_subrev_u32_e32 v166, s2, v180
	v_cmp_gt_i32_e64 s[62:63], 26, v166
	v_cmp_gt_i32_e64 s[64:65], 27, v166
	v_cmp_gt_i32_e64 s[60:61], 25, v166
	s_and_b64 s[2:3], s[64:65], s[62:63]
	v_cmp_gt_i32_e64 s[58:59], 24, v166
	v_cndmask_b32_e64 v158, v158, 0, s[2:3]
	s_and_b64 s[2:3], s[2:3], s[60:61]
	v_cmp_gt_i32_e64 s[56:57], 19, v166
	v_cndmask_b32_e64 v157, v157, 0, s[2:3]
	s_and_b64 s[2:3], s[2:3], s[58:59]
	v_cmp_gt_i32_e64 s[54:55], 18, v166
	v_cndmask_b32_e64 v156, v156, 0, s[2:3]
	s_and_b64 s[2:3], s[2:3], s[56:57]
	v_cmp_gt_i32_e64 s[52:53], 17, v166
	v_cndmask_b32_e64 v155, v155, 0, s[2:3]
	s_and_b64 s[2:3], s[2:3], s[54:55]
	v_cmp_gt_i32_e64 s[50:51], 16, v166
	v_cndmask_b32_e64 v154, v154, 0, s[2:3]
	s_and_b64 s[2:3], s[2:3], s[52:53]
	v_cmp_gt_i32_e64 s[48:49], 11, v166
	v_cndmask_b32_e64 v153, v153, 0, s[2:3]
	s_and_b64 s[2:3], s[2:3], s[50:51]
	v_cmp_gt_i32_e64 s[46:47], 10, v166
	v_cndmask_b32_e64 v152, v152, 0, s[2:3]
	s_and_b64 s[2:3], s[2:3], s[48:49]
	v_cmp_gt_i32_e64 s[44:45], 9, v166
	v_cndmask_b32_e64 v151, v151, 0, s[2:3]
	s_and_b64 s[2:3], s[2:3], s[46:47]
	v_cmp_gt_i32_e64 s[42:43], 8, v166
	v_cndmask_b32_e64 v150, v150, 0, s[2:3]
	s_and_b64 s[2:3], s[2:3], s[44:45]
	v_cmp_gt_i32_e64 s[40:41], 3, v166
	v_cndmask_b32_e64 v149, v149, 0, s[2:3]
	s_and_b64 s[2:3], s[2:3], s[42:43]
	v_cmp_gt_i32_e64 s[38:39], 2, v166
	v_cndmask_b32_e64 v148, v148, 0, s[2:3]
	s_and_b64 s[2:3], s[2:3], s[40:41]
	v_cmp_gt_i32_e64 s[36:37], 1, v166
	v_cndmask_b32_e64 v147, v147, 0, s[2:3]
	s_and_b64 s[2:3], s[2:3], s[38:39]
	v_cmp_gt_i32_e64 s[34:35], 0, v166
	v_cndmask_b32_e64 v146, v146, 0, s[2:3]
	s_and_b64 s[2:3], s[2:3], s[36:37]
	v_cmp_gt_i32_e64 s[30:31], 58, v166
	v_cndmask_b32_e64 v145, v145, 0, s[2:3]
	s_and_b64 s[2:3], s[2:3], s[34:35]
	v_cmp_gt_i32_e64 s[34:35], 59, v166
	v_cmp_gt_i32_e64 s[28:29], 57, v166
	v_cndmask_b32_e64 v144, v144, 0, s[2:3]
	s_and_b64 s[2:3], s[34:35], s[30:31]
	v_cmp_gt_i32_e64 s[26:27], 56, v166
	v_cndmask_b32_e64 v142, v142, 0, s[2:3]
	s_and_b64 s[2:3], s[2:3], s[28:29]
	v_cmp_gt_i32_e64 s[24:25], 51, v166
	v_cndmask_b32_e64 v141, v141, 0, s[2:3]
	s_and_b64 s[2:3], s[2:3], s[26:27]
	v_cmp_gt_i32_e64 s[22:23], 50, v166
	v_cndmask_b32_e64 v140, v140, 0, s[2:3]
	s_and_b64 s[2:3], s[2:3], s[24:25]
	v_cmp_gt_i32_e64 s[20:21], 49, v166
	v_cndmask_b32_e64 v139, v139, 0, s[2:3]
	s_and_b64 s[2:3], s[2:3], s[22:23]
	v_cmp_gt_i32_e64 s[18:19], 48, v166
	v_cndmask_b32_e64 v138, v138, 0, s[2:3]
	s_and_b64 s[2:3], s[2:3], s[20:21]
	v_cmp_gt_i32_e64 s[16:17], 43, v166
	v_cndmask_b32_e64 v137, v137, 0, s[2:3]
	s_and_b64 s[2:3], s[2:3], s[18:19]
	v_cmp_gt_i32_e64 s[14:15], 42, v166
	v_cndmask_b32_e64 v136, v136, 0, s[2:3]
	s_and_b64 s[2:3], s[2:3], s[16:17]
	v_cmp_gt_i32_e64 s[12:13], 41, v166
	v_cndmask_b32_e64 v135, v135, 0, s[2:3]
	s_and_b64 s[2:3], s[2:3], s[14:15]
	v_cmp_gt_i32_e64 s[10:11], 40, v166
	v_cndmask_b32_e64 v134, v134, 0, s[2:3]
	s_and_b64 s[2:3], s[2:3], s[12:13]
	v_cmp_gt_i32_e64 s[8:9], 35, v166
	v_cndmask_b32_e64 v133, v133, 0, s[2:3]
	s_and_b64 s[2:3], s[2:3], s[10:11]
	v_cmp_gt_i32_e64 s[6:7], 34, v166
	v_cndmask_b32_e64 v132, v132, 0, s[2:3]
	s_and_b64 s[2:3], s[2:3], s[8:9]
	v_cmp_gt_i32_e64 s[4:5], 33, v166
	v_cndmask_b32_e64 v131, v131, 0, s[2:3]
	s_and_b64 s[2:3], s[2:3], s[6:7]
	v_cmp_gt_i32_e32 vcc, 32, v166
	v_cndmask_b32_e64 v130, v130, 0, s[2:3]
	s_and_b64 s[2:3], s[2:3], s[4:5]
	v_cndmask_b32_e64 v129, v129, 0, s[2:3]
	s_and_b64 s[2:3], s[2:3], vcc
	v_cndmask_b32_e64 v159, v159, 0, s[64:65]
	s_mov_b64 s[62:63], 0x100
	v_cndmask_b32_e64 v143, v143, 0, s[34:35]
	v_cndmask_b32_e64 v128, v128, 0, s[2:3]
	s_branch .LBB0_514

.LBB0_554:
	s_or_b64 exec, exec, s[4:5]
	s_ashr_i32 s95, s94, 31
	s_add_u32 s4, s2, s16
	s_addc_u32 s3, s3, 0
	v_mov_b32_e32 v38, v165
	s_add_u32 s2, s4, 0x2800
	s_addc_u32 s33, s3, 0
	v_readfirstlane_b32 s5, v38
	s_ashr_i32 s79, s5, 6
	v_bfe_u32 v0, v38, 5, 1
	v_and_b32_e32 v175, 31, v38
	s_lshl_b32 s92, s79, 5
	v_lshlrev_b32_e32 v32, 2, v0
	s_add_i32 s82, s92, s78
	v_sub_u32_e32 v1, v175, v32
	v_lshlrev_b32_e32 v176, 4, v0
	s_lshl_b32 s76, s79, 3
	v_bfe_u32 v0, v38, 4, 2
	v_writelane_b32 v255, s16, 17
	v_add_u32_e32 v179, s82, v1
	v_or_b32_e32 v1, s76, v0
	v_and_b32_e32 v2, 15, v38
	s_lshl_b32 s5, s79, 12
	v_and_b32_e32 v39, 63, v38
	v_bitop3_b32 v3, v0, v38, 15 bitop3:0x78
	v_mul_lo_u32 v1, v1, s84
	v_bitop3_b32 v0, v0, v2, 4 bitop3:0x36
	s_add_i32 s93, s5, s77
	s_mul_i32 s5, s79, 0x1c00
	v_readlane_b32 s7, v255, 51
	s_waitcnt vmcnt(0)
	v_lshlrev_b32_e32 v40, 4, v39
	v_lshl_or_b32 v0, v0, 4, v1
	s_lshl_b32 s83, s79, 11
	v_readlane_b32 s6, v255, 53
	s_add_i32 s5, s7, s5
	v_lshl_or_b32 v160, v3, 4, v1
	v_add_u32_e32 v170, 0x1a000, v0
	s_add_i32 s83, s83, s6
	v_add_u32_e32 v180, s5, v40
	s_waitcnt vmcnt(0) lgkmcnt(0)
	ds_write_b128 v180, v[128:131]
	ds_write_b128 v180, v[132:135] offset:1024
	ds_write_b128 v180, v[136:139] offset:2048
	ds_write_b128 v180, v[140:143] offset:3072
	ds_write_b128 v180, v[144:147] offset:4096
	ds_write_b128 v180, v[148:151] offset:5120
	ds_write_b128 v180, v[152:155] offset:6144
	s_add_u32 s4, s4, 0x1a2800
	s_addc_u32 s5, s3, 0
	v_lshl_add_u64 v[0:1], s[4:5], 0, v[160:161]
	s_add_i32 s84, s83, 0x4000
	s_mov_b32 s3, m0
	s_mov_b32 m0, s84
	s_nop 0
	global_load_lds_dwordx4 v[0:1], off
	s_mov_b32 m0, s3
	v_mov_b32_e32 v171, v161
	v_lshl_add_u64 v[0:1], s[4:5], 0, v[170:171]
	s_add_i32 s85, s83, 0x4400
	s_mov_b32 s3, m0
	s_mov_b32 m0, s85
	s_nop 0
	global_load_lds_dwordx4 v[0:1], off
	s_mov_b32 m0, s3
	s_waitcnt lgkmcnt(0)
	s_barrier
	v_lshlrev_b32_e32 v0, 4, v38
	s_movk_i32 s3, 0x70
	v_lshlrev_b32_e32 v33, 8, v175
	v_and_b32_e32 v1, 0x70, v0
	v_bitop3_b32 v34, v176, v0, s3 bitop3:0x78
	s_movk_i32 s3, 0x60
	v_add_u32_e32 v2, s6, v33
	v_bitop3_b32 v35, v176, v1, 32 bitop3:0x36
	v_bitop3_b32 v36, v176, v1, 64 bitop3:0x36
	v_bitop3_b32 v37, v176, v1, s3 bitop3:0x36
	v_add_u32_e32 v181, v34, v2
	v_add_u32_e32 v182, v35, v2
	v_add_u32_e32 v183, v36, v2
	v_add_u32_e32 v184, v37, v2
	ds_read_b128 v[0:3], v181 offset:0
	ds_read_b128 v[4:7], v181 offset:0x2000
	ds_read_b128 v[8:11], v180 offset:0
	ds_read_b128 v[42:45], v182 offset:0
	ds_read_b128 v[46:49], v182 offset:0x2000
	ds_read_b128 v[50:53], v180 offset:0x400
	s_waitcnt lgkmcnt(3)
	s_nop 0
	v_mfma_f32_32x32x16_bf16 v[16:31], v[0:3], v[8:11], 0
	v_mfma_f32_32x32x16_bf16 v[0:15], v[4:7], v[8:11], 0
	ds_read_b128 v[54:57], v183 offset:0
	ds_read_b128 v[58:61], v183 offset:0x2000
	ds_read_b128 v[62:65], v180 offset:0x800
	s_waitcnt lgkmcnt(3)
	v_mfma_f32_32x32x16_bf16 v[16:31], v[42:45], v[50:53], v[16:31]
	v_mfma_f32_32x32x16_bf16 v[0:15], v[46:49], v[50:53], v[0:15]
	ds_read_b128 v[42:45], v184 offset:0
	ds_read_b128 v[46:49], v184 offset:0x2000
	ds_read_b128 v[50:53], v180 offset:0xc00
	s_waitcnt lgkmcnt(3)
	v_mfma_f32_32x32x16_bf16 v[16:31], v[54:57], v[62:65], v[16:31]
	v_mfma_f32_32x32x16_bf16 v[0:15], v[58:61], v[62:65], v[0:15]
	ds_read_b128 v[54:57], v181 offset:0x80
	ds_read_b128 v[58:61], v181 offset:0x2080
	ds_read_b128 v[62:65], v180 offset:0x1000
	s_waitcnt lgkmcnt(3)
	v_mfma_f32_32x32x16_bf16 v[16:31], v[42:45], v[50:53], v[16:31]
	v_mfma_f32_32x32x16_bf16 v[0:15], v[46:49], v[50:53], v[0:15]
	ds_read_b128 v[42:45], v182 offset:0x80
	ds_read_b128 v[46:49], v182 offset:0x2080
	ds_read_b128 v[50:53], v180 offset:0x1400
	s_waitcnt lgkmcnt(3)
	v_mfma_f32_32x32x16_bf16 v[16:31], v[54:57], v[62:65], v[16:31]
	v_mfma_f32_32x32x16_bf16 v[0:15], v[58:61], v[62:65], v[0:15]
	ds_read_b128 v[54:57], v183 offset:0x80
	ds_read_b128 v[58:61], v183 offset:0x2080
	ds_read_b128 v[62:65], v180 offset:0x1800
	s_waitcnt lgkmcnt(3)
	v_mfma_f32_32x32x16_bf16 v[16:31], v[42:45], v[50:53], v[16:31]
	v_mfma_f32_32x32x16_bf16 v[0:15], v[46:49], v[50:53], v[0:15]
	ds_read_b128 v[42:45], v184 offset:0x80
	ds_read_b128 v[46:49], v184 offset:0x2080
	s_waitcnt lgkmcnt(2)
	v_mfma_f32_32x32x16_bf16 v[16:31], v[54:57], v[62:65], v[16:31]
	v_mfma_f32_32x32x16_bf16 v[0:15], v[58:61], v[62:65], v[0:15]
	s_waitcnt lgkmcnt(0)
	v_mfma_f32_32x32x16_bf16 v[16:31], v[42:45], v[166:169], v[16:31]
	v_mfma_f32_32x32x16_bf16 v[0:15], v[46:49], v[166:169], v[0:15]
	s_bitcmp0_b32 s100, 8
	s_cbranch_scc1 .Lstg_a9
	s_waitcnt vmcnt(0)
	s_waitcnt lgkmcnt(0)
	s_barrier
.Lstg_a9:
	v_writelane_b32 v255, s12, 57
	v_writelane_b32 v255, s13, 16
	v_writelane_b32 v255, s14, 26
	s_cmp_gt_i32 s82, 62
	v_writelane_b32 v255, s15, 31
	s_cbranch_scc1 .LBB0_556
	v_cmp_gt_i32_e64 s[62:63], 26, v179
	v_cmp_gt_i32_e64 s[64:65], 27, v179
	v_cmp_gt_i32_e64 s[60:61], 25, v179
	s_and_b64 s[62:63], s[64:65], s[62:63]
	v_cmp_gt_i32_e64 s[58:59], 24, v179
	s_and_b64 s[60:61], s[62:63], s[60:61]
	v_cmp_gt_i32_e64 s[56:57], 19, v179
	s_and_b64 s[58:59], s[60:61], s[58:59]
	v_cmp_gt_i32_e64 s[54:55], 18, v179
	s_and_b64 s[56:57], s[58:59], s[56:57]
	v_cmp_gt_i32_e64 s[52:53], 17, v179
	s_and_b64 s[54:55], s[56:57], s[54:55]
	v_cmp_gt_i32_e64 s[50:51], 16, v179
	s_and_b64 s[52:53], s[54:55], s[52:53]
	v_cmp_gt_i32_e64 s[48:49], 11, v179
	s_and_b64 s[50:51], s[52:53], s[50:51]
	v_cmp_gt_i32_e64 s[46:47], 10, v179
	s_and_b64 s[48:49], s[50:51], s[48:49]
	v_cmp_gt_i32_e64 s[44:45], 9, v179
	s_and_b64 s[46:47], s[48:49], s[46:47]
	v_cmp_gt_i32_e64 s[42:43], 8, v179
	s_and_b64 s[44:45], s[46:47], s[44:45]
	v_cmp_gt_i32_e64 s[40:41], 3, v179
	s_and_b64 s[42:43], s[44:45], s[42:43]
	v_cmp_gt_i32_e64 s[38:39], 2, v179
	s_and_b64 s[40:41], s[42:43], s[40:41]
	v_cmp_gt_i32_e64 s[36:37], 1, v179
	s_and_b64 s[38:39], s[40:41], s[38:39]
	v_cmp_gt_i32_e64 s[34:35], 0, v179
	s_and_b64 s[36:37], s[38:39], s[36:37]
	s_and_b64 s[34:35], s[36:37], s[34:35]
	v_cmp_gt_i32_e64 s[30:31], 58, v179
	v_cndmask_b32_e64 v16, v16, v226, s[34:35]
	v_cmp_gt_i32_e64 s[34:35], 59, v179
	v_cmp_gt_i32_e64 s[28:29], 57, v179
	s_and_b64 s[30:31], s[34:35], s[30:31]
	v_cmp_gt_i32_e64 s[26:27], 56, v179
	s_and_b64 s[28:29], s[30:31], s[28:29]
	v_cmp_gt_i32_e64 s[24:25], 51, v179
	s_and_b64 s[26:27], s[28:29], s[26:27]
	v_cmp_gt_i32_e64 s[22:23], 50, v179
	s_and_b64 s[24:25], s[26:27], s[24:25]
	v_cmp_gt_i32_e64 s[20:21], 49, v179
	s_and_b64 s[22:23], s[24:25], s[22:23]
	v_cmp_gt_i32_e64 s[18:19], 48, v179
	s_and_b64 s[20:21], s[22:23], s[20:21]
	v_cmp_gt_i32_e64 s[16:17], 43, v179
	s_and_b64 s[18:19], s[20:21], s[18:19]
	v_cmp_gt_i32_e64 s[14:15], 42, v179
	s_and_b64 s[16:17], s[18:19], s[16:17]
	v_cmp_gt_i32_e64 s[12:13], 41, v179
	s_and_b64 s[14:15], s[16:17], s[14:15]
	v_cmp_gt_i32_e64 s[10:11], 40, v179
	s_and_b64 s[12:13], s[14:15], s[12:13]
	v_cmp_gt_i32_e64 s[8:9], 35, v179
	s_and_b64 s[10:11], s[12:13], s[10:11]
	v_cmp_gt_i32_e64 s[6:7], 34, v179
	s_and_b64 s[8:9], s[10:11], s[8:9]
	v_cmp_gt_i32_e64 s[4:5], 33, v179
	s_and_b64 s[6:7], s[8:9], s[6:7]
	v_cmp_gt_i32_e32 vcc, 32, v179
	s_and_b64 s[4:5], s[6:7], s[4:5]
	s_and_b64 vcc, s[4:5], vcc
	v_cndmask_b32_e64 v31, v31, v226, s[64:65]
	v_cndmask_b32_e64 v30, v30, v226, s[62:63]
	s_mov_b64 s[62:63], 0x100
	v_cndmask_b32_e64 v29, v29, v226, s[60:61]
	v_cndmask_b32_e64 v28, v28, v226, s[58:59]
	v_cndmask_b32_e64 v27, v27, v226, s[56:57]
	v_cndmask_b32_e64 v26, v26, v226, s[54:55]
	v_cndmask_b32_e64 v25, v25, v226, s[52:53]
	v_cndmask_b32_e64 v24, v24, v226, s[50:51]
	v_cndmask_b32_e64 v23, v23, v226, s[48:49]
	v_cndmask_b32_e64 v22, v22, v226, s[46:47]
	v_cndmask_b32_e64 v21, v21, v226, s[44:45]
	v_cndmask_b32_e64 v20, v20, v226, s[42:43]
	v_cndmask_b32_e64 v19, v19, v226, s[40:41]
	v_cndmask_b32_e64 v18, v18, v226, s[38:39]
	v_cndmask_b32_e64 v17, v17, v226, s[36:37]
	v_cndmask_b32_e64 v15, v15, v226, s[34:35]
	v_cndmask_b32_e64 v14, v14, v226, s[30:31]
	v_cndmask_b32_e64 v13, v13, v226, s[28:29]
	v_cndmask_b32_e64 v12, v12, v226, s[26:27]
	v_cndmask_b32_e64 v11, v11, v226, s[24:25]
	v_cndmask_b32_e64 v10, v10, v226, s[22:23]
	v_cndmask_b32_e64 v9, v9, v226, s[20:21]
	v_cndmask_b32_e64 v8, v8, v226, s[18:19]
	v_cndmask_b32_e64 v7, v7, v226, s[16:17]
	v_cndmask_b32_e64 v6, v6, v226, s[14:15]
	v_cndmask_b32_e64 v5, v5, v226, s[12:13]
	v_cndmask_b32_e64 v4, v4, v226, s[10:11]
	v_cndmask_b32_e64 v3, v3, v226, s[8:9]
	v_cndmask_b32_e64 v2, v2, v226, s[6:7]
	v_cndmask_b32_e64 v1, v1, v226, s[4:5]
	v_cndmask_b32_e32 v0, v0, v226, vcc
.LBB0_556:
	v_lshlrev_b32_e32 v41, 3, v39
	v_and_b32_e32 v40, 0xc0, v40
	v_lshlrev_b32_e32 v39, 1, v39
	v_and_or_b32 v40, v41, 24, v40
	v_and_b32_e32 v39, 32, v39
	v_and_b32_e32 v41, 0x100, v41
	v_or3_b32 v39, v40, v39, v41
	v_add_u32_e32 v177, s77, v39
	v_lshrrev_b32_e32 v39, 2, v175
	v_lshrrev_b32_e32 v40, 1, v175
	s_lshr_b32 s4, s76, 1
	v_bitop3_b32 v39, s76, v228, v39 bitop3:0xc8
	v_and_b32_e32 v40, 8, v40
	s_and_b32 s4, s4, 4
	v_or3_b32 v39, v40, v39, s4
	v_and_b32_e32 v40, 32, v38
	v_lshlrev_b32_e32 v38, 3, v38
	v_and_b32_e32 v38, 24, v38
	v_mul_u32_u24_e32 v39, 0x3400, v39
	v_or3_b32 v38, v40, v38, v39
	v_lshlrev_b32_e32 v162, 1, v38
	v_max_f32_e32 v38, v17, v17
	v_max_f32_e32 v39, v16, v16
	v_max_f32_e32 v38, v39, v38
	v_max3_f32 v38, v38, v18, v19
	v_max3_f32 v38, v38, v20, v21
	v_max3_f32 v38, v38, v22, v23
	v_max3_f32 v38, v38, v24, v25
	v_max3_f32 v38, v38, v26, v27
	v_max3_f32 v38, v38, v28, v29
	v_max3_f32 v38, v38, v30, v31
	v_max3_f32 v38, v38, v0, v1
	v_max3_f32 v38, v38, v2, v3
	v_max3_f32 v38, v38, v4, v5
	v_max3_f32 v38, v38, v6, v7
	v_max3_f32 v38, v38, v8, v9
	v_max3_f32 v38, v38, v10, v11
	v_max3_f32 v38, v38, v12, v13
	v_max3_f32 v38, v38, v14, v15
	v_mov_b32_e32 v39, v38
	s_nop 1
	v_permlane32_swap_b32_e32 v38, v39
	s_lshr_b32 s75, s78, 6
	s_and_b32 s4, s68, 0xe00
	v_max_f32_e32 v39, v39, v39
	v_max_f32_e32 v38, v38, v38
	s_add_i32 s75, s75, 4
	s_or_b32 s4, s74, s4
	v_readlane_b32 s5, v255, 27
	v_max_f32_e32 v38, v38, v39
	s_add_u32 s76, s5, s4
	v_readlane_b32 s4, v255, 29
	v_add_f32_e32 v39, 0x7149f2ca, v38
	s_addc_u32 s77, s4, s69
	v_mul_f32_e32 v39, 0x3db504f3, v39
	s_mov_b32 s4, 0x41000000
	v_max_f32_e32 v38, 0xf149f2ca, v38
	v_cmp_ge_f32_e32 vcc, s4, v39
	v_sub_f32_e32 v39, 0xf149f2ca, v38
	v_mul_f32_e32 v39, 0x3e0293ee, v39
	v_exp_f32_e32 v39, v39
	s_cmp_eq_u64 vcc, exec
	s_cselect_b64 vcc, -1, 0
	v_mov_b32_e32 v40, 0xf149f2ca
	v_cndmask_b32_e32 v190, v38, v40, vcc
	v_cndmask_b32_e64 v38, v39, 1.0, vcc
	v_mul_f32_e32 v39, 0xbe0293ee, v190
	v_fmamk_f32 v16, v16, 0x3e0293ee, v39
	v_fmamk_f32 v17, v17, 0x3e0293ee, v39
	v_fmamk_f32 v18, v18, 0x3e0293ee, v39
	v_fmamk_f32 v19, v19, 0x3e0293ee, v39
	v_fmamk_f32 v20, v20, 0x3e0293ee, v39
	v_fmamk_f32 v21, v21, 0x3e0293ee, v39
	v_fmamk_f32 v22, v22, 0x3e0293ee, v39
	v_fmamk_f32 v23, v23, 0x3e0293ee, v39
	v_fmamk_f32 v24, v24, 0x3e0293ee, v39
	v_fmamk_f32 v25, v25, 0x3e0293ee, v39
	v_fmamk_f32 v26, v26, 0x3e0293ee, v39
	v_fmamk_f32 v27, v27, 0x3e0293ee, v39
	v_fmamk_f32 v28, v28, 0x3e0293ee, v39
	v_fmamk_f32 v29, v29, 0x3e0293ee, v39
	v_fmamk_f32 v30, v30, 0x3e0293ee, v39
	v_fmamk_f32 v31, v31, 0x3e0293ee, v39
	v_fmamk_f32 v0, v0, 0x3e0293ee, v39
	v_fmamk_f32 v1, v1, 0x3e0293ee, v39
	v_fmamk_f32 v2, v2, 0x3e0293ee, v39
	v_fmamk_f32 v3, v3, 0x3e0293ee, v39
	v_fmamk_f32 v4, v4, 0x3e0293ee, v39
	v_fmamk_f32 v5, v5, 0x3e0293ee, v39
	v_fmamk_f32 v6, v6, 0x3e0293ee, v39
	v_fmamk_f32 v7, v7, 0x3e0293ee, v39
	v_fmamk_f32 v8, v8, 0x3e0293ee, v39
	v_fmamk_f32 v9, v9, 0x3e0293ee, v39
	v_fmamk_f32 v10, v10, 0x3e0293ee, v39
	v_fmamk_f32 v11, v11, 0x3e0293ee, v39
	v_fmamk_f32 v12, v12, 0x3e0293ee, v39
	v_fmamk_f32 v13, v13, 0x3e0293ee, v39
	v_fmamk_f32 v14, v14, 0x3e0293ee, v39
	v_fmac_f32_e32 v39, 0x3e0293ee, v15
	v_exp_f32_e32 v15, v16
	v_exp_f32_e32 v16, v17
	v_exp_f32_e32 v17, v18
	v_exp_f32_e32 v18, v19
	v_exp_f32_e32 v19, v20
	v_exp_f32_e32 v20, v21
	v_exp_f32_e32 v21, v22
	v_exp_f32_e32 v22, v23
	v_exp_f32_e32 v23, v24
	v_exp_f32_e32 v24, v25
	v_exp_f32_e32 v25, v26
	v_exp_f32_e32 v26, v27
	v_exp_f32_e32 v27, v28
	v_exp_f32_e32 v28, v29
	v_exp_f32_e32 v29, v30
	v_exp_f32_e32 v30, v31
	v_exp_f32_e32 v31, v39
	v_add_f32_e32 v39, 0, v15
	v_add_f32_e32 v39, v16, v39
	v_add_f32_e32 v39, v17, v39
	v_add_f32_e32 v39, v18, v39
	v_add_f32_e32 v39, v19, v39
	v_add_f32_e32 v39, v20, v39
	v_add_f32_e32 v39, v21, v39
	v_add_f32_e32 v39, v22, v39
	v_add_f32_e32 v39, v23, v39
	v_add_f32_e32 v39, v24, v39
	v_add_f32_e32 v39, v25, v39
	v_add_f32_e32 v39, v26, v39
	v_exp_f32_e32 v0, v0
	v_add_f32_e32 v39, v27, v39
	v_exp_f32_e32 v1, v1
	v_add_f32_e32 v39, v28, v39
	v_exp_f32_e32 v2, v2
	v_add_f32_e32 v39, v29, v39
	v_exp_f32_e32 v3, v3
	v_add_f32_e32 v39, v30, v39
	v_exp_f32_e32 v4, v4
	v_add_f32_e32 v39, v0, v39
	v_exp_f32_e32 v5, v5
	v_add_f32_e32 v39, v1, v39
	v_exp_f32_e32 v6, v6
	v_add_f32_e32 v39, v2, v39
	v_exp_f32_e32 v7, v7
	v_add_f32_e32 v39, v3, v39
	v_exp_f32_e32 v8, v8
	v_add_f32_e32 v39, v4, v39
	v_exp_f32_e32 v9, v9
	v_add_f32_e32 v39, v5, v39
	v_exp_f32_e32 v10, v10
	v_add_f32_e32 v39, v6, v39
	v_exp_f32_e32 v11, v11
	v_add_f32_e32 v39, v7, v39
	v_exp_f32_e32 v12, v12
	v_add_f32_e32 v39, v8, v39
	v_exp_f32_e32 v13, v13
	v_add_f32_e32 v39, v9, v39
	v_exp_f32_e32 v14, v14
	v_add_f32_e32 v39, v10, v39
	v_add_f32_e32 v39, v11, v39
	v_add_f32_e32 v39, v12, v39
	v_add_f32_e32 v39, v13, v39
	v_add_f32_e32 v39, v14, v39
	v_add_f32_e32 v39, v31, v39
	v_mov_b32_e32 v40, v39
	s_nop 1
	v_permlane32_swap_b32_e32 v39, v40
	v_add_f32_e32 v178, v39, v40
	v_cvt_pk_bf16_f32 v128, v15, v16
	v_cvt_pk_bf16_f32 v129, v17, v18
	v_cvt_pk_bf16_f32 v130, v19, v20
	v_cvt_pk_bf16_f32 v131, v21, v22
	v_cvt_pk_bf16_f32 v132, v23, v24
	v_cvt_pk_bf16_f32 v133, v25, v26
	v_cvt_pk_bf16_f32 v134, v27, v28
	v_cvt_pk_bf16_f32 v135, v29, v30
	v_cvt_pk_bf16_f32 v136, v0, v1
	v_cvt_pk_bf16_f32 v137, v2, v3
	v_cvt_pk_bf16_f32 v138, v4, v5
	v_cvt_pk_bf16_f32 v139, v6, v7
	v_cvt_pk_bf16_f32 v140, v8, v9
	v_cvt_pk_bf16_f32 v141, v10, v11
	v_cvt_pk_bf16_f32 v142, v12, v13
	v_cvt_pk_bf16_f32 v143, v14, v31
	s_mov_b32 s3, 4
	v_mul_f32_e32 v39, 0, v38
	v_fmac_f32_e32 v178, 0, v38
	v_permlane32_swap_b32_e32 v128, v130
	v_permlane32_swap_b32_e32 v129, v131
	v_permlane32_swap_b32_e32 v132, v134
	v_permlane32_swap_b32_e32 v133, v135
	v_permlane32_swap_b32_e32 v136, v138
	v_permlane32_swap_b32_e32 v137, v139
	v_permlane32_swap_b32_e32 v140, v142
	v_permlane32_swap_b32_e32 v141, v143
	s_bitcmp1_b32 s100, 8
	s_cbranch_scc1 .Lstg_b13
	s_waitcnt vmcnt(0)
	s_waitcnt lgkmcnt(0)
	s_barrier
.Lstg_b13:
	s_add_u32 s4, s2, 0x340000
	s_addc_u32 s5, s33, 0
	v_lshl_add_u64 v[0:1], s[4:5], 0, v[160:161]
	s_mov_b32 s6, s78
	s_add_i32 s78, s83, 0x400
	s_mov_b32 s2, m0
	s_mov_b32 m0, s83
	s_nop 0
	global_load_lds_dwordx4 v[0:1], off
	s_mov_b32 m0, s2
	v_lshl_add_u64 v[0:1], s[4:5], 0, v[170:171]
	s_add_u32 s4, s66, 0x1a0000
	s_mov_b32 s2, m0
	s_mov_b32 m0, s78
	s_nop 0
	global_load_lds_dwordx4 v[0:1], off
	s_mov_b32 m0, s2
	s_addc_u32 s5, s67, 0
	v_mov_b32_e32 v163, v161
	v_writelane_b32 v255, s4, 41
	s_add_i32 s90, s93, 0x8000
	s_add_i32 s91, s93, 0x8400
	v_lshl_add_u64 v[0:1], s[4:5], 0, v[162:163]
	s_mov_b32 s2, m0
	s_mov_b32 m0, s90
	s_nop 0
	global_load_lds_dwordx4 v[0:1], off
	s_mov_b32 m0, s2
	v_lshl_add_u64 v[2:3], v[0:1], 0, s[86:87]
	s_mov_b32 s2, m0
	s_mov_b32 m0, s91
	s_nop 0
	global_load_lds_dwordx4 v[2:3], off
	s_mov_b32 m0, s2
	v_writelane_b32 v255, s5, 42
	v_lshl_add_u64 v[2:3], v[0:1], 0, s[62:63]
	s_add_i32 s88, s93, 0x8800
	s_mov_b32 s2, m0
	s_mov_b32 m0, s88
	s_nop 0
	global_load_lds_dwordx4 v[2:3], off
	s_mov_b32 m0, s2
	s_mov_b64 s[4:5], 0x180
	v_lshl_add_u64 v[0:1], v[0:1], 0, s[4:5]
	s_add_i32 s89, s93, 0x8c00
	s_mov_b32 s2, m0
	s_mov_b32 m0, s89
	s_nop 0
	global_load_lds_dwordx4 v[0:1], off
	s_mov_b32 m0, s2
	v_cmp_gt_f32_e32 vcc, 1.0, v38
	s_cmp_lg_u64 vcc, 0
	s_cselect_b64 vcc, -1, 0
	v_readlane_b32 s2, v255, 56
	s_add_i32 s4, s6, 0xffffff80
	v_cndmask_b32_e32 v80, 0, v39, vcc
	v_add_u32_e32 v0, s2, v33
	v_writelane_b32 v255, s4, 40
	s_add_i32 s4, s4, s92
	v_mov_b32_e32 v81, v80
	v_mov_b32_e32 v94, v80
	v_mov_b32_e32 v95, v80
	v_add_u32_e32 v188, v34, v0
	v_add_u32_e32 v187, v35, v0
	v_add_u32_e32 v186, v36, v0
	v_add_u32_e32 v185, v37, v0
	v_add_u32_e32 v0, s4, v175
	v_mov_b32_e32 v82, v80
	v_mov_b32_e32 v83, v80
	v_mov_b32_e32 v84, v80
	v_mov_b32_e32 v85, v80
	v_mov_b32_e32 v86, v80
	v_mov_b32_e32 v87, v80
	v_mov_b32_e32 v88, v80
	v_mov_b32_e32 v89, v80
	v_mov_b32_e32 v90, v80
	v_mov_b32_e32 v91, v80
	v_mov_b32_e32 v92, v80
	v_mov_b32_e32 v93, v80
	v_sub_u32_e32 v189, v0, v32
	v_mov_b64_e32 v[126:127], v[94:95]
	v_mov_b64_e32 v[110:111], v[94:95]
	v_mov_b64_e32 v[64:65], v[80:81]
	v_mov_b64_e32 v[48:49], v[80:81]
	v_mov_b64_e32 v[32:33], v[80:81]
	v_mov_b64_e32 v[16:17], v[80:81]
	v_mov_b64_e32 v[0:1], v[80:81]
	s_add_i32 s2, s93, 0x400
	s_add_i32 s69, s93, 0x800
	s_add_i32 s68, s93, 0xc00
	s_mov_b32 s33, s6
	s_movk_i32 s74, 0xbf
	s_mov_b64 s[66:67], s[76:77]
	v_mov_b64_e32 v[124:125], v[92:93]
	v_mov_b64_e32 v[122:123], v[90:91]
	v_mov_b64_e32 v[120:121], v[88:89]
	v_mov_b64_e32 v[118:119], v[86:87]
	v_mov_b64_e32 v[116:117], v[84:85]
	v_mov_b64_e32 v[114:115], v[82:83]
	v_mov_b64_e32 v[112:113], v[80:81]
	v_mov_b64_e32 v[108:109], v[92:93]
	v_mov_b64_e32 v[106:107], v[90:91]
	v_mov_b64_e32 v[104:105], v[88:89]
	v_mov_b64_e32 v[102:103], v[86:87]
	v_mov_b64_e32 v[100:101], v[84:85]
	v_mov_b64_e32 v[98:99], v[82:83]
	v_mov_b64_e32 v[96:97], v[80:81]
	v_mov_b64_e32 v[66:67], v[82:83]
	v_mov_b64_e32 v[68:69], v[84:85]
	v_mov_b64_e32 v[70:71], v[86:87]
	v_mov_b64_e32 v[72:73], v[88:89]
	v_mov_b64_e32 v[74:75], v[90:91]
	v_mov_b64_e32 v[76:77], v[92:93]
	v_mov_b64_e32 v[78:79], v[94:95]
	v_mov_b64_e32 v[50:51], v[82:83]
	v_mov_b64_e32 v[52:53], v[84:85]
	v_mov_b64_e32 v[54:55], v[86:87]
	v_mov_b64_e32 v[56:57], v[88:89]
	v_mov_b64_e32 v[58:59], v[90:91]
	v_mov_b64_e32 v[60:61], v[92:93]
	v_mov_b64_e32 v[62:63], v[94:95]
	v_mov_b64_e32 v[34:35], v[82:83]
	v_mov_b64_e32 v[36:37], v[84:85]
	v_mov_b64_e32 v[38:39], v[86:87]
	v_mov_b64_e32 v[40:41], v[88:89]
	v_mov_b64_e32 v[42:43], v[90:91]
	v_mov_b64_e32 v[44:45], v[92:93]
	v_mov_b64_e32 v[46:47], v[94:95]
	v_mov_b64_e32 v[18:19], v[82:83]
	v_mov_b64_e32 v[20:21], v[84:85]
	v_mov_b64_e32 v[22:23], v[86:87]
	v_mov_b64_e32 v[24:25], v[88:89]
	v_mov_b64_e32 v[26:27], v[90:91]
	v_mov_b64_e32 v[28:29], v[92:93]
	v_mov_b64_e32 v[30:31], v[94:95]
	v_mov_b64_e32 v[2:3], v[82:83]
	v_mov_b64_e32 v[4:5], v[84:85]
	v_mov_b64_e32 v[6:7], v[86:87]
	v_mov_b64_e32 v[8:9], v[88:89]
	v_mov_b64_e32 v[10:11], v[90:91]
	v_mov_b64_e32 v[12:13], v[92:93]
	v_mov_b64_e32 v[14:15], v[94:95]
.LBB0_557:
	ds_read_b64_tr_b16 v[144:145], v177 offset:0
	ds_read_b64_tr_b16 v[146:147], v177 offset:0x1000
	ds_read_b64_tr_b16 v[148:149], v177 offset:0x2000
	ds_read_b64_tr_b16 v[150:151], v177 offset:0x3000
	ds_read_b64_tr_b16 v[152:153], v177 offset:0x4000
	ds_read_b64_tr_b16 v[154:155], v177 offset:0x5000
	ds_read_b64_tr_b16 v[156:157], v177 offset:0x6000
	ds_read_b64_tr_b16 v[158:159], v177 offset:0x7000
	ds_read_b64_tr_b16 v[192:193], v177 offset:0x200
	ds_read_b64_tr_b16 v[194:195], v177 offset:0x1200
	ds_read_b64_tr_b16 v[196:197], v177 offset:0x2200
	ds_read_b64_tr_b16 v[198:199], v177 offset:0x3200
	ds_read_b64_tr_b16 v[200:201], v177 offset:0x4200
	ds_read_b64_tr_b16 v[202:203], v177 offset:0x5200
	ds_read_b64_tr_b16 v[204:205], v177 offset:0x6200
	ds_read_b64_tr_b16 v[206:207], v177 offset:0x7200
	s_waitcnt lgkmcnt(8)
	s_nop 0
	v_mfma_f32_32x32x16_bf16 v[112:127], v[144:147], v[128:131], v[112:127]
	v_mfma_f32_32x32x16_bf16 v[112:127], v[148:151], v[132:135], v[112:127]
	v_mfma_f32_32x32x16_bf16 v[112:127], v[152:155], v[136:139], v[112:127]
	v_mfma_f32_32x32x16_bf16 v[112:127], v[156:159], v[140:143], v[112:127]
	ds_read_b64_tr_b16 v[144:145], v177 offset:0x400
	ds_read_b64_tr_b16 v[146:147], v177 offset:0x1400
	ds_read_b64_tr_b16 v[148:149], v177 offset:0x2400
	ds_read_b64_tr_b16 v[150:151], v177 offset:0x3400
	ds_read_b64_tr_b16 v[152:153], v177 offset:0x4400
	ds_read_b64_tr_b16 v[154:155], v177 offset:0x5400
	ds_read_b64_tr_b16 v[156:157], v177 offset:0x6400
	ds_read_b64_tr_b16 v[158:159], v177 offset:0x7400
	s_waitcnt lgkmcnt(8)
	v_mfma_f32_32x32x16_bf16 v[80:95], v[192:195], v[128:131], v[80:95]
	v_mfma_f32_32x32x16_bf16 v[80:95], v[196:199], v[132:135], v[80:95]
	v_mfma_f32_32x32x16_bf16 v[80:95], v[200:203], v[136:139], v[80:95]
	v_mfma_f32_32x32x16_bf16 v[80:95], v[204:207], v[140:143], v[80:95]
	ds_read_b64_tr_b16 v[192:193], v177 offset:0x600
	ds_read_b64_tr_b16 v[194:195], v177 offset:0x1600
	ds_read_b64_tr_b16 v[196:197], v177 offset:0x2600
	ds_read_b64_tr_b16 v[198:199], v177 offset:0x3600
	ds_read_b64_tr_b16 v[200:201], v177 offset:0x4600
	ds_read_b64_tr_b16 v[202:203], v177 offset:0x5600
	ds_read_b64_tr_b16 v[204:205], v177 offset:0x6600
	ds_read_b64_tr_b16 v[206:207], v177 offset:0x7600
	s_waitcnt lgkmcnt(8)
	v_mfma_f32_32x32x16_bf16 v[96:111], v[144:147], v[128:131], v[96:111]
	v_mfma_f32_32x32x16_bf16 v[96:111], v[148:151], v[132:135], v[96:111]
	v_mfma_f32_32x32x16_bf16 v[96:111], v[152:155], v[136:139], v[96:111]
	v_mfma_f32_32x32x16_bf16 v[96:111], v[156:159], v[140:143], v[96:111]
	ds_read_b64_tr_b16 v[144:145], v177 offset:0x800
	ds_read_b64_tr_b16 v[146:147], v177 offset:0x1800
	ds_read_b64_tr_b16 v[148:149], v177 offset:0x2800
	ds_read_b64_tr_b16 v[150:151], v177 offset:0x3800
	ds_read_b64_tr_b16 v[152:153], v177 offset:0x4800
	ds_read_b64_tr_b16 v[154:155], v177 offset:0x5800
	ds_read_b64_tr_b16 v[156:157], v177 offset:0x6800
	ds_read_b64_tr_b16 v[158:159], v177 offset:0x7800
	s_waitcnt lgkmcnt(8)
	v_mfma_f32_32x32x16_bf16 v[64:79], v[192:195], v[128:131], v[64:79]
	v_mfma_f32_32x32x16_bf16 v[64:79], v[196:199], v[132:135], v[64:79]
	v_mfma_f32_32x32x16_bf16 v[64:79], v[200:203], v[136:139], v[64:79]
	v_mfma_f32_32x32x16_bf16 v[64:79], v[204:207], v[140:143], v[64:79]
	ds_read_b64_tr_b16 v[192:193], v177 offset:0xa00
	ds_read_b64_tr_b16 v[194:195], v177 offset:0x1a00
	ds_read_b64_tr_b16 v[196:197], v177 offset:0x2a00
	ds_read_b64_tr_b16 v[198:199], v177 offset:0x3a00
	ds_read_b64_tr_b16 v[200:201], v177 offset:0x4a00
	ds_read_b64_tr_b16 v[202:203], v177 offset:0x5a00
	ds_read_b64_tr_b16 v[204:205], v177 offset:0x6a00
	ds_read_b64_tr_b16 v[206:207], v177 offset:0x7a00
	s_waitcnt lgkmcnt(8)
	v_mfma_f32_32x32x16_bf16 v[48:63], v[144:147], v[128:131], v[48:63]
	v_mfma_f32_32x32x16_bf16 v[48:63], v[148:151], v[132:135], v[48:63]
	v_mfma_f32_32x32x16_bf16 v[48:63], v[152:155], v[136:139], v[48:63]
	v_mfma_f32_32x32x16_bf16 v[48:63], v[156:159], v[140:143], v[48:63]
	ds_read_b64_tr_b16 v[144:145], v177 offset:0xc00
	ds_read_b64_tr_b16 v[146:147], v177 offset:0x1c00
	ds_read_b64_tr_b16 v[148:149], v177 offset:0x2c00
	ds_read_b64_tr_b16 v[150:151], v177 offset:0x3c00
	ds_read_b64_tr_b16 v[152:153], v177 offset:0x4c00
	ds_read_b64_tr_b16 v[154:155], v177 offset:0x5c00
	ds_read_b64_tr_b16 v[156:157], v177 offset:0x6c00
	ds_read_b64_tr_b16 v[158:159], v177 offset:0x7c00
	s_waitcnt lgkmcnt(8)
	v_mfma_f32_32x32x16_bf16 v[32:47], v[192:195], v[128:131], v[32:47]
	v_mfma_f32_32x32x16_bf16 v[32:47], v[196:199], v[132:135], v[32:47]
	v_mfma_f32_32x32x16_bf16 v[32:47], v[200:203], v[136:139], v[32:47]
	v_mfma_f32_32x32x16_bf16 v[32:47], v[204:207], v[140:143], v[32:47]
	ds_read_b64_tr_b16 v[192:193], v177 offset:0xe00
	ds_read_b64_tr_b16 v[194:195], v177 offset:0x1e00
	ds_read_b64_tr_b16 v[196:197], v177 offset:0x2e00
	ds_read_b64_tr_b16 v[198:199], v177 offset:0x3e00
	ds_read_b64_tr_b16 v[200:201], v177 offset:0x4e00
	ds_read_b64_tr_b16 v[202:203], v177 offset:0x5e00
	ds_read_b64_tr_b16 v[204:205], v177 offset:0x6e00
	ds_read_b64_tr_b16 v[206:207], v177 offset:0x7e00
	s_waitcnt lgkmcnt(8)
	v_mfma_f32_32x32x16_bf16 v[16:31], v[144:147], v[128:131], v[16:31]
	v_mfma_f32_32x32x16_bf16 v[16:31], v[148:151], v[132:135], v[16:31]
	v_mfma_f32_32x32x16_bf16 v[16:31], v[152:155], v[136:139], v[16:31]
	v_mfma_f32_32x32x16_bf16 v[16:31], v[156:159], v[140:143], v[16:31]
	s_waitcnt lgkmcnt(0)
	v_mfma_f32_32x32x16_bf16 v[0:15], v[192:195], v[128:131], v[0:15]
	v_mfma_f32_32x32x16_bf16 v[0:15], v[196:199], v[132:135], v[0:15]
	v_mfma_f32_32x32x16_bf16 v[0:15], v[200:203], v[136:139], v[0:15]
	v_mfma_f32_32x32x16_bf16 v[0:15], v[204:207], v[140:143], v[0:15]
	ds_read_b128 v[128:131], v188 offset:0
	ds_read_b128 v[132:135], v188 offset:0x2000
	ds_read_b128 v[136:139], v180 offset:0
	ds_read_b128 v[192:195], v187 offset:0
	ds_read_b128 v[196:199], v187 offset:0x2000
	ds_read_b128 v[200:203], v180 offset:0x400
	s_waitcnt lgkmcnt(3)
	s_nop 0
	v_mfma_f32_32x32x16_bf16 v[144:159], v[128:131], v[136:139], 0
	v_mfma_f32_32x32x16_bf16 v[128:143], v[132:135], v[136:139], 0
	ds_read_b128 v[204:207], v186 offset:0
	ds_read_b128 v[208:211], v186 offset:0x2000
	ds_read_b128 v[212:215], v180 offset:0x800
	s_waitcnt lgkmcnt(3)
	v_mfma_f32_32x32x16_bf16 v[144:159], v[192:195], v[200:203], v[144:159]
	v_mfma_f32_32x32x16_bf16 v[128:143], v[196:199], v[200:203], v[128:143]
	ds_read_b128 v[192:195], v185 offset:0
	ds_read_b128 v[196:199], v185 offset:0x2000
	ds_read_b128 v[200:203], v180 offset:0xc00
	s_waitcnt lgkmcnt(3)
	v_mfma_f32_32x32x16_bf16 v[144:159], v[204:207], v[212:215], v[144:159]
	v_mfma_f32_32x32x16_bf16 v[128:143], v[208:211], v[212:215], v[128:143]
	ds_read_b128 v[204:207], v188 offset:0x80
	ds_read_b128 v[208:211], v188 offset:0x2080
	ds_read_b128 v[212:215], v180 offset:0x1000
	s_waitcnt lgkmcnt(3)
	v_mfma_f32_32x32x16_bf16 v[144:159], v[192:195], v[200:203], v[144:159]
	v_mfma_f32_32x32x16_bf16 v[128:143], v[196:199], v[200:203], v[128:143]
	ds_read_b128 v[192:195], v187 offset:0x80
	ds_read_b128 v[196:199], v187 offset:0x2080
	ds_read_b128 v[200:203], v180 offset:0x1400
	s_waitcnt lgkmcnt(3)
	v_mfma_f32_32x32x16_bf16 v[144:159], v[204:207], v[212:215], v[144:159]
	v_mfma_f32_32x32x16_bf16 v[128:143], v[208:211], v[212:215], v[128:143]
	ds_read_b128 v[204:207], v186 offset:0x80
	ds_read_b128 v[208:211], v186 offset:0x2080
	ds_read_b128 v[212:215], v180 offset:0x1800
	s_waitcnt lgkmcnt(3)
	v_mfma_f32_32x32x16_bf16 v[144:159], v[192:195], v[200:203], v[144:159]
	v_mfma_f32_32x32x16_bf16 v[128:143], v[196:199], v[200:203], v[128:143]
	ds_read_b128 v[192:195], v185 offset:0x80
	ds_read_b128 v[196:199], v185 offset:0x2080
	s_waitcnt lgkmcnt(2)
	v_mfma_f32_32x32x16_bf16 v[144:159], v[204:207], v[212:215], v[144:159]
	v_mfma_f32_32x32x16_bf16 v[128:143], v[208:211], v[212:215], v[128:143]
	s_waitcnt lgkmcnt(0)
	v_mfma_f32_32x32x16_bf16 v[144:159], v[192:195], v[166:169], v[144:159]
	v_mfma_f32_32x32x16_bf16 v[128:143], v[196:199], v[166:169], v[128:143]
	s_bitcmp0_b32 s100, 8
	s_cbranch_scc1 .Lstg_a10
	s_waitcnt vmcnt(0)
	s_waitcnt lgkmcnt(0)
	s_barrier
.Lstg_a10:
	s_sub_i32 s4, s74, 64
	s_cmp_le_i32 s4, s82
	s_cbranch_scc1 .LBB0_559
	v_add_u32_e32 v172, 64, v189
	v_cmp_gt_i32_e64 s[62:63], 26, v172
	v_cmp_gt_i32_e64 s[64:65], 27, v172
	v_cmp_gt_i32_e64 s[60:61], 25, v172
	s_and_b64 s[62:63], s[64:65], s[62:63]
	v_cmp_gt_i32_e64 s[58:59], 24, v172
	s_and_b64 s[60:61], s[62:63], s[60:61]
	v_cmp_gt_i32_e64 s[56:57], 19, v172
	s_and_b64 s[58:59], s[60:61], s[58:59]
	v_cmp_gt_i32_e64 s[54:55], 18, v172
	s_and_b64 s[56:57], s[58:59], s[56:57]
	v_cmp_gt_i32_e64 s[52:53], 17, v172
	s_and_b64 s[54:55], s[56:57], s[54:55]
	v_cmp_gt_i32_e64 s[50:51], 16, v172
	s_and_b64 s[52:53], s[54:55], s[52:53]
	v_cmp_gt_i32_e64 s[48:49], 11, v172
	s_and_b64 s[50:51], s[52:53], s[50:51]
	v_cmp_gt_i32_e64 s[46:47], 10, v172
	s_and_b64 s[48:49], s[50:51], s[48:49]
	v_cmp_gt_i32_e64 s[44:45], 9, v172
	s_and_b64 s[46:47], s[48:49], s[46:47]
	v_cmp_gt_i32_e64 s[42:43], 8, v172
	s_and_b64 s[44:45], s[46:47], s[44:45]
	v_cmp_gt_i32_e64 s[40:41], 3, v172
	s_and_b64 s[42:43], s[44:45], s[42:43]
	v_cmp_gt_i32_e64 s[38:39], 2, v172
	s_and_b64 s[40:41], s[42:43], s[40:41]
	v_cmp_gt_i32_e64 s[36:37], 1, v172
	s_and_b64 s[38:39], s[40:41], s[38:39]
	v_cmp_gt_i32_e64 s[34:35], 0, v172
	s_and_b64 s[36:37], s[38:39], s[36:37]
	s_and_b64 s[34:35], s[36:37], s[34:35]
	v_cmp_gt_i32_e64 s[30:31], 58, v172
	v_cndmask_b32_e64 v144, v144, v226, s[34:35]
	v_cmp_gt_i32_e64 s[34:35], 59, v172
	v_cmp_gt_i32_e64 s[28:29], 57, v172
	s_and_b64 s[30:31], s[34:35], s[30:31]
	v_cmp_gt_i32_e64 s[26:27], 56, v172
	s_and_b64 s[28:29], s[30:31], s[28:29]
	v_cmp_gt_i32_e64 s[24:25], 51, v172
	s_and_b64 s[26:27], s[28:29], s[26:27]
	v_cmp_gt_i32_e64 s[22:23], 50, v172
	s_and_b64 s[24:25], s[26:27], s[24:25]
	v_cmp_gt_i32_e64 s[20:21], 49, v172
	s_and_b64 s[22:23], s[24:25], s[22:23]
	v_cmp_gt_i32_e64 s[18:19], 48, v172
	s_and_b64 s[20:21], s[22:23], s[20:21]
	v_cmp_gt_i32_e64 s[16:17], 43, v172
	s_and_b64 s[18:19], s[20:21], s[18:19]
	v_cmp_gt_i32_e64 s[14:15], 42, v172
	s_and_b64 s[16:17], s[18:19], s[16:17]
	v_cmp_gt_i32_e64 s[12:13], 41, v172
	s_and_b64 s[14:15], s[16:17], s[14:15]
	v_cmp_gt_i32_e64 s[10:11], 40, v172
	s_and_b64 s[12:13], s[14:15], s[12:13]
	v_cmp_gt_i32_e64 s[8:9], 35, v172
	s_and_b64 s[10:11], s[12:13], s[10:11]
	v_cmp_gt_i32_e64 s[6:7], 34, v172
	s_and_b64 s[8:9], s[10:11], s[8:9]
	v_cmp_gt_i32_e64 s[4:5], 33, v172
	s_and_b64 s[6:7], s[8:9], s[6:7]
	v_cmp_gt_i32_e32 vcc, 32, v172
	s_and_b64 s[4:5], s[6:7], s[4:5]
	s_and_b64 vcc, s[4:5], vcc
	v_cndmask_b32_e64 v159, v159, v226, s[64:65]
	v_cndmask_b32_e64 v158, v158, v226, s[62:63]
	s_mov_b64 s[62:63], 0x100
	v_cndmask_b32_e64 v157, v157, v226, s[60:61]
	v_cndmask_b32_e64 v156, v156, v226, s[58:59]
	v_cndmask_b32_e64 v155, v155, v226, s[56:57]
	v_cndmask_b32_e64 v154, v154, v226, s[54:55]
	v_cndmask_b32_e64 v153, v153, v226, s[52:53]
	v_cndmask_b32_e64 v152, v152, v226, s[50:51]
	v_cndmask_b32_e64 v151, v151, v226, s[48:49]
	v_cndmask_b32_e64 v150, v150, v226, s[46:47]
	v_cndmask_b32_e64 v149, v149, v226, s[44:45]
	v_cndmask_b32_e64 v148, v148, v226, s[42:43]
	v_cndmask_b32_e64 v147, v147, v226, s[40:41]
	v_cndmask_b32_e64 v146, v146, v226, s[38:39]
	v_cndmask_b32_e64 v145, v145, v226, s[36:37]
	v_cndmask_b32_e64 v143, v143, v226, s[34:35]
	v_cndmask_b32_e64 v142, v142, v226, s[30:31]
	v_cndmask_b32_e64 v141, v141, v226, s[28:29]
	v_cndmask_b32_e64 v140, v140, v226, s[26:27]
	v_cndmask_b32_e64 v139, v139, v226, s[24:25]
	v_cndmask_b32_e64 v138, v138, v226, s[22:23]
	v_cndmask_b32_e64 v137, v137, v226, s[20:21]
	v_cndmask_b32_e64 v136, v136, v226, s[18:19]
	v_cndmask_b32_e64 v135, v135, v226, s[16:17]
	v_cndmask_b32_e64 v134, v134, v226, s[14:15]
	v_cndmask_b32_e64 v133, v133, v226, s[12:13]
	v_cndmask_b32_e64 v132, v132, v226, s[10:11]
	v_cndmask_b32_e64 v131, v131, v226, s[8:9]
	v_cndmask_b32_e64 v130, v130, v226, s[6:7]
	v_cndmask_b32_e64 v129, v129, v226, s[4:5]
	v_cndmask_b32_e32 v128, v128, v226, vcc
.LBB0_559:
	s_nop 7
	v_max_f32_e32 v172, v145, v145
	v_max_f32_e32 v191, v144, v144
	v_max_f32_e32 v172, v191, v172
	v_max3_f32 v172, v172, v146, v147
	v_max3_f32 v172, v172, v148, v149
	v_max3_f32 v172, v172, v150, v151
	v_max3_f32 v172, v172, v152, v153
	v_max3_f32 v172, v172, v154, v155
	v_max3_f32 v172, v172, v156, v157
	v_max3_f32 v172, v172, v158, v159
	v_max3_f32 v172, v172, v128, v129
	v_max3_f32 v172, v172, v130, v131
	v_max3_f32 v172, v172, v132, v133
	v_max3_f32 v172, v172, v134, v135
	v_max3_f32 v172, v172, v136, v137
	v_max3_f32 v172, v172, v138, v139
	v_max3_f32 v172, v172, v140, v141
	v_max3_f32 v172, v172, v142, v143
	v_mov_b32_e32 v191, v172
	s_nop 1
	v_permlane32_swap_b32_e32 v172, v191
	v_max_f32_e32 v191, v191, v191
	v_max_f32_e32 v172, v172, v172
	v_max_f32_e32 v172, v172, v191
	v_sub_f32_e32 v191, v172, v190
	v_mul_f32_e32 v191, 0x3db504f3, v191
	s_mov_b32 s4, 0x41000000
	v_cmp_ge_f32_e32 vcc, s4, v191
	s_cmp_eq_u64 vcc, exec
	v_max_f32_e32 v191, v190, v190
	v_max_f32_e32 v172, v191, v172
	s_cselect_b64 s[4:5], -1, 0
	v_cndmask_b32_e64 v193, v172, v190, s[4:5]
	v_mul_f32_e32 v191, 0xbe0293ee, v193
	v_fmamk_f32 v144, v144, 0x3e0293ee, v191
	v_fmamk_f32 v145, v145, 0x3e0293ee, v191
	v_fmamk_f32 v146, v146, 0x3e0293ee, v191
	v_fmamk_f32 v147, v147, 0x3e0293ee, v191
	v_fmamk_f32 v148, v148, 0x3e0293ee, v191
	v_fmamk_f32 v149, v149, 0x3e0293ee, v191
	v_fmamk_f32 v150, v150, 0x3e0293ee, v191
	v_fmamk_f32 v151, v151, 0x3e0293ee, v191
	v_fmamk_f32 v152, v152, 0x3e0293ee, v191
	v_fmamk_f32 v153, v153, 0x3e0293ee, v191
	v_fmamk_f32 v154, v154, 0x3e0293ee, v191
	v_fmamk_f32 v155, v155, 0x3e0293ee, v191
	v_fmamk_f32 v156, v156, 0x3e0293ee, v191
	v_fmamk_f32 v157, v157, 0x3e0293ee, v191
	v_fmamk_f32 v158, v158, 0x3e0293ee, v191
	v_fmamk_f32 v159, v159, 0x3e0293ee, v191
	v_fmamk_f32 v128, v128, 0x3e0293ee, v191
	v_fmamk_f32 v129, v129, 0x3e0293ee, v191
	v_fmamk_f32 v130, v130, 0x3e0293ee, v191
	v_fmamk_f32 v131, v131, 0x3e0293ee, v191
	v_fmamk_f32 v132, v132, 0x3e0293ee, v191
	v_fmamk_f32 v133, v133, 0x3e0293ee, v191
	v_fmamk_f32 v134, v134, 0x3e0293ee, v191
	v_fmamk_f32 v135, v135, 0x3e0293ee, v191
	v_fmamk_f32 v136, v136, 0x3e0293ee, v191
	v_fmamk_f32 v137, v137, 0x3e0293ee, v191
	v_fmamk_f32 v138, v138, 0x3e0293ee, v191
	v_fmamk_f32 v139, v139, 0x3e0293ee, v191
	v_fmamk_f32 v140, v140, 0x3e0293ee, v191
	v_fmamk_f32 v141, v141, 0x3e0293ee, v191
	v_fmamk_f32 v142, v142, 0x3e0293ee, v191
	v_fmac_f32_e32 v191, 0x3e0293ee, v143
	v_exp_f32_e32 v143, v144
	v_exp_f32_e32 v144, v145
	v_exp_f32_e32 v145, v146
	v_exp_f32_e32 v146, v147
	v_exp_f32_e32 v147, v148
	v_exp_f32_e32 v148, v149
	v_exp_f32_e32 v149, v150
	v_exp_f32_e32 v150, v151
	v_exp_f32_e32 v151, v152
	v_exp_f32_e32 v152, v153
	v_exp_f32_e32 v153, v154
	v_exp_f32_e32 v154, v155
	v_exp_f32_e32 v155, v156
	v_exp_f32_e32 v156, v157
	v_exp_f32_e32 v157, v158
	v_exp_f32_e32 v158, v159
	v_exp_f32_e32 v159, v128
	v_add_f32_e32 v128, 0, v143
	v_add_f32_e32 v128, v144, v128
	v_add_f32_e32 v128, v145, v128
	v_add_f32_e32 v128, v146, v128
	v_add_f32_e32 v128, v147, v128
	v_add_f32_e32 v128, v148, v128
	v_add_f32_e32 v128, v149, v128
	v_add_f32_e32 v128, v150, v128
	v_add_f32_e32 v128, v151, v128
	v_add_f32_e32 v128, v152, v128
	v_add_f32_e32 v128, v153, v128
	v_add_f32_e32 v128, v154, v128
	v_add_f32_e32 v128, v155, v128
	v_exp_f32_e32 v194, v129
	v_add_f32_e32 v128, v156, v128
	v_exp_f32_e32 v195, v130
	v_add_f32_e32 v128, v157, v128
	v_exp_f32_e32 v196, v131
	v_add_f32_e32 v128, v158, v128
	v_exp_f32_e32 v197, v132
	v_add_f32_e32 v128, v159, v128
	v_exp_f32_e32 v198, v133
	v_add_f32_e32 v128, v194, v128
	v_exp_f32_e32 v199, v134
	v_add_f32_e32 v128, v195, v128
	v_exp_f32_e32 v200, v135
	v_add_f32_e32 v128, v196, v128
	v_exp_f32_e32 v201, v136
	v_add_f32_e32 v128, v197, v128
	v_exp_f32_e32 v202, v137
	v_add_f32_e32 v128, v198, v128
	v_exp_f32_e32 v203, v138
	v_add_f32_e32 v128, v199, v128
	v_exp_f32_e32 v204, v139
	v_add_f32_e32 v128, v200, v128
	v_exp_f32_e32 v205, v140
	v_add_f32_e32 v128, v201, v128
	v_exp_f32_e32 v206, v141
	v_add_f32_e32 v128, v202, v128
	v_exp_f32_e32 v207, v142
	v_add_f32_e32 v128, v203, v128
	v_exp_f32_e32 v208, v191
	v_add_f32_e32 v128, v204, v128
	v_add_f32_e32 v128, v205, v128
	v_add_f32_e32 v128, v206, v128
	v_add_f32_e32 v128, v207, v128
	v_add_f32_e32 v191, v208, v128
	v_mov_b32_e32 v192, v191
	v_cvt_pk_bf16_f32 v128, v143, v144
	v_cvt_pk_bf16_f32 v129, v145, v146
	v_cvt_pk_bf16_f32 v130, v147, v148
	v_cvt_pk_bf16_f32 v131, v149, v150
	v_cvt_pk_bf16_f32 v132, v151, v152
	v_cvt_pk_bf16_f32 v133, v153, v154
	v_cvt_pk_bf16_f32 v134, v155, v156
	v_cvt_pk_bf16_f32 v135, v157, v158
	v_cvt_pk_bf16_f32 v136, v159, v194
	v_cvt_pk_bf16_f32 v137, v195, v196
	v_cvt_pk_bf16_f32 v138, v197, v198
	v_cvt_pk_bf16_f32 v139, v199, v200
	v_cvt_pk_bf16_f32 v140, v201, v202
	v_cvt_pk_bf16_f32 v141, v203, v204
	v_cvt_pk_bf16_f32 v142, v205, v206
	v_cvt_pk_bf16_f32 v143, v207, v208
	s_nop 1
	v_permlane32_swap_b32_e32 v191, v192
	v_permlane32_swap_b32_e32 v128, v130
	v_permlane32_swap_b32_e32 v129, v131
	v_permlane32_swap_b32_e32 v132, v134
	v_permlane32_swap_b32_e32 v133, v135
	v_permlane32_swap_b32_e32 v136, v138
	v_permlane32_swap_b32_e32 v137, v139
	v_permlane32_swap_b32_e32 v140, v142
	v_permlane32_swap_b32_e32 v141, v143
	s_bitcmp1_b32 s100, 8
	s_cbranch_scc1 .Lstg_b14
	s_waitcnt vmcnt(0)
	s_waitcnt lgkmcnt(0)
	s_barrier
.Lstg_b14:
	s_add_i32 s8, s3, -1
	s_cmp_ge_u32 s8, s75
	s_cselect_b64 s[96:97], -1, 0
	s_mov_b64 s[6:7], -1
	s_and_b64 vcc, exec, s[96:97]
	s_cbranch_vccz .LBB0_561
	v_mov_b64_e32 v[144:145], s[80:81]
	flat_load_dword v146, v[144:145] sc0 sc1
	s_waitcnt vmcnt(0)
	v_mov_b64_e32 v[144:145], s[72:73]
	flat_load_dword v144, v[144:145] sc0 sc1
	s_waitcnt vmcnt(0) lgkmcnt(0)
	v_readfirstlane_b32 s6, v146
	v_readfirstlane_b32 s7, v144
	s_nop 1
	v_lshl_add_u64 v[144:145], s[6:7], 0, v[160:161]
	s_mov_b32 s8, m0
	s_mov_b32 m0, s83
	s_nop 0
	global_load_lds_dwordx4 v[144:145], off
	s_mov_b32 m0, s8
	v_lshl_add_u64 v[144:145], s[6:7], 0, v[170:171]
	s_mov_b32 s6, m0
	s_mov_b32 m0, s78
	s_nop 0
	global_load_lds_dwordx4 v[144:145], off
	s_mov_b32 m0, s6
	s_mov_b64 s[6:7], 0

.LBB0_565:
	ds_read_b64_tr_b16 v[144:145], v177 offset:0x8000
	ds_read_b64_tr_b16 v[146:147], v177 offset:0x9000
	ds_read_b64_tr_b16 v[148:149], v177 offset:0xa000
	ds_read_b64_tr_b16 v[150:151], v177 offset:0xb000
	ds_read_b64_tr_b16 v[152:153], v177 offset:0xc000
	ds_read_b64_tr_b16 v[154:155], v177 offset:0xd000
	ds_read_b64_tr_b16 v[156:157], v177 offset:0xe000
	ds_read_b64_tr_b16 v[158:159], v177 offset:0xf000
	ds_read_b64_tr_b16 v[194:195], v177 offset:0x8200
	ds_read_b64_tr_b16 v[196:197], v177 offset:0x9200
	ds_read_b64_tr_b16 v[198:199], v177 offset:0xa200
	ds_read_b64_tr_b16 v[200:201], v177 offset:0xb200
	ds_read_b64_tr_b16 v[202:203], v177 offset:0xc200
	ds_read_b64_tr_b16 v[204:205], v177 offset:0xd200
	ds_read_b64_tr_b16 v[206:207], v177 offset:0xe200
	ds_read_b64_tr_b16 v[208:209], v177 offset:0xf200
	s_waitcnt lgkmcnt(8)
	s_nop 0
	v_mfma_f32_32x32x16_bf16 v[112:127], v[144:147], v[128:131], v[112:127]
	v_mfma_f32_32x32x16_bf16 v[112:127], v[148:151], v[132:135], v[112:127]
	v_mfma_f32_32x32x16_bf16 v[112:127], v[152:155], v[136:139], v[112:127]
	v_mfma_f32_32x32x16_bf16 v[112:127], v[156:159], v[140:143], v[112:127]
	ds_read_b64_tr_b16 v[144:145], v177 offset:0x8400
	ds_read_b64_tr_b16 v[146:147], v177 offset:0x9400
	ds_read_b64_tr_b16 v[148:149], v177 offset:0xa400
	ds_read_b64_tr_b16 v[150:151], v177 offset:0xb400
	ds_read_b64_tr_b16 v[152:153], v177 offset:0xc400
	ds_read_b64_tr_b16 v[154:155], v177 offset:0xd400
	ds_read_b64_tr_b16 v[156:157], v177 offset:0xe400
	ds_read_b64_tr_b16 v[158:159], v177 offset:0xf400
	s_waitcnt lgkmcnt(8)
	v_mfma_f32_32x32x16_bf16 v[80:95], v[194:197], v[128:131], v[80:95]
	v_mfma_f32_32x32x16_bf16 v[80:95], v[198:201], v[132:135], v[80:95]
	v_mfma_f32_32x32x16_bf16 v[80:95], v[202:205], v[136:139], v[80:95]
	v_mfma_f32_32x32x16_bf16 v[80:95], v[206:209], v[140:143], v[80:95]
	ds_read_b64_tr_b16 v[194:195], v177 offset:0x8600
	ds_read_b64_tr_b16 v[196:197], v177 offset:0x9600
	ds_read_b64_tr_b16 v[198:199], v177 offset:0xa600
	ds_read_b64_tr_b16 v[200:201], v177 offset:0xb600
	ds_read_b64_tr_b16 v[202:203], v177 offset:0xc600
	ds_read_b64_tr_b16 v[204:205], v177 offset:0xd600
	ds_read_b64_tr_b16 v[206:207], v177 offset:0xe600
	ds_read_b64_tr_b16 v[208:209], v177 offset:0xf600
	s_waitcnt lgkmcnt(8)
	v_mfma_f32_32x32x16_bf16 v[96:111], v[144:147], v[128:131], v[96:111]
	v_mfma_f32_32x32x16_bf16 v[96:111], v[148:151], v[132:135], v[96:111]
	v_mfma_f32_32x32x16_bf16 v[96:111], v[152:155], v[136:139], v[96:111]
	v_mfma_f32_32x32x16_bf16 v[96:111], v[156:159], v[140:143], v[96:111]
	ds_read_b64_tr_b16 v[144:145], v177 offset:0x8800
	ds_read_b64_tr_b16 v[146:147], v177 offset:0x9800
	ds_read_b64_tr_b16 v[148:149], v177 offset:0xa800
	ds_read_b64_tr_b16 v[150:151], v177 offset:0xb800
	ds_read_b64_tr_b16 v[152:153], v177 offset:0xc800
	ds_read_b64_tr_b16 v[154:155], v177 offset:0xd800
	ds_read_b64_tr_b16 v[156:157], v177 offset:0xe800
	ds_read_b64_tr_b16 v[158:159], v177 offset:0xf800
	s_waitcnt lgkmcnt(8)
	v_mfma_f32_32x32x16_bf16 v[64:79], v[194:197], v[128:131], v[64:79]
	v_mfma_f32_32x32x16_bf16 v[64:79], v[198:201], v[132:135], v[64:79]
	v_mfma_f32_32x32x16_bf16 v[64:79], v[202:205], v[136:139], v[64:79]
	v_mfma_f32_32x32x16_bf16 v[64:79], v[206:209], v[140:143], v[64:79]
	ds_read_b64_tr_b16 v[194:195], v177 offset:0x8a00
	ds_read_b64_tr_b16 v[196:197], v177 offset:0x9a00
	ds_read_b64_tr_b16 v[198:199], v177 offset:0xaa00
	ds_read_b64_tr_b16 v[200:201], v177 offset:0xba00
	ds_read_b64_tr_b16 v[202:203], v177 offset:0xca00
	ds_read_b64_tr_b16 v[204:205], v177 offset:0xda00
	ds_read_b64_tr_b16 v[206:207], v177 offset:0xea00
	ds_read_b64_tr_b16 v[208:209], v177 offset:0xfa00
	s_waitcnt lgkmcnt(8)
	v_mfma_f32_32x32x16_bf16 v[48:63], v[144:147], v[128:131], v[48:63]
	v_mfma_f32_32x32x16_bf16 v[48:63], v[148:151], v[132:135], v[48:63]
	v_mfma_f32_32x32x16_bf16 v[48:63], v[152:155], v[136:139], v[48:63]
	v_mfma_f32_32x32x16_bf16 v[48:63], v[156:159], v[140:143], v[48:63]
	ds_read_b64_tr_b16 v[144:145], v177 offset:0x8c00
	ds_read_b64_tr_b16 v[146:147], v177 offset:0x9c00
	ds_read_b64_tr_b16 v[148:149], v177 offset:0xac00
	ds_read_b64_tr_b16 v[150:151], v177 offset:0xbc00
	ds_read_b64_tr_b16 v[152:153], v177 offset:0xcc00
	ds_read_b64_tr_b16 v[154:155], v177 offset:0xdc00
	ds_read_b64_tr_b16 v[156:157], v177 offset:0xec00
	ds_read_b64_tr_b16 v[158:159], v177 offset:0xfc00
	s_waitcnt lgkmcnt(8)
	v_mfma_f32_32x32x16_bf16 v[32:47], v[194:197], v[128:131], v[32:47]
	v_mfma_f32_32x32x16_bf16 v[32:47], v[198:201], v[132:135], v[32:47]
	v_mfma_f32_32x32x16_bf16 v[32:47], v[202:205], v[136:139], v[32:47]
	v_mfma_f32_32x32x16_bf16 v[32:47], v[206:209], v[140:143], v[32:47]
	ds_read_b64_tr_b16 v[194:195], v177 offset:0x8e00
	ds_read_b64_tr_b16 v[196:197], v177 offset:0x9e00
	ds_read_b64_tr_b16 v[198:199], v177 offset:0xae00
	ds_read_b64_tr_b16 v[200:201], v177 offset:0xbe00
	ds_read_b64_tr_b16 v[202:203], v177 offset:0xce00
	ds_read_b64_tr_b16 v[204:205], v177 offset:0xde00
	ds_read_b64_tr_b16 v[206:207], v177 offset:0xee00
	ds_read_b64_tr_b16 v[208:209], v177 offset:0xfe00
	s_waitcnt lgkmcnt(8)
	v_mfma_f32_32x32x16_bf16 v[16:31], v[144:147], v[128:131], v[16:31]
	v_mfma_f32_32x32x16_bf16 v[16:31], v[148:151], v[132:135], v[16:31]
	v_mfma_f32_32x32x16_bf16 v[16:31], v[152:155], v[136:139], v[16:31]
	v_mfma_f32_32x32x16_bf16 v[16:31], v[156:159], v[140:143], v[16:31]
	s_waitcnt lgkmcnt(0)
	v_mfma_f32_32x32x16_bf16 v[0:15], v[194:197], v[128:131], v[0:15]
	v_mfma_f32_32x32x16_bf16 v[0:15], v[198:201], v[132:135], v[0:15]
	v_mfma_f32_32x32x16_bf16 v[0:15], v[202:205], v[136:139], v[0:15]
	v_mfma_f32_32x32x16_bf16 v[0:15], v[206:209], v[140:143], v[0:15]
	ds_read_b128 v[128:131], v181 offset:0
	ds_read_b128 v[132:135], v181 offset:0x2000
	ds_read_b128 v[136:139], v180 offset:0
	ds_read_b128 v[194:197], v182 offset:0
	ds_read_b128 v[198:201], v182 offset:0x2000
	ds_read_b128 v[202:205], v180 offset:0x400
	s_waitcnt lgkmcnt(3)
	s_nop 0
	v_mfma_f32_32x32x16_bf16 v[144:159], v[128:131], v[136:139], 0
	v_mfma_f32_32x32x16_bf16 v[128:143], v[132:135], v[136:139], 0
	ds_read_b128 v[206:209], v183 offset:0
	ds_read_b128 v[210:213], v183 offset:0x2000
	ds_read_b128 v[214:217], v180 offset:0x800
	s_waitcnt lgkmcnt(3)
	v_mfma_f32_32x32x16_bf16 v[144:159], v[194:197], v[202:205], v[144:159]
	v_mfma_f32_32x32x16_bf16 v[128:143], v[198:201], v[202:205], v[128:143]
	ds_read_b128 v[194:197], v184 offset:0
	ds_read_b128 v[198:201], v184 offset:0x2000
	ds_read_b128 v[202:205], v180 offset:0xc00
	s_waitcnt lgkmcnt(3)
	v_mfma_f32_32x32x16_bf16 v[144:159], v[206:209], v[214:217], v[144:159]
	v_mfma_f32_32x32x16_bf16 v[128:143], v[210:213], v[214:217], v[128:143]
	ds_read_b128 v[206:209], v181 offset:0x80
	ds_read_b128 v[210:213], v181 offset:0x2080
	ds_read_b128 v[214:217], v180 offset:0x1000
	s_waitcnt lgkmcnt(3)
	v_mfma_f32_32x32x16_bf16 v[144:159], v[194:197], v[202:205], v[144:159]
	v_mfma_f32_32x32x16_bf16 v[128:143], v[198:201], v[202:205], v[128:143]
	ds_read_b128 v[194:197], v182 offset:0x80
	ds_read_b128 v[198:201], v182 offset:0x2080
	ds_read_b128 v[202:205], v180 offset:0x1400
	s_waitcnt lgkmcnt(3)
	v_mfma_f32_32x32x16_bf16 v[144:159], v[206:209], v[214:217], v[144:159]
	v_mfma_f32_32x32x16_bf16 v[128:143], v[210:213], v[214:217], v[128:143]
	ds_read_b128 v[206:209], v183 offset:0x80
	ds_read_b128 v[210:213], v183 offset:0x2080
	ds_read_b128 v[214:217], v180 offset:0x1800
	s_waitcnt lgkmcnt(3)
	v_mfma_f32_32x32x16_bf16 v[144:159], v[194:197], v[202:205], v[144:159]
	v_mfma_f32_32x32x16_bf16 v[128:143], v[198:201], v[202:205], v[128:143]
	ds_read_b128 v[194:197], v184 offset:0x80
	ds_read_b128 v[198:201], v184 offset:0x2080
	s_waitcnt lgkmcnt(2)
	v_mfma_f32_32x32x16_bf16 v[144:159], v[206:209], v[214:217], v[144:159]
	v_mfma_f32_32x32x16_bf16 v[128:143], v[210:213], v[214:217], v[128:143]
	s_waitcnt lgkmcnt(0)
	v_mfma_f32_32x32x16_bf16 v[144:159], v[194:197], v[166:169], v[144:159]
	v_mfma_f32_32x32x16_bf16 v[128:143], v[198:201], v[166:169], v[128:143]
	s_bitcmp0_b32 s100, 8
	s_cbranch_scc1 .Lstg_a11
	s_waitcnt vmcnt(0)
	s_waitcnt lgkmcnt(0)
	s_barrier
.Lstg_a11:
	s_cmp_le_i32 s74, s82
	s_cbranch_scc1 .LBB0_567
	v_cmp_gt_i32_e64 s[62:63], 26, v189
	v_cmp_gt_i32_e64 s[64:65], 27, v189
	v_cmp_gt_i32_e64 s[60:61], 25, v189
	s_and_b64 s[62:63], s[64:65], s[62:63]
	v_cmp_gt_i32_e64 s[58:59], 24, v189
	s_and_b64 s[60:61], s[62:63], s[60:61]
	v_cmp_gt_i32_e64 s[56:57], 19, v189
	s_and_b64 s[58:59], s[60:61], s[58:59]
	v_cmp_gt_i32_e64 s[54:55], 18, v189
	s_and_b64 s[56:57], s[58:59], s[56:57]
	v_cmp_gt_i32_e64 s[52:53], 17, v189
	s_and_b64 s[54:55], s[56:57], s[54:55]
	v_cmp_gt_i32_e64 s[50:51], 16, v189
	s_and_b64 s[52:53], s[54:55], s[52:53]
	v_cmp_gt_i32_e64 s[48:49], 11, v189
	s_and_b64 s[50:51], s[52:53], s[50:51]
	v_cmp_gt_i32_e64 s[46:47], 10, v189
	s_and_b64 s[48:49], s[50:51], s[48:49]
	v_cmp_gt_i32_e64 s[44:45], 9, v189
	s_and_b64 s[46:47], s[48:49], s[46:47]
	v_cmp_gt_i32_e64 s[42:43], 8, v189
	s_and_b64 s[44:45], s[46:47], s[44:45]
	v_cmp_gt_i32_e64 s[40:41], 3, v189
	s_and_b64 s[42:43], s[44:45], s[42:43]
	v_cmp_gt_i32_e64 s[38:39], 2, v189
	s_and_b64 s[40:41], s[42:43], s[40:41]
	v_cmp_gt_i32_e64 s[36:37], 1, v189
	s_and_b64 s[38:39], s[40:41], s[38:39]
	v_cmp_gt_i32_e64 s[34:35], 0, v189
	s_and_b64 s[36:37], s[38:39], s[36:37]
	s_and_b64 s[34:35], s[36:37], s[34:35]
	v_cmp_gt_i32_e64 s[30:31], 58, v189
	v_cndmask_b32_e64 v144, v144, v226, s[34:35]
	v_cmp_gt_i32_e64 s[34:35], 59, v189
	v_cmp_gt_i32_e64 s[28:29], 57, v189
	s_and_b64 s[30:31], s[34:35], s[30:31]
	v_cmp_gt_i32_e64 s[26:27], 56, v189
	s_and_b64 s[28:29], s[30:31], s[28:29]
	v_cmp_gt_i32_e64 s[24:25], 51, v189
	s_and_b64 s[26:27], s[28:29], s[26:27]
	v_cmp_gt_i32_e64 s[22:23], 50, v189
	s_and_b64 s[24:25], s[26:27], s[24:25]
	v_cmp_gt_i32_e64 s[20:21], 49, v189
	s_and_b64 s[22:23], s[24:25], s[22:23]
	v_cmp_gt_i32_e64 s[18:19], 48, v189
	s_and_b64 s[20:21], s[22:23], s[20:21]
	v_cmp_gt_i32_e64 s[16:17], 43, v189
	s_and_b64 s[18:19], s[20:21], s[18:19]
	v_cmp_gt_i32_e64 s[14:15], 42, v189
	s_and_b64 s[16:17], s[18:19], s[16:17]
	v_cmp_gt_i32_e64 s[12:13], 41, v189
	s_and_b64 s[14:15], s[16:17], s[14:15]
	v_cmp_gt_i32_e64 s[10:11], 40, v189
	s_and_b64 s[12:13], s[14:15], s[12:13]
	v_cmp_gt_i32_e64 s[8:9], 35, v189
	s_and_b64 s[10:11], s[12:13], s[10:11]
	v_cmp_gt_i32_e64 s[6:7], 34, v189
	s_and_b64 s[8:9], s[10:11], s[8:9]
	v_cmp_gt_i32_e64 s[4:5], 33, v189
	s_and_b64 s[6:7], s[8:9], s[6:7]
	v_cmp_gt_i32_e32 vcc, 32, v189
	s_and_b64 s[4:5], s[6:7], s[4:5]
	s_and_b64 vcc, s[4:5], vcc
	v_cndmask_b32_e64 v159, v159, v226, s[64:65]
	v_cndmask_b32_e64 v158, v158, v226, s[62:63]
	s_mov_b64 s[62:63], 0x100
	v_cndmask_b32_e64 v157, v157, v226, s[60:61]
	v_cndmask_b32_e64 v156, v156, v226, s[58:59]
	v_cndmask_b32_e64 v155, v155, v226, s[56:57]
	v_cndmask_b32_e64 v154, v154, v226, s[54:55]
	v_cndmask_b32_e64 v153, v153, v226, s[52:53]
	v_cndmask_b32_e64 v152, v152, v226, s[50:51]
	v_cndmask_b32_e64 v151, v151, v226, s[48:49]
	v_cndmask_b32_e64 v150, v150, v226, s[46:47]
	v_cndmask_b32_e64 v149, v149, v226, s[44:45]
	v_cndmask_b32_e64 v148, v148, v226, s[42:43]
	v_cndmask_b32_e64 v147, v147, v226, s[40:41]
	v_cndmask_b32_e64 v146, v146, v226, s[38:39]
	v_cndmask_b32_e64 v145, v145, v226, s[36:37]
	v_cndmask_b32_e64 v143, v143, v226, s[34:35]
	v_cndmask_b32_e64 v142, v142, v226, s[30:31]
	v_cndmask_b32_e64 v141, v141, v226, s[28:29]
	v_cndmask_b32_e64 v140, v140, v226, s[26:27]
	v_cndmask_b32_e64 v139, v139, v226, s[24:25]
	v_cndmask_b32_e64 v138, v138, v226, s[22:23]
	v_cndmask_b32_e64 v137, v137, v226, s[20:21]
	v_cndmask_b32_e64 v136, v136, v226, s[18:19]
	v_cndmask_b32_e64 v135, v135, v226, s[16:17]
	v_cndmask_b32_e64 v134, v134, v226, s[14:15]
	v_cndmask_b32_e64 v133, v133, v226, s[12:13]
	v_cndmask_b32_e64 v132, v132, v226, s[10:11]
	v_cndmask_b32_e64 v131, v131, v226, s[8:9]
	v_cndmask_b32_e64 v130, v130, v226, s[6:7]
	v_cndmask_b32_e64 v129, v129, v226, s[4:5]
	v_cndmask_b32_e32 v128, v128, v226, vcc
.LBB0_567:
	s_nop 8
	v_max_f32_e32 v190, v145, v145
	v_max_f32_e32 v194, v144, v144
	v_max_f32_e32 v190, v194, v190
	v_max3_f32 v190, v190, v146, v147
	v_max3_f32 v190, v190, v148, v149
	v_max3_f32 v190, v190, v150, v151
	v_max3_f32 v190, v190, v152, v153
	v_max3_f32 v190, v190, v154, v155
	v_max3_f32 v190, v190, v156, v157
	v_max3_f32 v190, v190, v158, v159
	v_max3_f32 v190, v190, v128, v129
	v_max3_f32 v190, v190, v130, v131
	v_max3_f32 v190, v190, v132, v133
	v_max3_f32 v190, v190, v134, v135
	v_max3_f32 v190, v190, v136, v137
	v_max3_f32 v190, v190, v138, v139
	v_max3_f32 v190, v190, v140, v141
	v_max3_f32 v190, v190, v142, v143
	v_mov_b32_e32 v194, v190
	s_nop 1
	v_permlane32_swap_b32_e32 v190, v194
	v_max_f32_e32 v194, v194, v194
	v_max_f32_e32 v190, v190, v190
	v_max_f32_e32 v190, v190, v194
	v_sub_f32_e32 v194, v190, v193
	v_mul_f32_e32 v194, 0x3db504f3, v194
	s_mov_b32 s4, 0x41000000
	v_cmp_ge_f32_e32 vcc, s4, v194
	s_cmp_eq_u64 vcc, exec
	v_max_f32_e32 v194, v193, v193
	v_max_f32_e32 v198, v194, v190
	s_cselect_b64 s[4:5], -1, 0
	v_cndmask_b32_e64 v190, v198, v193, s[4:5]
	v_mul_f32_e32 v194, 0xbe0293ee, v190
	v_fmamk_f32 v144, v144, 0x3e0293ee, v194
	v_fmamk_f32 v145, v145, 0x3e0293ee, v194
	v_fmamk_f32 v146, v146, 0x3e0293ee, v194
	v_fmamk_f32 v147, v147, 0x3e0293ee, v194
	v_fmamk_f32 v148, v148, 0x3e0293ee, v194
	v_fmamk_f32 v149, v149, 0x3e0293ee, v194
	v_fmamk_f32 v150, v150, 0x3e0293ee, v194
	v_fmamk_f32 v151, v151, 0x3e0293ee, v194
	v_fmamk_f32 v152, v152, 0x3e0293ee, v194
	v_fmamk_f32 v153, v153, 0x3e0293ee, v194
	v_fmamk_f32 v154, v154, 0x3e0293ee, v194
	v_fmamk_f32 v155, v155, 0x3e0293ee, v194
	v_fmamk_f32 v156, v156, 0x3e0293ee, v194
	v_fmamk_f32 v157, v157, 0x3e0293ee, v194
	v_fmamk_f32 v158, v158, 0x3e0293ee, v194
	v_fmamk_f32 v159, v159, 0x3e0293ee, v194
	v_fmamk_f32 v128, v128, 0x3e0293ee, v194
	v_fmamk_f32 v129, v129, 0x3e0293ee, v194
	v_fmamk_f32 v130, v130, 0x3e0293ee, v194
	v_fmamk_f32 v131, v131, 0x3e0293ee, v194
	v_fmamk_f32 v132, v132, 0x3e0293ee, v194
	v_fmamk_f32 v133, v133, 0x3e0293ee, v194
	v_fmamk_f32 v134, v134, 0x3e0293ee, v194
	v_fmamk_f32 v135, v135, 0x3e0293ee, v194
	v_fmamk_f32 v136, v136, 0x3e0293ee, v194
	v_fmamk_f32 v137, v137, 0x3e0293ee, v194
	v_fmamk_f32 v138, v138, 0x3e0293ee, v194
	v_fmamk_f32 v139, v139, 0x3e0293ee, v194
	v_fmamk_f32 v140, v140, 0x3e0293ee, v194
	v_fmamk_f32 v141, v141, 0x3e0293ee, v194
	v_fmamk_f32 v142, v142, 0x3e0293ee, v194
	v_fmac_f32_e32 v194, 0x3e0293ee, v143
	v_exp_f32_e32 v143, v144
	v_exp_f32_e32 v144, v145
	v_exp_f32_e32 v195, v146
	v_exp_f32_e32 v147, v147
	v_exp_f32_e32 v148, v148
	v_exp_f32_e32 v196, v128
	v_add_f32_e32 v128, 0, v143
	v_exp_f32_e32 v149, v149
	v_add_f32_e32 v128, v144, v128
	v_exp_f32_e32 v150, v150
	v_add_f32_e32 v128, v195, v128
	v_exp_f32_e32 v151, v151
	v_add_f32_e32 v128, v147, v128
	v_exp_f32_e32 v152, v152
	v_add_f32_e32 v128, v148, v128
	v_exp_f32_e32 v153, v153
	v_add_f32_e32 v128, v149, v128
	v_exp_f32_e32 v154, v154
	v_add_f32_e32 v128, v150, v128
	v_exp_f32_e32 v155, v155
	v_add_f32_e32 v128, v151, v128
	v_exp_f32_e32 v156, v156
	v_add_f32_e32 v128, v152, v128
	v_exp_f32_e32 v157, v157
	v_add_f32_e32 v128, v153, v128
	v_exp_f32_e32 v158, v158
	v_add_f32_e32 v128, v154, v128
	v_exp_f32_e32 v159, v159
	v_add_f32_e32 v128, v155, v128
	v_add_f32_e32 v128, v156, v128
	v_exp_f32_e32 v197, v129
	v_add_f32_e32 v128, v157, v128
	v_exp_f32_e32 v199, v130
	v_add_f32_e32 v128, v158, v128
	v_exp_f32_e32 v200, v131
	v_add_f32_e32 v128, v159, v128
	v_exp_f32_e32 v201, v132
	v_add_f32_e32 v128, v196, v128
	v_exp_f32_e32 v202, v133
	v_add_f32_e32 v128, v197, v128
	v_exp_f32_e32 v203, v134
	v_add_f32_e32 v128, v199, v128
	v_exp_f32_e32 v204, v135
	v_add_f32_e32 v128, v200, v128
	v_exp_f32_e32 v205, v136
	v_add_f32_e32 v128, v201, v128
	v_exp_f32_e32 v206, v137
	v_add_f32_e32 v128, v202, v128
	v_exp_f32_e32 v207, v138
	v_add_f32_e32 v128, v203, v128
	v_exp_f32_e32 v208, v139
	v_add_f32_e32 v128, v204, v128
	v_exp_f32_e32 v209, v140
	v_add_f32_e32 v128, v205, v128
	v_exp_f32_e32 v210, v141
	v_add_f32_e32 v128, v206, v128
	v_exp_f32_e32 v211, v142
	v_add_f32_e32 v128, v207, v128
	v_exp_f32_e32 v194, v194
	v_add_f32_e32 v128, v208, v128
	v_add_f32_e32 v128, v209, v128
	v_add_f32_e32 v128, v210, v128
	v_add_f32_e32 v128, v211, v128
	v_add_f32_e32 v145, v194, v128
	v_mov_b32_e32 v146, v145
	v_cvt_pk_bf16_f32 v128, v143, v144
	v_cvt_pk_bf16_f32 v129, v195, v147
	v_cvt_pk_bf16_f32 v130, v148, v149
	v_cvt_pk_bf16_f32 v131, v150, v151
	v_cvt_pk_bf16_f32 v132, v152, v153
	v_cvt_pk_bf16_f32 v133, v154, v155
	v_cvt_pk_bf16_f32 v134, v156, v157
	v_cvt_pk_bf16_f32 v135, v158, v159
	v_cvt_pk_bf16_f32 v136, v196, v197
	v_cvt_pk_bf16_f32 v137, v199, v200
	v_cvt_pk_bf16_f32 v138, v201, v202
	v_cvt_pk_bf16_f32 v139, v203, v204
	v_cvt_pk_bf16_f32 v140, v205, v206
	v_cvt_pk_bf16_f32 v141, v207, v208
	v_cvt_pk_bf16_f32 v142, v209, v210
	v_cvt_pk_bf16_f32 v143, v211, v194
	s_nop 1
	v_permlane32_swap_b32_e32 v145, v146
	v_permlane32_swap_b32_e32 v128, v130
	v_permlane32_swap_b32_e32 v129, v131
	v_permlane32_swap_b32_e32 v132, v134
	v_permlane32_swap_b32_e32 v133, v135
	v_permlane32_swap_b32_e32 v136, v138
	v_permlane32_swap_b32_e32 v137, v139
	v_permlane32_swap_b32_e32 v140, v142
	v_permlane32_swap_b32_e32 v141, v143
	s_bitcmp1_b32 s100, 8
	s_cbranch_scc1 .Lstg_b15
	s_waitcnt vmcnt(0)
	s_waitcnt lgkmcnt(0)
	s_barrier
.Lstg_b15:
	s_cmp_gt_u32 s3, s75
	s_cbranch_scc1 .LBB0_572
	s_cmp_ge_u32 s3, s75
	s_mov_b64 s[6:7], -1
	s_cbranch_scc0 .LBB0_570
	v_mov_b64_e32 v[148:149], s[80:81]
	flat_load_dword v144, v[148:149] sc0 sc1
	s_waitcnt vmcnt(0)
	v_mov_b64_e32 v[148:149], s[72:73]
	flat_load_dword v147, v[148:149] sc0 sc1
	s_waitcnt vmcnt(0) lgkmcnt(0)
	v_readfirstlane_b32 s6, v144
	v_readfirstlane_b32 s7, v147
	s_nop 1
	v_lshl_add_u64 v[148:149], s[6:7], 0, v[160:161]
	s_mov_b32 s8, m0
	s_mov_b32 m0, s83
	s_nop 0
	global_load_lds_dwordx4 v[148:149], off
	s_mov_b32 m0, s8
	v_lshl_add_u64 v[148:149], s[6:7], 0, v[170:171]
	s_mov_b32 s6, m0
	s_mov_b32 m0, s78
	s_nop 0
	global_load_lds_dwordx4 v[148:149], off
	s_mov_b32 m0, s6
	s_mov_b64 s[6:7], 0

.LBB0_580:
	ds_read_b64_tr_b16 v[144:145], v177 offset:0
	ds_read_b64_tr_b16 v[146:147], v177 offset:0x1000
	ds_read_b64_tr_b16 v[148:149], v177 offset:0x2000
	ds_read_b64_tr_b16 v[150:151], v177 offset:0x3000
	ds_read_b64_tr_b16 v[152:153], v177 offset:0x4000
	ds_read_b64_tr_b16 v[154:155], v177 offset:0x5000
	ds_read_b64_tr_b16 v[156:157], v177 offset:0x6000
	ds_read_b64_tr_b16 v[158:159], v177 offset:0x7000
	ds_read_b64_tr_b16 v[192:193], v177 offset:0x200
	ds_read_b64_tr_b16 v[194:195], v177 offset:0x1200
	ds_read_b64_tr_b16 v[196:197], v177 offset:0x2200
	ds_read_b64_tr_b16 v[198:199], v177 offset:0x3200
	ds_read_b64_tr_b16 v[200:201], v177 offset:0x4200
	ds_read_b64_tr_b16 v[202:203], v177 offset:0x5200
	ds_read_b64_tr_b16 v[204:205], v177 offset:0x6200
	ds_read_b64_tr_b16 v[206:207], v177 offset:0x7200
	s_waitcnt lgkmcnt(8)
	s_nop 0
	v_mfma_f32_32x32x16_bf16 v[112:127], v[144:147], v[128:131], v[112:127]
	v_mfma_f32_32x32x16_bf16 v[112:127], v[148:151], v[132:135], v[112:127]
	v_mfma_f32_32x32x16_bf16 v[112:127], v[152:155], v[136:139], v[112:127]
	v_mfma_f32_32x32x16_bf16 v[112:127], v[156:159], v[140:143], v[112:127]
	ds_read_b64_tr_b16 v[144:145], v177 offset:0x400
	ds_read_b64_tr_b16 v[146:147], v177 offset:0x1400
	ds_read_b64_tr_b16 v[148:149], v177 offset:0x2400
	ds_read_b64_tr_b16 v[150:151], v177 offset:0x3400
	ds_read_b64_tr_b16 v[152:153], v177 offset:0x4400
	ds_read_b64_tr_b16 v[154:155], v177 offset:0x5400
	ds_read_b64_tr_b16 v[156:157], v177 offset:0x6400
	ds_read_b64_tr_b16 v[158:159], v177 offset:0x7400
	s_waitcnt lgkmcnt(8)
	v_mfma_f32_32x32x16_bf16 v[80:95], v[192:195], v[128:131], v[80:95]
	v_mfma_f32_32x32x16_bf16 v[80:95], v[196:199], v[132:135], v[80:95]
	v_mfma_f32_32x32x16_bf16 v[80:95], v[200:203], v[136:139], v[80:95]
	v_mfma_f32_32x32x16_bf16 v[80:95], v[204:207], v[140:143], v[80:95]
	ds_read_b64_tr_b16 v[192:193], v177 offset:0x600
	ds_read_b64_tr_b16 v[194:195], v177 offset:0x1600
	ds_read_b64_tr_b16 v[196:197], v177 offset:0x2600
	ds_read_b64_tr_b16 v[198:199], v177 offset:0x3600
	ds_read_b64_tr_b16 v[200:201], v177 offset:0x4600
	ds_read_b64_tr_b16 v[202:203], v177 offset:0x5600
	ds_read_b64_tr_b16 v[204:205], v177 offset:0x6600
	ds_read_b64_tr_b16 v[206:207], v177 offset:0x7600
	s_waitcnt lgkmcnt(8)
	v_mfma_f32_32x32x16_bf16 v[96:111], v[144:147], v[128:131], v[96:111]
	v_mfma_f32_32x32x16_bf16 v[96:111], v[148:151], v[132:135], v[96:111]
	v_mfma_f32_32x32x16_bf16 v[96:111], v[152:155], v[136:139], v[96:111]
	v_mfma_f32_32x32x16_bf16 v[96:111], v[156:159], v[140:143], v[96:111]
	ds_read_b64_tr_b16 v[144:145], v177 offset:0x800
	ds_read_b64_tr_b16 v[146:147], v177 offset:0x1800
	ds_read_b64_tr_b16 v[148:149], v177 offset:0x2800
	ds_read_b64_tr_b16 v[150:151], v177 offset:0x3800
	ds_read_b64_tr_b16 v[152:153], v177 offset:0x4800
	ds_read_b64_tr_b16 v[154:155], v177 offset:0x5800
	ds_read_b64_tr_b16 v[156:157], v177 offset:0x6800
	ds_read_b64_tr_b16 v[158:159], v177 offset:0x7800
	s_waitcnt lgkmcnt(8)
	v_mfma_f32_32x32x16_bf16 v[64:79], v[192:195], v[128:131], v[64:79]
	v_mfma_f32_32x32x16_bf16 v[64:79], v[196:199], v[132:135], v[64:79]
	v_mfma_f32_32x32x16_bf16 v[64:79], v[200:203], v[136:139], v[64:79]
	v_mfma_f32_32x32x16_bf16 v[64:79], v[204:207], v[140:143], v[64:79]
	ds_read_b64_tr_b16 v[192:193], v177 offset:0xa00
	ds_read_b64_tr_b16 v[194:195], v177 offset:0x1a00
	ds_read_b64_tr_b16 v[196:197], v177 offset:0x2a00
	ds_read_b64_tr_b16 v[198:199], v177 offset:0x3a00
	ds_read_b64_tr_b16 v[200:201], v177 offset:0x4a00
	ds_read_b64_tr_b16 v[202:203], v177 offset:0x5a00
	ds_read_b64_tr_b16 v[204:205], v177 offset:0x6a00
	ds_read_b64_tr_b16 v[206:207], v177 offset:0x7a00
	s_waitcnt lgkmcnt(8)
	v_mfma_f32_32x32x16_bf16 v[48:63], v[144:147], v[128:131], v[48:63]
	v_mfma_f32_32x32x16_bf16 v[48:63], v[148:151], v[132:135], v[48:63]
	v_mfma_f32_32x32x16_bf16 v[48:63], v[152:155], v[136:139], v[48:63]
	v_mfma_f32_32x32x16_bf16 v[48:63], v[156:159], v[140:143], v[48:63]
	ds_read_b64_tr_b16 v[144:145], v177 offset:0xc00
	ds_read_b64_tr_b16 v[146:147], v177 offset:0x1c00
	ds_read_b64_tr_b16 v[148:149], v177 offset:0x2c00
	ds_read_b64_tr_b16 v[150:151], v177 offset:0x3c00
	ds_read_b64_tr_b16 v[152:153], v177 offset:0x4c00
	ds_read_b64_tr_b16 v[154:155], v177 offset:0x5c00
	ds_read_b64_tr_b16 v[156:157], v177 offset:0x6c00
	ds_read_b64_tr_b16 v[158:159], v177 offset:0x7c00
	s_waitcnt lgkmcnt(8)
	v_mfma_f32_32x32x16_bf16 v[32:47], v[192:195], v[128:131], v[32:47]
	v_mfma_f32_32x32x16_bf16 v[32:47], v[196:199], v[132:135], v[32:47]
	v_mfma_f32_32x32x16_bf16 v[32:47], v[200:203], v[136:139], v[32:47]
	v_mfma_f32_32x32x16_bf16 v[32:47], v[204:207], v[140:143], v[32:47]
	ds_read_b64_tr_b16 v[192:193], v177 offset:0xe00
	ds_read_b64_tr_b16 v[194:195], v177 offset:0x1e00
	ds_read_b64_tr_b16 v[196:197], v177 offset:0x2e00
	ds_read_b64_tr_b16 v[198:199], v177 offset:0x3e00
	ds_read_b64_tr_b16 v[200:201], v177 offset:0x4e00
	ds_read_b64_tr_b16 v[202:203], v177 offset:0x5e00
	ds_read_b64_tr_b16 v[204:205], v177 offset:0x6e00
	ds_read_b64_tr_b16 v[206:207], v177 offset:0x7e00
	s_waitcnt lgkmcnt(8)
	v_mfma_f32_32x32x16_bf16 v[16:31], v[144:147], v[128:131], v[16:31]
	v_mfma_f32_32x32x16_bf16 v[16:31], v[148:151], v[132:135], v[16:31]
	v_mfma_f32_32x32x16_bf16 v[16:31], v[152:155], v[136:139], v[16:31]
	v_mfma_f32_32x32x16_bf16 v[16:31], v[156:159], v[140:143], v[16:31]
	s_waitcnt lgkmcnt(0)
	v_mfma_f32_32x32x16_bf16 v[0:15], v[192:195], v[128:131], v[0:15]
	v_mfma_f32_32x32x16_bf16 v[0:15], v[196:199], v[132:135], v[0:15]
	v_mfma_f32_32x32x16_bf16 v[0:15], v[200:203], v[136:139], v[0:15]
	v_mfma_f32_32x32x16_bf16 v[0:15], v[204:207], v[140:143], v[0:15]
	ds_read_b128 v[128:131], v188 offset:0
	ds_read_b128 v[132:135], v188 offset:0x2000
	ds_read_b128 v[136:139], v180 offset:0
	ds_read_b128 v[192:195], v187 offset:0
	ds_read_b128 v[196:199], v187 offset:0x2000
	ds_read_b128 v[200:203], v180 offset:0x400
	s_waitcnt lgkmcnt(3)
	s_nop 0
	v_mfma_f32_32x32x16_bf16 v[144:159], v[128:131], v[136:139], 0
	v_mfma_f32_32x32x16_bf16 v[128:143], v[132:135], v[136:139], 0
	ds_read_b128 v[204:207], v186 offset:0
	ds_read_b128 v[208:211], v186 offset:0x2000
	ds_read_b128 v[212:215], v180 offset:0x800
	s_waitcnt lgkmcnt(3)
	v_mfma_f32_32x32x16_bf16 v[144:159], v[192:195], v[200:203], v[144:159]
	v_mfma_f32_32x32x16_bf16 v[128:143], v[196:199], v[200:203], v[128:143]
	ds_read_b128 v[192:195], v185 offset:0
	ds_read_b128 v[196:199], v185 offset:0x2000
	ds_read_b128 v[200:203], v180 offset:0xc00
	s_waitcnt lgkmcnt(3)
	v_mfma_f32_32x32x16_bf16 v[144:159], v[204:207], v[212:215], v[144:159]
	v_mfma_f32_32x32x16_bf16 v[128:143], v[208:211], v[212:215], v[128:143]
	ds_read_b128 v[204:207], v188 offset:0x80
	ds_read_b128 v[208:211], v188 offset:0x2080
	ds_read_b128 v[212:215], v180 offset:0x1000
	s_waitcnt lgkmcnt(3)
	v_mfma_f32_32x32x16_bf16 v[144:159], v[192:195], v[200:203], v[144:159]
	v_mfma_f32_32x32x16_bf16 v[128:143], v[196:199], v[200:203], v[128:143]
	ds_read_b128 v[192:195], v187 offset:0x80
	ds_read_b128 v[196:199], v187 offset:0x2080
	ds_read_b128 v[200:203], v180 offset:0x1400
	s_waitcnt lgkmcnt(3)
	v_mfma_f32_32x32x16_bf16 v[144:159], v[204:207], v[212:215], v[144:159]
	v_mfma_f32_32x32x16_bf16 v[128:143], v[208:211], v[212:215], v[128:143]
	ds_read_b128 v[204:207], v186 offset:0x80
	ds_read_b128 v[208:211], v186 offset:0x2080
	ds_read_b128 v[186:189], v180 offset:0x1800
	s_waitcnt lgkmcnt(3)
	v_mfma_f32_32x32x16_bf16 v[144:159], v[192:195], v[200:203], v[144:159]
	v_mfma_f32_32x32x16_bf16 v[128:143], v[196:199], v[200:203], v[128:143]
	ds_read_b128 v[180:183], v185 offset:0x80
	ds_read_b128 v[192:195], v185 offset:0x2080
	s_waitcnt lgkmcnt(2)
	v_mfma_f32_32x32x16_bf16 v[144:159], v[204:207], v[186:189], v[144:159]
	v_mfma_f32_32x32x16_bf16 v[128:143], v[208:211], v[186:189], v[128:143]
	s_waitcnt lgkmcnt(0)
	v_mfma_f32_32x32x16_bf16 v[144:159], v[180:183], v[166:169], v[144:159]
	v_mfma_f32_32x32x16_bf16 v[128:143], v[192:195], v[166:169], v[128:143]
	s_bitcmp0_b32 s100, 8
	s_cbranch_scc1 .Lstg_a12
	s_waitcnt vmcnt(0)
	s_waitcnt lgkmcnt(0)
	s_barrier
.Lstg_a12:
	s_or_b32 s96, s33, 0xc0
	s_mov_b32 s74, s33
	s_cmp_lt_i32 s79, 8
	s_cbranch_scc0 .LBB0_582
	v_subrev_u32_e32 v160, s96, v179
	v_cmp_gt_i32_e64 s[62:63], 26, v160
	v_cmp_gt_i32_e64 s[64:65], 27, v160
	v_cmp_gt_i32_e64 s[60:61], 25, v160
	s_and_b64 s[62:63], s[64:65], s[62:63]
	v_cmp_gt_i32_e64 s[58:59], 24, v160
	s_and_b64 s[60:61], s[62:63], s[60:61]
	v_cmp_gt_i32_e64 s[56:57], 19, v160
	s_and_b64 s[58:59], s[60:61], s[58:59]
	v_cmp_gt_i32_e64 s[54:55], 18, v160
	s_and_b64 s[56:57], s[58:59], s[56:57]
	v_cmp_gt_i32_e64 s[52:53], 17, v160
	s_and_b64 s[54:55], s[56:57], s[54:55]
	v_cmp_gt_i32_e64 s[50:51], 16, v160
	s_and_b64 s[52:53], s[54:55], s[52:53]
	v_cmp_gt_i32_e64 s[48:49], 11, v160
	s_and_b64 s[50:51], s[52:53], s[50:51]
	v_cmp_gt_i32_e64 s[46:47], 10, v160
	s_and_b64 s[48:49], s[50:51], s[48:49]
	v_cmp_gt_i32_e64 s[44:45], 9, v160
	s_and_b64 s[46:47], s[48:49], s[46:47]
	v_cmp_gt_i32_e64 s[42:43], 8, v160
	s_and_b64 s[44:45], s[46:47], s[44:45]
	v_cmp_gt_i32_e64 s[40:41], 3, v160
	s_and_b64 s[42:43], s[44:45], s[42:43]
	v_cmp_gt_i32_e64 s[38:39], 2, v160
	s_and_b64 s[40:41], s[42:43], s[40:41]
	v_cmp_gt_i32_e64 s[36:37], 1, v160
	s_and_b64 s[38:39], s[40:41], s[38:39]
	v_cmp_gt_i32_e64 s[34:35], 0, v160
	s_and_b64 s[36:37], s[38:39], s[36:37]
	s_and_b64 s[34:35], s[36:37], s[34:35]
	v_cmp_gt_i32_e64 s[30:31], 58, v160
	v_cndmask_b32_e64 v144, v144, v226, s[34:35]
	v_cmp_gt_i32_e64 s[34:35], 59, v160
	v_cmp_gt_i32_e64 s[28:29], 57, v160
	s_and_b64 s[30:31], s[34:35], s[30:31]
	v_cmp_gt_i32_e64 s[26:27], 56, v160
	s_and_b64 s[28:29], s[30:31], s[28:29]
	v_cmp_gt_i32_e64 s[24:25], 51, v160
	s_and_b64 s[26:27], s[28:29], s[26:27]
	v_cmp_gt_i32_e64 s[22:23], 50, v160
	s_and_b64 s[24:25], s[26:27], s[24:25]
	v_cmp_gt_i32_e64 s[20:21], 49, v160
	s_and_b64 s[22:23], s[24:25], s[22:23]
	v_cmp_gt_i32_e64 s[18:19], 48, v160
	s_and_b64 s[20:21], s[22:23], s[20:21]
	v_cmp_gt_i32_e64 s[16:17], 43, v160
	s_and_b64 s[18:19], s[20:21], s[18:19]
	v_cmp_gt_i32_e64 s[14:15], 42, v160
	s_and_b64 s[16:17], s[18:19], s[16:17]
	v_cmp_gt_i32_e64 s[12:13], 41, v160
	s_and_b64 s[14:15], s[16:17], s[14:15]
	v_cmp_gt_i32_e64 s[10:11], 40, v160
	s_and_b64 s[12:13], s[14:15], s[12:13]
	v_cmp_gt_i32_e64 s[8:9], 35, v160
	s_and_b64 s[10:11], s[12:13], s[10:11]
	v_cmp_gt_i32_e64 s[6:7], 34, v160
	s_and_b64 s[8:9], s[10:11], s[8:9]
	v_cmp_gt_i32_e64 s[4:5], 33, v160
	s_and_b64 s[6:7], s[8:9], s[6:7]
	v_cmp_gt_i32_e32 vcc, 32, v160
	s_and_b64 s[4:5], s[6:7], s[4:5]
	s_and_b64 vcc, s[4:5], vcc
	v_cndmask_b32_e64 v159, v159, v226, s[64:65]
	v_cndmask_b32_e64 v158, v158, v226, s[62:63]
	s_mov_b64 s[62:63], 0x100
	v_cndmask_b32_e64 v157, v157, v226, s[60:61]
	v_cndmask_b32_e64 v156, v156, v226, s[58:59]
	v_cndmask_b32_e64 v155, v155, v226, s[56:57]
	v_cndmask_b32_e64 v154, v154, v226, s[54:55]
	v_cndmask_b32_e64 v153, v153, v226, s[52:53]
	v_cndmask_b32_e64 v152, v152, v226, s[50:51]
	v_cndmask_b32_e64 v151, v151, v226, s[48:49]
	v_cndmask_b32_e64 v150, v150, v226, s[46:47]
	v_cndmask_b32_e64 v149, v149, v226, s[44:45]
	v_cndmask_b32_e64 v148, v148, v226, s[42:43]
	v_cndmask_b32_e64 v147, v147, v226, s[40:41]
	v_cndmask_b32_e64 v146, v146, v226, s[38:39]
	v_cndmask_b32_e64 v145, v145, v226, s[36:37]
	v_cndmask_b32_e64 v143, v143, v226, s[34:35]
	v_cndmask_b32_e64 v142, v142, v226, s[30:31]
	v_cndmask_b32_e64 v141, v141, v226, s[28:29]
	v_cndmask_b32_e64 v140, v140, v226, s[26:27]
	v_cndmask_b32_e64 v139, v139, v226, s[24:25]
	v_cndmask_b32_e64 v138, v138, v226, s[22:23]
	v_cndmask_b32_e64 v137, v137, v226, s[20:21]
	v_cndmask_b32_e64 v136, v136, v226, s[18:19]
	v_cndmask_b32_e64 v135, v135, v226, s[16:17]
	v_cndmask_b32_e64 v134, v134, v226, s[14:15]
	v_cndmask_b32_e64 v133, v133, v226, s[12:13]
	v_cndmask_b32_e64 v132, v132, v226, s[10:11]
	v_cndmask_b32_e64 v131, v131, v226, s[8:9]
	v_cndmask_b32_e64 v130, v130, v226, s[6:7]
	v_cndmask_b32_e64 v129, v129, v226, s[4:5]
	v_cndmask_b32_e32 v128, v128, v226, vcc
.LBB0_582:
	s_nop 6
	v_max_f32_e32 v160, v145, v145
	v_max_f32_e32 v166, v144, v144
	v_max_f32_e32 v160, v166, v160
	v_max3_f32 v160, v160, v146, v147
	v_max3_f32 v160, v160, v148, v149
	v_max3_f32 v160, v160, v150, v151
	v_max3_f32 v160, v160, v152, v153
	v_max3_f32 v160, v160, v154, v155
	v_max3_f32 v160, v160, v156, v157
	v_max3_f32 v160, v160, v158, v159
	v_max3_f32 v160, v160, v128, v129
	v_max3_f32 v160, v160, v130, v131
	v_max3_f32 v160, v160, v132, v133
	v_max3_f32 v160, v160, v134, v135
	v_max3_f32 v160, v160, v136, v137
	v_max3_f32 v160, v160, v138, v139
	v_max3_f32 v160, v160, v140, v141
	v_max3_f32 v160, v160, v142, v143
	v_mov_b32_e32 v166, v160
	s_nop 1
	v_permlane32_swap_b32_e32 v160, v166
	v_max_f32_e32 v166, v166, v166
	v_max_f32_e32 v160, v160, v160
	v_max_f32_e32 v160, v160, v166
	v_sub_f32_e32 v166, v160, v190
	v_mul_f32_e32 v166, 0x3db504f3, v166
	s_mov_b32 s3, 0x41000000
	v_cmp_ge_f32_e32 vcc, s3, v166
	s_cmp_eq_u64 vcc, exec
	v_max_f32_e32 v166, v190, v190
	s_cselect_b64 vcc, -1, 0
	v_max_f32_e32 v166, v166, v160
	v_sub_f32_e32 v160, v190, v166
	v_cndmask_b32_e32 v166, v166, v190, vcc
	v_mul_f32_e32 v166, 0xbe0293ee, v166
	v_fmamk_f32 v144, v144, 0x3e0293ee, v166
	v_fmamk_f32 v145, v145, 0x3e0293ee, v166
	v_fmamk_f32 v146, v146, 0x3e0293ee, v166
	v_fmamk_f32 v147, v147, 0x3e0293ee, v166
	v_fmamk_f32 v148, v148, 0x3e0293ee, v166
	v_fmamk_f32 v149, v149, 0x3e0293ee, v166
	v_fmamk_f32 v150, v150, 0x3e0293ee, v166
	v_fmamk_f32 v151, v151, 0x3e0293ee, v166
	v_fmamk_f32 v152, v152, 0x3e0293ee, v166
	v_fmamk_f32 v153, v153, 0x3e0293ee, v166
	v_fmamk_f32 v154, v154, 0x3e0293ee, v166
	v_fmamk_f32 v155, v155, 0x3e0293ee, v166
	v_fmamk_f32 v156, v156, 0x3e0293ee, v166
	v_fmamk_f32 v157, v157, 0x3e0293ee, v166
	v_fmamk_f32 v158, v158, 0x3e0293ee, v166
	v_fmamk_f32 v159, v159, 0x3e0293ee, v166
	v_fmamk_f32 v128, v128, 0x3e0293ee, v166
	v_fmamk_f32 v129, v129, 0x3e0293ee, v166
	v_fmamk_f32 v130, v130, 0x3e0293ee, v166
	v_fmamk_f32 v131, v131, 0x3e0293ee, v166
	v_fmamk_f32 v132, v132, 0x3e0293ee, v166
	v_fmamk_f32 v133, v133, 0x3e0293ee, v166
	v_fmamk_f32 v134, v134, 0x3e0293ee, v166
	v_fmamk_f32 v135, v135, 0x3e0293ee, v166
	v_fmamk_f32 v136, v136, 0x3e0293ee, v166
	v_fmamk_f32 v137, v137, 0x3e0293ee, v166
	v_fmamk_f32 v138, v138, 0x3e0293ee, v166
	v_fmamk_f32 v139, v139, 0x3e0293ee, v166
	v_fmamk_f32 v140, v140, 0x3e0293ee, v166
	v_fmamk_f32 v141, v141, 0x3e0293ee, v166
	v_fmamk_f32 v142, v142, 0x3e0293ee, v166
	v_fmac_f32_e32 v166, 0x3e0293ee, v143
	v_exp_f32_e32 v143, v144
	v_exp_f32_e32 v167, v145
	v_exp_f32_e32 v146, v146
	v_exp_f32_e32 v147, v147
	v_exp_f32_e32 v148, v148
	v_exp_f32_e32 v168, v128
	v_add_f32_e32 v128, 0, v143
	v_exp_f32_e32 v149, v149
	v_add_f32_e32 v128, v167, v128
	v_exp_f32_e32 v150, v150
	v_add_f32_e32 v128, v146, v128
	v_exp_f32_e32 v151, v151
	v_add_f32_e32 v128, v147, v128
	v_exp_f32_e32 v152, v152
	v_add_f32_e32 v128, v148, v128
	v_exp_f32_e32 v153, v153
	v_add_f32_e32 v128, v149, v128
	v_exp_f32_e32 v154, v154
	v_add_f32_e32 v128, v150, v128
	v_exp_f32_e32 v155, v155
	v_add_f32_e32 v128, v151, v128
	v_exp_f32_e32 v156, v156
	v_add_f32_e32 v128, v152, v128
	v_exp_f32_e32 v157, v157
	v_add_f32_e32 v128, v153, v128
	v_exp_f32_e32 v158, v158
	v_add_f32_e32 v128, v154, v128
	v_exp_f32_e32 v159, v159
	v_add_f32_e32 v128, v155, v128
	v_add_f32_e32 v128, v156, v128
	v_exp_f32_e32 v169, v129
	v_add_f32_e32 v128, v157, v128
	v_exp_f32_e32 v170, v130
	v_add_f32_e32 v128, v158, v128
	v_exp_f32_e32 v171, v131
	v_add_f32_e32 v128, v159, v128
	v_exp_f32_e32 v172, v132
	v_add_f32_e32 v128, v168, v128
	v_exp_f32_e32 v179, v133
	v_add_f32_e32 v128, v169, v128
	v_exp_f32_e32 v180, v134
	v_add_f32_e32 v128, v170, v128
	v_exp_f32_e32 v181, v135
	v_add_f32_e32 v128, v171, v128
	v_exp_f32_e32 v182, v136
	v_add_f32_e32 v128, v172, v128
	v_exp_f32_e32 v183, v137
	v_add_f32_e32 v128, v179, v128
	v_exp_f32_e32 v184, v138
	v_add_f32_e32 v128, v180, v128
	v_exp_f32_e32 v185, v139
	v_add_f32_e32 v128, v181, v128
	v_exp_f32_e32 v186, v140
	v_add_f32_e32 v128, v182, v128
	v_exp_f32_e32 v187, v141
	v_add_f32_e32 v128, v183, v128
	v_exp_f32_e32 v188, v142
	v_add_f32_e32 v128, v184, v128
	v_exp_f32_e32 v166, v166
	v_add_f32_e32 v128, v185, v128
	v_mul_f32_e32 v160, 0x3e0293ee, v160
	v_add_f32_e32 v128, v186, v128
	v_exp_f32_e32 v160, v160
	v_add_f32_e32 v128, v187, v128
	v_add_f32_e32 v128, v188, v128
	v_add_f32_e32 v144, v166, v128
	v_mov_b32_e32 v145, v144
	v_cvt_pk_bf16_f32 v128, v143, v167
	v_cvt_pk_bf16_f32 v129, v146, v147
	v_cvt_pk_bf16_f32 v130, v148, v149
	v_cvt_pk_bf16_f32 v131, v150, v151
	v_cvt_pk_bf16_f32 v132, v152, v153
	v_cvt_pk_bf16_f32 v133, v154, v155
	v_cvt_pk_bf16_f32 v134, v156, v157
	v_cvt_pk_bf16_f32 v135, v158, v159
	v_cvt_pk_bf16_f32 v136, v168, v169
	v_cvt_pk_bf16_f32 v137, v170, v171
	v_cvt_pk_bf16_f32 v138, v172, v179
	v_cvt_pk_bf16_f32 v139, v180, v181
	v_cvt_pk_bf16_f32 v140, v182, v183
	v_cvt_pk_bf16_f32 v141, v184, v185
	v_cvt_pk_bf16_f32 v142, v186, v187
	v_cvt_pk_bf16_f32 v143, v188, v166
	s_movk_i32 s14, 0x6800
	v_readlane_b32 s33, v255, 48
	v_readlane_b32 s6, v255, 25
	v_readlane_b32 s66, v255, 26
	v_readlane_b32 s67, v255, 31
	v_cndmask_b32_e64 v160, v160, 1.0, vcc
	v_permlane32_swap_b32_e32 v144, v145
	v_permlane32_swap_b32_e32 v128, v130
	v_permlane32_swap_b32_e32 v129, v131
	v_permlane32_swap_b32_e32 v132, v134
	v_permlane32_swap_b32_e32 v133, v135
	v_permlane32_swap_b32_e32 v136, v138
	v_permlane32_swap_b32_e32 v137, v139
	v_permlane32_swap_b32_e32 v140, v142
	v_permlane32_swap_b32_e32 v141, v143
	s_bitcmp1_b32 s100, 8
	s_cbranch_scc1 .Lstg_b16
	s_waitcnt vmcnt(0)
	s_waitcnt lgkmcnt(0)
	s_barrier
.Lstg_b16:
	v_mov_b64_e32 v[146:147], s[0:1]
	flat_load_dword v148, v[146:147] sc0 sc1
	s_waitcnt vmcnt(0)
	v_mov_b64_e32 v[146:147], s[70:71]
	flat_load_dword v146, v[146:147] sc0 sc1
	s_waitcnt vmcnt(0) lgkmcnt(0)
	v_readfirstlane_b32 s4, v148
	v_readfirstlane_b32 s5, v146
	s_nop 1
	v_lshl_add_u64 v[146:147], s[4:5], 0, v[162:163]
	s_mov_b32 s3, m0
	s_mov_b32 m0, s93
	s_nop 0
	global_load_lds_dwordx4 v[146:147], off
	s_mov_b32 m0, s3
	v_lshl_add_u64 v[148:149], v[146:147], 0, s[86:87]
	s_mov_b32 s3, m0
	s_mov_b32 m0, s2
	s_nop 0
	global_load_lds_dwordx4 v[148:149], off
	s_mov_b32 m0, s3
	v_lshl_add_u64 v[148:149], v[146:147], 0, s[62:63]
	s_mov_b32 s2, m0
	s_mov_b32 m0, s69
	s_nop 0
	global_load_lds_dwordx4 v[148:149], off
	s_mov_b32 m0, s2
	s_mov_b64 s[2:3], 0x180
	v_lshl_add_u64 v[146:147], v[146:147], 0, s[2:3]
	s_mov_b32 s2, m0
	s_mov_b32 m0, s68
	s_nop 0
	global_load_lds_dwordx4 v[146:147], off
	s_mov_b32 m0, s2
	v_cmp_gt_f32_e32 vcc, 1.0, v160
	s_cbranch_vccz .LBB0_584
	v_pk_mul_f32 v[126:127], v[126:127], v[160:161] op_sel_hi:[1,0]
	v_pk_mul_f32 v[124:125], v[124:125], v[160:161] op_sel_hi:[1,0]
	v_pk_mul_f32 v[122:123], v[122:123], v[160:161] op_sel_hi:[1,0]
	v_pk_mul_f32 v[120:121], v[120:121], v[160:161] op_sel_hi:[1,0]
	v_pk_mul_f32 v[118:119], v[118:119], v[160:161] op_sel_hi:[1,0]
	v_pk_mul_f32 v[116:117], v[116:117], v[160:161] op_sel_hi:[1,0]
	v_pk_mul_f32 v[114:115], v[114:115], v[160:161] op_sel_hi:[1,0]
	v_pk_mul_f32 v[112:113], v[112:113], v[160:161] op_sel_hi:[1,0]
	v_pk_mul_f32 v[94:95], v[94:95], v[160:161] op_sel_hi:[1,0]
	v_pk_mul_f32 v[92:93], v[92:93], v[160:161] op_sel_hi:[1,0]
	v_pk_mul_f32 v[90:91], v[90:91], v[160:161] op_sel_hi:[1,0]
	v_pk_mul_f32 v[88:89], v[88:89], v[160:161] op_sel_hi:[1,0]
	v_pk_mul_f32 v[86:87], v[86:87], v[160:161] op_sel_hi:[1,0]
	v_pk_mul_f32 v[84:85], v[84:85], v[160:161] op_sel_hi:[1,0]
	v_pk_mul_f32 v[82:83], v[82:83], v[160:161] op_sel_hi:[1,0]
	v_pk_mul_f32 v[80:81], v[80:81], v[160:161] op_sel_hi:[1,0]
	v_pk_mul_f32 v[110:111], v[110:111], v[160:161] op_sel_hi:[1,0]
	v_pk_mul_f32 v[108:109], v[108:109], v[160:161] op_sel_hi:[1,0]
	v_pk_mul_f32 v[106:107], v[106:107], v[160:161] op_sel_hi:[1,0]
	v_pk_mul_f32 v[104:105], v[104:105], v[160:161] op_sel_hi:[1,0]
	v_pk_mul_f32 v[102:103], v[102:103], v[160:161] op_sel_hi:[1,0]
	v_pk_mul_f32 v[100:101], v[100:101], v[160:161] op_sel_hi:[1,0]
	v_pk_mul_f32 v[98:99], v[98:99], v[160:161] op_sel_hi:[1,0]
	v_pk_mul_f32 v[96:97], v[96:97], v[160:161] op_sel_hi:[1,0]
	v_pk_mul_f32 v[78:79], v[78:79], v[160:161] op_sel_hi:[1,0]
	v_pk_mul_f32 v[76:77], v[76:77], v[160:161] op_sel_hi:[1,0]
	v_pk_mul_f32 v[74:75], v[74:75], v[160:161] op_sel_hi:[1,0]
	v_pk_mul_f32 v[72:73], v[72:73], v[160:161] op_sel_hi:[1,0]
	v_pk_mul_f32 v[70:71], v[70:71], v[160:161] op_sel_hi:[1,0]
	v_pk_mul_f32 v[68:69], v[68:69], v[160:161] op_sel_hi:[1,0]
	v_pk_mul_f32 v[66:67], v[66:67], v[160:161] op_sel_hi:[1,0]
	v_pk_mul_f32 v[64:65], v[64:65], v[160:161] op_sel_hi:[1,0]
	v_pk_mul_f32 v[62:63], v[62:63], v[160:161] op_sel_hi:[1,0]
	v_pk_mul_f32 v[60:61], v[60:61], v[160:161] op_sel_hi:[1,0]
	v_pk_mul_f32 v[58:59], v[58:59], v[160:161] op_sel_hi:[1,0]
	v_pk_mul_f32 v[56:57], v[56:57], v[160:161] op_sel_hi:[1,0]
	v_pk_mul_f32 v[54:55], v[54:55], v[160:161] op_sel_hi:[1,0]
	v_pk_mul_f32 v[52:53], v[52:53], v[160:161] op_sel_hi:[1,0]
	v_pk_mul_f32 v[50:51], v[50:51], v[160:161] op_sel_hi:[1,0]
	v_pk_mul_f32 v[48:49], v[48:49], v[160:161] op_sel_hi:[1,0]
	v_pk_mul_f32 v[46:47], v[46:47], v[160:161] op_sel_hi:[1,0]
	v_pk_mul_f32 v[44:45], v[44:45], v[160:161] op_sel_hi:[1,0]
	v_pk_mul_f32 v[42:43], v[42:43], v[160:161] op_sel_hi:[1,0]
	v_pk_mul_f32 v[40:41], v[40:41], v[160:161] op_sel_hi:[1,0]
	v_pk_mul_f32 v[38:39], v[38:39], v[160:161] op_sel_hi:[1,0]
	v_pk_mul_f32 v[36:37], v[36:37], v[160:161] op_sel_hi:[1,0]
	v_pk_mul_f32 v[34:35], v[34:35], v[160:161] op_sel_hi:[1,0]
	v_pk_mul_f32 v[32:33], v[32:33], v[160:161] op_sel_hi:[1,0]
	v_pk_mul_f32 v[30:31], v[30:31], v[160:161] op_sel_hi:[1,0]
	v_pk_mul_f32 v[28:29], v[28:29], v[160:161] op_sel_hi:[1,0]
	v_pk_mul_f32 v[26:27], v[26:27], v[160:161] op_sel_hi:[1,0]
	v_pk_mul_f32 v[24:25], v[24:25], v[160:161] op_sel_hi:[1,0]
	v_pk_mul_f32 v[22:23], v[22:23], v[160:161] op_sel_hi:[1,0]
	v_pk_mul_f32 v[20:21], v[20:21], v[160:161] op_sel_hi:[1,0]
	v_pk_mul_f32 v[18:19], v[18:19], v[160:161] op_sel_hi:[1,0]
	v_pk_mul_f32 v[16:17], v[16:17], v[160:161] op_sel_hi:[1,0]
	v_pk_mul_f32 v[14:15], v[14:15], v[160:161] op_sel_hi:[1,0]
	v_pk_mul_f32 v[12:13], v[12:13], v[160:161] op_sel_hi:[1,0]
	v_pk_mul_f32 v[10:11], v[10:11], v[160:161] op_sel_hi:[1,0]
	v_pk_mul_f32 v[8:9], v[8:9], v[160:161] op_sel_hi:[1,0]
	v_pk_mul_f32 v[6:7], v[6:7], v[160:161] op_sel_hi:[1,0]
	v_pk_mul_f32 v[4:5], v[4:5], v[160:161] op_sel_hi:[1,0]
	v_pk_mul_f32 v[2:3], v[2:3], v[160:161] op_sel_hi:[1,0]
	v_pk_mul_f32 v[0:1], v[0:1], v[160:161] op_sel_hi:[1,0]

.LBB0_586:
	s_or_b64 exec, exec, s[4:5]
	v_mov_b32_e32 v38, v165
	v_readlane_b32 s5, v255, 51
	v_readfirstlane_b32 s2, v38
	s_ashr_i32 s79, s2, 6
	v_bfe_u32 v0, v38, 5, 1
	v_and_b32_e32 v176, 31, v38
	s_lshl_b32 s92, s79, 5
	v_lshlrev_b32_e32 v32, 2, v0
	s_add_i32 s74, s92, s74
	v_sub_u32_e32 v1, v176, v32
	v_lshlrev_b32_e32 v175, 4, v0
	s_lshl_b32 s2, s79, 3
	v_bfe_u32 v0, v38, 4, 2
	v_add_u32_e32 v179, s74, v1
	v_or_b32_e32 v1, s2, v0
	v_and_b32_e32 v2, 15, v38
	v_and_b32_e32 v39, 63, v38
	v_bitop3_b32 v3, v0, v38, 15 bitop3:0x78
	v_mul_lo_u32 v1, v1, s14
	v_bitop3_b32 v0, v0, v2, 4 bitop3:0x36
	s_mul_i32 s4, s79, 0x1c00
	s_waitcnt vmcnt(0)
	v_lshlrev_b32_e32 v40, 4, v39
	v_lshl_or_b32 v0, v0, 4, v1
	s_lshl_b32 s78, s79, 11
	v_readlane_b32 s7, v255, 53
	s_lshl_b32 s3, s79, 12
	s_add_i32 s4, s5, s4
	v_lshl_or_b32 v160, v3, 4, v1
	v_add_u32_e32 v170, 0x1a000, v0
	s_add_i32 s78, s78, s7
	s_add_i32 s3, s3, s33
	v_add_u32_e32 v180, s4, v40
	s_waitcnt vmcnt(0) lgkmcnt(0)
	ds_write_b128 v180, v[128:131]
	ds_write_b128 v180, v[132:135] offset:1024
	ds_write_b128 v180, v[136:139] offset:2048
	ds_write_b128 v180, v[140:143] offset:3072
	ds_write_b128 v180, v[144:147] offset:4096
	ds_write_b128 v180, v[148:151] offset:5120
	ds_write_b128 v180, v[152:155] offset:6144
	s_add_u32 s4, s66, 0x1a2900
	s_addc_u32 s5, s67, 0
	v_lshl_add_u64 v[0:1], s[4:5], 0, v[160:161]
	s_add_i32 s82, s78, 0x4000
	s_mov_b32 s6, m0
	s_mov_b32 m0, s82
	s_nop 0
	global_load_lds_dwordx4 v[0:1], off
	s_mov_b32 m0, s6
	v_mov_b32_e32 v171, v161
	v_lshl_add_u64 v[0:1], s[4:5], 0, v[170:171]
	s_add_i32 s84, s78, 0x4400
	s_mov_b32 s4, m0
	s_mov_b32 m0, s84
	s_nop 0
	global_load_lds_dwordx4 v[0:1], off
	s_mov_b32 m0, s4
	s_waitcnt lgkmcnt(0)
	s_barrier
	v_lshlrev_b32_e32 v0, 4, v38
	s_movk_i32 s4, 0x70
	v_lshlrev_b32_e32 v33, 8, v176
	v_and_b32_e32 v1, 0x70, v0
	v_bitop3_b32 v34, v175, v0, s4 bitop3:0x78
	s_movk_i32 s4, 0x60
	v_add_u32_e32 v2, s7, v33
	v_bitop3_b32 v35, v175, v1, 32 bitop3:0x36
	v_bitop3_b32 v36, v175, v1, 64 bitop3:0x36
	v_bitop3_b32 v37, v175, v1, s4 bitop3:0x36
	v_add_u32_e32 v181, v34, v2
	v_add_u32_e32 v182, v35, v2
	v_add_u32_e32 v183, v36, v2
	v_add_u32_e32 v184, v37, v2
	ds_read_b128 v[0:3], v181 offset:0
	ds_read_b128 v[4:7], v181 offset:0x2000
	ds_read_b128 v[8:11], v180 offset:0
	ds_read_b128 v[42:45], v182 offset:0
	ds_read_b128 v[46:49], v182 offset:0x2000
	ds_read_b128 v[50:53], v180 offset:0x400
	s_waitcnt lgkmcnt(3)
	s_nop 0
	v_mfma_f32_32x32x16_bf16 v[16:31], v[0:3], v[8:11], 0
	v_mfma_f32_32x32x16_bf16 v[0:15], v[4:7], v[8:11], 0
	ds_read_b128 v[54:57], v183 offset:0
	ds_read_b128 v[58:61], v183 offset:0x2000
	ds_read_b128 v[62:65], v180 offset:0x800
	s_waitcnt lgkmcnt(3)
	v_mfma_f32_32x32x16_bf16 v[16:31], v[42:45], v[50:53], v[16:31]
	v_mfma_f32_32x32x16_bf16 v[0:15], v[46:49], v[50:53], v[0:15]
	ds_read_b128 v[42:45], v184 offset:0
	ds_read_b128 v[46:49], v184 offset:0x2000
	ds_read_b128 v[50:53], v180 offset:0xc00
	s_waitcnt lgkmcnt(3)
	v_mfma_f32_32x32x16_bf16 v[16:31], v[54:57], v[62:65], v[16:31]
	v_mfma_f32_32x32x16_bf16 v[0:15], v[58:61], v[62:65], v[0:15]
	ds_read_b128 v[54:57], v181 offset:0x80
	ds_read_b128 v[58:61], v181 offset:0x2080
	ds_read_b128 v[62:65], v180 offset:0x1000
	s_waitcnt lgkmcnt(3)
	v_mfma_f32_32x32x16_bf16 v[16:31], v[42:45], v[50:53], v[16:31]
	v_mfma_f32_32x32x16_bf16 v[0:15], v[46:49], v[50:53], v[0:15]
	ds_read_b128 v[42:45], v182 offset:0x80
	ds_read_b128 v[46:49], v182 offset:0x2080
	ds_read_b128 v[50:53], v180 offset:0x1400
	s_waitcnt lgkmcnt(3)
	v_mfma_f32_32x32x16_bf16 v[16:31], v[54:57], v[62:65], v[16:31]
	v_mfma_f32_32x32x16_bf16 v[0:15], v[58:61], v[62:65], v[0:15]
	ds_read_b128 v[54:57], v183 offset:0x80
	ds_read_b128 v[58:61], v183 offset:0x2080
	ds_read_b128 v[62:65], v180 offset:0x1800
	s_waitcnt lgkmcnt(3)
	v_mfma_f32_32x32x16_bf16 v[16:31], v[42:45], v[50:53], v[16:31]
	v_mfma_f32_32x32x16_bf16 v[0:15], v[46:49], v[50:53], v[0:15]
	ds_read_b128 v[42:45], v184 offset:0x80
	ds_read_b128 v[46:49], v184 offset:0x2080
	s_waitcnt lgkmcnt(2)
	v_mfma_f32_32x32x16_bf16 v[16:31], v[54:57], v[62:65], v[16:31]
	v_mfma_f32_32x32x16_bf16 v[0:15], v[58:61], v[62:65], v[0:15]
	s_waitcnt lgkmcnt(0)
	v_mfma_f32_32x32x16_bf16 v[16:31], v[42:45], v[166:169], v[16:31]
	v_mfma_f32_32x32x16_bf16 v[0:15], v[46:49], v[166:169], v[0:15]
	s_bitcmp0_b32 s100, 8
	s_cbranch_scc1 .Lstg_a17
	s_waitcnt vmcnt(0)
	s_waitcnt lgkmcnt(0)
	s_barrier
.Lstg_a17:
	s_cmp_gt_i32 s74, 62
	s_cbranch_scc1 .LBB0_588
	v_cmp_gt_i32_e64 s[62:63], 26, v179
	v_cmp_gt_i32_e64 s[64:65], 27, v179
	v_cmp_gt_i32_e64 s[60:61], 25, v179
	s_and_b64 s[62:63], s[64:65], s[62:63]
	v_cmp_gt_i32_e64 s[58:59], 24, v179
	s_and_b64 s[60:61], s[62:63], s[60:61]
	v_cmp_gt_i32_e64 s[56:57], 19, v179
	s_and_b64 s[58:59], s[60:61], s[58:59]
	v_cmp_gt_i32_e64 s[54:55], 18, v179
	s_and_b64 s[56:57], s[58:59], s[56:57]
	v_cmp_gt_i32_e64 s[52:53], 17, v179
	s_and_b64 s[54:55], s[56:57], s[54:55]
	v_cmp_gt_i32_e64 s[50:51], 16, v179
	s_and_b64 s[52:53], s[54:55], s[52:53]
	v_cmp_gt_i32_e64 s[48:49], 11, v179
	s_and_b64 s[50:51], s[52:53], s[50:51]
	v_cmp_gt_i32_e64 s[46:47], 10, v179
	s_and_b64 s[48:49], s[50:51], s[48:49]
	v_cmp_gt_i32_e64 s[44:45], 9, v179
	s_and_b64 s[46:47], s[48:49], s[46:47]
	v_cmp_gt_i32_e64 s[42:43], 8, v179
	s_and_b64 s[44:45], s[46:47], s[44:45]
	v_cmp_gt_i32_e64 s[40:41], 3, v179
	s_and_b64 s[42:43], s[44:45], s[42:43]
	v_cmp_gt_i32_e64 s[38:39], 2, v179
	s_and_b64 s[40:41], s[42:43], s[40:41]
	v_cmp_gt_i32_e64 s[36:37], 1, v179
	s_and_b64 s[38:39], s[40:41], s[38:39]
	v_cmp_gt_i32_e64 s[34:35], 0, v179
	s_and_b64 s[36:37], s[38:39], s[36:37]
	s_and_b64 s[34:35], s[36:37], s[34:35]
	v_cmp_gt_i32_e64 s[30:31], 58, v179
	v_cndmask_b32_e64 v16, v16, v226, s[34:35]
	v_cmp_gt_i32_e64 s[34:35], 59, v179
	v_cmp_gt_i32_e64 s[28:29], 57, v179
	s_and_b64 s[30:31], s[34:35], s[30:31]
	v_cmp_gt_i32_e64 s[26:27], 56, v179
	s_and_b64 s[28:29], s[30:31], s[28:29]
	v_cmp_gt_i32_e64 s[24:25], 51, v179
	s_and_b64 s[26:27], s[28:29], s[26:27]
	v_cmp_gt_i32_e64 s[22:23], 50, v179
	s_and_b64 s[24:25], s[26:27], s[24:25]
	v_cmp_gt_i32_e64 s[20:21], 49, v179
	s_and_b64 s[22:23], s[24:25], s[22:23]
	v_cmp_gt_i32_e64 s[18:19], 48, v179
	s_and_b64 s[20:21], s[22:23], s[20:21]
	v_cmp_gt_i32_e64 s[16:17], 43, v179
	s_and_b64 s[18:19], s[20:21], s[18:19]
	v_cmp_gt_i32_e64 s[14:15], 42, v179
	s_and_b64 s[16:17], s[18:19], s[16:17]
	v_cmp_gt_i32_e64 s[12:13], 41, v179
	s_and_b64 s[14:15], s[16:17], s[14:15]
	v_cmp_gt_i32_e64 s[10:11], 40, v179
	s_and_b64 s[12:13], s[14:15], s[12:13]
	v_cmp_gt_i32_e64 s[8:9], 35, v179
	s_and_b64 s[10:11], s[12:13], s[10:11]
	v_cmp_gt_i32_e64 s[6:7], 34, v179
	s_and_b64 s[8:9], s[10:11], s[8:9]
	v_cmp_gt_i32_e64 s[4:5], 33, v179
	s_and_b64 s[6:7], s[8:9], s[6:7]
	v_cmp_gt_i32_e32 vcc, 32, v179
	s_and_b64 s[4:5], s[6:7], s[4:5]
	s_and_b64 vcc, s[4:5], vcc
	v_cndmask_b32_e64 v31, v31, v226, s[64:65]
	v_cndmask_b32_e64 v30, v30, v226, s[62:63]
	s_mov_b64 s[62:63], 0x100
	v_cndmask_b32_e64 v29, v29, v226, s[60:61]
	v_cndmask_b32_e64 v28, v28, v226, s[58:59]
	v_cndmask_b32_e64 v27, v27, v226, s[56:57]
	v_cndmask_b32_e64 v26, v26, v226, s[54:55]
	v_cndmask_b32_e64 v25, v25, v226, s[52:53]
	v_cndmask_b32_e64 v24, v24, v226, s[50:51]
	v_cndmask_b32_e64 v23, v23, v226, s[48:49]
	v_cndmask_b32_e64 v22, v22, v226, s[46:47]
	v_cndmask_b32_e64 v21, v21, v226, s[44:45]
	v_cndmask_b32_e64 v20, v20, v226, s[42:43]
	v_cndmask_b32_e64 v19, v19, v226, s[40:41]
	v_cndmask_b32_e64 v18, v18, v226, s[38:39]
	v_cndmask_b32_e64 v17, v17, v226, s[36:37]
	v_cndmask_b32_e64 v15, v15, v226, s[34:35]
	v_cndmask_b32_e64 v14, v14, v226, s[30:31]
	v_cndmask_b32_e64 v13, v13, v226, s[28:29]
	v_cndmask_b32_e64 v12, v12, v226, s[26:27]
	v_cndmask_b32_e64 v11, v11, v226, s[24:25]
	v_cndmask_b32_e64 v10, v10, v226, s[22:23]
	v_cndmask_b32_e64 v9, v9, v226, s[20:21]
	v_cndmask_b32_e64 v8, v8, v226, s[18:19]
	v_cndmask_b32_e64 v7, v7, v226, s[16:17]
	v_cndmask_b32_e64 v6, v6, v226, s[14:15]
	v_cndmask_b32_e64 v5, v5, v226, s[12:13]
	v_cndmask_b32_e64 v4, v4, v226, s[10:11]
	v_cndmask_b32_e64 v3, v3, v226, s[8:9]
	v_cndmask_b32_e64 v2, v2, v226, s[6:7]
	v_cndmask_b32_e64 v1, v1, v226, s[4:5]
	v_cndmask_b32_e32 v0, v0, v226, vcc
.LBB0_588:
	v_lshlrev_b32_e32 v41, 3, v39
	v_and_b32_e32 v40, 0xc0, v40
	v_lshlrev_b32_e32 v39, 1, v39
	v_and_or_b32 v40, v41, 24, v40
	v_and_b32_e32 v39, 32, v39
	v_and_b32_e32 v41, 0x100, v41
	v_or3_b32 v39, v40, v39, v41
	v_add_u32_e32 v177, s33, v39
	v_lshrrev_b32_e32 v39, 2, v176
	v_bitop3_b32 v39, s2, v228, v39 bitop3:0xc8
	v_lshrrev_b32_e32 v40, 1, v176
	s_lshr_b32 s2, s2, 1
	v_and_b32_e32 v40, 8, v40
	s_and_b32 s2, s2, 4
	v_or3_b32 v39, v40, v39, s2
	v_and_b32_e32 v40, 32, v38
	v_lshlrev_b32_e32 v38, 3, v38
	v_and_b32_e32 v38, 24, v38
	v_mul_u32_u24_e32 v39, 0x3400, v39
	v_or3_b32 v38, v40, v38, v39
	v_lshlrev_b32_e32 v162, 1, v38
	v_max_f32_e32 v38, v17, v17
	v_max_f32_e32 v39, v16, v16
	v_max_f32_e32 v38, v39, v38
	v_max3_f32 v38, v38, v18, v19
	v_max3_f32 v38, v38, v20, v21
	v_max3_f32 v38, v38, v22, v23
	v_max3_f32 v38, v38, v24, v25
	v_max3_f32 v38, v38, v26, v27
	v_max3_f32 v38, v38, v28, v29
	v_max3_f32 v38, v38, v30, v31
	v_max3_f32 v38, v38, v0, v1
	v_max3_f32 v38, v38, v2, v3
	v_max3_f32 v38, v38, v4, v5
	v_max3_f32 v38, v38, v6, v7
	v_max3_f32 v38, v38, v8, v9
	v_max3_f32 v38, v38, v10, v11
	v_max3_f32 v38, v38, v12, v13
	v_max3_f32 v38, v38, v14, v15
	v_mov_b32_e32 v39, v38
	s_nop 1
	v_permlane32_swap_b32_e32 v38, v39
	v_max_f32_e32 v39, v39, v39
	v_max_f32_e32 v38, v38, v38
	v_max_f32_e32 v38, v38, v39
	v_add_f32_e32 v39, 0x7149f2ca, v38
	v_mul_f32_e32 v39, 0x3db504f3, v39
	s_mov_b32 s2, 0x41000000
	v_max_f32_e32 v38, 0xf149f2ca, v38
	v_cmp_ge_f32_e32 vcc, s2, v39
	v_sub_f32_e32 v39, 0xf149f2ca, v38
	v_mul_f32_e32 v39, 0x3e0293ee, v39
	v_exp_f32_e32 v39, v39
	s_cmp_eq_u64 vcc, exec
	s_cselect_b64 vcc, -1, 0
	v_mov_b32_e32 v40, 0xf149f2ca
	v_cndmask_b32_e32 v190, v38, v40, vcc
	v_cndmask_b32_e64 v38, v39, 1.0, vcc
	v_mul_f32_e32 v39, 0xbe0293ee, v190
	v_fmamk_f32 v16, v16, 0x3e0293ee, v39
	v_fmamk_f32 v17, v17, 0x3e0293ee, v39
	v_fmamk_f32 v18, v18, 0x3e0293ee, v39
	v_fmamk_f32 v19, v19, 0x3e0293ee, v39
	v_fmamk_f32 v20, v20, 0x3e0293ee, v39
	v_fmamk_f32 v21, v21, 0x3e0293ee, v39
	v_fmamk_f32 v22, v22, 0x3e0293ee, v39
	v_fmamk_f32 v23, v23, 0x3e0293ee, v39
	v_fmamk_f32 v24, v24, 0x3e0293ee, v39
	v_fmamk_f32 v25, v25, 0x3e0293ee, v39
	v_fmamk_f32 v26, v26, 0x3e0293ee, v39
	v_fmamk_f32 v27, v27, 0x3e0293ee, v39
	v_fmamk_f32 v28, v28, 0x3e0293ee, v39
	v_fmamk_f32 v29, v29, 0x3e0293ee, v39
	v_fmamk_f32 v30, v30, 0x3e0293ee, v39
	v_fmamk_f32 v31, v31, 0x3e0293ee, v39
	v_fmamk_f32 v0, v0, 0x3e0293ee, v39
	v_fmamk_f32 v1, v1, 0x3e0293ee, v39
	v_fmamk_f32 v2, v2, 0x3e0293ee, v39
	v_fmamk_f32 v3, v3, 0x3e0293ee, v39
	v_fmamk_f32 v4, v4, 0x3e0293ee, v39
	v_fmamk_f32 v5, v5, 0x3e0293ee, v39
	v_fmamk_f32 v6, v6, 0x3e0293ee, v39
	v_fmamk_f32 v7, v7, 0x3e0293ee, v39
	v_fmamk_f32 v8, v8, 0x3e0293ee, v39
	v_fmamk_f32 v9, v9, 0x3e0293ee, v39
	v_fmamk_f32 v10, v10, 0x3e0293ee, v39
	v_fmamk_f32 v11, v11, 0x3e0293ee, v39
	v_fmamk_f32 v12, v12, 0x3e0293ee, v39
	v_fmamk_f32 v13, v13, 0x3e0293ee, v39
	v_fmamk_f32 v14, v14, 0x3e0293ee, v39
	v_fmac_f32_e32 v39, 0x3e0293ee, v15
	v_exp_f32_e32 v15, v16
	v_exp_f32_e32 v16, v17
	v_exp_f32_e32 v17, v18
	v_exp_f32_e32 v18, v19
	v_exp_f32_e32 v19, v20
	v_exp_f32_e32 v20, v21
	v_exp_f32_e32 v21, v22
	v_exp_f32_e32 v22, v23
	v_exp_f32_e32 v23, v24
	v_exp_f32_e32 v24, v25
	v_exp_f32_e32 v25, v26
	v_exp_f32_e32 v26, v27
	v_exp_f32_e32 v27, v28
	v_exp_f32_e32 v28, v29
	v_exp_f32_e32 v29, v30
	v_exp_f32_e32 v30, v31
	v_exp_f32_e32 v31, v39
	v_add_f32_e32 v39, 0, v15
	v_add_f32_e32 v39, v16, v39
	v_add_f32_e32 v39, v17, v39
	v_add_f32_e32 v39, v18, v39
	v_add_f32_e32 v39, v19, v39
	v_add_f32_e32 v39, v20, v39
	v_add_f32_e32 v39, v21, v39
	v_add_f32_e32 v39, v22, v39
	v_add_f32_e32 v39, v23, v39
	v_add_f32_e32 v39, v24, v39
	v_add_f32_e32 v39, v25, v39
	v_add_f32_e32 v39, v26, v39
	v_exp_f32_e32 v0, v0
	v_add_f32_e32 v39, v27, v39
	v_exp_f32_e32 v1, v1
	v_add_f32_e32 v39, v28, v39
	v_exp_f32_e32 v2, v2
	v_add_f32_e32 v39, v29, v39
	v_exp_f32_e32 v3, v3
	v_add_f32_e32 v39, v30, v39
	v_exp_f32_e32 v4, v4
	v_add_f32_e32 v39, v0, v39
	v_exp_f32_e32 v5, v5
	v_add_f32_e32 v39, v1, v39
	v_exp_f32_e32 v6, v6
	v_add_f32_e32 v39, v2, v39
	v_exp_f32_e32 v7, v7
	v_add_f32_e32 v39, v3, v39
	v_exp_f32_e32 v8, v8
	v_add_f32_e32 v39, v4, v39
	v_exp_f32_e32 v9, v9
	v_add_f32_e32 v39, v5, v39
	v_exp_f32_e32 v10, v10
	v_add_f32_e32 v39, v6, v39
	v_exp_f32_e32 v11, v11
	v_add_f32_e32 v39, v7, v39
	v_exp_f32_e32 v12, v12
	v_add_f32_e32 v39, v8, v39
	v_exp_f32_e32 v13, v13
	v_add_f32_e32 v39, v9, v39
	v_exp_f32_e32 v14, v14
	v_add_f32_e32 v39, v10, v39
	v_add_f32_e32 v39, v11, v39
	v_add_f32_e32 v39, v12, v39
	v_add_f32_e32 v39, v13, v39
	v_add_f32_e32 v39, v14, v39
	v_add_f32_e32 v39, v31, v39
	v_mov_b32_e32 v40, v39
	s_nop 1
	v_permlane32_swap_b32_e32 v39, v40
	v_add_f32_e32 v178, v39, v40
	v_cvt_pk_bf16_f32 v128, v15, v16
	v_cvt_pk_bf16_f32 v129, v17, v18
	v_cvt_pk_bf16_f32 v130, v19, v20
	v_cvt_pk_bf16_f32 v131, v21, v22
	v_cvt_pk_bf16_f32 v132, v23, v24
	v_cvt_pk_bf16_f32 v133, v25, v26
	v_cvt_pk_bf16_f32 v134, v27, v28
	v_cvt_pk_bf16_f32 v135, v29, v30
	v_cvt_pk_bf16_f32 v136, v0, v1
	v_cvt_pk_bf16_f32 v137, v2, v3
	v_cvt_pk_bf16_f32 v138, v4, v5
	v_cvt_pk_bf16_f32 v139, v6, v7
	v_cvt_pk_bf16_f32 v140, v8, v9
	v_cvt_pk_bf16_f32 v141, v10, v11
	v_cvt_pk_bf16_f32 v142, v12, v13
	v_cvt_pk_bf16_f32 v143, v14, v31
	s_mov_b32 s85, 4
	v_mul_f32_e32 v39, 0, v38
	v_fmac_f32_e32 v178, 0, v38
	v_permlane32_swap_b32_e32 v128, v130
	v_permlane32_swap_b32_e32 v129, v131
	v_permlane32_swap_b32_e32 v132, v134
	v_permlane32_swap_b32_e32 v133, v135
	v_permlane32_swap_b32_e32 v136, v138
	v_permlane32_swap_b32_e32 v137, v139
	v_permlane32_swap_b32_e32 v140, v142
	v_permlane32_swap_b32_e32 v141, v143
	s_bitcmp1_b32 s100, 8
	s_cbranch_scc1 .Lstg_b21
	s_waitcnt vmcnt(0)
	s_waitcnt lgkmcnt(0)
	s_barrier
.Lstg_b21:
	s_add_u32 s4, s66, 0x342900
	s_addc_u32 s5, s67, 0
	v_lshl_add_u64 v[0:1], s[4:5], 0, v[160:161]
	s_mov_b32 s2, m0
	s_mov_b32 m0, s78
	s_nop 0
	global_load_lds_dwordx4 v[0:1], off
	s_mov_b32 m0, s2
	v_lshl_add_u64 v[0:1], s[4:5], 0, v[170:171]
	v_readlane_b32 s4, v255, 41
	s_add_i32 s93, s78, 0x400
	s_mov_b32 s2, m0
	s_mov_b32 m0, s93
	s_nop 0
	global_load_lds_dwordx4 v[0:1], off
	s_mov_b32 m0, s2
	v_mov_b32_e32 v163, v161
	v_readlane_b32 s5, v255, 42
	s_add_i32 s90, s3, 0x8000
	s_add_i32 s91, s3, 0x8400
	v_lshl_add_u64 v[0:1], s[4:5], 0, v[162:163]
	s_mov_b32 s2, m0
	s_mov_b32 m0, s90
	s_nop 0
	global_load_lds_dwordx4 v[0:1], off
	s_mov_b32 m0, s2
	v_lshl_add_u64 v[2:3], v[0:1], 0, s[86:87]
	s_mov_b32 s2, m0
	s_mov_b32 m0, s91
	s_nop 0
	global_load_lds_dwordx4 v[2:3], off
	s_mov_b32 m0, s2
	v_lshl_add_u64 v[2:3], v[0:1], 0, s[62:63]
	s_add_i32 s88, s3, 0x8800
	s_mov_b32 s2, m0
	s_mov_b32 m0, s88
	s_nop 0
	global_load_lds_dwordx4 v[2:3], off
	s_mov_b32 m0, s2
	s_mov_b64 s[4:5], 0x180
	v_lshl_add_u64 v[0:1], v[0:1], 0, s[4:5]
	s_add_i32 s89, s3, 0x8c00
	s_mov_b32 s2, m0
	s_mov_b32 m0, s89
	s_nop 0
	global_load_lds_dwordx4 v[0:1], off
	s_mov_b32 m0, s2
	v_cmp_gt_f32_e32 vcc, 1.0, v38
	s_cmp_lg_u64 vcc, 0
	s_cselect_b64 vcc, -1, 0
	v_readlane_b32 s2, v255, 56
	v_readlane_b32 s4, v255, 40
	v_cndmask_b32_e32 v96, 0, v39, vcc
	v_add_u32_e32 v0, s2, v33
	s_add_i32 s4, s4, s92
	v_mov_b32_e32 v97, v96
	v_mov_b32_e32 v110, v96
	v_mov_b32_e32 v111, v96
	v_add_u32_e32 v188, v34, v0
	v_add_u32_e32 v187, v35, v0
	v_add_u32_e32 v186, v36, v0
	v_add_u32_e32 v185, v37, v0
	v_add_u32_e32 v0, s4, v176
	v_mov_b32_e32 v98, v96
	v_mov_b32_e32 v99, v96
	v_mov_b32_e32 v100, v96
	v_mov_b32_e32 v101, v96
	v_mov_b32_e32 v102, v96
	v_mov_b32_e32 v103, v96
	v_mov_b32_e32 v104, v96
	v_mov_b32_e32 v105, v96
	v_mov_b32_e32 v106, v96
	v_mov_b32_e32 v107, v96
	v_mov_b32_e32 v108, v96
	v_mov_b32_e32 v109, v96
	v_sub_u32_e32 v189, v0, v32
	v_mov_b64_e32 v[126:127], v[110:111]
	v_mov_b64_e32 v[80:81], v[96:97]
	v_mov_b64_e32 v[64:65], v[96:97]
	v_mov_b64_e32 v[48:49], v[96:97]
	v_mov_b64_e32 v[32:33], v[96:97]
	v_mov_b64_e32 v[16:17], v[96:97]
	v_mov_b64_e32 v[0:1], v[96:97]
	s_add_i32 s69, s3, 0x400
	s_add_i32 s68, s3, 0x800
	s_add_i32 s2, s3, 0xc00
	s_movk_i32 s97, 0xbf
	v_mov_b64_e32 v[124:125], v[108:109]
	v_mov_b64_e32 v[122:123], v[106:107]
	v_mov_b64_e32 v[120:121], v[104:105]
	v_mov_b64_e32 v[118:119], v[102:103]
	v_mov_b64_e32 v[116:117], v[100:101]
	v_mov_b64_e32 v[114:115], v[98:99]
	v_mov_b64_e32 v[112:113], v[96:97]
	v_mov_b64_e32 v[82:83], v[98:99]
	v_mov_b64_e32 v[84:85], v[100:101]
	v_mov_b64_e32 v[86:87], v[102:103]
	v_mov_b64_e32 v[88:89], v[104:105]
	v_mov_b64_e32 v[90:91], v[106:107]
	v_mov_b64_e32 v[92:93], v[108:109]
	v_mov_b64_e32 v[94:95], v[110:111]
	v_mov_b64_e32 v[66:67], v[98:99]
	v_mov_b64_e32 v[68:69], v[100:101]
	v_mov_b64_e32 v[70:71], v[102:103]
	v_mov_b64_e32 v[72:73], v[104:105]
	v_mov_b64_e32 v[74:75], v[106:107]
	v_mov_b64_e32 v[76:77], v[108:109]
	v_mov_b64_e32 v[78:79], v[110:111]
	v_mov_b64_e32 v[50:51], v[98:99]
	v_mov_b64_e32 v[52:53], v[100:101]
	v_mov_b64_e32 v[54:55], v[102:103]
	v_mov_b64_e32 v[56:57], v[104:105]
	v_mov_b64_e32 v[58:59], v[106:107]
	v_mov_b64_e32 v[60:61], v[108:109]
	v_mov_b64_e32 v[62:63], v[110:111]
	v_mov_b64_e32 v[34:35], v[98:99]
	v_mov_b64_e32 v[36:37], v[100:101]
	v_mov_b64_e32 v[38:39], v[102:103]
	v_mov_b64_e32 v[40:41], v[104:105]
	v_mov_b64_e32 v[42:43], v[106:107]
	v_mov_b64_e32 v[44:45], v[108:109]
	v_mov_b64_e32 v[46:47], v[110:111]
	v_mov_b64_e32 v[18:19], v[98:99]
	v_mov_b64_e32 v[20:21], v[100:101]
	v_mov_b64_e32 v[22:23], v[102:103]
	v_mov_b64_e32 v[24:25], v[104:105]
	v_mov_b64_e32 v[26:27], v[106:107]
	v_mov_b64_e32 v[28:29], v[108:109]
	v_mov_b64_e32 v[30:31], v[110:111]
	v_mov_b64_e32 v[2:3], v[98:99]
	v_mov_b64_e32 v[4:5], v[100:101]
	v_mov_b64_e32 v[6:7], v[102:103]
	v_mov_b64_e32 v[8:9], v[104:105]
	v_mov_b64_e32 v[10:11], v[106:107]
	v_mov_b64_e32 v[12:13], v[108:109]
	v_mov_b64_e32 v[14:15], v[110:111]
.LBB0_589:
	ds_read_b64_tr_b16 v[144:145], v177 offset:0
	ds_read_b64_tr_b16 v[146:147], v177 offset:0x1000
	ds_read_b64_tr_b16 v[148:149], v177 offset:0x2000
	ds_read_b64_tr_b16 v[150:151], v177 offset:0x3000
	ds_read_b64_tr_b16 v[152:153], v177 offset:0x4000
	ds_read_b64_tr_b16 v[154:155], v177 offset:0x5000
	ds_read_b64_tr_b16 v[156:157], v177 offset:0x6000
	ds_read_b64_tr_b16 v[158:159], v177 offset:0x7000
	ds_read_b64_tr_b16 v[192:193], v177 offset:0x200
	ds_read_b64_tr_b16 v[194:195], v177 offset:0x1200
	ds_read_b64_tr_b16 v[196:197], v177 offset:0x2200
	ds_read_b64_tr_b16 v[198:199], v177 offset:0x3200
	ds_read_b64_tr_b16 v[200:201], v177 offset:0x4200
	ds_read_b64_tr_b16 v[202:203], v177 offset:0x5200
	ds_read_b64_tr_b16 v[204:205], v177 offset:0x6200
	ds_read_b64_tr_b16 v[206:207], v177 offset:0x7200
	s_waitcnt lgkmcnt(8)
	s_nop 0
	v_mfma_f32_32x32x16_bf16 v[112:127], v[144:147], v[128:131], v[112:127]
	v_mfma_f32_32x32x16_bf16 v[112:127], v[148:151], v[132:135], v[112:127]
	v_mfma_f32_32x32x16_bf16 v[112:127], v[152:155], v[136:139], v[112:127]
	v_mfma_f32_32x32x16_bf16 v[112:127], v[156:159], v[140:143], v[112:127]
	ds_read_b64_tr_b16 v[144:145], v177 offset:0x400
	ds_read_b64_tr_b16 v[146:147], v177 offset:0x1400
	ds_read_b64_tr_b16 v[148:149], v177 offset:0x2400
	ds_read_b64_tr_b16 v[150:151], v177 offset:0x3400
	ds_read_b64_tr_b16 v[152:153], v177 offset:0x4400
	ds_read_b64_tr_b16 v[154:155], v177 offset:0x5400
	ds_read_b64_tr_b16 v[156:157], v177 offset:0x6400
	ds_read_b64_tr_b16 v[158:159], v177 offset:0x7400
	s_waitcnt lgkmcnt(8)
	v_mfma_f32_32x32x16_bf16 v[96:111], v[192:195], v[128:131], v[96:111]
	v_mfma_f32_32x32x16_bf16 v[96:111], v[196:199], v[132:135], v[96:111]
	v_mfma_f32_32x32x16_bf16 v[96:111], v[200:203], v[136:139], v[96:111]
	v_mfma_f32_32x32x16_bf16 v[96:111], v[204:207], v[140:143], v[96:111]
	ds_read_b64_tr_b16 v[192:193], v177 offset:0x600
	ds_read_b64_tr_b16 v[194:195], v177 offset:0x1600
	ds_read_b64_tr_b16 v[196:197], v177 offset:0x2600
	ds_read_b64_tr_b16 v[198:199], v177 offset:0x3600
	ds_read_b64_tr_b16 v[200:201], v177 offset:0x4600
	ds_read_b64_tr_b16 v[202:203], v177 offset:0x5600
	ds_read_b64_tr_b16 v[204:205], v177 offset:0x6600
	ds_read_b64_tr_b16 v[206:207], v177 offset:0x7600
	s_waitcnt lgkmcnt(8)
	v_mfma_f32_32x32x16_bf16 v[80:95], v[144:147], v[128:131], v[80:95]
	v_mfma_f32_32x32x16_bf16 v[80:95], v[148:151], v[132:135], v[80:95]
	v_mfma_f32_32x32x16_bf16 v[80:95], v[152:155], v[136:139], v[80:95]
	v_mfma_f32_32x32x16_bf16 v[80:95], v[156:159], v[140:143], v[80:95]
	ds_read_b64_tr_b16 v[144:145], v177 offset:0x800
	ds_read_b64_tr_b16 v[146:147], v177 offset:0x1800
	ds_read_b64_tr_b16 v[148:149], v177 offset:0x2800
	ds_read_b64_tr_b16 v[150:151], v177 offset:0x3800
	ds_read_b64_tr_b16 v[152:153], v177 offset:0x4800
	ds_read_b64_tr_b16 v[154:155], v177 offset:0x5800
	ds_read_b64_tr_b16 v[156:157], v177 offset:0x6800
	ds_read_b64_tr_b16 v[158:159], v177 offset:0x7800
	s_waitcnt lgkmcnt(8)
	v_mfma_f32_32x32x16_bf16 v[64:79], v[192:195], v[128:131], v[64:79]
	v_mfma_f32_32x32x16_bf16 v[64:79], v[196:199], v[132:135], v[64:79]
	v_mfma_f32_32x32x16_bf16 v[64:79], v[200:203], v[136:139], v[64:79]
	v_mfma_f32_32x32x16_bf16 v[64:79], v[204:207], v[140:143], v[64:79]
	ds_read_b64_tr_b16 v[192:193], v177 offset:0xa00
	ds_read_b64_tr_b16 v[194:195], v177 offset:0x1a00
	ds_read_b64_tr_b16 v[196:197], v177 offset:0x2a00
	ds_read_b64_tr_b16 v[198:199], v177 offset:0x3a00
	ds_read_b64_tr_b16 v[200:201], v177 offset:0x4a00
	ds_read_b64_tr_b16 v[202:203], v177 offset:0x5a00
	ds_read_b64_tr_b16 v[204:205], v177 offset:0x6a00
	ds_read_b64_tr_b16 v[206:207], v177 offset:0x7a00
	s_waitcnt lgkmcnt(8)
	v_mfma_f32_32x32x16_bf16 v[48:63], v[144:147], v[128:131], v[48:63]
	v_mfma_f32_32x32x16_bf16 v[48:63], v[148:151], v[132:135], v[48:63]
	v_mfma_f32_32x32x16_bf16 v[48:63], v[152:155], v[136:139], v[48:63]
	v_mfma_f32_32x32x16_bf16 v[48:63], v[156:159], v[140:143], v[48:63]
	ds_read_b64_tr_b16 v[144:145], v177 offset:0xc00
	ds_read_b64_tr_b16 v[146:147], v177 offset:0x1c00
	ds_read_b64_tr_b16 v[148:149], v177 offset:0x2c00
	ds_read_b64_tr_b16 v[150:151], v177 offset:0x3c00
	ds_read_b64_tr_b16 v[152:153], v177 offset:0x4c00
	ds_read_b64_tr_b16 v[154:155], v177 offset:0x5c00
	ds_read_b64_tr_b16 v[156:157], v177 offset:0x6c00
	ds_read_b64_tr_b16 v[158:159], v177 offset:0x7c00
	s_waitcnt lgkmcnt(8)
	v_mfma_f32_32x32x16_bf16 v[32:47], v[192:195], v[128:131], v[32:47]
	v_mfma_f32_32x32x16_bf16 v[32:47], v[196:199], v[132:135], v[32:47]
	v_mfma_f32_32x32x16_bf16 v[32:47], v[200:203], v[136:139], v[32:47]
	v_mfma_f32_32x32x16_bf16 v[32:47], v[204:207], v[140:143], v[32:47]
	ds_read_b64_tr_b16 v[192:193], v177 offset:0xe00
	ds_read_b64_tr_b16 v[194:195], v177 offset:0x1e00
	ds_read_b64_tr_b16 v[196:197], v177 offset:0x2e00
	ds_read_b64_tr_b16 v[198:199], v177 offset:0x3e00
	ds_read_b64_tr_b16 v[200:201], v177 offset:0x4e00
	ds_read_b64_tr_b16 v[202:203], v177 offset:0x5e00
	ds_read_b64_tr_b16 v[204:205], v177 offset:0x6e00
	ds_read_b64_tr_b16 v[206:207], v177 offset:0x7e00
	s_waitcnt lgkmcnt(8)
	v_mfma_f32_32x32x16_bf16 v[16:31], v[144:147], v[128:131], v[16:31]
	v_mfma_f32_32x32x16_bf16 v[16:31], v[148:151], v[132:135], v[16:31]
	v_mfma_f32_32x32x16_bf16 v[16:31], v[152:155], v[136:139], v[16:31]
	v_mfma_f32_32x32x16_bf16 v[16:31], v[156:159], v[140:143], v[16:31]
	s_waitcnt lgkmcnt(0)
	v_mfma_f32_32x32x16_bf16 v[0:15], v[192:195], v[128:131], v[0:15]
	v_mfma_f32_32x32x16_bf16 v[0:15], v[196:199], v[132:135], v[0:15]
	v_mfma_f32_32x32x16_bf16 v[0:15], v[200:203], v[136:139], v[0:15]
	v_mfma_f32_32x32x16_bf16 v[0:15], v[204:207], v[140:143], v[0:15]
	ds_read_b128 v[128:131], v188 offset:0
	ds_read_b128 v[132:135], v188 offset:0x2000
	ds_read_b128 v[136:139], v180 offset:0
	ds_read_b128 v[192:195], v187 offset:0
	ds_read_b128 v[196:199], v187 offset:0x2000
	ds_read_b128 v[200:203], v180 offset:0x400
	s_waitcnt lgkmcnt(3)
	s_nop 0
	v_mfma_f32_32x32x16_bf16 v[144:159], v[128:131], v[136:139], 0
	v_mfma_f32_32x32x16_bf16 v[128:143], v[132:135], v[136:139], 0
	ds_read_b128 v[204:207], v186 offset:0
	ds_read_b128 v[208:211], v186 offset:0x2000
	ds_read_b128 v[212:215], v180 offset:0x800
	s_waitcnt lgkmcnt(3)
	v_mfma_f32_32x32x16_bf16 v[144:159], v[192:195], v[200:203], v[144:159]
	v_mfma_f32_32x32x16_bf16 v[128:143], v[196:199], v[200:203], v[128:143]
	ds_read_b128 v[192:195], v185 offset:0
	ds_read_b128 v[196:199], v185 offset:0x2000
	ds_read_b128 v[200:203], v180 offset:0xc00
	s_waitcnt lgkmcnt(3)
	v_mfma_f32_32x32x16_bf16 v[144:159], v[204:207], v[212:215], v[144:159]
	v_mfma_f32_32x32x16_bf16 v[128:143], v[208:211], v[212:215], v[128:143]
	ds_read_b128 v[204:207], v188 offset:0x80
	ds_read_b128 v[208:211], v188 offset:0x2080
	ds_read_b128 v[212:215], v180 offset:0x1000
	s_waitcnt lgkmcnt(3)
	v_mfma_f32_32x32x16_bf16 v[144:159], v[192:195], v[200:203], v[144:159]
	v_mfma_f32_32x32x16_bf16 v[128:143], v[196:199], v[200:203], v[128:143]
	ds_read_b128 v[192:195], v187 offset:0x80
	ds_read_b128 v[196:199], v187 offset:0x2080
	ds_read_b128 v[200:203], v180 offset:0x1400
	s_waitcnt lgkmcnt(3)
	v_mfma_f32_32x32x16_bf16 v[144:159], v[204:207], v[212:215], v[144:159]
	v_mfma_f32_32x32x16_bf16 v[128:143], v[208:211], v[212:215], v[128:143]
	ds_read_b128 v[204:207], v186 offset:0x80
	ds_read_b128 v[208:211], v186 offset:0x2080
	ds_read_b128 v[212:215], v180 offset:0x1800
	s_waitcnt lgkmcnt(3)
	v_mfma_f32_32x32x16_bf16 v[144:159], v[192:195], v[200:203], v[144:159]
	v_mfma_f32_32x32x16_bf16 v[128:143], v[196:199], v[200:203], v[128:143]
	ds_read_b128 v[192:195], v185 offset:0x80
	ds_read_b128 v[196:199], v185 offset:0x2080
	s_waitcnt lgkmcnt(2)
	v_mfma_f32_32x32x16_bf16 v[144:159], v[204:207], v[212:215], v[144:159]
	v_mfma_f32_32x32x16_bf16 v[128:143], v[208:211], v[212:215], v[128:143]
	s_waitcnt lgkmcnt(0)
	v_mfma_f32_32x32x16_bf16 v[144:159], v[192:195], v[166:169], v[144:159]
	v_mfma_f32_32x32x16_bf16 v[128:143], v[196:199], v[166:169], v[128:143]
	s_bitcmp0_b32 s100, 8
	s_cbranch_scc1 .Lstg_a18
	s_waitcnt vmcnt(0)
	s_waitcnt lgkmcnt(0)
	s_barrier
.Lstg_a18:
	s_sub_i32 s4, s97, 64
	s_cmp_le_i32 s4, s74
	s_cbranch_scc1 .LBB0_591
	v_add_u32_e32 v172, 64, v189
	v_cmp_gt_i32_e64 s[62:63], 26, v172
	v_cmp_gt_i32_e64 s[64:65], 27, v172
	v_cmp_gt_i32_e64 s[60:61], 25, v172
	s_and_b64 s[62:63], s[64:65], s[62:63]
	v_cmp_gt_i32_e64 s[58:59], 24, v172
	s_and_b64 s[60:61], s[62:63], s[60:61]
	v_cmp_gt_i32_e64 s[56:57], 19, v172
	s_and_b64 s[58:59], s[60:61], s[58:59]
	v_cmp_gt_i32_e64 s[54:55], 18, v172
	s_and_b64 s[56:57], s[58:59], s[56:57]
	v_cmp_gt_i32_e64 s[52:53], 17, v172
	s_and_b64 s[54:55], s[56:57], s[54:55]
	v_cmp_gt_i32_e64 s[50:51], 16, v172
	s_and_b64 s[52:53], s[54:55], s[52:53]
	v_cmp_gt_i32_e64 s[48:49], 11, v172
	s_and_b64 s[50:51], s[52:53], s[50:51]
	v_cmp_gt_i32_e64 s[46:47], 10, v172
	s_and_b64 s[48:49], s[50:51], s[48:49]
	v_cmp_gt_i32_e64 s[44:45], 9, v172
	s_and_b64 s[46:47], s[48:49], s[46:47]
	v_cmp_gt_i32_e64 s[42:43], 8, v172
	s_and_b64 s[44:45], s[46:47], s[44:45]
	v_cmp_gt_i32_e64 s[40:41], 3, v172
	s_and_b64 s[42:43], s[44:45], s[42:43]
	v_cmp_gt_i32_e64 s[38:39], 2, v172
	s_and_b64 s[40:41], s[42:43], s[40:41]
	v_cmp_gt_i32_e64 s[36:37], 1, v172
	s_and_b64 s[38:39], s[40:41], s[38:39]
	v_cmp_gt_i32_e64 s[34:35], 0, v172
	s_and_b64 s[36:37], s[38:39], s[36:37]
	s_and_b64 s[34:35], s[36:37], s[34:35]
	v_cmp_gt_i32_e64 s[30:31], 58, v172
	v_cndmask_b32_e64 v144, v144, v226, s[34:35]
	v_cmp_gt_i32_e64 s[34:35], 59, v172
	v_cmp_gt_i32_e64 s[28:29], 57, v172
	s_and_b64 s[30:31], s[34:35], s[30:31]
	v_cmp_gt_i32_e64 s[26:27], 56, v172
	s_and_b64 s[28:29], s[30:31], s[28:29]
	v_cmp_gt_i32_e64 s[24:25], 51, v172
	s_and_b64 s[26:27], s[28:29], s[26:27]
	v_cmp_gt_i32_e64 s[22:23], 50, v172
	s_and_b64 s[24:25], s[26:27], s[24:25]
	v_cmp_gt_i32_e64 s[20:21], 49, v172
	s_and_b64 s[22:23], s[24:25], s[22:23]
	v_cmp_gt_i32_e64 s[18:19], 48, v172
	s_and_b64 s[20:21], s[22:23], s[20:21]
	v_cmp_gt_i32_e64 s[16:17], 43, v172
	s_and_b64 s[18:19], s[20:21], s[18:19]
	v_cmp_gt_i32_e64 s[14:15], 42, v172
	s_and_b64 s[16:17], s[18:19], s[16:17]
	v_cmp_gt_i32_e64 s[12:13], 41, v172
	s_and_b64 s[14:15], s[16:17], s[14:15]
	v_cmp_gt_i32_e64 s[10:11], 40, v172
	s_and_b64 s[12:13], s[14:15], s[12:13]
	v_cmp_gt_i32_e64 s[8:9], 35, v172
	s_and_b64 s[10:11], s[12:13], s[10:11]
	v_cmp_gt_i32_e64 s[6:7], 34, v172
	s_and_b64 s[8:9], s[10:11], s[8:9]
	v_cmp_gt_i32_e64 s[4:5], 33, v172
	s_and_b64 s[6:7], s[8:9], s[6:7]
	v_cmp_gt_i32_e32 vcc, 32, v172
	s_and_b64 s[4:5], s[6:7], s[4:5]
	s_and_b64 vcc, s[4:5], vcc
	v_cndmask_b32_e64 v159, v159, v226, s[64:65]
	v_cndmask_b32_e64 v158, v158, v226, s[62:63]
	s_mov_b64 s[62:63], 0x100
	v_cndmask_b32_e64 v157, v157, v226, s[60:61]
	v_cndmask_b32_e64 v156, v156, v226, s[58:59]
	v_cndmask_b32_e64 v155, v155, v226, s[56:57]
	v_cndmask_b32_e64 v154, v154, v226, s[54:55]
	v_cndmask_b32_e64 v153, v153, v226, s[52:53]
	v_cndmask_b32_e64 v152, v152, v226, s[50:51]
	v_cndmask_b32_e64 v151, v151, v226, s[48:49]
	v_cndmask_b32_e64 v150, v150, v226, s[46:47]
	v_cndmask_b32_e64 v149, v149, v226, s[44:45]
	v_cndmask_b32_e64 v148, v148, v226, s[42:43]
	v_cndmask_b32_e64 v147, v147, v226, s[40:41]
	v_cndmask_b32_e64 v146, v146, v226, s[38:39]
	v_cndmask_b32_e64 v145, v145, v226, s[36:37]
	v_cndmask_b32_e64 v143, v143, v226, s[34:35]
	v_cndmask_b32_e64 v142, v142, v226, s[30:31]
	v_cndmask_b32_e64 v141, v141, v226, s[28:29]
	v_cndmask_b32_e64 v140, v140, v226, s[26:27]
	v_cndmask_b32_e64 v139, v139, v226, s[24:25]
	v_cndmask_b32_e64 v138, v138, v226, s[22:23]
	v_cndmask_b32_e64 v137, v137, v226, s[20:21]
	v_cndmask_b32_e64 v136, v136, v226, s[18:19]
	v_cndmask_b32_e64 v135, v135, v226, s[16:17]
	v_cndmask_b32_e64 v134, v134, v226, s[14:15]
	v_cndmask_b32_e64 v133, v133, v226, s[12:13]
	v_cndmask_b32_e64 v132, v132, v226, s[10:11]
	v_cndmask_b32_e64 v131, v131, v226, s[8:9]
	v_cndmask_b32_e64 v130, v130, v226, s[6:7]
	v_cndmask_b32_e64 v129, v129, v226, s[4:5]
	v_cndmask_b32_e32 v128, v128, v226, vcc

.Lstg_b22:
	s_add_i32 s8, s85, -1
	s_cmp_ge_u32 s8, s75
	s_cselect_b64 s[66:67], -1, 0
	s_mov_b64 s[6:7], -1
	s_and_b64 vcc, exec, s[66:67]
	s_cbranch_vccz .LBB0_593
	v_mov_b64_e32 v[144:145], s[80:81]
	flat_load_dword v146, v[144:145] sc0 sc1
	s_waitcnt vmcnt(0)
	v_mov_b64_e32 v[144:145], s[72:73]
	flat_load_dword v144, v[144:145] sc0 sc1
	s_waitcnt vmcnt(0) lgkmcnt(0)
	v_readfirstlane_b32 s6, v146
	v_readfirstlane_b32 s7, v144
	s_nop 1
	v_lshl_add_u64 v[144:145], s[6:7], 0, v[160:161]
	s_mov_b32 s8, m0
	s_mov_b32 m0, s78
	s_nop 0
	global_load_lds_dwordx4 v[144:145], off
	s_mov_b32 m0, s8
	v_lshl_add_u64 v[144:145], s[6:7], 0, v[170:171]
	s_mov_b32 s6, m0
	s_mov_b32 m0, s93
	s_nop 0
	global_load_lds_dwordx4 v[144:145], off
	s_mov_b32 m0, s6
	s_mov_b64 s[6:7], 0

.LBB0_597:
	ds_read_b64_tr_b16 v[144:145], v177 offset:0x8000
	ds_read_b64_tr_b16 v[146:147], v177 offset:0x9000
	ds_read_b64_tr_b16 v[148:149], v177 offset:0xa000
	ds_read_b64_tr_b16 v[150:151], v177 offset:0xb000
	ds_read_b64_tr_b16 v[152:153], v177 offset:0xc000
	ds_read_b64_tr_b16 v[154:155], v177 offset:0xd000
	ds_read_b64_tr_b16 v[156:157], v177 offset:0xe000
	ds_read_b64_tr_b16 v[158:159], v177 offset:0xf000
	ds_read_b64_tr_b16 v[194:195], v177 offset:0x8200
	ds_read_b64_tr_b16 v[196:197], v177 offset:0x9200
	ds_read_b64_tr_b16 v[198:199], v177 offset:0xa200
	ds_read_b64_tr_b16 v[200:201], v177 offset:0xb200
	ds_read_b64_tr_b16 v[202:203], v177 offset:0xc200
	ds_read_b64_tr_b16 v[204:205], v177 offset:0xd200
	ds_read_b64_tr_b16 v[206:207], v177 offset:0xe200
	ds_read_b64_tr_b16 v[208:209], v177 offset:0xf200
	s_waitcnt lgkmcnt(8)
	s_nop 0
	v_mfma_f32_32x32x16_bf16 v[112:127], v[144:147], v[128:131], v[112:127]
	v_mfma_f32_32x32x16_bf16 v[112:127], v[148:151], v[132:135], v[112:127]
	v_mfma_f32_32x32x16_bf16 v[112:127], v[152:155], v[136:139], v[112:127]
	v_mfma_f32_32x32x16_bf16 v[112:127], v[156:159], v[140:143], v[112:127]
	ds_read_b64_tr_b16 v[144:145], v177 offset:0x8400
	ds_read_b64_tr_b16 v[146:147], v177 offset:0x9400
	ds_read_b64_tr_b16 v[148:149], v177 offset:0xa400
	ds_read_b64_tr_b16 v[150:151], v177 offset:0xb400
	ds_read_b64_tr_b16 v[152:153], v177 offset:0xc400
	ds_read_b64_tr_b16 v[154:155], v177 offset:0xd400
	ds_read_b64_tr_b16 v[156:157], v177 offset:0xe400
	ds_read_b64_tr_b16 v[158:159], v177 offset:0xf400
	s_waitcnt lgkmcnt(8)
	v_mfma_f32_32x32x16_bf16 v[96:111], v[194:197], v[128:131], v[96:111]
	v_mfma_f32_32x32x16_bf16 v[96:111], v[198:201], v[132:135], v[96:111]
	v_mfma_f32_32x32x16_bf16 v[96:111], v[202:205], v[136:139], v[96:111]
	v_mfma_f32_32x32x16_bf16 v[96:111], v[206:209], v[140:143], v[96:111]
	ds_read_b64_tr_b16 v[194:195], v177 offset:0x8600
	ds_read_b64_tr_b16 v[196:197], v177 offset:0x9600
	ds_read_b64_tr_b16 v[198:199], v177 offset:0xa600
	ds_read_b64_tr_b16 v[200:201], v177 offset:0xb600
	ds_read_b64_tr_b16 v[202:203], v177 offset:0xc600
	ds_read_b64_tr_b16 v[204:205], v177 offset:0xd600
	ds_read_b64_tr_b16 v[206:207], v177 offset:0xe600
	ds_read_b64_tr_b16 v[208:209], v177 offset:0xf600
	s_waitcnt lgkmcnt(8)
	v_mfma_f32_32x32x16_bf16 v[80:95], v[144:147], v[128:131], v[80:95]
	v_mfma_f32_32x32x16_bf16 v[80:95], v[148:151], v[132:135], v[80:95]
	v_mfma_f32_32x32x16_bf16 v[80:95], v[152:155], v[136:139], v[80:95]
	v_mfma_f32_32x32x16_bf16 v[80:95], v[156:159], v[140:143], v[80:95]
	ds_read_b64_tr_b16 v[144:145], v177 offset:0x8800
	ds_read_b64_tr_b16 v[146:147], v177 offset:0x9800
	ds_read_b64_tr_b16 v[148:149], v177 offset:0xa800
	ds_read_b64_tr_b16 v[150:151], v177 offset:0xb800
	ds_read_b64_tr_b16 v[152:153], v177 offset:0xc800
	ds_read_b64_tr_b16 v[154:155], v177 offset:0xd800
	ds_read_b64_tr_b16 v[156:157], v177 offset:0xe800
	ds_read_b64_tr_b16 v[158:159], v177 offset:0xf800
	s_waitcnt lgkmcnt(8)
	v_mfma_f32_32x32x16_bf16 v[64:79], v[194:197], v[128:131], v[64:79]
	v_mfma_f32_32x32x16_bf16 v[64:79], v[198:201], v[132:135], v[64:79]
	v_mfma_f32_32x32x16_bf16 v[64:79], v[202:205], v[136:139], v[64:79]
	v_mfma_f32_32x32x16_bf16 v[64:79], v[206:209], v[140:143], v[64:79]
	ds_read_b64_tr_b16 v[194:195], v177 offset:0x8a00
	ds_read_b64_tr_b16 v[196:197], v177 offset:0x9a00
	ds_read_b64_tr_b16 v[198:199], v177 offset:0xaa00
	ds_read_b64_tr_b16 v[200:201], v177 offset:0xba00
	ds_read_b64_tr_b16 v[202:203], v177 offset:0xca00
	ds_read_b64_tr_b16 v[204:205], v177 offset:0xda00
	ds_read_b64_tr_b16 v[206:207], v177 offset:0xea00
	ds_read_b64_tr_b16 v[208:209], v177 offset:0xfa00
	s_waitcnt lgkmcnt(8)
	v_mfma_f32_32x32x16_bf16 v[48:63], v[144:147], v[128:131], v[48:63]
	v_mfma_f32_32x32x16_bf16 v[48:63], v[148:151], v[132:135], v[48:63]
	v_mfma_f32_32x32x16_bf16 v[48:63], v[152:155], v[136:139], v[48:63]
	v_mfma_f32_32x32x16_bf16 v[48:63], v[156:159], v[140:143], v[48:63]
	ds_read_b64_tr_b16 v[144:145], v177 offset:0x8c00
	ds_read_b64_tr_b16 v[146:147], v177 offset:0x9c00
	ds_read_b64_tr_b16 v[148:149], v177 offset:0xac00
	ds_read_b64_tr_b16 v[150:151], v177 offset:0xbc00
	ds_read_b64_tr_b16 v[152:153], v177 offset:0xcc00
	ds_read_b64_tr_b16 v[154:155], v177 offset:0xdc00
	ds_read_b64_tr_b16 v[156:157], v177 offset:0xec00
	ds_read_b64_tr_b16 v[158:159], v177 offset:0xfc00
	s_waitcnt lgkmcnt(8)
	v_mfma_f32_32x32x16_bf16 v[32:47], v[194:197], v[128:131], v[32:47]
	v_mfma_f32_32x32x16_bf16 v[32:47], v[198:201], v[132:135], v[32:47]
	v_mfma_f32_32x32x16_bf16 v[32:47], v[202:205], v[136:139], v[32:47]
	v_mfma_f32_32x32x16_bf16 v[32:47], v[206:209], v[140:143], v[32:47]
	ds_read_b64_tr_b16 v[194:195], v177 offset:0x8e00
	ds_read_b64_tr_b16 v[196:197], v177 offset:0x9e00
	ds_read_b64_tr_b16 v[198:199], v177 offset:0xae00
	ds_read_b64_tr_b16 v[200:201], v177 offset:0xbe00
	ds_read_b64_tr_b16 v[202:203], v177 offset:0xce00
	ds_read_b64_tr_b16 v[204:205], v177 offset:0xde00
	ds_read_b64_tr_b16 v[206:207], v177 offset:0xee00
	ds_read_b64_tr_b16 v[208:209], v177 offset:0xfe00
	s_waitcnt lgkmcnt(8)
	v_mfma_f32_32x32x16_bf16 v[16:31], v[144:147], v[128:131], v[16:31]
	v_mfma_f32_32x32x16_bf16 v[16:31], v[148:151], v[132:135], v[16:31]
	v_mfma_f32_32x32x16_bf16 v[16:31], v[152:155], v[136:139], v[16:31]
	v_mfma_f32_32x32x16_bf16 v[16:31], v[156:159], v[140:143], v[16:31]
	s_waitcnt lgkmcnt(0)
	v_mfma_f32_32x32x16_bf16 v[0:15], v[194:197], v[128:131], v[0:15]
	v_mfma_f32_32x32x16_bf16 v[0:15], v[198:201], v[132:135], v[0:15]
	v_mfma_f32_32x32x16_bf16 v[0:15], v[202:205], v[136:139], v[0:15]
	v_mfma_f32_32x32x16_bf16 v[0:15], v[206:209], v[140:143], v[0:15]
	ds_read_b128 v[128:131], v181 offset:0
	ds_read_b128 v[132:135], v181 offset:0x2000
	ds_read_b128 v[136:139], v180 offset:0
	ds_read_b128 v[194:197], v182 offset:0
	ds_read_b128 v[198:201], v182 offset:0x2000
	ds_read_b128 v[202:205], v180 offset:0x400
	s_waitcnt lgkmcnt(3)
	s_nop 0
	v_mfma_f32_32x32x16_bf16 v[144:159], v[128:131], v[136:139], 0
	v_mfma_f32_32x32x16_bf16 v[128:143], v[132:135], v[136:139], 0
	ds_read_b128 v[206:209], v183 offset:0
	ds_read_b128 v[210:213], v183 offset:0x2000
	ds_read_b128 v[214:217], v180 offset:0x800
	s_waitcnt lgkmcnt(3)
	v_mfma_f32_32x32x16_bf16 v[144:159], v[194:197], v[202:205], v[144:159]
	v_mfma_f32_32x32x16_bf16 v[128:143], v[198:201], v[202:205], v[128:143]
	ds_read_b128 v[194:197], v184 offset:0
	ds_read_b128 v[198:201], v184 offset:0x2000
	ds_read_b128 v[202:205], v180 offset:0xc00
	s_waitcnt lgkmcnt(3)
	v_mfma_f32_32x32x16_bf16 v[144:159], v[206:209], v[214:217], v[144:159]
	v_mfma_f32_32x32x16_bf16 v[128:143], v[210:213], v[214:217], v[128:143]
	ds_read_b128 v[206:209], v181 offset:0x80
	ds_read_b128 v[210:213], v181 offset:0x2080
	ds_read_b128 v[214:217], v180 offset:0x1000
	s_waitcnt lgkmcnt(3)
	v_mfma_f32_32x32x16_bf16 v[144:159], v[194:197], v[202:205], v[144:159]
	v_mfma_f32_32x32x16_bf16 v[128:143], v[198:201], v[202:205], v[128:143]
	ds_read_b128 v[194:197], v182 offset:0x80
	ds_read_b128 v[198:201], v182 offset:0x2080
	ds_read_b128 v[202:205], v180 offset:0x1400
	s_waitcnt lgkmcnt(3)
	v_mfma_f32_32x32x16_bf16 v[144:159], v[206:209], v[214:217], v[144:159]
	v_mfma_f32_32x32x16_bf16 v[128:143], v[210:213], v[214:217], v[128:143]
	ds_read_b128 v[206:209], v183 offset:0x80
	ds_read_b128 v[210:213], v183 offset:0x2080
	ds_read_b128 v[214:217], v180 offset:0x1800
	s_waitcnt lgkmcnt(3)
	v_mfma_f32_32x32x16_bf16 v[144:159], v[194:197], v[202:205], v[144:159]
	v_mfma_f32_32x32x16_bf16 v[128:143], v[198:201], v[202:205], v[128:143]
	ds_read_b128 v[194:197], v184 offset:0x80
	ds_read_b128 v[198:201], v184 offset:0x2080
	s_waitcnt lgkmcnt(2)
	v_mfma_f32_32x32x16_bf16 v[144:159], v[206:209], v[214:217], v[144:159]
	v_mfma_f32_32x32x16_bf16 v[128:143], v[210:213], v[214:217], v[128:143]
	s_waitcnt lgkmcnt(0)
	v_mfma_f32_32x32x16_bf16 v[144:159], v[194:197], v[166:169], v[144:159]
	v_mfma_f32_32x32x16_bf16 v[128:143], v[198:201], v[166:169], v[128:143]
	s_bitcmp0_b32 s100, 8
	s_cbranch_scc1 .Lstg_a19
	s_waitcnt vmcnt(0)
	s_waitcnt lgkmcnt(0)
	s_barrier
.Lstg_a19:
	s_cmp_le_i32 s97, s74
	s_cbranch_scc1 .LBB0_599
	v_cmp_gt_i32_e64 s[62:63], 26, v189
	v_cmp_gt_i32_e64 s[64:65], 27, v189
	v_cmp_gt_i32_e64 s[60:61], 25, v189
	s_and_b64 s[62:63], s[64:65], s[62:63]
	v_cmp_gt_i32_e64 s[58:59], 24, v189
	s_and_b64 s[60:61], s[62:63], s[60:61]
	v_cmp_gt_i32_e64 s[56:57], 19, v189
	s_and_b64 s[58:59], s[60:61], s[58:59]
	v_cmp_gt_i32_e64 s[54:55], 18, v189
	s_and_b64 s[56:57], s[58:59], s[56:57]
	v_cmp_gt_i32_e64 s[52:53], 17, v189
	s_and_b64 s[54:55], s[56:57], s[54:55]
	v_cmp_gt_i32_e64 s[50:51], 16, v189
	s_and_b64 s[52:53], s[54:55], s[52:53]
	v_cmp_gt_i32_e64 s[48:49], 11, v189
	s_and_b64 s[50:51], s[52:53], s[50:51]
	v_cmp_gt_i32_e64 s[46:47], 10, v189
	s_and_b64 s[48:49], s[50:51], s[48:49]
	v_cmp_gt_i32_e64 s[44:45], 9, v189
	s_and_b64 s[46:47], s[48:49], s[46:47]
	v_cmp_gt_i32_e64 s[42:43], 8, v189
	s_and_b64 s[44:45], s[46:47], s[44:45]
	v_cmp_gt_i32_e64 s[40:41], 3, v189
	s_and_b64 s[42:43], s[44:45], s[42:43]
	v_cmp_gt_i32_e64 s[38:39], 2, v189
	s_and_b64 s[40:41], s[42:43], s[40:41]
	v_cmp_gt_i32_e64 s[36:37], 1, v189
	s_and_b64 s[38:39], s[40:41], s[38:39]
	v_cmp_gt_i32_e64 s[34:35], 0, v189
	s_and_b64 s[36:37], s[38:39], s[36:37]
	s_and_b64 s[34:35], s[36:37], s[34:35]
	v_cmp_gt_i32_e64 s[30:31], 58, v189
	v_cndmask_b32_e64 v144, v144, v226, s[34:35]
	v_cmp_gt_i32_e64 s[34:35], 59, v189
	v_cmp_gt_i32_e64 s[28:29], 57, v189
	s_and_b64 s[30:31], s[34:35], s[30:31]
	v_cmp_gt_i32_e64 s[26:27], 56, v189
	s_and_b64 s[28:29], s[30:31], s[28:29]
	v_cmp_gt_i32_e64 s[24:25], 51, v189
	s_and_b64 s[26:27], s[28:29], s[26:27]
	v_cmp_gt_i32_e64 s[22:23], 50, v189
	s_and_b64 s[24:25], s[26:27], s[24:25]
	v_cmp_gt_i32_e64 s[20:21], 49, v189
	s_and_b64 s[22:23], s[24:25], s[22:23]
	v_cmp_gt_i32_e64 s[18:19], 48, v189
	s_and_b64 s[20:21], s[22:23], s[20:21]
	v_cmp_gt_i32_e64 s[16:17], 43, v189
	s_and_b64 s[18:19], s[20:21], s[18:19]
	v_cmp_gt_i32_e64 s[14:15], 42, v189
	s_and_b64 s[16:17], s[18:19], s[16:17]
	v_cmp_gt_i32_e64 s[12:13], 41, v189
	s_and_b64 s[14:15], s[16:17], s[14:15]
	v_cmp_gt_i32_e64 s[10:11], 40, v189
	s_and_b64 s[12:13], s[14:15], s[12:13]
	v_cmp_gt_i32_e64 s[8:9], 35, v189
	s_and_b64 s[10:11], s[12:13], s[10:11]
	v_cmp_gt_i32_e64 s[6:7], 34, v189
	s_and_b64 s[8:9], s[10:11], s[8:9]
	v_cmp_gt_i32_e64 s[4:5], 33, v189
	s_and_b64 s[6:7], s[8:9], s[6:7]
	v_cmp_gt_i32_e32 vcc, 32, v189
	s_and_b64 s[4:5], s[6:7], s[4:5]
	s_and_b64 vcc, s[4:5], vcc
	v_cndmask_b32_e64 v159, v159, v226, s[64:65]
	v_cndmask_b32_e64 v158, v158, v226, s[62:63]
	s_mov_b64 s[62:63], 0x100
	v_cndmask_b32_e64 v157, v157, v226, s[60:61]
	v_cndmask_b32_e64 v156, v156, v226, s[58:59]
	v_cndmask_b32_e64 v155, v155, v226, s[56:57]
	v_cndmask_b32_e64 v154, v154, v226, s[54:55]
	v_cndmask_b32_e64 v153, v153, v226, s[52:53]
	v_cndmask_b32_e64 v152, v152, v226, s[50:51]
	v_cndmask_b32_e64 v151, v151, v226, s[48:49]
	v_cndmask_b32_e64 v150, v150, v226, s[46:47]
	v_cndmask_b32_e64 v149, v149, v226, s[44:45]
	v_cndmask_b32_e64 v148, v148, v226, s[42:43]
	v_cndmask_b32_e64 v147, v147, v226, s[40:41]
	v_cndmask_b32_e64 v146, v146, v226, s[38:39]
	v_cndmask_b32_e64 v145, v145, v226, s[36:37]
	v_cndmask_b32_e64 v143, v143, v226, s[34:35]
	v_cndmask_b32_e64 v142, v142, v226, s[30:31]
	v_cndmask_b32_e64 v141, v141, v226, s[28:29]
	v_cndmask_b32_e64 v140, v140, v226, s[26:27]
	v_cndmask_b32_e64 v139, v139, v226, s[24:25]
	v_cndmask_b32_e64 v138, v138, v226, s[22:23]
	v_cndmask_b32_e64 v137, v137, v226, s[20:21]
	v_cndmask_b32_e64 v136, v136, v226, s[18:19]
	v_cndmask_b32_e64 v135, v135, v226, s[16:17]
	v_cndmask_b32_e64 v134, v134, v226, s[14:15]
	v_cndmask_b32_e64 v133, v133, v226, s[12:13]
	v_cndmask_b32_e64 v132, v132, v226, s[10:11]
	v_cndmask_b32_e64 v131, v131, v226, s[8:9]
	v_cndmask_b32_e64 v130, v130, v226, s[6:7]
	v_cndmask_b32_e64 v129, v129, v226, s[4:5]
	v_cndmask_b32_e32 v128, v128, v226, vcc

.Lstg_b23:
	s_cmp_gt_u32 s85, s75
	s_cbranch_scc1 .LBB0_604
	s_cmp_ge_u32 s85, s75
	s_mov_b64 s[6:7], -1
	s_cbranch_scc0 .LBB0_602
	v_mov_b64_e32 v[148:149], s[80:81]
	flat_load_dword v144, v[148:149] sc0 sc1
	s_waitcnt vmcnt(0)
	v_mov_b64_e32 v[148:149], s[72:73]
	flat_load_dword v147, v[148:149] sc0 sc1
	s_waitcnt vmcnt(0) lgkmcnt(0)
	v_readfirstlane_b32 s6, v144
	v_readfirstlane_b32 s7, v147
	s_nop 1
	v_lshl_add_u64 v[148:149], s[6:7], 0, v[160:161]
	s_mov_b32 s8, m0
	s_mov_b32 m0, s78
	s_nop 0
	global_load_lds_dwordx4 v[148:149], off
	s_mov_b32 m0, s8
	v_lshl_add_u64 v[148:149], s[6:7], 0, v[170:171]
	s_mov_b32 s6, m0
	s_mov_b32 m0, s93
	s_nop 0
	global_load_lds_dwordx4 v[148:149], off
	s_mov_b32 m0, s6
	s_mov_b64 s[6:7], 0

.LBB0_612:
	ds_read_b64_tr_b16 v[144:145], v177 offset:0
	ds_read_b64_tr_b16 v[146:147], v177 offset:0x1000
	ds_read_b64_tr_b16 v[148:149], v177 offset:0x2000
	ds_read_b64_tr_b16 v[150:151], v177 offset:0x3000
	ds_read_b64_tr_b16 v[152:153], v177 offset:0x4000
	ds_read_b64_tr_b16 v[154:155], v177 offset:0x5000
	ds_read_b64_tr_b16 v[156:157], v177 offset:0x6000
	ds_read_b64_tr_b16 v[158:159], v177 offset:0x7000
	ds_read_b64_tr_b16 v[192:193], v177 offset:0x200
	ds_read_b64_tr_b16 v[194:195], v177 offset:0x1200
	ds_read_b64_tr_b16 v[196:197], v177 offset:0x2200
	ds_read_b64_tr_b16 v[198:199], v177 offset:0x3200
	ds_read_b64_tr_b16 v[200:201], v177 offset:0x4200
	ds_read_b64_tr_b16 v[202:203], v177 offset:0x5200
	ds_read_b64_tr_b16 v[204:205], v177 offset:0x6200
	ds_read_b64_tr_b16 v[206:207], v177 offset:0x7200
	s_waitcnt lgkmcnt(8)
	s_nop 0
	v_mfma_f32_32x32x16_bf16 v[112:127], v[144:147], v[128:131], v[112:127]
	v_mfma_f32_32x32x16_bf16 v[112:127], v[148:151], v[132:135], v[112:127]
	v_mfma_f32_32x32x16_bf16 v[112:127], v[152:155], v[136:139], v[112:127]
	v_mfma_f32_32x32x16_bf16 v[112:127], v[156:159], v[140:143], v[112:127]
	ds_read_b64_tr_b16 v[144:145], v177 offset:0x400
	ds_read_b64_tr_b16 v[146:147], v177 offset:0x1400
	ds_read_b64_tr_b16 v[148:149], v177 offset:0x2400
	ds_read_b64_tr_b16 v[150:151], v177 offset:0x3400
	ds_read_b64_tr_b16 v[152:153], v177 offset:0x4400
	ds_read_b64_tr_b16 v[154:155], v177 offset:0x5400
	ds_read_b64_tr_b16 v[156:157], v177 offset:0x6400
	ds_read_b64_tr_b16 v[158:159], v177 offset:0x7400
	s_waitcnt lgkmcnt(8)
	v_mfma_f32_32x32x16_bf16 v[96:111], v[192:195], v[128:131], v[96:111]
	v_mfma_f32_32x32x16_bf16 v[96:111], v[196:199], v[132:135], v[96:111]
	v_mfma_f32_32x32x16_bf16 v[96:111], v[200:203], v[136:139], v[96:111]
	v_mfma_f32_32x32x16_bf16 v[96:111], v[204:207], v[140:143], v[96:111]
	ds_read_b64_tr_b16 v[192:193], v177 offset:0x600
	ds_read_b64_tr_b16 v[194:195], v177 offset:0x1600
	ds_read_b64_tr_b16 v[196:197], v177 offset:0x2600
	ds_read_b64_tr_b16 v[198:199], v177 offset:0x3600
	ds_read_b64_tr_b16 v[200:201], v177 offset:0x4600
	ds_read_b64_tr_b16 v[202:203], v177 offset:0x5600
	ds_read_b64_tr_b16 v[204:205], v177 offset:0x6600
	ds_read_b64_tr_b16 v[206:207], v177 offset:0x7600
	s_waitcnt lgkmcnt(8)
	v_mfma_f32_32x32x16_bf16 v[80:95], v[144:147], v[128:131], v[80:95]
	v_mfma_f32_32x32x16_bf16 v[80:95], v[148:151], v[132:135], v[80:95]
	v_mfma_f32_32x32x16_bf16 v[80:95], v[152:155], v[136:139], v[80:95]
	v_mfma_f32_32x32x16_bf16 v[80:95], v[156:159], v[140:143], v[80:95]
	ds_read_b64_tr_b16 v[144:145], v177 offset:0x800
	ds_read_b64_tr_b16 v[146:147], v177 offset:0x1800
	ds_read_b64_tr_b16 v[148:149], v177 offset:0x2800
	ds_read_b64_tr_b16 v[150:151], v177 offset:0x3800
	ds_read_b64_tr_b16 v[152:153], v177 offset:0x4800
	ds_read_b64_tr_b16 v[154:155], v177 offset:0x5800
	ds_read_b64_tr_b16 v[156:157], v177 offset:0x6800
	ds_read_b64_tr_b16 v[158:159], v177 offset:0x7800
	s_waitcnt lgkmcnt(8)
	v_mfma_f32_32x32x16_bf16 v[64:79], v[192:195], v[128:131], v[64:79]
	v_mfma_f32_32x32x16_bf16 v[64:79], v[196:199], v[132:135], v[64:79]
	v_mfma_f32_32x32x16_bf16 v[64:79], v[200:203], v[136:139], v[64:79]
	v_mfma_f32_32x32x16_bf16 v[64:79], v[204:207], v[140:143], v[64:79]
	ds_read_b64_tr_b16 v[192:193], v177 offset:0xa00
	ds_read_b64_tr_b16 v[194:195], v177 offset:0x1a00
	ds_read_b64_tr_b16 v[196:197], v177 offset:0x2a00
	ds_read_b64_tr_b16 v[198:199], v177 offset:0x3a00
	ds_read_b64_tr_b16 v[200:201], v177 offset:0x4a00
	ds_read_b64_tr_b16 v[202:203], v177 offset:0x5a00
	ds_read_b64_tr_b16 v[204:205], v177 offset:0x6a00
	ds_read_b64_tr_b16 v[206:207], v177 offset:0x7a00
	s_waitcnt lgkmcnt(8)
	v_mfma_f32_32x32x16_bf16 v[48:63], v[144:147], v[128:131], v[48:63]
	v_mfma_f32_32x32x16_bf16 v[48:63], v[148:151], v[132:135], v[48:63]
	v_mfma_f32_32x32x16_bf16 v[48:63], v[152:155], v[136:139], v[48:63]
	v_mfma_f32_32x32x16_bf16 v[48:63], v[156:159], v[140:143], v[48:63]
	ds_read_b64_tr_b16 v[144:145], v177 offset:0xc00
	ds_read_b64_tr_b16 v[146:147], v177 offset:0x1c00
	ds_read_b64_tr_b16 v[148:149], v177 offset:0x2c00
	ds_read_b64_tr_b16 v[150:151], v177 offset:0x3c00
	ds_read_b64_tr_b16 v[152:153], v177 offset:0x4c00
	ds_read_b64_tr_b16 v[154:155], v177 offset:0x5c00
	ds_read_b64_tr_b16 v[156:157], v177 offset:0x6c00
	ds_read_b64_tr_b16 v[158:159], v177 offset:0x7c00
	s_waitcnt lgkmcnt(8)
	v_mfma_f32_32x32x16_bf16 v[32:47], v[192:195], v[128:131], v[32:47]
	v_mfma_f32_32x32x16_bf16 v[32:47], v[196:199], v[132:135], v[32:47]
	v_mfma_f32_32x32x16_bf16 v[32:47], v[200:203], v[136:139], v[32:47]
	v_mfma_f32_32x32x16_bf16 v[32:47], v[204:207], v[140:143], v[32:47]
	ds_read_b64_tr_b16 v[192:193], v177 offset:0xe00
	ds_read_b64_tr_b16 v[194:195], v177 offset:0x1e00
	ds_read_b64_tr_b16 v[196:197], v177 offset:0x2e00
	ds_read_b64_tr_b16 v[198:199], v177 offset:0x3e00
	ds_read_b64_tr_b16 v[200:201], v177 offset:0x4e00
	ds_read_b64_tr_b16 v[202:203], v177 offset:0x5e00
	ds_read_b64_tr_b16 v[204:205], v177 offset:0x6e00
	ds_read_b64_tr_b16 v[206:207], v177 offset:0x7e00
	s_waitcnt lgkmcnt(8)
	v_mfma_f32_32x32x16_bf16 v[16:31], v[144:147], v[128:131], v[16:31]
	v_mfma_f32_32x32x16_bf16 v[16:31], v[148:151], v[132:135], v[16:31]
	v_mfma_f32_32x32x16_bf16 v[16:31], v[152:155], v[136:139], v[16:31]
	v_mfma_f32_32x32x16_bf16 v[16:31], v[156:159], v[140:143], v[16:31]
	s_waitcnt lgkmcnt(0)
	v_mfma_f32_32x32x16_bf16 v[0:15], v[192:195], v[128:131], v[0:15]
	v_mfma_f32_32x32x16_bf16 v[0:15], v[196:199], v[132:135], v[0:15]
	v_mfma_f32_32x32x16_bf16 v[0:15], v[200:203], v[136:139], v[0:15]
	v_mfma_f32_32x32x16_bf16 v[0:15], v[204:207], v[140:143], v[0:15]
	ds_read_b128 v[128:131], v188 offset:0
	ds_read_b128 v[132:135], v188 offset:0x2000
	ds_read_b128 v[136:139], v180 offset:0
	ds_read_b128 v[192:195], v187 offset:0
	ds_read_b128 v[196:199], v187 offset:0x2000
	ds_read_b128 v[200:203], v180 offset:0x400
	s_waitcnt lgkmcnt(3)
	s_nop 0
	v_mfma_f32_32x32x16_bf16 v[144:159], v[128:131], v[136:139], 0
	v_mfma_f32_32x32x16_bf16 v[128:143], v[132:135], v[136:139], 0
	ds_read_b128 v[204:207], v186 offset:0
	ds_read_b128 v[208:211], v186 offset:0x2000
	ds_read_b128 v[212:215], v180 offset:0x800
	s_waitcnt lgkmcnt(3)
	v_mfma_f32_32x32x16_bf16 v[144:159], v[192:195], v[200:203], v[144:159]
	v_mfma_f32_32x32x16_bf16 v[128:143], v[196:199], v[200:203], v[128:143]
	ds_read_b128 v[192:195], v185 offset:0
	ds_read_b128 v[196:199], v185 offset:0x2000
	ds_read_b128 v[200:203], v180 offset:0xc00
	s_waitcnt lgkmcnt(3)
	v_mfma_f32_32x32x16_bf16 v[144:159], v[204:207], v[212:215], v[144:159]
	v_mfma_f32_32x32x16_bf16 v[128:143], v[208:211], v[212:215], v[128:143]
	ds_read_b128 v[204:207], v188 offset:0x80
	ds_read_b128 v[208:211], v188 offset:0x2080
	ds_read_b128 v[212:215], v180 offset:0x1000
	s_waitcnt lgkmcnt(3)
	v_mfma_f32_32x32x16_bf16 v[144:159], v[192:195], v[200:203], v[144:159]
	v_mfma_f32_32x32x16_bf16 v[128:143], v[196:199], v[200:203], v[128:143]
	ds_read_b128 v[192:195], v187 offset:0x80
	ds_read_b128 v[196:199], v187 offset:0x2080
	ds_read_b128 v[200:203], v180 offset:0x1400
	s_waitcnt lgkmcnt(3)
	v_mfma_f32_32x32x16_bf16 v[144:159], v[204:207], v[212:215], v[144:159]
	v_mfma_f32_32x32x16_bf16 v[128:143], v[208:211], v[212:215], v[128:143]
	ds_read_b128 v[204:207], v186 offset:0x80
	ds_read_b128 v[208:211], v186 offset:0x2080
	ds_read_b128 v[186:189], v180 offset:0x1800
	s_waitcnt lgkmcnt(3)
	v_mfma_f32_32x32x16_bf16 v[144:159], v[192:195], v[200:203], v[144:159]
	v_mfma_f32_32x32x16_bf16 v[128:143], v[196:199], v[200:203], v[128:143]
	ds_read_b128 v[180:183], v185 offset:0x80
	ds_read_b128 v[192:195], v185 offset:0x2080
	s_waitcnt lgkmcnt(2)
	v_mfma_f32_32x32x16_bf16 v[144:159], v[204:207], v[186:189], v[144:159]
	v_mfma_f32_32x32x16_bf16 v[128:143], v[208:211], v[186:189], v[128:143]
	s_waitcnt lgkmcnt(0)
	v_mfma_f32_32x32x16_bf16 v[144:159], v[180:183], v[166:169], v[144:159]
	v_mfma_f32_32x32x16_bf16 v[128:143], v[192:195], v[166:169], v[128:143]
	s_bitcmp0_b32 s100, 8
	s_cbranch_scc1 .Lstg_a20
	s_waitcnt vmcnt(0)
	s_waitcnt lgkmcnt(0)
	s_barrier
.Lstg_a20:
	s_cmp_lt_i32 s79, 8
	s_cbranch_scc0 .LBB0_614
	v_subrev_u32_e32 v160, s96, v179
	v_cmp_gt_i32_e64 s[62:63], 26, v160
	v_cmp_gt_i32_e64 s[64:65], 27, v160
	v_cmp_gt_i32_e64 s[60:61], 25, v160
	s_and_b64 s[62:63], s[64:65], s[62:63]
	v_cmp_gt_i32_e64 s[58:59], 24, v160
	s_and_b64 s[60:61], s[62:63], s[60:61]
	v_cmp_gt_i32_e64 s[56:57], 19, v160
	s_and_b64 s[58:59], s[60:61], s[58:59]
	v_cmp_gt_i32_e64 s[54:55], 18, v160
	s_and_b64 s[56:57], s[58:59], s[56:57]
	v_cmp_gt_i32_e64 s[52:53], 17, v160
	s_and_b64 s[54:55], s[56:57], s[54:55]
	v_cmp_gt_i32_e64 s[50:51], 16, v160
	s_and_b64 s[52:53], s[54:55], s[52:53]
	v_cmp_gt_i32_e64 s[48:49], 11, v160
	s_and_b64 s[50:51], s[52:53], s[50:51]
	v_cmp_gt_i32_e64 s[46:47], 10, v160
	s_and_b64 s[48:49], s[50:51], s[48:49]
	v_cmp_gt_i32_e64 s[44:45], 9, v160
	s_and_b64 s[46:47], s[48:49], s[46:47]
	v_cmp_gt_i32_e64 s[42:43], 8, v160
	s_and_b64 s[44:45], s[46:47], s[44:45]
	v_cmp_gt_i32_e64 s[40:41], 3, v160
	s_and_b64 s[42:43], s[44:45], s[42:43]
	v_cmp_gt_i32_e64 s[38:39], 2, v160
	s_and_b64 s[40:41], s[42:43], s[40:41]
	v_cmp_gt_i32_e64 s[36:37], 1, v160
	s_and_b64 s[38:39], s[40:41], s[38:39]
	v_cmp_gt_i32_e64 s[34:35], 0, v160
	s_and_b64 s[36:37], s[38:39], s[36:37]
	s_and_b64 s[34:35], s[36:37], s[34:35]
	v_cmp_gt_i32_e64 s[30:31], 58, v160
	v_cndmask_b32_e64 v144, v144, v226, s[34:35]
	v_cmp_gt_i32_e64 s[34:35], 59, v160
	v_cmp_gt_i32_e64 s[28:29], 57, v160
	s_and_b64 s[30:31], s[34:35], s[30:31]
	v_cmp_gt_i32_e64 s[26:27], 56, v160
	s_and_b64 s[28:29], s[30:31], s[28:29]
	v_cmp_gt_i32_e64 s[24:25], 51, v160
	s_and_b64 s[26:27], s[28:29], s[26:27]
	v_cmp_gt_i32_e64 s[22:23], 50, v160
	s_and_b64 s[24:25], s[26:27], s[24:25]
	v_cmp_gt_i32_e64 s[20:21], 49, v160
	s_and_b64 s[22:23], s[24:25], s[22:23]
	v_cmp_gt_i32_e64 s[18:19], 48, v160
	s_and_b64 s[20:21], s[22:23], s[20:21]
	v_cmp_gt_i32_e64 s[16:17], 43, v160
	s_and_b64 s[18:19], s[20:21], s[18:19]
	v_cmp_gt_i32_e64 s[14:15], 42, v160
	s_and_b64 s[16:17], s[18:19], s[16:17]
	v_cmp_gt_i32_e64 s[12:13], 41, v160
	s_and_b64 s[14:15], s[16:17], s[14:15]
	v_cmp_gt_i32_e64 s[10:11], 40, v160
	s_and_b64 s[12:13], s[14:15], s[12:13]
	v_cmp_gt_i32_e64 s[8:9], 35, v160
	s_and_b64 s[10:11], s[12:13], s[10:11]
	v_cmp_gt_i32_e64 s[6:7], 34, v160
	s_and_b64 s[8:9], s[10:11], s[8:9]
	v_cmp_gt_i32_e64 s[4:5], 33, v160
	s_and_b64 s[6:7], s[8:9], s[6:7]
	v_cmp_gt_i32_e32 vcc, 32, v160
	s_and_b64 s[4:5], s[6:7], s[4:5]
	s_and_b64 vcc, s[4:5], vcc
	v_cndmask_b32_e64 v159, v159, v226, s[64:65]
	v_cndmask_b32_e64 v158, v158, v226, s[62:63]
	s_mov_b64 s[62:63], 0x100
	v_cndmask_b32_e64 v157, v157, v226, s[60:61]
	v_cndmask_b32_e64 v156, v156, v226, s[58:59]
	v_cndmask_b32_e64 v155, v155, v226, s[56:57]
	v_cndmask_b32_e64 v154, v154, v226, s[54:55]
	v_cndmask_b32_e64 v153, v153, v226, s[52:53]
	v_cndmask_b32_e64 v152, v152, v226, s[50:51]
	v_cndmask_b32_e64 v151, v151, v226, s[48:49]
	v_cndmask_b32_e64 v150, v150, v226, s[46:47]
	v_cndmask_b32_e64 v149, v149, v226, s[44:45]
	v_cndmask_b32_e64 v148, v148, v226, s[42:43]
	v_cndmask_b32_e64 v147, v147, v226, s[40:41]
	v_cndmask_b32_e64 v146, v146, v226, s[38:39]
	v_cndmask_b32_e64 v145, v145, v226, s[36:37]
	v_cndmask_b32_e64 v143, v143, v226, s[34:35]
	v_cndmask_b32_e64 v142, v142, v226, s[30:31]
	v_cndmask_b32_e64 v141, v141, v226, s[28:29]
	v_cndmask_b32_e64 v140, v140, v226, s[26:27]
	v_cndmask_b32_e64 v139, v139, v226, s[24:25]
	v_cndmask_b32_e64 v138, v138, v226, s[22:23]
	v_cndmask_b32_e64 v137, v137, v226, s[20:21]
	v_cndmask_b32_e64 v136, v136, v226, s[18:19]
	v_cndmask_b32_e64 v135, v135, v226, s[16:17]
	v_cndmask_b32_e64 v134, v134, v226, s[14:15]
	v_cndmask_b32_e64 v133, v133, v226, s[12:13]
	v_cndmask_b32_e64 v132, v132, v226, s[10:11]
	v_cndmask_b32_e64 v131, v131, v226, s[8:9]
	v_cndmask_b32_e64 v130, v130, v226, s[6:7]
	v_cndmask_b32_e64 v129, v129, v226, s[4:5]
	v_cndmask_b32_e32 v128, v128, v226, vcc
.LBB0_614:
	s_nop 8
	v_max_f32_e32 v160, v145, v145
	v_max_f32_e32 v166, v144, v144
	v_max_f32_e32 v160, v166, v160
	v_max3_f32 v160, v160, v146, v147
	v_max3_f32 v160, v160, v148, v149
	v_max3_f32 v160, v160, v150, v151
	v_max3_f32 v160, v160, v152, v153
	v_max3_f32 v160, v160, v154, v155
	v_max3_f32 v160, v160, v156, v157
	v_max3_f32 v160, v160, v158, v159
	v_max3_f32 v160, v160, v128, v129
	v_max3_f32 v160, v160, v130, v131
	v_max3_f32 v160, v160, v132, v133
	v_max3_f32 v160, v160, v134, v135
	v_max3_f32 v160, v160, v136, v137
	v_max3_f32 v160, v160, v138, v139
	v_max3_f32 v160, v160, v140, v141
	v_max3_f32 v160, v160, v142, v143
	v_mov_b32_e32 v166, v160
	s_nop 1
	v_permlane32_swap_b32_e32 v160, v166
	v_max_f32_e32 v166, v166, v166
	v_max_f32_e32 v160, v160, v160
	v_max_f32_e32 v160, v160, v166
	v_sub_f32_e32 v166, v160, v190
	v_mul_f32_e32 v166, 0x3db504f3, v166
	s_mov_b32 s4, 0x41000000
	v_cmp_ge_f32_e32 vcc, s4, v166
	s_cmp_eq_u64 vcc, exec
	v_max_f32_e32 v166, v190, v190
	s_cselect_b64 vcc, -1, 0
	v_max_f32_e32 v166, v166, v160
	v_sub_f32_e32 v160, v190, v166
	v_cndmask_b32_e32 v166, v166, v190, vcc
	v_mul_f32_e32 v166, 0xbe0293ee, v166
	v_fmamk_f32 v144, v144, 0x3e0293ee, v166
	v_fmamk_f32 v145, v145, 0x3e0293ee, v166
	v_fmamk_f32 v146, v146, 0x3e0293ee, v166
	v_fmamk_f32 v147, v147, 0x3e0293ee, v166
	v_fmamk_f32 v148, v148, 0x3e0293ee, v166
	v_fmamk_f32 v149, v149, 0x3e0293ee, v166
	v_fmamk_f32 v150, v150, 0x3e0293ee, v166
	v_fmamk_f32 v151, v151, 0x3e0293ee, v166
	v_fmamk_f32 v152, v152, 0x3e0293ee, v166
	v_fmamk_f32 v153, v153, 0x3e0293ee, v166
	v_fmamk_f32 v154, v154, 0x3e0293ee, v166
	v_fmamk_f32 v155, v155, 0x3e0293ee, v166
	v_fmamk_f32 v156, v156, 0x3e0293ee, v166
	v_fmamk_f32 v157, v157, 0x3e0293ee, v166
	v_fmamk_f32 v158, v158, 0x3e0293ee, v166
	v_fmamk_f32 v159, v159, 0x3e0293ee, v166
	v_fmamk_f32 v128, v128, 0x3e0293ee, v166
	v_fmamk_f32 v129, v129, 0x3e0293ee, v166
	v_fmamk_f32 v130, v130, 0x3e0293ee, v166
	v_fmamk_f32 v131, v131, 0x3e0293ee, v166
	v_fmamk_f32 v132, v132, 0x3e0293ee, v166
	v_fmamk_f32 v133, v133, 0x3e0293ee, v166
	v_fmamk_f32 v134, v134, 0x3e0293ee, v166
	v_fmamk_f32 v135, v135, 0x3e0293ee, v166
	v_fmamk_f32 v136, v136, 0x3e0293ee, v166
	v_fmamk_f32 v137, v137, 0x3e0293ee, v166
	v_fmamk_f32 v138, v138, 0x3e0293ee, v166
	v_fmamk_f32 v139, v139, 0x3e0293ee, v166
	v_fmamk_f32 v140, v140, 0x3e0293ee, v166
	v_fmamk_f32 v141, v141, 0x3e0293ee, v166
	v_fmamk_f32 v142, v142, 0x3e0293ee, v166
	v_fmac_f32_e32 v166, 0x3e0293ee, v143
	v_exp_f32_e32 v143, v144
	v_exp_f32_e32 v167, v145
	v_exp_f32_e32 v146, v146
	v_exp_f32_e32 v147, v147
	v_exp_f32_e32 v148, v148
	v_exp_f32_e32 v168, v128
	v_add_f32_e32 v128, 0, v143
	v_exp_f32_e32 v149, v149
	v_add_f32_e32 v128, v167, v128
	v_exp_f32_e32 v150, v150
	v_add_f32_e32 v128, v146, v128
	v_exp_f32_e32 v151, v151
	v_add_f32_e32 v128, v147, v128
	v_exp_f32_e32 v152, v152
	v_add_f32_e32 v128, v148, v128
	v_exp_f32_e32 v153, v153
	v_add_f32_e32 v128, v149, v128
	v_exp_f32_e32 v154, v154
	v_add_f32_e32 v128, v150, v128
	v_exp_f32_e32 v155, v155
	v_add_f32_e32 v128, v151, v128
	v_exp_f32_e32 v156, v156
	v_add_f32_e32 v128, v152, v128
	v_exp_f32_e32 v157, v157
	v_add_f32_e32 v128, v153, v128
	v_exp_f32_e32 v158, v158
	v_add_f32_e32 v128, v154, v128
	v_exp_f32_e32 v159, v159
	v_add_f32_e32 v128, v155, v128
	v_add_f32_e32 v128, v156, v128
	v_exp_f32_e32 v169, v129
	v_add_f32_e32 v128, v157, v128
	v_exp_f32_e32 v170, v130
	v_add_f32_e32 v128, v158, v128
	v_exp_f32_e32 v171, v131
	v_add_f32_e32 v128, v159, v128
	v_exp_f32_e32 v172, v132
	v_add_f32_e32 v128, v168, v128
	v_exp_f32_e32 v179, v133
	v_add_f32_e32 v128, v169, v128
	v_exp_f32_e32 v180, v134
	v_add_f32_e32 v128, v170, v128
	v_exp_f32_e32 v181, v135
	v_add_f32_e32 v128, v171, v128
	v_exp_f32_e32 v182, v136
	v_add_f32_e32 v128, v172, v128
	v_exp_f32_e32 v183, v137
	v_add_f32_e32 v128, v179, v128
	v_exp_f32_e32 v184, v138
	v_add_f32_e32 v128, v180, v128
	v_exp_f32_e32 v185, v139
	v_add_f32_e32 v128, v181, v128
	v_exp_f32_e32 v186, v140
	v_add_f32_e32 v128, v182, v128
	v_exp_f32_e32 v187, v141
	v_add_f32_e32 v128, v183, v128
	v_exp_f32_e32 v188, v142
	v_add_f32_e32 v128, v184, v128
	v_exp_f32_e32 v166, v166
	v_add_f32_e32 v128, v185, v128
	v_mul_f32_e32 v160, 0x3e0293ee, v160
	v_add_f32_e32 v128, v186, v128
	v_exp_f32_e32 v160, v160
	v_add_f32_e32 v128, v187, v128
	v_add_f32_e32 v128, v188, v128
	v_add_f32_e32 v144, v166, v128
	v_mov_b32_e32 v145, v144
	v_cvt_pk_bf16_f32 v128, v143, v167
	v_cvt_pk_bf16_f32 v129, v146, v147
	v_cvt_pk_bf16_f32 v130, v148, v149
	v_cvt_pk_bf16_f32 v131, v150, v151
	v_cvt_pk_bf16_f32 v132, v152, v153
	v_cvt_pk_bf16_f32 v133, v154, v155
	v_cvt_pk_bf16_f32 v134, v156, v157
	v_cvt_pk_bf16_f32 v135, v158, v159
	v_cvt_pk_bf16_f32 v136, v168, v169
	v_cvt_pk_bf16_f32 v137, v170, v171
	v_cvt_pk_bf16_f32 v138, v172, v179
	v_cvt_pk_bf16_f32 v139, v180, v181
	v_cvt_pk_bf16_f32 v140, v182, v183
	v_cvt_pk_bf16_f32 v141, v184, v185
	v_cvt_pk_bf16_f32 v142, v186, v187
	v_cvt_pk_bf16_f32 v143, v188, v166
	s_movk_i32 s75, 0x7fff
	s_mov_b32 s76, 0xf800000
	s_movk_i32 s84, 0x6800
	v_readlane_b32 s77, v255, 48
	v_readlane_b32 s6, v255, 57
	v_cndmask_b32_e64 v160, v160, 1.0, vcc
	v_permlane32_swap_b32_e32 v144, v145
	v_permlane32_swap_b32_e32 v128, v130
	v_permlane32_swap_b32_e32 v129, v131
	v_permlane32_swap_b32_e32 v132, v134
	v_permlane32_swap_b32_e32 v133, v135
	v_permlane32_swap_b32_e32 v136, v138
	v_permlane32_swap_b32_e32 v137, v139
	v_permlane32_swap_b32_e32 v140, v142
	v_permlane32_swap_b32_e32 v141, v143
	s_bitcmp1_b32 s100, 8
	s_cbranch_scc1 .Lstg_b24
	s_waitcnt vmcnt(0)
	s_waitcnt lgkmcnt(0)
	s_barrier
.Lstg_b24:
	v_mov_b64_e32 v[146:147], s[0:1]
	flat_load_dword v148, v[146:147] sc0 sc1
	s_waitcnt vmcnt(0)
	v_mov_b64_e32 v[146:147], s[70:71]
	flat_load_dword v146, v[146:147] sc0 sc1
	s_waitcnt vmcnt(0) lgkmcnt(0)
	v_readfirstlane_b32 s4, v148
	v_readfirstlane_b32 s5, v146
	s_nop 1
	v_lshl_add_u64 v[146:147], s[4:5], 0, v[162:163]
	s_mov_b32 s4, m0
	s_mov_b32 m0, s3
	s_nop 0
	global_load_lds_dwordx4 v[146:147], off
	s_mov_b32 m0, s4
	v_lshl_add_u64 v[148:149], v[146:147], 0, s[86:87]
	s_mov_b32 s3, m0
	s_mov_b32 m0, s69
	s_nop 0
	global_load_lds_dwordx4 v[148:149], off
	s_mov_b32 m0, s3
	v_lshl_add_u64 v[148:149], v[146:147], 0, s[62:63]
	s_mov_b32 s3, m0
	s_mov_b32 m0, s68
	s_nop 0
	global_load_lds_dwordx4 v[148:149], off
	s_mov_b32 m0, s3
	s_mov_b64 s[4:5], 0x180
	v_lshl_add_u64 v[146:147], v[146:147], 0, s[4:5]
	s_mov_b32 s3, m0
	s_mov_b32 m0, s2
	s_nop 0
	global_load_lds_dwordx4 v[146:147], off
	s_mov_b32 m0, s3
	v_cmp_gt_f32_e32 vcc, 1.0, v160
	s_cbranch_vccz .LBB0_551
	v_pk_mul_f32 v[126:127], v[126:127], v[160:161] op_sel_hi:[1,0]
	v_pk_mul_f32 v[124:125], v[124:125], v[160:161] op_sel_hi:[1,0]
	v_pk_mul_f32 v[122:123], v[122:123], v[160:161] op_sel_hi:[1,0]
	v_pk_mul_f32 v[120:121], v[120:121], v[160:161] op_sel_hi:[1,0]
	v_pk_mul_f32 v[118:119], v[118:119], v[160:161] op_sel_hi:[1,0]
	v_pk_mul_f32 v[116:117], v[116:117], v[160:161] op_sel_hi:[1,0]
	v_pk_mul_f32 v[114:115], v[114:115], v[160:161] op_sel_hi:[1,0]
	v_pk_mul_f32 v[112:113], v[112:113], v[160:161] op_sel_hi:[1,0]
	v_pk_mul_f32 v[110:111], v[110:111], v[160:161] op_sel_hi:[1,0]
	v_pk_mul_f32 v[108:109], v[108:109], v[160:161] op_sel_hi:[1,0]
	v_pk_mul_f32 v[106:107], v[106:107], v[160:161] op_sel_hi:[1,0]
	v_pk_mul_f32 v[104:105], v[104:105], v[160:161] op_sel_hi:[1,0]
	v_pk_mul_f32 v[102:103], v[102:103], v[160:161] op_sel_hi:[1,0]
	v_pk_mul_f32 v[100:101], v[100:101], v[160:161] op_sel_hi:[1,0]
	v_pk_mul_f32 v[98:99], v[98:99], v[160:161] op_sel_hi:[1,0]
	v_pk_mul_f32 v[96:97], v[96:97], v[160:161] op_sel_hi:[1,0]
	v_pk_mul_f32 v[94:95], v[94:95], v[160:161] op_sel_hi:[1,0]
	v_pk_mul_f32 v[92:93], v[92:93], v[160:161] op_sel_hi:[1,0]
	v_pk_mul_f32 v[90:91], v[90:91], v[160:161] op_sel_hi:[1,0]
	v_pk_mul_f32 v[88:89], v[88:89], v[160:161] op_sel_hi:[1,0]
	v_pk_mul_f32 v[86:87], v[86:87], v[160:161] op_sel_hi:[1,0]
	v_pk_mul_f32 v[84:85], v[84:85], v[160:161] op_sel_hi:[1,0]
	v_pk_mul_f32 v[82:83], v[82:83], v[160:161] op_sel_hi:[1,0]
	v_pk_mul_f32 v[80:81], v[80:81], v[160:161] op_sel_hi:[1,0]
	v_pk_mul_f32 v[78:79], v[78:79], v[160:161] op_sel_hi:[1,0]
	v_pk_mul_f32 v[76:77], v[76:77], v[160:161] op_sel_hi:[1,0]
	v_pk_mul_f32 v[74:75], v[74:75], v[160:161] op_sel_hi:[1,0]
	v_pk_mul_f32 v[72:73], v[72:73], v[160:161] op_sel_hi:[1,0]
	v_pk_mul_f32 v[70:71], v[70:71], v[160:161] op_sel_hi:[1,0]
	v_pk_mul_f32 v[68:69], v[68:69], v[160:161] op_sel_hi:[1,0]
	v_pk_mul_f32 v[66:67], v[66:67], v[160:161] op_sel_hi:[1,0]
	v_pk_mul_f32 v[64:65], v[64:65], v[160:161] op_sel_hi:[1,0]
	v_pk_mul_f32 v[62:63], v[62:63], v[160:161] op_sel_hi:[1,0]
	v_pk_mul_f32 v[60:61], v[60:61], v[160:161] op_sel_hi:[1,0]
	v_pk_mul_f32 v[58:59], v[58:59], v[160:161] op_sel_hi:[1,0]
	v_pk_mul_f32 v[56:57], v[56:57], v[160:161] op_sel_hi:[1,0]
	v_pk_mul_f32 v[54:55], v[54:55], v[160:161] op_sel_hi:[1,0]
	v_pk_mul_f32 v[52:53], v[52:53], v[160:161] op_sel_hi:[1,0]
	v_pk_mul_f32 v[50:51], v[50:51], v[160:161] op_sel_hi:[1,0]
	v_pk_mul_f32 v[48:49], v[48:49], v[160:161] op_sel_hi:[1,0]
	v_pk_mul_f32 v[46:47], v[46:47], v[160:161] op_sel_hi:[1,0]
	v_pk_mul_f32 v[44:45], v[44:45], v[160:161] op_sel_hi:[1,0]
	v_pk_mul_f32 v[42:43], v[42:43], v[160:161] op_sel_hi:[1,0]
	v_pk_mul_f32 v[40:41], v[40:41], v[160:161] op_sel_hi:[1,0]
	v_pk_mul_f32 v[38:39], v[38:39], v[160:161] op_sel_hi:[1,0]
	v_pk_mul_f32 v[36:37], v[36:37], v[160:161] op_sel_hi:[1,0]
	v_pk_mul_f32 v[34:35], v[34:35], v[160:161] op_sel_hi:[1,0]
	v_pk_mul_f32 v[32:33], v[32:33], v[160:161] op_sel_hi:[1,0]
	v_pk_mul_f32 v[30:31], v[30:31], v[160:161] op_sel_hi:[1,0]
	v_pk_mul_f32 v[28:29], v[28:29], v[160:161] op_sel_hi:[1,0]
	v_pk_mul_f32 v[26:27], v[26:27], v[160:161] op_sel_hi:[1,0]
	v_pk_mul_f32 v[24:25], v[24:25], v[160:161] op_sel_hi:[1,0]
	v_pk_mul_f32 v[22:23], v[22:23], v[160:161] op_sel_hi:[1,0]
	v_pk_mul_f32 v[20:21], v[20:21], v[160:161] op_sel_hi:[1,0]
	v_pk_mul_f32 v[18:19], v[18:19], v[160:161] op_sel_hi:[1,0]
	v_pk_mul_f32 v[16:17], v[16:17], v[160:161] op_sel_hi:[1,0]
	v_pk_mul_f32 v[14:15], v[14:15], v[160:161] op_sel_hi:[1,0]
	v_pk_mul_f32 v[12:13], v[12:13], v[160:161] op_sel_hi:[1,0]
	v_pk_mul_f32 v[10:11], v[10:11], v[160:161] op_sel_hi:[1,0]
	v_pk_mul_f32 v[8:9], v[8:9], v[160:161] op_sel_hi:[1,0]
	v_pk_mul_f32 v[6:7], v[6:7], v[160:161] op_sel_hi:[1,0]
	v_pk_mul_f32 v[4:5], v[4:5], v[160:161] op_sel_hi:[1,0]
	v_pk_mul_f32 v[2:3], v[2:3], v[160:161] op_sel_hi:[1,0]
	v_pk_mul_f32 v[0:1], v[0:1], v[160:161] op_sel_hi:[1,0]
	s_branch .LBB0_551

	.amdhsa_kernel _Z10hybrid_fwd4Args
		.amdhsa_group_segment_fixed_size 0
		.amdhsa_private_segment_fixed_size 0
		.amdhsa_kernarg_size 456
		.amdhsa_user_sgpr_count 2
		.amdhsa_user_sgpr_dispatch_ptr 0
		.amdhsa_user_sgpr_queue_ptr 0
		.amdhsa_user_sgpr_kernarg_segment_ptr 1
		.amdhsa_user_sgpr_dispatch_id 0
		.amdhsa_user_sgpr_kernarg_preload_length 0
		.amdhsa_user_sgpr_kernarg_preload_offset 0
		.amdhsa_user_sgpr_private_segment_size 0
		.amdhsa_uses_dynamic_stack 0
		.amdhsa_enable_private_segment 0
		.amdhsa_system_sgpr_workgroup_id_x 1
		.amdhsa_system_sgpr_workgroup_id_y 0
		.amdhsa_system_sgpr_workgroup_id_z 0
		.amdhsa_system_sgpr_workgroup_info 0
		.amdhsa_system_vgpr_workitem_id 0
		.amdhsa_next_free_vgpr 256
		.amdhsa_next_free_sgpr 102
		.amdhsa_accum_offset 256
		.amdhsa_reserve_vcc 1
		.amdhsa_float_round_mode_32 0
		.amdhsa_float_round_mode_16_64 0
		.amdhsa_float_denorm_mode_32 3
		.amdhsa_float_denorm_mode_16_64 3
		.amdhsa_dx10_clamp 1
		.amdhsa_ieee_mode 1
		.amdhsa_fp16_overflow 0
		.amdhsa_tg_split 0
		.amdhsa_exception_fp_ieee_invalid_op 0
		.amdhsa_exception_fp_denorm_src 0
		.amdhsa_exception_fp_ieee_div_zero 0
		.amdhsa_exception_fp_ieee_overflow 0
		.amdhsa_exception_fp_ieee_underflow 0
		.amdhsa_exception_fp_ieee_inexact 0
		.amdhsa_exception_int_div_zero 0
	.end_amdhsa_kernel

amdhsa.kernels:
  - .agpr_count:     0
    .args:
      - .offset:         0
        .size:           200
        .value_kind:     by_value
      - .offset:         200
        .size:           4
        .value_kind:     hidden_block_count_x
      - .offset:         204
        .size:           4
        .value_kind:     hidden_block_count_y
      - .offset:         208
        .size:           4
        .value_kind:     hidden_block_count_z
      - .offset:         212
        .size:           2
        .value_kind:     hidden_group_size_x
      - .offset:         214
        .size:           2
        .value_kind:     hidden_group_size_y
      - .offset:         216
        .size:           2
        .value_kind:     hidden_group_size_z
      - .offset:         218
        .size:           2
        .value_kind:     hidden_remainder_x
      - .offset:         220
        .size:           2
        .value_kind:     hidden_remainder_y
      - .offset:         222
        .size:           2
        .value_kind:     hidden_remainder_z
      - .offset:         240
        .size:           8
        .value_kind:     hidden_global_offset_x
      - .offset:         248
        .size:           8
        .value_kind:     hidden_global_offset_y
      - .offset:         256
        .size:           8
        .value_kind:     hidden_global_offset_z
      - .offset:         264
        .size:           2
        .value_kind:     hidden_grid_dims
      - .offset:         320
        .size:           4
        .value_kind:     hidden_dynamic_lds_size
    .group_segment_fixed_size: 0
    .kernarg_segment_align: 8
    .kernarg_segment_size: 456
    .language:       OpenCL C
    .language_version:
      - 2
      - 0
    .max_flat_workgroup_size: 512
    .name:           _Z10hybrid_fwd4Args
    .private_segment_fixed_size: 0
    .sgpr_count:     108
    .sgpr_spill_count: 92
    .symbol:         _Z10hybrid_fwd4Args.kd
    .uniform_work_group_size: 1
    .uses_dynamic_stack: false
    .vgpr_count:     256
    .vgpr_spill_count: 0
    .wavefront_size: 64
